# all 128 per-phase s_setprio flips in the 8 GEMM K-loops deleted (A/B of lever 4 step b)
# speedup vs baseline: 1.0031x; 1.0031x over previous
; #define PG8_STAGE(bufoff, gbase, v0, v1) do { \
;         __builtin_amdgcn_global_load_lds((const unsigned*)((const char*)(gbase) + (v0)), (LAS unsigned*)(lds + (bufoff) + ldsw), 16, 0, 0); \
;         __builtin_amdgcn_global_load_lds((const unsigned*)((const char*)(gbase) + (v1)), (LAS unsigned*)(lds + (bufoff) + ldsw + 8192), 16, 0, 0); } while (0)
; #define PG8_LDA(dst, b, h) do { _Pragma("unroll") for (int m = 0; m < 4; ++m) _Pragma("unroll") for (int k = 0; k < 2; ++k) dst[m][k] = *(const LAS bf16x8*)(lds + PG8_SA(b, h) + aoff + m * 2048 + k * 1024); } while (0)
; #define PG8_LDB(dst, b, h) do { _Pragma("unroll") for (int n = 0; n < 2; ++n) _Pragma("unroll") for (int k = 0; k < 2; ++k) dst[n][k] = *(const LAS bf16x8*)(lds + PG8_SB(b, h) + boff + n * 2048 + k * 1024); } while (0)
; #define PG8_MMA(ai, bj, At, Bt) do { __builtin_amdgcn_s_setprio(1); _Pragma("unroll") for (int m = 0; m < 4; ++m) _Pragma("unroll") for (int n = 0; n < 2; ++n) _Pragma("unroll") for (int k = 0; k < 2; ++k) \
;         acc[ai][bj][m][n] = __builtin_amdgcn_mfma_f32_16x16x32_bf16(Bt[n][k], At[m][k], acc[ai][bj][m][n], 0, 0, 0); __builtin_amdgcn_s_setprio(0); } while (0)
; #define PG8_WAIT_V(n) asm volatile("s_waitcnt vmcnt(" #n ")" ::: "memory")
; #define PG8_WAIT_L(n) asm volatile("s_waitcnt lgkmcnt(" #n ")" ::: "memory")
; #define PG8_BAR __builtin_amdgcn_s_barrier()
; #define PG8_SCHED __builtin_amdgcn_sched_barrier(0)
; template <class Epi, class Sched>
; __device__ __forceinline__ void gemm_phase(LAS unsigned char* lds, const int K, const Sched& S, const Epi& E) {
;     ...
;             PG8_LDB(B0, 0, 0); PG8_SCHED; PG8_LDA(At, 0, 0); PG8_STAGE(PG8_SA(1, 1), a1, c10, c11);
;             PG8_WAIT_L(8); PG8_BAR; PG8_WAIT_L(0); PG8_MMA(0, 0, At, B0); PG8_BAR; PG8_SCHED;
;             PG8_LDB(B1, 0, 1); PG8_STAGE(PG8_SB(0, 0), b2, voffB0, voffB1);
;             PG8_BAR; PG8_WAIT_L(0); PG8_MMA(0, 1, At, B1); PG8_BAR;
;             PG8_LDA(At, 0, 1); PG8_STAGE(PG8_SA(0, 0), a2, x00, x01);
;             PG8_BAR; PG8_WAIT_L(0); PG8_MMA(1, 0, At, B0); PG8_BAR; PG8_SCHED;
;             PG8_STAGE(PG8_SB(0, 1), b2 + hstep, voffB0, voffB1);
;             PG8_WAIT_V(6); PG8_BAR; PG8_MMA(1, 1, At, B1); PG8_BAR;
.LBB0_246:
	s_add_u32 s22, s4, s20
	s_addc_u32 s23, s5, s21
	s_add_u32 s24, s22, 0x34c30100
	ds_read_b128 v[166:169], v158
	ds_read_b128 v[170:173], v158 offset:1024
	ds_read_b128 v[174:177], v158 offset:2048
	ds_read_b128 v[178:181], v158 offset:3072
	s_addc_u32 s25, s23, 0
	s_add_u32 s47, s19, s20
	s_addc_u32 s48, s45, s21
	s_cmpk_eq_i32 s20, 0xf00
	s_cselect_b64 vcc, -1, 0
	s_and_b64 s[22:23], vcc, exec
	v_cndmask_b32_e32 v134, v141, v161, vcc
	s_cselect_b32 s25, s7, s25
	s_cselect_b32 s24, s6, s24
	v_cndmask_b32_e32 v143, v142, v163, vcc
	s_cselect_b32 s23, s3, s48
	s_cselect_b32 s22, s2, s47
	v_cndmask_b32_e32 v206, v140, v162, vcc
	s_mov_b32 m0, s40
	v_lshl_add_u64 v[216:217], v[148:149], 0, s[20:21]
	ds_read_b128 v[182:185], v159
	ds_read_b128 v[186:189], v159 offset:1024
	ds_read_b128 v[190:193], v159 offset:2048
	ds_read_b128 v[194:197], v159 offset:3072
	ds_read_b128 v[198:201], v159 offset:4096
	ds_read_b128 v[202:205], v159 offset:5120
	ds_read_b128 v[208:211], v159 offset:6144
	ds_read_b128 v[212:215], v159 offset:7168
	global_load_lds_dwordx4 v[216:217], off
	v_lshl_add_u64 v[216:217], v[146:147], 0, s[20:21]
	s_add_i32 m0, s29, 0xe000
	s_nop 0
	global_load_lds_dwordx4 v[216:217], off
	s_waitcnt lgkmcnt(8)
	s_barrier
	s_waitcnt lgkmcnt(0)
	s_waitcnt lgkmcnt(0)
	v_mfma_f32_16x16x32_bf16 v[126:129], v[166:169], v[182:185], v[126:129]
	v_mfma_f32_16x16x32_bf16 v[122:125], v[174:177], v[182:185], v[122:125]
	v_mfma_f32_16x16x32_bf16 v[118:121], v[166:169], v[190:193], v[118:121]
	v_mfma_f32_16x16x32_bf16 v[110:113], v[174:177], v[190:193], v[110:113]
	v_mfma_f32_16x16x32_bf16 v[102:105], v[166:169], v[198:201], v[102:105]
	v_mfma_f32_16x16x32_bf16 v[94:97], v[174:177], v[198:201], v[94:97]
	v_mfma_f32_16x16x32_bf16 v[86:89], v[166:169], v[208:211], v[86:89]
	v_mfma_f32_16x16x32_bf16 v[78:81], v[174:177], v[208:211], v[78:81]
	v_mfma_f32_16x16x32_bf16 v[126:129], v[170:173], v[186:189], v[126:129]
	v_mfma_f32_16x16x32_bf16 v[122:125], v[178:181], v[186:189], v[122:125]
	v_mfma_f32_16x16x32_bf16 v[118:121], v[170:173], v[194:197], v[118:121]
	v_mfma_f32_16x16x32_bf16 v[110:113], v[178:181], v[194:197], v[110:113]
	v_mfma_f32_16x16x32_bf16 v[102:105], v[170:173], v[202:205], v[102:105]
	v_mfma_f32_16x16x32_bf16 v[94:97], v[178:181], v[202:205], v[94:97]
	v_mfma_f32_16x16x32_bf16 v[86:89], v[170:173], v[212:215], v[86:89]
	v_mfma_f32_16x16x32_bf16 v[78:81], v[178:181], v[212:215], v[78:81]
	s_barrier
	s_add_i32 s47, s37, s27
	v_lshl_add_u64 v[232:233], s[22:23], 0, v[132:133]
	s_mov_b32 m0, s47
	ds_read_b128 v[216:219], v160
	ds_read_b128 v[220:223], v160 offset:1024
	ds_read_b128 v[224:227], v160 offset:2048
	ds_read_b128 v[228:231], v160 offset:3072
	global_load_lds_dwordx4 v[232:233], off
	v_lshl_add_u64 v[234:235], s[22:23], 0, v[130:131]
	s_add_i32 m0, s47, 0x2000
	s_nop 0
	global_load_lds_dwordx4 v[234:235], off
	s_barrier
	s_waitcnt lgkmcnt(0)
	s_waitcnt lgkmcnt(0)
	v_mfma_f32_16x16x32_bf16 v[114:117], v[216:219], v[182:185], v[114:117]
	v_mfma_f32_16x16x32_bf16 v[106:109], v[224:227], v[182:185], v[106:109]
	v_mfma_f32_16x16x32_bf16 v[98:101], v[216:219], v[190:193], v[98:101]
	v_mfma_f32_16x16x32_bf16 v[90:93], v[224:227], v[190:193], v[90:93]
	v_mfma_f32_16x16x32_bf16 v[82:85], v[216:219], v[198:201], v[82:85]
	v_mfma_f32_16x16x32_bf16 v[74:77], v[224:227], v[198:201], v[74:77]
	v_mfma_f32_16x16x32_bf16 v[70:73], v[216:219], v[208:211], v[70:73]
	v_mfma_f32_16x16x32_bf16 v[66:69], v[224:227], v[208:211], v[66:69]
	v_mfma_f32_16x16x32_bf16 v[114:117], v[220:223], v[186:189], v[114:117]
	v_mfma_f32_16x16x32_bf16 v[106:109], v[228:231], v[186:189], v[106:109]
	v_mfma_f32_16x16x32_bf16 v[98:101], v[220:223], v[194:197], v[98:101]
	v_mfma_f32_16x16x32_bf16 v[90:93], v[228:231], v[194:197], v[90:93]
	v_mfma_f32_16x16x32_bf16 v[82:85], v[220:223], v[202:205], v[82:85]
	v_mfma_f32_16x16x32_bf16 v[74:77], v[228:231], v[202:205], v[74:77]
	v_mfma_f32_16x16x32_bf16 v[70:73], v[220:223], v[212:215], v[70:73]
	v_mfma_f32_16x16x32_bf16 v[66:69], v[228:231], v[212:215], v[66:69]
	s_mov_b32 m0, s29
	s_barrier
	ds_read_b128 v[182:185], v159 offset:16384
	ds_read_b128 v[186:189], v159 offset:17408
	ds_read_b128 v[190:193], v159 offset:18432
	ds_read_b128 v[194:197], v159 offset:19456
	ds_read_b128 v[198:201], v159 offset:20480
	ds_read_b128 v[202:205], v159 offset:21504
	ds_read_b128 v[208:211], v159 offset:22528
	ds_read_b128 v[212:215], v159 offset:23552
	global_load_lds_dwordx4 v134, s[24:25]
	s_mov_b32 m0, s30
	v_mov_b32_e32 v207, v135
	global_load_lds_dwordx4 v206, s[24:25]
	s_barrier
	s_waitcnt lgkmcnt(0)
	v_lshl_add_u64 v[236:237], s[24:25], 0, v[134:135]
	v_lshl_add_u64 v[206:207], s[24:25], 0, v[206:207]
	s_waitcnt lgkmcnt(0)
	v_mfma_f32_16x16x32_bf16 v[62:65], v[166:169], v[182:185], v[62:65]
	v_mfma_f32_16x16x32_bf16 v[58:61], v[174:177], v[182:185], v[58:61]
	v_mfma_f32_16x16x32_bf16 v[54:57], v[166:169], v[190:193], v[54:57]
	v_mfma_f32_16x16x32_bf16 v[46:49], v[174:177], v[190:193], v[46:49]
	v_mfma_f32_16x16x32_bf16 v[38:41], v[166:169], v[198:201], v[38:41]
	v_mfma_f32_16x16x32_bf16 v[30:33], v[174:177], v[198:201], v[30:33]
	v_mfma_f32_16x16x32_bf16 v[22:25], v[166:169], v[208:211], v[22:25]
	v_mfma_f32_16x16x32_bf16 v[14:17], v[174:177], v[208:211], v[14:17]
	v_mfma_f32_16x16x32_bf16 v[62:65], v[170:173], v[186:189], v[62:65]
	v_mfma_f32_16x16x32_bf16 v[58:61], v[178:181], v[186:189], v[58:61]
	v_mfma_f32_16x16x32_bf16 v[54:57], v[170:173], v[194:197], v[54:57]
	v_mfma_f32_16x16x32_bf16 v[46:49], v[178:181], v[194:197], v[46:49]
	v_mfma_f32_16x16x32_bf16 v[38:41], v[170:173], v[202:205], v[38:41]
	v_mfma_f32_16x16x32_bf16 v[30:33], v[178:181], v[202:205], v[30:33]
	v_mfma_f32_16x16x32_bf16 v[22:25], v[170:173], v[212:215], v[22:25]
	v_mfma_f32_16x16x32_bf16 v[14:17], v[178:181], v[212:215], v[14:17]
	s_barrier
; #define PG8_STAGE(bufoff, gbase, v0, v1) do { \
;         __builtin_amdgcn_global_load_lds((const unsigned*)((const char*)(gbase) + (v0)), (LAS unsigned*)(lds + (bufoff) + ldsw), 16, 0, 0); \
;         __builtin_amdgcn_global_load_lds((const unsigned*)((const char*)(gbase) + (v1)), (LAS unsigned*)(lds + (bufoff) + ldsw + 8192), 16, 0, 0); } while (0)
; #define PG8_LDA(dst, b, h) do { _Pragma("unroll") for (int m = 0; m < 4; ++m) _Pragma("unroll") for (int k = 0; k < 2; ++k) dst[m][k] = *(const LAS bf16x8*)(lds + PG8_SA(b, h) + aoff + m * 2048 + k * 1024); } while (0)
; #define PG8_LDB(dst, b, h) do { _Pragma("unroll") for (int n = 0; n < 2; ++n) _Pragma("unroll") for (int k = 0; k < 2; ++k) dst[n][k] = *(const LAS bf16x8*)(lds + PG8_SB(b, h) + boff + n * 2048 + k * 1024); } while (0)
; #define PG8_MMA(ai, bj, At, Bt) do { __builtin_amdgcn_s_setprio(1); _Pragma("unroll") for (int m = 0; m < 4; ++m) _Pragma("unroll") for (int n = 0; n < 2; ++n) _Pragma("unroll") for (int k = 0; k < 2; ++k) \
;         acc[ai][bj][m][n] = __builtin_amdgcn_mfma_f32_16x16x32_bf16(Bt[n][k], At[m][k], acc[ai][bj][m][n], 0, 0, 0); __builtin_amdgcn_s_setprio(0); } while (0)
; #define PG8_WAIT_V(n) asm volatile("s_waitcnt vmcnt(" #n ")" ::: "memory")
; #define PG8_WAIT_L(n) asm volatile("s_waitcnt lgkmcnt(" #n ")" ::: "memory")
; #define PG8_BAR __builtin_amdgcn_s_barrier()
; #define PG8_SCHED __builtin_amdgcn_sched_barrier(0)
; template <class Epi, class Sched>
; __device__ __forceinline__ void gemm_phase(LAS unsigned char* lds, const int K, const Sched& S, const Epi& E) {
;     ...
;             PG8_WAIT_V(6); PG8_BAR; PG8_MMA(1, 1, At, B1); PG8_BAR;
;             PG8_LDB(B0, 1, 0); PG8_SCHED; PG8_LDA(At, 1, 0); PG8_STAGE(PG8_SA(0, 1), a2, x10, x11);
;             PG8_WAIT_L(8); PG8_BAR; PG8_WAIT_L(0); PG8_MMA(0, 0, At, B0); PG8_BAR; PG8_SCHED;
;             PG8_LDB(B1, 1, 1); PG8_STAGE(PG8_SB(1, 0), b3, voffB0, voffB1);
;             PG8_BAR; PG8_WAIT_L(0); PG8_MMA(0, 1, At, B1); PG8_BAR;
;             PG8_LDA(At, 1, 1); PG8_STAGE(PG8_SA(1, 0), a3, x00, x01);
;             PG8_BAR; PG8_WAIT_L(0); PG8_MMA(1, 0, At, B0); PG8_BAR; PG8_SCHED;
	s_add_u32 s48, s22, 0x80000
	s_addc_u32 s49, s23, 0
	s_add_i32 s47, s38, s27
	v_lshl_add_u64 v[166:167], s[48:49], 0, v[132:133]
	s_mov_b32 m0, s47
	s_nop 0
	global_load_lds_dwordx4 v[166:167], off
	v_lshl_add_u64 v[166:167], s[48:49], 0, v[130:131]
	s_add_i32 m0, s47, 0x2000
	s_nop 0
	global_load_lds_dwordx4 v[166:167], off
	s_waitcnt vmcnt(6)
	s_barrier
	v_mfma_f32_16x16x32_bf16 v[50:53], v[216:219], v[182:185], v[50:53]
	v_mfma_f32_16x16x32_bf16 v[42:45], v[224:227], v[182:185], v[42:45]
	v_mfma_f32_16x16x32_bf16 v[34:37], v[216:219], v[190:193], v[34:37]
	v_mfma_f32_16x16x32_bf16 v[26:29], v[224:227], v[190:193], v[26:29]
	v_mfma_f32_16x16x32_bf16 v[18:21], v[216:219], v[198:201], v[18:21]
	v_mfma_f32_16x16x32_bf16 v[10:13], v[224:227], v[198:201], v[10:13]
	v_mfma_f32_16x16x32_bf16 v[6:9], v[216:219], v[208:211], v[6:9]
	v_mfma_f32_16x16x32_bf16 v[2:5], v[224:227], v[208:211], v[2:5]
	v_mfma_f32_16x16x32_bf16 v[50:53], v[220:223], v[186:189], v[50:53]
	v_mfma_f32_16x16x32_bf16 v[42:45], v[228:231], v[186:189], v[42:45]
	v_mfma_f32_16x16x32_bf16 v[34:37], v[220:223], v[194:197], v[34:37]
	v_mfma_f32_16x16x32_bf16 v[26:29], v[228:231], v[194:197], v[26:29]
	v_mfma_f32_16x16x32_bf16 v[18:21], v[220:223], v[202:205], v[18:21]
	v_mfma_f32_16x16x32_bf16 v[10:13], v[228:231], v[202:205], v[10:13]
	v_mfma_f32_16x16x32_bf16 v[6:9], v[220:223], v[212:215], v[6:9]
	v_mfma_f32_16x16x32_bf16 v[2:5], v[228:231], v[212:215], v[2:5]
	s_add_i32 s47, 0, 0x18000
	v_add_u32_e32 v134, s47, v156
	s_barrier
	ds_read_b128 v[166:169], v134
	ds_read_b128 v[170:173], v134 offset:1024
	ds_read_b128 v[174:177], v134 offset:2048
	ds_read_b128 v[178:181], v134 offset:3072
	s_mov_b32 m0, s31
	ds_read_b128 v[182:185], v159 offset:32768
	ds_read_b128 v[186:189], v159 offset:33792
	ds_read_b128 v[190:193], v159 offset:34816
	ds_read_b128 v[194:197], v159 offset:35840
	ds_read_b128 v[198:201], v159 offset:36864
	ds_read_b128 v[202:205], v159 offset:37888
	ds_read_b128 v[208:211], v159 offset:38912
	ds_read_b128 v[212:215], v159 offset:39936
	v_cndmask_b32_e32 v134, v144, v164, vcc
	global_load_lds_dwordx4 v143, s[24:25]
	s_mov_b32 m0, s33
	s_nop 0
	global_load_lds_dwordx4 v134, s[24:25]
	s_waitcnt lgkmcnt(8)
	s_barrier
	s_waitcnt lgkmcnt(0)
	s_waitcnt lgkmcnt(0)
	v_mfma_f32_16x16x32_bf16 v[126:129], v[166:169], v[182:185], v[126:129]
	v_mfma_f32_16x16x32_bf16 v[122:125], v[174:177], v[182:185], v[122:125]
	v_mfma_f32_16x16x32_bf16 v[118:121], v[166:169], v[190:193], v[118:121]
	v_mfma_f32_16x16x32_bf16 v[110:113], v[174:177], v[190:193], v[110:113]
	v_mfma_f32_16x16x32_bf16 v[102:105], v[166:169], v[198:201], v[102:105]
	v_mfma_f32_16x16x32_bf16 v[94:97], v[174:177], v[198:201], v[94:97]
	v_mfma_f32_16x16x32_bf16 v[86:89], v[166:169], v[208:211], v[86:89]
	v_mfma_f32_16x16x32_bf16 v[78:81], v[174:177], v[208:211], v[78:81]
	v_mfma_f32_16x16x32_bf16 v[126:129], v[170:173], v[186:189], v[126:129]
	v_mfma_f32_16x16x32_bf16 v[122:125], v[178:181], v[186:189], v[122:125]
	v_mfma_f32_16x16x32_bf16 v[118:121], v[170:173], v[194:197], v[118:121]
	v_mfma_f32_16x16x32_bf16 v[110:113], v[178:181], v[194:197], v[110:113]
	v_mfma_f32_16x16x32_bf16 v[102:105], v[170:173], v[202:205], v[102:105]
	v_mfma_f32_16x16x32_bf16 v[94:97], v[178:181], v[202:205], v[94:97]
	v_mfma_f32_16x16x32_bf16 v[86:89], v[170:173], v[212:215], v[86:89]
	v_mfma_f32_16x16x32_bf16 v[78:81], v[178:181], v[212:215], v[78:81]
	s_barrier
	s_add_i32 s24, 0, 0x1c000
	s_add_i32 s25, s47, s27
	v_add_u32_e32 v134, s24, v156
	v_lshl_add_u64 v[232:233], v[232:233], 0, s[14:15]
	s_mov_b32 m0, s25
	ds_read_b128 v[216:219], v134
	ds_read_b128 v[220:223], v134 offset:1024
	ds_read_b128 v[224:227], v134 offset:2048
	ds_read_b128 v[228:231], v134 offset:3072
	global_load_lds_dwordx4 v[232:233], off
	v_lshl_add_u64 v[232:233], v[234:235], 0, s[14:15]
	s_add_i32 m0, s25, 0x2000
	s_nop 0
	global_load_lds_dwordx4 v[232:233], off
	s_barrier
	s_waitcnt lgkmcnt(0)
	s_waitcnt lgkmcnt(0)
	v_mfma_f32_16x16x32_bf16 v[114:117], v[216:219], v[182:185], v[114:117]
	v_mfma_f32_16x16x32_bf16 v[106:109], v[224:227], v[182:185], v[106:109]
	v_mfma_f32_16x16x32_bf16 v[98:101], v[216:219], v[190:193], v[98:101]
	v_mfma_f32_16x16x32_bf16 v[90:93], v[224:227], v[190:193], v[90:93]
	v_mfma_f32_16x16x32_bf16 v[82:85], v[216:219], v[198:201], v[82:85]
	v_mfma_f32_16x16x32_bf16 v[74:77], v[224:227], v[198:201], v[74:77]
	v_mfma_f32_16x16x32_bf16 v[70:73], v[216:219], v[208:211], v[70:73]
	v_mfma_f32_16x16x32_bf16 v[66:69], v[224:227], v[208:211], v[66:69]
	v_mfma_f32_16x16x32_bf16 v[114:117], v[220:223], v[186:189], v[114:117]
	v_mfma_f32_16x16x32_bf16 v[106:109], v[228:231], v[186:189], v[106:109]
	v_mfma_f32_16x16x32_bf16 v[98:101], v[220:223], v[194:197], v[98:101]
	v_mfma_f32_16x16x32_bf16 v[90:93], v[228:231], v[194:197], v[90:93]
	v_mfma_f32_16x16x32_bf16 v[82:85], v[220:223], v[202:205], v[82:85]
	v_mfma_f32_16x16x32_bf16 v[74:77], v[228:231], v[202:205], v[74:77]
	v_mfma_f32_16x16x32_bf16 v[70:73], v[220:223], v[212:215], v[70:73]
	v_mfma_f32_16x16x32_bf16 v[66:69], v[228:231], v[212:215], v[66:69]
	s_mov_b32 m0, s35
	v_lshl_add_u64 v[232:233], v[236:237], 0, s[14:15]
	s_barrier
	ds_read_b128 v[182:185], v159 offset:49152
	ds_read_b128 v[186:189], v159 offset:50176
	ds_read_b128 v[190:193], v159 offset:51200
	ds_read_b128 v[194:197], v159 offset:52224
	ds_read_b128 v[198:201], v159 offset:53248
	ds_read_b128 v[202:205], v159 offset:54272
	ds_read_b128 v[208:211], v159 offset:55296
	ds_read_b128 v[212:215], v159 offset:56320
	global_load_lds_dwordx4 v[232:233], off
	v_lshl_add_u64 v[206:207], v[206:207], 0, s[14:15]
	s_mov_b32 m0, s36
	s_nop 0
	global_load_lds_dwordx4 v[206:207], off
	s_barrier
; #define PG8_STAGE(bufoff, gbase, v0, v1) do { \
;         __builtin_amdgcn_global_load_lds((const unsigned*)((const char*)(gbase) + (v0)), (LAS unsigned*)(lds + (bufoff) + ldsw), 16, 0, 0); \
;         __builtin_amdgcn_global_load_lds((const unsigned*)((const char*)(gbase) + (v1)), (LAS unsigned*)(lds + (bufoff) + ldsw + 8192), 16, 0, 0); } while (0)
; #define PG8_MMA(ai, bj, At, Bt) do { __builtin_amdgcn_s_setprio(1); _Pragma("unroll") for (int m = 0; m < 4; ++m) _Pragma("unroll") for (int n = 0; n < 2; ++n) _Pragma("unroll") for (int k = 0; k < 2; ++k) \
;         acc[ai][bj][m][n] = __builtin_amdgcn_mfma_f32_16x16x32_bf16(Bt[n][k], At[m][k], acc[ai][bj][m][n], 0, 0, 0); __builtin_amdgcn_s_setprio(0); } while (0)
; #define PG8_WAIT_V(n) asm volatile("s_waitcnt vmcnt(" #n ")" ::: "memory")
; #define PG8_WAIT_L(n) asm volatile("s_waitcnt lgkmcnt(" #n ")" ::: "memory")
; #define PG8_BAR __builtin_amdgcn_s_barrier()
; #define PG8_SCHED __builtin_amdgcn_sched_barrier(0)
; template <class Epi, class Sched>
; __device__ __forceinline__ void gemm_phase(LAS unsigned char* lds, const int K, const Sched& S, const Epi& E) {
;     ...
;             PG8_BAR; PG8_WAIT_L(0); PG8_MMA(1, 0, At, B0); PG8_BAR; PG8_SCHED;
;             PG8_STAGE(PG8_SB(1, 1), b3 + hstep, voffB0, voffB1);
;             PG8_WAIT_V(6); PG8_BAR; PG8_MMA(1, 1, At, B1); PG8_BAR;
	s_waitcnt lgkmcnt(0)
	s_waitcnt lgkmcnt(0)
	v_mfma_f32_16x16x32_bf16 v[62:65], v[166:169], v[182:185], v[62:65]
	v_mfma_f32_16x16x32_bf16 v[58:61], v[174:177], v[182:185], v[58:61]
	v_mfma_f32_16x16x32_bf16 v[54:57], v[166:169], v[190:193], v[54:57]
	v_mfma_f32_16x16x32_bf16 v[46:49], v[174:177], v[190:193], v[46:49]
	v_mfma_f32_16x16x32_bf16 v[38:41], v[166:169], v[198:201], v[38:41]
	v_mfma_f32_16x16x32_bf16 v[30:33], v[174:177], v[198:201], v[30:33]
	v_mfma_f32_16x16x32_bf16 v[22:25], v[166:169], v[208:211], v[22:25]
	v_mfma_f32_16x16x32_bf16 v[14:17], v[174:177], v[208:211], v[14:17]
	v_mfma_f32_16x16x32_bf16 v[62:65], v[170:173], v[186:189], v[62:65]
	v_mfma_f32_16x16x32_bf16 v[58:61], v[178:181], v[186:189], v[58:61]
	v_mfma_f32_16x16x32_bf16 v[54:57], v[170:173], v[194:197], v[54:57]
	v_mfma_f32_16x16x32_bf16 v[46:49], v[178:181], v[194:197], v[46:49]
	v_mfma_f32_16x16x32_bf16 v[38:41], v[170:173], v[202:205], v[38:41]
	v_mfma_f32_16x16x32_bf16 v[30:33], v[178:181], v[202:205], v[30:33]
	v_mfma_f32_16x16x32_bf16 v[22:25], v[170:173], v[212:215], v[22:25]
	v_mfma_f32_16x16x32_bf16 v[14:17], v[178:181], v[212:215], v[14:17]
	s_barrier
	s_add_u32 s22, s22, 0x80080
	s_addc_u32 s23, s23, 0
	s_add_i32 s24, s24, s27
	v_lshl_add_u64 v[166:167], s[22:23], 0, v[132:133]
	s_mov_b32 m0, s24
	s_nop 0
	global_load_lds_dwordx4 v[166:167], off
	v_lshl_add_u64 v[166:167], s[22:23], 0, v[130:131]
	s_add_i32 m0, s24, 0x2000
	s_nop 0
	global_load_lds_dwordx4 v[166:167], off
	s_waitcnt vmcnt(6)
	s_barrier
	v_mfma_f32_16x16x32_bf16 v[50:53], v[216:219], v[182:185], v[50:53]
	v_mfma_f32_16x16x32_bf16 v[42:45], v[224:227], v[182:185], v[42:45]
	v_mfma_f32_16x16x32_bf16 v[34:37], v[216:219], v[190:193], v[34:37]
	v_mfma_f32_16x16x32_bf16 v[26:29], v[224:227], v[190:193], v[26:29]
	v_mfma_f32_16x16x32_bf16 v[18:21], v[216:219], v[198:201], v[18:21]
	v_mfma_f32_16x16x32_bf16 v[10:13], v[224:227], v[198:201], v[10:13]
	v_mfma_f32_16x16x32_bf16 v[6:9], v[216:219], v[208:211], v[6:9]
	v_mfma_f32_16x16x32_bf16 v[2:5], v[224:227], v[208:211], v[2:5]
	v_mfma_f32_16x16x32_bf16 v[50:53], v[220:223], v[186:189], v[50:53]
	v_mfma_f32_16x16x32_bf16 v[42:45], v[228:231], v[186:189], v[42:45]
	v_mfma_f32_16x16x32_bf16 v[34:37], v[220:223], v[194:197], v[34:37]
	v_mfma_f32_16x16x32_bf16 v[26:29], v[228:231], v[194:197], v[26:29]
	v_mfma_f32_16x16x32_bf16 v[18:21], v[220:223], v[202:205], v[18:21]
	v_mfma_f32_16x16x32_bf16 v[10:13], v[228:231], v[202:205], v[10:13]
	v_mfma_f32_16x16x32_bf16 v[6:9], v[220:223], v[212:215], v[6:9]
	v_mfma_f32_16x16x32_bf16 v[2:5], v[228:231], v[212:215], v[2:5]
	s_add_i32 s46, s46, 2
	s_add_u32 s20, s20, 0x100
	s_addc_u32 s21, s21, 0
	s_cmp_gt_u32 s46, 29
	s_barrier
	s_cbranch_scc0 .LBB0_246
; __device__ __forceinline__ unsigned cvt_pk_bf16(float lo, float hi) { unsigned r; asm volatile("v_cvt_pk_bf16_f32 %0, %1, %2" : "=v"(r) : "v"(lo), "v"(hi)); return r; }
;     __device__ __forceinline__ void operator()(const f32x4 (&acc)[2][2][4][2], const Unit& u, int wr, int wc, int fr, int fq) const {
;         const int row0 = u.rbase + wr * 64 + fr, col0 = u.pn * BM + wc * 32 + 8 * fq;
; #pragma unroll
;         for (int ai = 0; ai < 2; ++ai)
; #pragma unroll
;             for (int m = 0; m < 4; ++m) { bf16_t* rowp = O + (size_t)(row0 + ai * HALF + m * 16) * ldc + col0;
; #pragma unroll
;                 for (int bj = 0; bj < 2; ++bj) { const f32x4 v0 = acc[ai][bj][m][0], v1 = acc[ai][bj][m][1];
;                     u32x4 w; w.x = cvt_pk_bf16(v0[0], v0[1]); w.y = cvt_pk_bf16(v0[2], v0[3]); w.z = cvt_pk_bf16(v1[0], v1[1]); w.w = cvt_pk_bf16(v1[2], v1[3]);
;                     *(u32x4*)(rowp + bj * HALF) = w; } }
;     }
	v_lshl_or_b32 v142, s44, 8, v157
	v_add_u32_e32 v134, s43, v155
	v_ashrrev_i32_e32 v143, 31, v142
	v_mov_b64_e32 v[140:141], s[8:9]
	v_mad_i64_i32 v[144:145], s[20:21], v134, s39, v[140:141]
	v_lshlrev_b64 v[142:143], 1, v[142:143]
	v_lshl_add_u64 v[144:145], v[144:145], 0, v[142:143]
	v_cvt_pk_bf16_f32 v126, v126, v127
	v_cvt_pk_bf16_f32 v127, v128, v129
	v_cvt_pk_bf16_f32 v128, v122, v123
	v_cvt_pk_bf16_f32 v129, v124, v125
	global_store_dwordx4 v[144:145], v[126:129], off
	v_cvt_pk_bf16_f32 v114, v114, v115
	v_cvt_pk_bf16_f32 v115, v116, v117
	v_cvt_pk_bf16_f32 v116, v106, v107
	v_add_u32_e32 v106, 16, v134
	v_mad_i64_i32 v[106:107], s[20:21], v106, s39, v[140:141]
	v_cvt_pk_bf16_f32 v117, v108, v109
	global_store_dwordx4 v[144:145], v[114:117], off offset:256
	s_and_b64 vcc, exec, s[0:1]
	s_mov_b32 s44, s18
	v_lshl_add_u64 v[114:115], v[106:107], 0, v[142:143]
	v_cvt_pk_bf16_f32 v106, v118, v119
	v_cvt_pk_bf16_f32 v107, v120, v121
	v_cvt_pk_bf16_f32 v108, v110, v111
	v_cvt_pk_bf16_f32 v109, v112, v113
	global_store_dwordx4 v[114:115], v[106:109], off
	v_cvt_pk_bf16_f32 v98, v98, v99
	v_cvt_pk_bf16_f32 v99, v100, v101
	v_cvt_pk_bf16_f32 v100, v90, v91
	v_add_u32_e32 v90, 32, v134
	v_mad_i64_i32 v[90:91], s[20:21], v90, s39, v[140:141]
	v_cvt_pk_bf16_f32 v101, v92, v93
	global_store_dwordx4 v[114:115], v[98:101], off offset:256
	s_mov_b32 s43, s41
	v_mov_b32_e32 v144, v164
	v_lshl_add_u64 v[98:99], v[90:91], 0, v[142:143]
	v_cvt_pk_bf16_f32 v90, v102, v103
	v_cvt_pk_bf16_f32 v91, v104, v105
	v_cvt_pk_bf16_f32 v92, v94, v95
	v_cvt_pk_bf16_f32 v93, v96, v97
	global_store_dwordx4 v[98:99], v[90:93], off
	v_cvt_pk_bf16_f32 v82, v82, v83
	v_cvt_pk_bf16_f32 v83, v84, v85
	v_cvt_pk_bf16_f32 v84, v74, v75
	v_add_u32_e32 v74, 48, v134
	v_mad_i64_i32 v[74:75], s[20:21], v74, s39, v[140:141]
	v_cvt_pk_bf16_f32 v85, v76, v77
	global_store_dwordx4 v[98:99], v[82:85], off offset:256
	s_nop 1
	v_lshl_add_u64 v[82:83], v[74:75], 0, v[142:143]
	v_cvt_pk_bf16_f32 v74, v86, v87
	v_cvt_pk_bf16_f32 v75, v88, v89
	v_cvt_pk_bf16_f32 v76, v78, v79
	v_cvt_pk_bf16_f32 v77, v80, v81
	global_store_dwordx4 v[82:83], v[74:77], off
	v_cvt_pk_bf16_f32 v70, v70, v71
	v_cvt_pk_bf16_f32 v71, v72, v73
	v_cvt_pk_bf16_f32 v72, v66, v67
	v_add_u32_e32 v66, 0x80, v134
	v_mad_i64_i32 v[66:67], s[20:21], v66, s39, v[140:141]
	v_lshl_add_u64 v[66:67], v[66:67], 0, v[142:143]
	v_cvt_pk_bf16_f32 v73, v68, v69
	global_store_dwordx4 v[82:83], v[70:73], off offset:256
	v_cvt_pk_bf16_f32 v62, v62, v63
	v_cvt_pk_bf16_f32 v63, v64, v65
	v_cvt_pk_bf16_f32 v64, v58, v59
	v_cvt_pk_bf16_f32 v65, v60, v61
	global_store_dwordx4 v[66:67], v[62:65], off
	v_cvt_pk_bf16_f32 v50, v50, v51
	v_cvt_pk_bf16_f32 v51, v52, v53
	v_cvt_pk_bf16_f32 v52, v42, v43
	v_add_u32_e32 v42, 0x90, v134
	v_mad_i64_i32 v[42:43], s[20:21], v42, s39, v[140:141]
	v_cvt_pk_bf16_f32 v53, v44, v45
	global_store_dwordx4 v[66:67], v[50:53], off offset:256
	s_nop 1
	v_lshl_add_u64 v[50:51], v[42:43], 0, v[142:143]
	v_cvt_pk_bf16_f32 v42, v54, v55
	v_cvt_pk_bf16_f32 v43, v56, v57
	v_cvt_pk_bf16_f32 v44, v46, v47
	v_cvt_pk_bf16_f32 v45, v48, v49
	global_store_dwordx4 v[50:51], v[42:45], off
	v_cvt_pk_bf16_f32 v34, v34, v35
	v_cvt_pk_bf16_f32 v35, v36, v37
	v_cvt_pk_bf16_f32 v36, v26, v27
	v_add_u32_e32 v26, 0xa0, v134
	v_mad_i64_i32 v[26:27], s[20:21], v26, s39, v[140:141]
	v_cvt_pk_bf16_f32 v37, v28, v29
	global_store_dwordx4 v[50:51], v[34:37], off offset:256
	s_nop 1
	v_lshl_add_u64 v[34:35], v[26:27], 0, v[142:143]
	v_cvt_pk_bf16_f32 v26, v38, v39
	v_cvt_pk_bf16_f32 v27, v40, v41
	v_cvt_pk_bf16_f32 v28, v30, v31
	v_cvt_pk_bf16_f32 v29, v32, v33
	global_store_dwordx4 v[34:35], v[26:29], off
	v_cvt_pk_bf16_f32 v18, v18, v19
	v_cvt_pk_bf16_f32 v19, v20, v21
	v_cvt_pk_bf16_f32 v20, v10, v11
	v_add_u32_e32 v10, 0xb0, v134
	v_mad_i64_i32 v[10:11], s[20:21], v10, s39, v[140:141]
	v_cvt_pk_bf16_f32 v21, v12, v13
	global_store_dwordx4 v[34:35], v[18:21], off offset:256
	v_mov_b32_e32 v141, v161
	v_mov_b32_e32 v140, v162
	v_lshl_add_u64 v[18:19], v[10:11], 0, v[142:143]
	v_mov_b32_e32 v142, v163
	s_mov_b64 s[20:21], s[2:3]
	v_cvt_pk_bf16_f32 v10, v22, v23
	v_cvt_pk_bf16_f32 v11, v24, v25
	v_cvt_pk_bf16_f32 v12, v14, v15
	v_cvt_pk_bf16_f32 v13, v16, v17
	global_store_dwordx4 v[18:19], v[10:13], off
	v_cvt_pk_bf16_f32 v6, v6, v7
	v_cvt_pk_bf16_f32 v7, v8, v9
	v_cvt_pk_bf16_f32 v8, v2, v3
	v_cvt_pk_bf16_f32 v9, v4, v5
	global_store_dwordx4 v[18:19], v[6:9], off offset:256
	s_cbranch_vccz .LBB0_241
	s_waitcnt vmcnt(0)
	s_cmpk_gt_u32 s13, 0xff
	s_cbranch_scc1 .LBB0_250
	s_barrier

; #define PG8_STAGE(bufoff, gbase, v0, v1) do { \
;         __builtin_amdgcn_global_load_lds((const unsigned*)((const char*)(gbase) + (v0)), (LAS unsigned*)(lds + (bufoff) + ldsw), 16, 0, 0); \
;         __builtin_amdgcn_global_load_lds((const unsigned*)((const char*)(gbase) + (v1)), (LAS unsigned*)(lds + (bufoff) + ldsw + 8192), 16, 0, 0); } while (0)
; #define PG8_LDA(dst, b, h) do { _Pragma("unroll") for (int m = 0; m < 4; ++m) _Pragma("unroll") for (int k = 0; k < 2; ++k) dst[m][k] = *(const LAS bf16x8*)(lds + PG8_SA(b, h) + aoff + m * 2048 + k * 1024); } while (0)
; #define PG8_LDB(dst, b, h) do { _Pragma("unroll") for (int n = 0; n < 2; ++n) _Pragma("unroll") for (int k = 0; k < 2; ++k) dst[n][k] = *(const LAS bf16x8*)(lds + PG8_SB(b, h) + boff + n * 2048 + k * 1024); } while (0)
; #define PG8_MMA(ai, bj, At, Bt) do { __builtin_amdgcn_s_setprio(1); _Pragma("unroll") for (int m = 0; m < 4; ++m) _Pragma("unroll") for (int n = 0; n < 2; ++n) _Pragma("unroll") for (int k = 0; k < 2; ++k) \
;         acc[ai][bj][m][n] = __builtin_amdgcn_mfma_f32_16x16x32_bf16(Bt[n][k], At[m][k], acc[ai][bj][m][n], 0, 0, 0); __builtin_amdgcn_s_setprio(0); } while (0)
; #define PG8_WAIT_V(n) asm volatile("s_waitcnt vmcnt(" #n ")" ::: "memory")
; #define PG8_WAIT_L(n) asm volatile("s_waitcnt lgkmcnt(" #n ")" ::: "memory")
; #define PG8_BAR __builtin_amdgcn_s_barrier()
; #define PG8_SCHED __builtin_amdgcn_sched_barrier(0)
; template <class Epi, class Sched>
; __device__ __forceinline__ void gemm_phase(LAS unsigned char* lds, const int K, const Sched& S, const Epi& E) {
;     ...
;             PG8_LDB(B0, 0, 0); PG8_SCHED; PG8_LDA(At, 0, 0); PG8_STAGE(PG8_SA(1, 1), a1, c10, c11);
;             PG8_WAIT_L(8); PG8_BAR; PG8_WAIT_L(0); PG8_MMA(0, 0, At, B0); PG8_BAR; PG8_SCHED;
;             PG8_LDB(B1, 0, 1); PG8_STAGE(PG8_SB(0, 0), b2, voffB0, voffB1);
;             PG8_BAR; PG8_WAIT_L(0); PG8_MMA(0, 1, At, B1); PG8_BAR;
;             PG8_LDA(At, 0, 1); PG8_STAGE(PG8_SA(0, 0), a2, x00, x01);
;             PG8_BAR; PG8_WAIT_L(0); PG8_MMA(1, 0, At, B0); PG8_BAR; PG8_SCHED;
;             PG8_STAGE(PG8_SB(0, 1), b2 + hstep, voffB0, voffB1);
;             PG8_WAIT_V(6); PG8_BAR; PG8_MMA(1, 1, At, B1); PG8_BAR;
.LBB0_942:
	s_add_u32 s38, s4, s36
	s_addc_u32 s39, s5, s37
	s_add_u32 s40, s38, 0x34c30100
	ds_read_b128 v[140:143], v170
	ds_read_b128 v[156:159], v170 offset:1024
	ds_read_b128 v[178:181], v170 offset:2048
	ds_read_b128 v[182:185], v170 offset:3072
	s_addc_u32 s41, s39, 0
	s_add_u32 s60, s35, s36
	s_addc_u32 s61, s58, s37
	s_cmpk_eq_i32 s36, 0xf00
	s_cselect_b64 vcc, -1, 0
	s_and_b64 s[38:39], vcc, exec
	v_cndmask_b32_e32 v150, v131, v173, vcc
	s_cselect_b32 s41, s9, s41
	s_cselect_b32 s40, s8, s40
	v_cndmask_b32_e32 v133, v132, v175, vcc
	s_cselect_b32 s39, s3, s61
	s_cselect_b32 s38, s2, s60
	v_cndmask_b32_e32 v144, v130, v174, vcc
	v_lshl_add_u64 v[160:161], v[138:139], 0, s[36:37]
	s_add_i32 m0, s45, 0xc000
	ds_read_b128 v[186:189], v171
	ds_read_b128 v[190:193], v171 offset:1024
	ds_read_b128 v[194:197], v171 offset:2048
	ds_read_b128 v[198:201], v171 offset:3072
	ds_read_b128 v[202:205], v171 offset:4096
	ds_read_b128 v[208:211], v171 offset:5120
	ds_read_b128 v[212:215], v171 offset:6144
	ds_read_b128 v[216:219], v171 offset:7168
	global_load_lds_dwordx4 v[160:161], off
	v_lshl_add_u64 v[160:161], v[136:137], 0, s[36:37]
	s_add_i32 m0, s45, 0xe000
	s_nop 0
	global_load_lds_dwordx4 v[160:161], off
	s_waitcnt lgkmcnt(8)
	s_barrier
	s_waitcnt lgkmcnt(0)
	s_waitcnt lgkmcnt(0)
	v_mfma_f32_16x16x32_bf16 v[126:129], v[140:143], v[186:189], v[126:129]
	v_mfma_f32_16x16x32_bf16 v[122:125], v[178:181], v[186:189], v[122:125]
	v_mfma_f32_16x16x32_bf16 v[118:121], v[140:143], v[194:197], v[118:121]
	v_mfma_f32_16x16x32_bf16 v[114:117], v[178:181], v[194:197], v[114:117]
	v_mfma_f32_16x16x32_bf16 v[110:113], v[140:143], v[202:205], v[110:113]
	v_mfma_f32_16x16x32_bf16 v[102:105], v[178:181], v[202:205], v[102:105]
	v_mfma_f32_16x16x32_bf16 v[94:97], v[140:143], v[212:215], v[94:97]
	v_mfma_f32_16x16x32_bf16 v[82:85], v[178:181], v[212:215], v[82:85]
	v_mfma_f32_16x16x32_bf16 v[126:129], v[156:159], v[190:193], v[126:129]
	v_mfma_f32_16x16x32_bf16 v[122:125], v[182:185], v[190:193], v[122:125]
	v_mfma_f32_16x16x32_bf16 v[118:121], v[156:159], v[198:201], v[118:121]
	v_mfma_f32_16x16x32_bf16 v[114:117], v[182:185], v[198:201], v[114:117]
	v_mfma_f32_16x16x32_bf16 v[110:113], v[156:159], v[208:211], v[110:113]
	v_mfma_f32_16x16x32_bf16 v[102:105], v[182:185], v[208:211], v[102:105]
	v_mfma_f32_16x16x32_bf16 v[94:97], v[156:159], v[216:219], v[94:97]
	v_mfma_f32_16x16x32_bf16 v[82:85], v[182:185], v[216:219], v[82:85]
	s_barrier
	s_add_i32 s60, s52, s44
	v_lshl_add_u64 v[160:161], s[38:39], 0, v[148:149]
	s_mov_b32 m0, s60
	ds_read_b128 v[220:223], v172
	ds_read_b128 v[224:227], v172 offset:1024
	ds_read_b128 v[228:231], v172 offset:2048
	ds_read_b128 v[232:235], v172 offset:3072
	global_load_lds_dwordx4 v[160:161], off
	v_lshl_add_u64 v[206:207], s[38:39], 0, v[146:147]
	s_add_i32 m0, s60, 0x2000
	s_nop 0
	global_load_lds_dwordx4 v[206:207], off
	s_barrier
	s_waitcnt lgkmcnt(0)
	s_waitcnt lgkmcnt(0)
	v_mfma_f32_16x16x32_bf16 v[106:109], v[220:223], v[186:189], v[106:109]
	v_mfma_f32_16x16x32_bf16 v[98:101], v[228:231], v[186:189], v[98:101]
	v_mfma_f32_16x16x32_bf16 v[90:93], v[220:223], v[194:197], v[90:93]
	v_mfma_f32_16x16x32_bf16 v[86:89], v[228:231], v[194:197], v[86:89]
	v_mfma_f32_16x16x32_bf16 v[78:81], v[220:223], v[202:205], v[78:81]
	v_mfma_f32_16x16x32_bf16 v[74:77], v[228:231], v[202:205], v[74:77]
	v_mfma_f32_16x16x32_bf16 v[70:73], v[220:223], v[212:215], v[70:73]
	v_mfma_f32_16x16x32_bf16 v[66:69], v[228:231], v[212:215], v[66:69]
	v_mfma_f32_16x16x32_bf16 v[106:109], v[224:227], v[190:193], v[106:109]
	v_mfma_f32_16x16x32_bf16 v[98:101], v[232:235], v[190:193], v[98:101]
	v_mfma_f32_16x16x32_bf16 v[90:93], v[224:227], v[198:201], v[90:93]
	v_mfma_f32_16x16x32_bf16 v[86:89], v[232:235], v[198:201], v[86:89]
	v_mfma_f32_16x16x32_bf16 v[78:81], v[224:227], v[208:211], v[78:81]
	v_mfma_f32_16x16x32_bf16 v[74:77], v[232:235], v[208:211], v[74:77]
	v_mfma_f32_16x16x32_bf16 v[70:73], v[224:227], v[216:219], v[70:73]
	v_mfma_f32_16x16x32_bf16 v[66:69], v[232:235], v[216:219], v[66:69]
	s_mov_b32 m0, s45
	s_barrier
	ds_read_b128 v[186:189], v171 offset:16384
	ds_read_b128 v[190:193], v171 offset:17408
	ds_read_b128 v[194:197], v171 offset:18432
	ds_read_b128 v[198:201], v171 offset:19456
	ds_read_b128 v[202:205], v171 offset:20480
	ds_read_b128 v[208:211], v171 offset:21504
	ds_read_b128 v[212:215], v171 offset:22528
	ds_read_b128 v[216:219], v171 offset:23552
	global_load_lds_dwordx4 v150, s[40:41]
	s_mov_b32 m0, s46
	v_mov_b32_e32 v145, v151
	global_load_lds_dwordx4 v144, s[40:41]
	s_barrier
	s_waitcnt lgkmcnt(0)
	v_lshl_add_u64 v[236:237], s[40:41], 0, v[150:151]
	v_lshl_add_u64 v[144:145], s[40:41], 0, v[144:145]
	s_waitcnt lgkmcnt(0)
	v_mfma_f32_16x16x32_bf16 v[62:65], v[140:143], v[186:189], v[62:65]
	v_mfma_f32_16x16x32_bf16 v[58:61], v[178:181], v[186:189], v[58:61]
	v_mfma_f32_16x16x32_bf16 v[54:57], v[140:143], v[194:197], v[54:57]
	v_mfma_f32_16x16x32_bf16 v[50:53], v[178:181], v[194:197], v[50:53]
	v_mfma_f32_16x16x32_bf16 v[46:49], v[140:143], v[202:205], v[46:49]
	v_mfma_f32_16x16x32_bf16 v[38:41], v[178:181], v[202:205], v[38:41]
	v_mfma_f32_16x16x32_bf16 v[30:33], v[140:143], v[212:215], v[30:33]
	v_mfma_f32_16x16x32_bf16 v[18:21], v[178:181], v[212:215], v[18:21]
	v_mfma_f32_16x16x32_bf16 v[62:65], v[156:159], v[190:193], v[62:65]
	v_mfma_f32_16x16x32_bf16 v[58:61], v[182:185], v[190:193], v[58:61]
	v_mfma_f32_16x16x32_bf16 v[54:57], v[156:159], v[198:201], v[54:57]
	v_mfma_f32_16x16x32_bf16 v[50:53], v[182:185], v[198:201], v[50:53]
	v_mfma_f32_16x16x32_bf16 v[46:49], v[156:159], v[208:211], v[46:49]
	v_mfma_f32_16x16x32_bf16 v[38:41], v[182:185], v[208:211], v[38:41]
	v_mfma_f32_16x16x32_bf16 v[30:33], v[156:159], v[216:219], v[30:33]
	v_mfma_f32_16x16x32_bf16 v[18:21], v[182:185], v[216:219], v[18:21]
	s_barrier
; #define PG8_STAGE(bufoff, gbase, v0, v1) do { \
;         __builtin_amdgcn_global_load_lds((const unsigned*)((const char*)(gbase) + (v0)), (LAS unsigned*)(lds + (bufoff) + ldsw), 16, 0, 0); \
;         __builtin_amdgcn_global_load_lds((const unsigned*)((const char*)(gbase) + (v1)), (LAS unsigned*)(lds + (bufoff) + ldsw + 8192), 16, 0, 0); } while (0)
; #define PG8_LDA(dst, b, h) do { _Pragma("unroll") for (int m = 0; m < 4; ++m) _Pragma("unroll") for (int k = 0; k < 2; ++k) dst[m][k] = *(const LAS bf16x8*)(lds + PG8_SA(b, h) + aoff + m * 2048 + k * 1024); } while (0)
; #define PG8_LDB(dst, b, h) do { _Pragma("unroll") for (int n = 0; n < 2; ++n) _Pragma("unroll") for (int k = 0; k < 2; ++k) dst[n][k] = *(const LAS bf16x8*)(lds + PG8_SB(b, h) + boff + n * 2048 + k * 1024); } while (0)
; #define PG8_MMA(ai, bj, At, Bt) do { __builtin_amdgcn_s_setprio(1); _Pragma("unroll") for (int m = 0; m < 4; ++m) _Pragma("unroll") for (int n = 0; n < 2; ++n) _Pragma("unroll") for (int k = 0; k < 2; ++k) \
;         acc[ai][bj][m][n] = __builtin_amdgcn_mfma_f32_16x16x32_bf16(Bt[n][k], At[m][k], acc[ai][bj][m][n], 0, 0, 0); __builtin_amdgcn_s_setprio(0); } while (0)
; #define PG8_WAIT_V(n) asm volatile("s_waitcnt vmcnt(" #n ")" ::: "memory")
; #define PG8_WAIT_L(n) asm volatile("s_waitcnt lgkmcnt(" #n ")" ::: "memory")
; #define PG8_BAR __builtin_amdgcn_s_barrier()
; #define PG8_SCHED __builtin_amdgcn_sched_barrier(0)
; template <class Epi, class Sched>
; __device__ __forceinline__ void gemm_phase(LAS unsigned char* lds, const int K, const Sched& S, const Epi& E) {
;     ...
;             PG8_WAIT_V(6); PG8_BAR; PG8_MMA(1, 1, At, B1); PG8_BAR;
;             PG8_LDB(B0, 1, 0); PG8_SCHED; PG8_LDA(At, 1, 0); PG8_STAGE(PG8_SA(0, 1), a2, x10, x11);
;             PG8_WAIT_L(8); PG8_BAR; PG8_WAIT_L(0); PG8_MMA(0, 0, At, B0); PG8_BAR; PG8_SCHED;
;             PG8_LDB(B1, 1, 1); PG8_STAGE(PG8_SB(1, 0), b3, voffB0, voffB1);
;             PG8_BAR; PG8_WAIT_L(0); PG8_MMA(0, 1, At, B1); PG8_BAR;
;             PG8_LDA(At, 1, 1); PG8_STAGE(PG8_SA(1, 0), a3, x00, x01);
;             PG8_BAR; PG8_WAIT_L(0); PG8_MMA(1, 0, At, B0); PG8_BAR; PG8_SCHED;
	s_add_u32 s60, s38, 0x80000
	s_addc_u32 s61, s39, 0
	s_add_i32 s62, s53, s44
	v_lshl_add_u64 v[140:141], s[60:61], 0, v[148:149]
	s_mov_b32 m0, s62
	s_nop 0
	global_load_lds_dwordx4 v[140:141], off
	v_lshl_add_u64 v[140:141], s[60:61], 0, v[146:147]
	s_add_i32 m0, s62, 0x2000
	s_nop 0
	global_load_lds_dwordx4 v[140:141], off
	s_waitcnt vmcnt(6)
	s_barrier
	v_mfma_f32_16x16x32_bf16 v[42:45], v[220:223], v[186:189], v[42:45]
	v_mfma_f32_16x16x32_bf16 v[34:37], v[228:231], v[186:189], v[34:37]
	v_mfma_f32_16x16x32_bf16 v[26:29], v[220:223], v[194:197], v[26:29]
	v_mfma_f32_16x16x32_bf16 v[22:25], v[228:231], v[194:197], v[22:25]
	v_mfma_f32_16x16x32_bf16 v[14:17], v[220:223], v[202:205], v[14:17]
	v_mfma_f32_16x16x32_bf16 v[10:13], v[228:231], v[202:205], v[10:13]
	v_mfma_f32_16x16x32_bf16 v[6:9], v[220:223], v[212:215], v[6:9]
	v_mfma_f32_16x16x32_bf16 v[2:5], v[228:231], v[212:215], v[2:5]
	v_mfma_f32_16x16x32_bf16 v[42:45], v[224:227], v[190:193], v[42:45]
	v_mfma_f32_16x16x32_bf16 v[34:37], v[232:235], v[190:193], v[34:37]
	v_mfma_f32_16x16x32_bf16 v[26:29], v[224:227], v[198:201], v[26:29]
	v_mfma_f32_16x16x32_bf16 v[22:25], v[232:235], v[198:201], v[22:25]
	v_mfma_f32_16x16x32_bf16 v[14:17], v[224:227], v[208:211], v[14:17]
	v_mfma_f32_16x16x32_bf16 v[10:13], v[232:235], v[208:211], v[10:13]
	v_mfma_f32_16x16x32_bf16 v[6:9], v[224:227], v[216:219], v[6:9]
	v_mfma_f32_16x16x32_bf16 v[2:5], v[232:235], v[216:219], v[2:5]
	s_add_i32 s60, 0, 0x18000
	v_add_u32_e32 v135, s60, v168
	s_barrier
	ds_read_b128 v[140:143], v135
	ds_read_b128 v[156:159], v135 offset:1024
	ds_read_b128 v[178:181], v135 offset:2048
	ds_read_b128 v[182:185], v135 offset:3072
	s_mov_b32 m0, s47
	ds_read_b128 v[186:189], v171 offset:32768
	ds_read_b128 v[190:193], v171 offset:33792
	ds_read_b128 v[194:197], v171 offset:34816
	ds_read_b128 v[198:201], v171 offset:35840
	ds_read_b128 v[202:205], v171 offset:36864
	ds_read_b128 v[208:211], v171 offset:37888
	ds_read_b128 v[212:215], v171 offset:38912
	ds_read_b128 v[216:219], v171 offset:39936
	v_cndmask_b32_e32 v135, v134, v176, vcc
	global_load_lds_dwordx4 v133, s[40:41]
	s_mov_b32 m0, s48
	s_nop 0
	global_load_lds_dwordx4 v135, s[40:41]
	s_waitcnt lgkmcnt(8)
	s_barrier
	s_waitcnt lgkmcnt(0)
	s_waitcnt lgkmcnt(0)
	v_mfma_f32_16x16x32_bf16 v[126:129], v[140:143], v[186:189], v[126:129]
	v_mfma_f32_16x16x32_bf16 v[122:125], v[178:181], v[186:189], v[122:125]
	v_mfma_f32_16x16x32_bf16 v[118:121], v[140:143], v[194:197], v[118:121]
	v_mfma_f32_16x16x32_bf16 v[114:117], v[178:181], v[194:197], v[114:117]
	v_mfma_f32_16x16x32_bf16 v[110:113], v[140:143], v[202:205], v[110:113]
	v_mfma_f32_16x16x32_bf16 v[102:105], v[178:181], v[202:205], v[102:105]
	v_mfma_f32_16x16x32_bf16 v[94:97], v[140:143], v[212:215], v[94:97]
	v_mfma_f32_16x16x32_bf16 v[82:85], v[178:181], v[212:215], v[82:85]
	v_mfma_f32_16x16x32_bf16 v[126:129], v[156:159], v[190:193], v[126:129]
	v_mfma_f32_16x16x32_bf16 v[122:125], v[182:185], v[190:193], v[122:125]
	v_mfma_f32_16x16x32_bf16 v[118:121], v[156:159], v[198:201], v[118:121]
	v_mfma_f32_16x16x32_bf16 v[114:117], v[182:185], v[198:201], v[114:117]
	v_mfma_f32_16x16x32_bf16 v[110:113], v[156:159], v[208:211], v[110:113]
	v_mfma_f32_16x16x32_bf16 v[102:105], v[182:185], v[208:211], v[102:105]
	v_mfma_f32_16x16x32_bf16 v[94:97], v[156:159], v[216:219], v[94:97]
	v_mfma_f32_16x16x32_bf16 v[82:85], v[182:185], v[216:219], v[82:85]
	s_barrier
	s_add_i32 s40, 0, 0x1c000
	s_add_i32 s41, s60, s44
	v_add_u32_e32 v133, s40, v168
	v_lshl_add_u64 v[160:161], v[160:161], 0, s[16:17]
	s_mov_b32 m0, s41
	ds_read_b128 v[220:223], v133
	ds_read_b128 v[224:227], v133 offset:1024
	ds_read_b128 v[228:231], v133 offset:2048
	ds_read_b128 v[232:235], v133 offset:3072
	global_load_lds_dwordx4 v[160:161], off
	v_lshl_add_u64 v[160:161], v[206:207], 0, s[16:17]
	s_add_i32 m0, s41, 0x2000
	s_nop 0
	global_load_lds_dwordx4 v[160:161], off
	s_barrier
	s_waitcnt lgkmcnt(0)
	s_waitcnt lgkmcnt(0)
	v_mfma_f32_16x16x32_bf16 v[106:109], v[220:223], v[186:189], v[106:109]
	v_mfma_f32_16x16x32_bf16 v[98:101], v[228:231], v[186:189], v[98:101]
	v_mfma_f32_16x16x32_bf16 v[90:93], v[220:223], v[194:197], v[90:93]
	v_mfma_f32_16x16x32_bf16 v[86:89], v[228:231], v[194:197], v[86:89]
	v_mfma_f32_16x16x32_bf16 v[78:81], v[220:223], v[202:205], v[78:81]
	v_mfma_f32_16x16x32_bf16 v[74:77], v[228:231], v[202:205], v[74:77]
	v_mfma_f32_16x16x32_bf16 v[70:73], v[220:223], v[212:215], v[70:73]
	v_mfma_f32_16x16x32_bf16 v[66:69], v[228:231], v[212:215], v[66:69]
	v_mfma_f32_16x16x32_bf16 v[106:109], v[224:227], v[190:193], v[106:109]
	v_mfma_f32_16x16x32_bf16 v[98:101], v[232:235], v[190:193], v[98:101]
	v_mfma_f32_16x16x32_bf16 v[90:93], v[224:227], v[198:201], v[90:93]
	v_mfma_f32_16x16x32_bf16 v[86:89], v[232:235], v[198:201], v[86:89]
	v_mfma_f32_16x16x32_bf16 v[78:81], v[224:227], v[208:211], v[78:81]
	v_mfma_f32_16x16x32_bf16 v[74:77], v[232:235], v[208:211], v[74:77]
	v_mfma_f32_16x16x32_bf16 v[70:73], v[224:227], v[216:219], v[70:73]
	v_mfma_f32_16x16x32_bf16 v[66:69], v[232:235], v[216:219], v[66:69]
	s_mov_b32 m0, s50
	v_lshl_add_u64 v[160:161], v[236:237], 0, s[16:17]
	s_barrier
	ds_read_b128 v[186:189], v171 offset:49152
	ds_read_b128 v[190:193], v171 offset:50176
	ds_read_b128 v[194:197], v171 offset:51200
	ds_read_b128 v[198:201], v171 offset:52224
	ds_read_b128 v[202:205], v171 offset:53248
	ds_read_b128 v[208:211], v171 offset:54272
	ds_read_b128 v[212:215], v171 offset:55296
	ds_read_b128 v[216:219], v171 offset:56320
	global_load_lds_dwordx4 v[160:161], off
	v_lshl_add_u64 v[144:145], v[144:145], 0, s[16:17]
	s_mov_b32 m0, s51
	s_nop 0
	global_load_lds_dwordx4 v[144:145], off
	s_barrier
; #define PG8_STAGE(bufoff, gbase, v0, v1) do { \
;         __builtin_amdgcn_global_load_lds((const unsigned*)((const char*)(gbase) + (v0)), (LAS unsigned*)(lds + (bufoff) + ldsw), 16, 0, 0); \
;         __builtin_amdgcn_global_load_lds((const unsigned*)((const char*)(gbase) + (v1)), (LAS unsigned*)(lds + (bufoff) + ldsw + 8192), 16, 0, 0); } while (0)
; #define PG8_MMA(ai, bj, At, Bt) do { __builtin_amdgcn_s_setprio(1); _Pragma("unroll") for (int m = 0; m < 4; ++m) _Pragma("unroll") for (int n = 0; n < 2; ++n) _Pragma("unroll") for (int k = 0; k < 2; ++k) \
;         acc[ai][bj][m][n] = __builtin_amdgcn_mfma_f32_16x16x32_bf16(Bt[n][k], At[m][k], acc[ai][bj][m][n], 0, 0, 0); __builtin_amdgcn_s_setprio(0); } while (0)
; #define PG8_WAIT_V(n) asm volatile("s_waitcnt vmcnt(" #n ")" ::: "memory")
; #define PG8_WAIT_L(n) asm volatile("s_waitcnt lgkmcnt(" #n ")" ::: "memory")
; #define PG8_BAR __builtin_amdgcn_s_barrier()
; #define PG8_SCHED __builtin_amdgcn_sched_barrier(0)
; template <class Epi, class Sched>
; __device__ __forceinline__ void gemm_phase(LAS unsigned char* lds, const int K, const Sched& S, const Epi& E) {
;     ...
;             PG8_BAR; PG8_WAIT_L(0); PG8_MMA(1, 0, At, B0); PG8_BAR; PG8_SCHED;
;             PG8_STAGE(PG8_SB(1, 1), b3 + hstep, voffB0, voffB1);
;             PG8_WAIT_V(6); PG8_BAR; PG8_MMA(1, 1, At, B1); PG8_BAR;
;     __device__ __forceinline__ void operator()(const f32x4 (&acc)[2][2][4][2], const Unit& u, int wr, int wc, int fr, int fq) const {
;     ...
;         f32x4 gv[2][2];
; #pragma unroll
;         for (int bj = 0; bj < 2; ++bj)
; #pragma unroll
;             for (int n = 0; n < 2; ++n) gv[bj][n] = *(const f32x4*)(gate + col0 + bj * HALF + n * 16);
; #pragma unroll
;         for (int ai = 0; ai < 2; ++ai) {
;             f32x4 xv[4][2][2];
; #pragma unroll
;             for (int m = 0; m < 4; ++m) { const size_t ro = (size_t)(row0 + ai * HALF + m * 16) * D + col0;
; #pragma unroll
;                 for (int bj = 0; bj < 2; ++bj)
; #pragma unroll
;                     for (int n = 0; n < 2; ++n) xv[m][bj][n] = *(const f32x4*)(xin + ro + bj * HALF + n * 16); }
	s_waitcnt lgkmcnt(0)
	s_waitcnt lgkmcnt(0)
	v_mfma_f32_16x16x32_bf16 v[62:65], v[140:143], v[186:189], v[62:65]
	v_mfma_f32_16x16x32_bf16 v[58:61], v[178:181], v[186:189], v[58:61]
	v_mfma_f32_16x16x32_bf16 v[54:57], v[140:143], v[194:197], v[54:57]
	v_mfma_f32_16x16x32_bf16 v[50:53], v[178:181], v[194:197], v[50:53]
	v_mfma_f32_16x16x32_bf16 v[46:49], v[140:143], v[202:205], v[46:49]
	v_mfma_f32_16x16x32_bf16 v[38:41], v[178:181], v[202:205], v[38:41]
	v_mfma_f32_16x16x32_bf16 v[30:33], v[140:143], v[212:215], v[30:33]
	v_mfma_f32_16x16x32_bf16 v[18:21], v[178:181], v[212:215], v[18:21]
	v_mfma_f32_16x16x32_bf16 v[62:65], v[156:159], v[190:193], v[62:65]
	v_mfma_f32_16x16x32_bf16 v[58:61], v[182:185], v[190:193], v[58:61]
	v_mfma_f32_16x16x32_bf16 v[54:57], v[156:159], v[198:201], v[54:57]
	v_mfma_f32_16x16x32_bf16 v[50:53], v[182:185], v[198:201], v[50:53]
	v_mfma_f32_16x16x32_bf16 v[46:49], v[156:159], v[208:211], v[46:49]
	v_mfma_f32_16x16x32_bf16 v[38:41], v[182:185], v[208:211], v[38:41]
	v_mfma_f32_16x16x32_bf16 v[30:33], v[156:159], v[216:219], v[30:33]
	v_mfma_f32_16x16x32_bf16 v[18:21], v[182:185], v[216:219], v[18:21]
	s_barrier
	s_add_u32 s38, s38, 0x80080
	s_addc_u32 s39, s39, 0
	s_add_i32 s40, s40, s44
	v_lshl_add_u64 v[140:141], s[38:39], 0, v[148:149]
	s_mov_b32 m0, s40
	s_nop 0
	global_load_lds_dwordx4 v[140:141], off
	v_lshl_add_u64 v[140:141], s[38:39], 0, v[146:147]
	s_add_i32 m0, s40, 0x2000
	s_nop 0
	global_load_lds_dwordx4 v[140:141], off
	s_waitcnt vmcnt(6)
	s_barrier
	v_mfma_f32_16x16x32_bf16 v[42:45], v[220:223], v[186:189], v[42:45]
	v_mfma_f32_16x16x32_bf16 v[34:37], v[228:231], v[186:189], v[34:37]
	v_mfma_f32_16x16x32_bf16 v[26:29], v[220:223], v[194:197], v[26:29]
	v_mfma_f32_16x16x32_bf16 v[22:25], v[228:231], v[194:197], v[22:25]
	v_mfma_f32_16x16x32_bf16 v[14:17], v[220:223], v[202:205], v[14:17]
	v_mfma_f32_16x16x32_bf16 v[10:13], v[228:231], v[202:205], v[10:13]
	v_mfma_f32_16x16x32_bf16 v[6:9], v[220:223], v[212:215], v[6:9]
	v_mfma_f32_16x16x32_bf16 v[2:5], v[228:231], v[212:215], v[2:5]
	v_mfma_f32_16x16x32_bf16 v[42:45], v[224:227], v[190:193], v[42:45]
	v_mfma_f32_16x16x32_bf16 v[34:37], v[232:235], v[190:193], v[34:37]
	v_mfma_f32_16x16x32_bf16 v[26:29], v[224:227], v[198:201], v[26:29]
	v_mfma_f32_16x16x32_bf16 v[22:25], v[232:235], v[198:201], v[22:25]
	v_mfma_f32_16x16x32_bf16 v[14:17], v[224:227], v[208:211], v[14:17]
	v_mfma_f32_16x16x32_bf16 v[10:13], v[232:235], v[208:211], v[10:13]
	v_mfma_f32_16x16x32_bf16 v[6:9], v[224:227], v[216:219], v[6:9]
	v_mfma_f32_16x16x32_bf16 v[2:5], v[232:235], v[216:219], v[2:5]
	s_add_i32 s59, s59, 2
	s_add_u32 s36, s36, 0x100
	s_addc_u32 s37, s37, 0
	s_cmp_gt_u32 s59, 29
	s_barrier
	s_cbranch_scc0 .LBB0_942
	v_lshl_or_b32 v130, s57, 8, v169
	v_add_u32_e32 v132, s56, v167
	v_ashrrev_i32_e32 v131, 31, v130
	v_ashrrev_i32_e32 v133, 31, v132
	v_lshlrev_b64 v[156:157], 2, v[130:131]
	v_lshlrev_b64 v[160:161], 13, v[132:133]
	v_lshl_add_u64 v[158:159], s[6:7], 0, v[156:157]
	v_lshl_add_u64 v[206:207], v[160:161], 0, s[18:19]
	v_lshl_add_u64 v[244:245], v[160:161], 0, s[20:21]
	v_lshl_add_u64 v[246:247], v[160:161], 0, s[22:23]
	v_lshl_add_u64 v[130:131], s[12:13], 0, v[156:157]
	v_lshl_add_u64 v[190:191], v[158:159], 0, v[160:161]
	v_lshl_add_u64 v[208:209], v[158:159], 0, v[206:207]
	v_lshl_add_u64 v[224:225], v[158:159], 0, v[244:245]
	v_lshl_add_u64 v[240:241], v[158:159], 0, v[246:247]
	global_load_dwordx4 v[142:145], v[130:131], off
	global_load_dwordx4 v[134:137], v[130:131], off offset:64
	global_load_dwordx4 v[178:181], v[190:191], off
	global_load_dwordx4 v[182:185], v[190:191], off offset:64
	global_load_dwordx4 v[138:141], v[130:131], off offset:512
	s_nop 0
	global_load_dwordx4 v[130:133], v[130:131], off offset:576
	s_nop 0
	global_load_dwordx4 v[186:189], v[190:191], off offset:512
	s_nop 0
	global_load_dwordx4 v[190:193], v[190:191], off offset:576
	s_nop 0
	global_load_dwordx4 v[194:197], v[208:209], off
	global_load_dwordx4 v[198:201], v[208:209], off offset:64
	global_load_dwordx4 v[202:205], v[208:209], off offset:512
	s_nop 0
	global_load_dwordx4 v[208:211], v[208:209], off offset:576
	s_nop 0
	global_load_dwordx4 v[212:215], v[224:225], off
	global_load_dwordx4 v[216:219], v[224:225], off offset:64
	global_load_dwordx4 v[220:223], v[224:225], off offset:512
	s_nop 0
	global_load_dwordx4 v[224:227], v[224:225], off offset:576
	s_nop 0
	global_load_dwordx4 v[228:231], v[240:241], off
	global_load_dwordx4 v[232:235], v[240:241], off offset:64
	global_load_dwordx4 v[236:239], v[240:241], off offset:512
	s_nop 0
	global_load_dwordx4 v[240:243], v[240:241], off offset:576
	v_lshl_add_u64 v[248:249], s[10:11], 0, v[160:161]
	v_lshl_add_u64 v[246:247], s[10:11], 0, v[246:247]
	v_lshl_add_u64 v[248:249], v[248:249], 0, v[156:157]
	v_lshl_add_u64 v[206:207], s[10:11], 0, v[206:207]
	v_lshl_add_u64 v[244:245], s[10:11], 0, v[244:245]
	v_lshl_add_u64 v[246:247], v[246:247], 0, v[156:157]
	v_lshl_add_u64 v[206:207], v[206:207], 0, v[156:157]
	v_lshl_add_u64 v[244:245], v[244:245], 0, v[156:157]
	s_and_b64 vcc, exec, s[0:1]
	s_mov_b32 s57, s34
	s_mov_b32 s56, s54
	s_mov_b64 s[36:37], s[2:3]
	s_waitcnt vmcnt(0)
;     __device__ __forceinline__ void operator()(const f32x4 (&acc)[2][2][4][2], const Unit& u, int wr, int wc, int fr, int fq) const {
;     ...
;         for (int ai = 0; ai < 2; ++ai) {
;             f32x4 xv[4][2][2];
; #pragma unroll
;             for (int m = 0; m < 4; ++m) { const size_t ro = (size_t)(row0 + ai * HALF + m * 16) * D + col0;
; #pragma unroll
;                 for (int bj = 0; bj < 2; ++bj)
; #pragma unroll
;                     for (int n = 0; n < 2; ++n) xv[m][bj][n] = *(const f32x4*)(xin + ro + bj * HALF + n * 16); }
; #pragma unroll
;             for (int m = 0; m < 4; ++m) { const size_t ro = (size_t)(row0 + ai * HALF + m * 16) * D + col0;
; #pragma unroll
;                 for (int bj = 0; bj < 2; ++bj)
; #pragma unroll
;                     for (int n = 0; n < 2; ++n) *(f32x4*)(out + ro + bj * HALF + n * 16) = xv[m][bj][n] + gv[bj][n] * acc[ai][bj][m][n]; }
	v_pk_fma_f32 v[128:129], v[128:129], v[144:145], v[180:181]
	v_pk_fma_f32 v[126:127], v[126:127], v[142:143], v[178:179]
	v_pk_fma_f32 v[122:123], v[122:123], v[134:135], v[182:183]
	v_pk_fma_f32 v[110:111], v[110:111], v[142:143], v[212:213]
	v_pk_fma_f32 v[78:79], v[78:79], v[138:139], v[220:221]
	v_pk_fma_f32 v[94:95], v[94:95], v[142:143], v[228:229]
	v_pk_fma_f32 v[68:69], v[68:69], v[132:133], v[242:243]
	v_pk_fma_f32 v[66:67], v[66:67], v[130:131], v[240:241]
	v_lshl_add_u64 v[178:179], v[160:161], 0, s[24:25]
	v_lshl_add_u64 v[180:181], v[160:161], 0, s[26:27]
	v_lshl_add_u64 v[182:183], v[160:161], 0, s[28:29]
	v_lshl_add_u64 v[160:161], v[160:161], 0, s[30:31]
	v_pk_fma_f32 v[124:125], v[124:125], v[136:137], v[184:185]
	v_pk_fma_f32 v[108:109], v[108:109], v[140:141], v[188:189]
	v_pk_fma_f32 v[106:107], v[106:107], v[138:139], v[186:187]
	v_pk_fma_f32 v[100:101], v[100:101], v[132:133], v[192:193]
	v_pk_fma_f32 v[98:99], v[98:99], v[130:131], v[190:191]
	v_pk_fma_f32 v[120:121], v[120:121], v[144:145], v[196:197]
	v_pk_fma_f32 v[118:119], v[118:119], v[142:143], v[194:195]
	v_pk_fma_f32 v[116:117], v[116:117], v[136:137], v[200:201]
	v_pk_fma_f32 v[114:115], v[114:115], v[134:135], v[198:199]
	v_pk_fma_f32 v[92:93], v[92:93], v[140:141], v[204:205]
	v_pk_fma_f32 v[90:91], v[90:91], v[138:139], v[202:203]
	v_pk_fma_f32 v[88:89], v[88:89], v[132:133], v[210:211]
	v_pk_fma_f32 v[86:87], v[86:87], v[130:131], v[208:209]
	v_pk_fma_f32 v[112:113], v[112:113], v[144:145], v[214:215]
	v_pk_fma_f32 v[104:105], v[104:105], v[136:137], v[218:219]
	v_pk_fma_f32 v[102:103], v[102:103], v[134:135], v[216:217]
	v_pk_fma_f32 v[80:81], v[80:81], v[140:141], v[222:223]
	v_pk_fma_f32 v[76:77], v[76:77], v[132:133], v[226:227]
	v_pk_fma_f32 v[74:75], v[74:75], v[130:131], v[224:225]
	v_pk_fma_f32 v[96:97], v[96:97], v[144:145], v[230:231]
	v_pk_fma_f32 v[84:85], v[84:85], v[136:137], v[234:235]
	v_pk_fma_f32 v[82:83], v[82:83], v[134:135], v[232:233]
	v_pk_fma_f32 v[72:73], v[72:73], v[140:141], v[238:239]
	v_pk_fma_f32 v[70:71], v[70:71], v[138:139], v[236:237]
	global_store_dwordx4 v[248:249], v[126:129], off
	global_store_dwordx4 v[248:249], v[122:125], off offset:64
	global_store_dwordx4 v[248:249], v[106:109], off offset:512
	global_store_dwordx4 v[248:249], v[98:101], off offset:576
	global_store_dwordx4 v[206:207], v[118:121], off
	global_store_dwordx4 v[206:207], v[114:117], off offset:64
	global_store_dwordx4 v[206:207], v[90:93], off offset:512
	global_store_dwordx4 v[206:207], v[86:89], off offset:576
	global_store_dwordx4 v[244:245], v[110:113], off
	global_store_dwordx4 v[244:245], v[102:105], off offset:64
	global_store_dwordx4 v[244:245], v[78:81], off offset:512
	global_store_dwordx4 v[244:245], v[74:77], off offset:576
	global_store_dwordx4 v[246:247], v[94:97], off
	global_store_dwordx4 v[246:247], v[82:85], off offset:64
	global_store_dwordx4 v[246:247], v[70:73], off offset:512
	global_store_dwordx4 v[246:247], v[66:69], off offset:576
	v_lshl_add_u64 v[78:79], v[158:159], 0, v[178:179]
	v_lshl_add_u64 v[94:95], v[158:159], 0, v[180:181]
	v_lshl_add_u64 v[110:111], v[158:159], 0, v[182:183]
	v_lshl_add_u64 v[126:127], v[158:159], 0, v[160:161]
	global_load_dwordx4 v[66:69], v[78:79], off
	global_load_dwordx4 v[70:73], v[78:79], off offset:64
	global_load_dwordx4 v[74:77], v[78:79], off offset:512
	s_nop 0
	global_load_dwordx4 v[78:81], v[78:79], off offset:576
	s_nop 0
	global_load_dwordx4 v[82:85], v[94:95], off
	global_load_dwordx4 v[86:89], v[94:95], off offset:64
	global_load_dwordx4 v[90:93], v[94:95], off offset:512
	s_nop 0
	global_load_dwordx4 v[94:97], v[94:95], off offset:576
	s_nop 0
	global_load_dwordx4 v[98:101], v[110:111], off
	global_load_dwordx4 v[102:105], v[110:111], off offset:64
	global_load_dwordx4 v[106:109], v[110:111], off offset:512
	v_lshl_add_u64 v[158:159], s[10:11], 0, v[178:179]
	global_load_dwordx4 v[110:113], v[110:111], off offset:576
	s_nop 0
	global_load_dwordx4 v[114:117], v[126:127], off
	global_load_dwordx4 v[118:121], v[126:127], off offset:64
	global_load_dwordx4 v[122:125], v[126:127], off offset:512
	s_nop 0
	global_load_dwordx4 v[126:129], v[126:127], off offset:576
	v_lshl_add_u64 v[178:179], s[10:11], 0, v[180:181]
	v_lshl_add_u64 v[180:181], s[10:11], 0, v[182:183]
	v_lshl_add_u64 v[160:161], s[10:11], 0, v[160:161]
	v_lshl_add_u64 v[158:159], v[158:159], 0, v[156:157]
	v_lshl_add_u64 v[178:179], v[178:179], 0, v[156:157]
	v_lshl_add_u64 v[180:181], v[180:181], 0, v[156:157]
	v_lshl_add_u64 v[156:157], v[160:161], 0, v[156:157]
	s_waitcnt vmcnt(0)
; #define PG8_WAIT_V(n) asm volatile("s_waitcnt vmcnt(" #n ")" ::: "memory")
; #define PG8_BAR __builtin_amdgcn_s_barrier()
; template <class Epi, class Sched>
; __device__ __forceinline__ void gemm_phase(LAS unsigned char* lds, const int K, const Sched& S, const Epi& E) {
;     ...
;         if (!has_next) break;
; #pragma unroll
;         for (int a = 0; a < 2; ++a)
; #pragma unroll
;             for (int b = 0; b < 2; ++b)
; #pragma unroll
;                 for (int m = 0; m < 4; ++m)
; #pragma unroll
;                     for (int n = 0; n < 2; ++n) acc[a][b][m][n] = (f32x4){0.f, 0.f, 0.f, 0.f};
;         cur = nxt; cB = nB; c00 = n00; c01 = n01; c10 = n10; c11 = n11; ++ui;
;     }
;     PG8_WAIT_V(0);
;     if (wr == 0) PG8_BAR;
;     PG8_BAR;
;     __device__ __forceinline__ void operator()(const f32x4 (&acc)[2][2][4][2], const Unit& u, int wr, int wc, int fr, int fq) const {
;     ...
;             for (int m = 0; m < 4; ++m) { const size_t ro = (size_t)(row0 + ai * HALF + m * 16) * D + col0;
; #pragma unroll
;                 for (int bj = 0; bj < 2; ++bj)
; #pragma unroll
;                     for (int n = 0; n < 2; ++n) *(f32x4*)(out + ro + bj * HALF + n * 16) = xv[m][bj][n] + gv[bj][n] * acc[ai][bj][m][n]; }
	v_pk_fma_f32 v[64:65], v[64:65], v[144:145], v[68:69]
	v_pk_fma_f32 v[62:63], v[62:63], v[142:143], v[66:67]
	v_pk_fma_f32 v[58:59], v[58:59], v[134:135], v[70:71]
	v_pk_fma_f32 v[36:37], v[36:37], v[132:133], v[80:81]
	v_pk_fma_f32 v[34:35], v[34:35], v[130:131], v[78:79]
	v_pk_fma_f32 v[50:51], v[50:51], v[134:135], v[86:87]
	v_pk_fma_f32 v[24:25], v[24:25], v[132:133], v[96:97]
	v_pk_fma_f32 v[22:23], v[22:23], v[130:131], v[94:95]
	v_pk_fma_f32 v[38:39], v[38:39], v[134:135], v[102:103]
	v_pk_fma_f32 v[12:13], v[12:13], v[132:133], v[112:113]
	v_pk_fma_f32 v[10:11], v[10:11], v[130:131], v[110:111]
	v_pk_fma_f32 v[18:19], v[18:19], v[134:135], v[118:119]
	v_pk_fma_f32 v[4:5], v[4:5], v[132:133], v[128:129]
	v_pk_fma_f32 v[2:3], v[2:3], v[130:131], v[126:127]
	v_mov_b32_e32 v131, v173
	v_mov_b32_e32 v130, v174
	v_mov_b32_e32 v132, v175
	v_mov_b32_e32 v134, v176
	v_pk_fma_f32 v[60:61], v[60:61], v[136:137], v[72:73]
	v_pk_fma_f32 v[44:45], v[44:45], v[140:141], v[76:77]
	v_pk_fma_f32 v[42:43], v[42:43], v[138:139], v[74:75]
	v_pk_fma_f32 v[56:57], v[56:57], v[144:145], v[84:85]
	v_pk_fma_f32 v[54:55], v[54:55], v[142:143], v[82:83]
	v_pk_fma_f32 v[52:53], v[52:53], v[136:137], v[88:89]
	v_pk_fma_f32 v[28:29], v[28:29], v[140:141], v[92:93]
	v_pk_fma_f32 v[26:27], v[26:27], v[138:139], v[90:91]
	v_pk_fma_f32 v[48:49], v[48:49], v[144:145], v[100:101]
	v_pk_fma_f32 v[46:47], v[46:47], v[142:143], v[98:99]
	v_pk_fma_f32 v[40:41], v[40:41], v[136:137], v[104:105]
	v_pk_fma_f32 v[16:17], v[16:17], v[140:141], v[108:109]
	v_pk_fma_f32 v[14:15], v[14:15], v[138:139], v[106:107]
	v_pk_fma_f32 v[32:33], v[32:33], v[144:145], v[116:117]
	v_pk_fma_f32 v[30:31], v[30:31], v[142:143], v[114:115]
	v_pk_fma_f32 v[20:21], v[20:21], v[136:137], v[120:121]
	v_pk_fma_f32 v[8:9], v[8:9], v[140:141], v[124:125]
	v_pk_fma_f32 v[6:7], v[6:7], v[138:139], v[122:123]
	global_store_dwordx4 v[158:159], v[62:65], off
	global_store_dwordx4 v[158:159], v[58:61], off offset:64
	global_store_dwordx4 v[158:159], v[42:45], off offset:512
	global_store_dwordx4 v[158:159], v[34:37], off offset:576
	global_store_dwordx4 v[178:179], v[54:57], off
	global_store_dwordx4 v[178:179], v[50:53], off offset:64
	global_store_dwordx4 v[178:179], v[26:29], off offset:512
	global_store_dwordx4 v[178:179], v[22:25], off offset:576
	global_store_dwordx4 v[180:181], v[46:49], off
	global_store_dwordx4 v[180:181], v[38:41], off offset:64
	global_store_dwordx4 v[180:181], v[14:17], off offset:512
	global_store_dwordx4 v[180:181], v[10:13], off offset:576
	global_store_dwordx4 v[156:157], v[30:33], off
	global_store_dwordx4 v[156:157], v[18:21], off offset:64
	global_store_dwordx4 v[156:157], v[6:9], off offset:512
	global_store_dwordx4 v[156:157], v[2:5], off offset:576
	s_cbranch_vccz .LBB0_933
	s_waitcnt vmcnt(0)
	s_cmpk_gt_u32 s33, 0xff
	s_cbranch_scc1 .LBB0_946
	s_barrier

; #define PG8_STAGE(bufoff, gbase, v0, v1) do { \
;         __builtin_amdgcn_global_load_lds((const unsigned*)((const char*)(gbase) + (v0)), (LAS unsigned*)(lds + (bufoff) + ldsw), 16, 0, 0); \
;         __builtin_amdgcn_global_load_lds((const unsigned*)((const char*)(gbase) + (v1)), (LAS unsigned*)(lds + (bufoff) + ldsw + 8192), 16, 0, 0); } while (0)
; #define PG8_LDA(dst, b, h) do { _Pragma("unroll") for (int m = 0; m < 4; ++m) _Pragma("unroll") for (int k = 0; k < 2; ++k) dst[m][k] = *(const LAS bf16x8*)(lds + PG8_SA(b, h) + aoff + m * 2048 + k * 1024); } while (0)
; #define PG8_LDB(dst, b, h) do { _Pragma("unroll") for (int n = 0; n < 2; ++n) _Pragma("unroll") for (int k = 0; k < 2; ++k) dst[n][k] = *(const LAS bf16x8*)(lds + PG8_SB(b, h) + boff + n * 2048 + k * 1024); } while (0)
; #define PG8_WAIT_V(n) asm volatile("s_waitcnt vmcnt(" #n ")" ::: "memory")
; #define PG8_WAIT_L(n) asm volatile("s_waitcnt lgkmcnt(" #n ")" ::: "memory")
; #define PG8_BAR __builtin_amdgcn_s_barrier()
; #define PG8_SCHED __builtin_amdgcn_sched_barrier(0)
; template <class Epi, class Sched>
; __device__ __forceinline__ void gemm_phase(LAS unsigned char* lds, const int K, const Sched& S, const Epi& E) {
;     ...
;         for (int t = 0; t < nt; t += 2) {
;             const bool last = (t == nt - 2);
;             const char* a1 = gA + (size_t)(t + 1) * kstep;
;             const char* a2 = last ? gA : gA + (size_t)(t + 2) * kstep; const char* b2 = last ? nB : cB + (size_t)(t + 2) * kstepB;
;             const char* a3 = a2 + kstep; const char* b3 = b2 + kstepB;
;             const unsigned x00 = last ? n00 : c00, x01 = last ? n01 : c01, x10 = last ? n10 : c10, x11 = last ? n11 : c11;
;             PG8_LDB(B0, 0, 0); PG8_SCHED; PG8_LDA(At, 0, 0); PG8_STAGE(PG8_SA(1, 1), a1, c10, c11);
;             PG8_WAIT_L(8); PG8_BAR; PG8_WAIT_L(0); PG8_MMA(0, 0, At, B0); PG8_BAR; PG8_SCHED;
;             PG8_LDB(B1, 0, 1); PG8_STAGE(PG8_SB(0, 0), b2, voffB0, voffB1);
;             PG8_BAR; PG8_WAIT_L(0); PG8_MMA(0, 1, At, B1); PG8_BAR;
;             PG8_LDA(At, 0, 1); PG8_STAGE(PG8_SA(0, 0), a2, x00, x01);
;             PG8_BAR; PG8_WAIT_L(0); PG8_MMA(1, 0, At, B0); PG8_BAR; PG8_SCHED;
;             PG8_STAGE(PG8_SB(0, 1), b2 + hstep, voffB0, voffB1);
;             PG8_WAIT_V(6); PG8_BAR; PG8_MMA(1, 1, At, B1); PG8_BAR;
.LBB0_1094:
	v_add_u32_e32 v139, s46, v149
	s_add_u32 s22, s0, s20
	ds_read_b128 v[160:163], v139
	ds_read_b128 v[164:167], v139 offset:1024
	ds_read_b128 v[168:171], v139 offset:2048
	ds_read_b128 v[172:175], v139 offset:3072
	s_addc_u32 s23, s1, s21
	s_add_u32 s24, s22, 0x34c30100
	s_addc_u32 s25, s23, 0
	s_cmpk_eq_i32 s20, 0xf00
	s_cselect_b64 vcc, -1, 0
	s_and_b64 s[22:23], vcc, exec
	v_cndmask_b32_e32 v134, v158, v156, vcc
	s_cselect_b32 s27, s3, s25
	s_cselect_b32 s26, s2, s24
	v_cndmask_b32_e32 v139, v138, v154, vcc
	s_cselect_b32 s23, s19, s15
	s_cselect_b32 s22, s18, s13
	v_cndmask_b32_e32 v204, v136, v155, vcc
	s_add_u32 s24, s22, 0x20000
	s_addc_u32 s25, s23, 0
	v_lshl_add_u64 v[206:207], v[144:145], 0, s[20:21]
	s_add_i32 m0, s37, 0xc000
	ds_read_b128 v[176:179], v151
	ds_read_b128 v[180:183], v151 offset:1024
	ds_read_b128 v[184:187], v151 offset:2048
	ds_read_b128 v[188:191], v151 offset:3072
	ds_read_b128 v[192:195], v151 offset:4096
	ds_read_b128 v[196:199], v151 offset:5120
	ds_read_b128 v[200:203], v151 offset:6144
	ds_read_b128 v[208:211], v151 offset:7168
	global_load_lds_dwordx4 v[206:207], off
	v_lshl_add_u64 v[206:207], v[142:143], 0, s[20:21]
	s_add_i32 m0, s37, 0xe000
	s_nop 0
	global_load_lds_dwordx4 v[206:207], off
	s_waitcnt lgkmcnt(8)
	s_barrier
	s_waitcnt lgkmcnt(0)
	s_waitcnt lgkmcnt(0)
	v_mfma_f32_16x16x32_bf16 v[126:129], v[160:163], v[176:179], v[126:129]
	v_mfma_f32_16x16x32_bf16 v[122:125], v[168:171], v[176:179], v[122:125]
	v_mfma_f32_16x16x32_bf16 v[110:113], v[160:163], v[184:187], v[110:113]
	v_mfma_f32_16x16x32_bf16 v[106:109], v[168:171], v[184:187], v[106:109]
	v_mfma_f32_16x16x32_bf16 v[94:97], v[160:163], v[192:195], v[94:97]
	v_mfma_f32_16x16x32_bf16 v[90:93], v[168:171], v[192:195], v[90:93]
	v_mfma_f32_16x16x32_bf16 v[78:81], v[160:163], v[200:203], v[78:81]
	v_mfma_f32_16x16x32_bf16 v[74:77], v[168:171], v[200:203], v[74:77]
	v_mfma_f32_16x16x32_bf16 v[126:129], v[164:167], v[180:183], v[126:129]
	v_mfma_f32_16x16x32_bf16 v[122:125], v[172:175], v[180:183], v[122:125]
	v_mfma_f32_16x16x32_bf16 v[110:113], v[164:167], v[188:191], v[110:113]
	v_mfma_f32_16x16x32_bf16 v[106:109], v[172:175], v[188:191], v[106:109]
	v_mfma_f32_16x16x32_bf16 v[94:97], v[164:167], v[196:199], v[94:97]
	v_mfma_f32_16x16x32_bf16 v[90:93], v[172:175], v[196:199], v[90:93]
	v_mfma_f32_16x16x32_bf16 v[78:81], v[164:167], v[208:211], v[78:81]
	v_mfma_f32_16x16x32_bf16 v[74:77], v[172:175], v[208:211], v[74:77]
	s_barrier
	s_add_i32 s55, s46, s36
	v_add_u32_e32 v141, s48, v149
	v_lshl_add_u64 v[206:207], s[22:23], 0, v[130:131]
	s_mov_b32 m0, s55
	ds_read_b128 v[212:215], v141
	ds_read_b128 v[216:219], v141 offset:1024
	ds_read_b128 v[220:223], v141 offset:2048
	ds_read_b128 v[224:227], v141 offset:3072
	global_load_lds_dwordx4 v[206:207], off
	v_lshl_add_u64 v[228:229], s[22:23], 0, v[132:133]
	s_add_i32 m0, s55, 0x2000
	s_nop 0
	global_load_lds_dwordx4 v[228:229], off
	s_barrier
	s_waitcnt lgkmcnt(0)
	s_waitcnt lgkmcnt(0)
	v_mfma_f32_16x16x32_bf16 v[118:121], v[212:215], v[176:179], v[118:121]
	v_mfma_f32_16x16x32_bf16 v[114:117], v[220:223], v[176:179], v[114:117]
	v_mfma_f32_16x16x32_bf16 v[102:105], v[212:215], v[184:187], v[102:105]
	v_mfma_f32_16x16x32_bf16 v[98:101], v[220:223], v[184:187], v[98:101]
	v_mfma_f32_16x16x32_bf16 v[86:89], v[212:215], v[192:195], v[86:89]
	v_mfma_f32_16x16x32_bf16 v[82:85], v[220:223], v[192:195], v[82:85]
	v_mfma_f32_16x16x32_bf16 v[70:73], v[212:215], v[200:203], v[70:73]
	v_mfma_f32_16x16x32_bf16 v[66:69], v[220:223], v[200:203], v[66:69]
	v_mfma_f32_16x16x32_bf16 v[118:121], v[216:219], v[180:183], v[118:121]
	v_mfma_f32_16x16x32_bf16 v[114:117], v[224:227], v[180:183], v[114:117]
	v_mfma_f32_16x16x32_bf16 v[102:105], v[216:219], v[188:191], v[102:105]
	v_mfma_f32_16x16x32_bf16 v[98:101], v[224:227], v[188:191], v[98:101]
	v_mfma_f32_16x16x32_bf16 v[86:89], v[216:219], v[196:199], v[86:89]
	v_mfma_f32_16x16x32_bf16 v[82:85], v[224:227], v[196:199], v[82:85]
	v_mfma_f32_16x16x32_bf16 v[70:73], v[216:219], v[208:211], v[70:73]
	v_mfma_f32_16x16x32_bf16 v[66:69], v[224:227], v[208:211], v[66:69]
	s_mov_b32 m0, s37
	s_barrier
	ds_read_b128 v[176:179], v151 offset:16384
	ds_read_b128 v[180:183], v151 offset:17408
	ds_read_b128 v[184:187], v151 offset:18432
	ds_read_b128 v[188:191], v151 offset:19456
	ds_read_b128 v[192:195], v151 offset:20480
	ds_read_b128 v[196:199], v151 offset:21504
	ds_read_b128 v[200:203], v151 offset:22528
	ds_read_b128 v[208:211], v151 offset:23552
	global_load_lds_dwordx4 v134, s[26:27]
	s_mov_b32 m0, s38
	v_mov_b32_e32 v205, v135
	global_load_lds_dwordx4 v204, s[26:27]
	s_barrier
	s_waitcnt lgkmcnt(0)
	v_lshl_add_u64 v[230:231], s[26:27], 0, v[134:135]
	v_lshl_add_u64 v[204:205], s[26:27], 0, v[204:205]
	s_waitcnt lgkmcnt(0)
	v_mfma_f32_16x16x32_bf16 v[62:65], v[160:163], v[176:179], v[62:65]
	v_mfma_f32_16x16x32_bf16 v[58:61], v[168:171], v[176:179], v[58:61]
	v_mfma_f32_16x16x32_bf16 v[46:49], v[160:163], v[184:187], v[46:49]
	v_mfma_f32_16x16x32_bf16 v[42:45], v[168:171], v[184:187], v[42:45]
	v_mfma_f32_16x16x32_bf16 v[30:33], v[160:163], v[192:195], v[30:33]
	v_mfma_f32_16x16x32_bf16 v[26:29], v[168:171], v[192:195], v[26:29]
	v_mfma_f32_16x16x32_bf16 v[14:17], v[160:163], v[200:203], v[14:17]
	v_mfma_f32_16x16x32_bf16 v[10:13], v[168:171], v[200:203], v[10:13]
	v_mfma_f32_16x16x32_bf16 v[62:65], v[164:167], v[180:183], v[62:65]
	v_mfma_f32_16x16x32_bf16 v[58:61], v[172:175], v[180:183], v[58:61]
	v_mfma_f32_16x16x32_bf16 v[46:49], v[164:167], v[188:191], v[46:49]
	v_mfma_f32_16x16x32_bf16 v[42:45], v[172:175], v[188:191], v[42:45]
	v_mfma_f32_16x16x32_bf16 v[30:33], v[164:167], v[196:199], v[30:33]
	v_mfma_f32_16x16x32_bf16 v[26:29], v[172:175], v[196:199], v[26:29]
	v_mfma_f32_16x16x32_bf16 v[14:17], v[164:167], v[208:211], v[14:17]
	v_mfma_f32_16x16x32_bf16 v[10:13], v[172:175], v[208:211], v[10:13]
	s_barrier
	s_add_i32 s55, s48, s36
	v_lshl_add_u64 v[160:161], v[206:207], 0, s[4:5]
	s_mov_b32 m0, s55
	s_nop 0
	global_load_lds_dwordx4 v[160:161], off
	v_lshl_add_u64 v[160:161], v[228:229], 0, s[4:5]
	s_add_i32 m0, s55, 0x2000
	s_nop 0
	global_load_lds_dwordx4 v[160:161], off
	s_cmp_eq_u32 s82, 0
	s_cbranch_scc1 .Lpb8_p4n
	s_waitcnt vmcnt(14)
	v_cvt_pk_bf16_f32 v244, v244, v245
	v_cvt_pk_bf16_f32 v245, v246, v247
	v_cvt_pk_bf16_f32 v246, v248, v249
	v_cvt_pk_bf16_f32 v247, v250, v251
	global_store_dwordx4 v253, v[244:247], s[78:79] nt
	s_mov_b32 s82, 0
	s_waitcnt vmcnt(7)
	s_branch .Lpb8_p4j

; #define PG8_STAGE(bufoff, gbase, v0, v1) do { \
;         __builtin_amdgcn_global_load_lds((const unsigned*)((const char*)(gbase) + (v0)), (LAS unsigned*)(lds + (bufoff) + ldsw), 16, 0, 0); \
;         __builtin_amdgcn_global_load_lds((const unsigned*)((const char*)(gbase) + (v1)), (LAS unsigned*)(lds + (bufoff) + ldsw + 8192), 16, 0, 0); } while (0)
; #define PG8_LDA(dst, b, h) do { _Pragma("unroll") for (int m = 0; m < 4; ++m) _Pragma("unroll") for (int k = 0; k < 2; ++k) dst[m][k] = *(const LAS bf16x8*)(lds + PG8_SA(b, h) + aoff + m * 2048 + k * 1024); } while (0)
; #define PG8_WAIT_V(n) asm volatile("s_waitcnt vmcnt(" #n ")" ::: "memory")
; #define PG8_WAIT_L(n) asm volatile("s_waitcnt lgkmcnt(" #n ")" ::: "memory")
; #define PG8_BAR __builtin_amdgcn_s_barrier()
; template <class Epi, class Sched>
; __device__ __forceinline__ void gemm_phase(LAS unsigned char* lds, const int K, const Sched& S, const Epi& E) {
;     ...
;             PG8_WAIT_V(6); PG8_BAR; PG8_MMA(1, 1, At, B1); PG8_BAR;
;             PG8_LDB(B0, 1, 0); PG8_SCHED; PG8_LDA(At, 1, 0); PG8_STAGE(PG8_SA(0, 1), a2, x10, x11);
;             PG8_WAIT_L(8); PG8_BAR; PG8_WAIT_L(0); PG8_MMA(0, 0, At, B0); PG8_BAR; PG8_SCHED;
;             PG8_LDB(B1, 1, 1); PG8_STAGE(PG8_SB(1, 0), b3, voffB0, voffB1);
;             PG8_BAR; PG8_WAIT_L(0); PG8_MMA(0, 1, At, B1); PG8_BAR;
;             PG8_LDA(At, 1, 1); PG8_STAGE(PG8_SA(1, 0), a3, x00, x01);
; __device__ __forceinline__ bool bg_decode(int st, int wg, int NW, int lane, KP kp, const float*& src, int& ldS, bf16_t*& dst, int& o2) {
;     ...
;     const int l = g / 98304, r = g - l * 98304;
;     unsigned char* ws = kp->ws;
;     if (r < 65536) {
;         const int e = r >> 10, kc = (r >> 2) & 255, kind = (r >> 1) & 1, cc = r & 1, n = cc * 256 + lane;
;         ldS = FF; o2 = 256 * 8;
;         src = kp->in[27 + kind] + ((size_t)(l * NE + e) * D + kc * 8) * FF + n;
;         const int drow = (n >> 7) * 256 + kind * 128 + (n & 127);
;         dst = (bf16_t*)(ws + WS_WGU) + l * WGU_L + (size_t)e * 1024 * D + ((size_t)kc * 1024 + drow) * 8;
;     } else {
;         const int r2 = r - 65536, e = r2 >> 9, kc = (r2 >> 3) & 63, cc = r2 & 7, n = cc * 256 + lane;
;         ldS = D; o2 = 128 * 8;
;         src = kp->in[29] + ((size_t)(l * NE + e) * FF + kc * 8) * D + n;
;         dst = (bf16_t*)(ws + WS_WD) + l * WD_L + (size_t)e * D * FF + ((size_t)kc * D + n) * 8;
.Lpb8_p4j:
	s_barrier
	v_mfma_f32_16x16x32_bf16 v[54:57], v[212:215], v[176:179], v[54:57]
	v_mfma_f32_16x16x32_bf16 v[50:53], v[220:223], v[176:179], v[50:53]
	v_mfma_f32_16x16x32_bf16 v[38:41], v[212:215], v[184:187], v[38:41]
	v_mfma_f32_16x16x32_bf16 v[34:37], v[220:223], v[184:187], v[34:37]
	v_mfma_f32_16x16x32_bf16 v[22:25], v[212:215], v[192:195], v[22:25]
	v_mfma_f32_16x16x32_bf16 v[18:21], v[220:223], v[192:195], v[18:21]
	v_mfma_f32_16x16x32_bf16 v[6:9], v[212:215], v[200:203], v[6:9]
	v_mfma_f32_16x16x32_bf16 v[2:5], v[220:223], v[200:203], v[2:5]
	v_mfma_f32_16x16x32_bf16 v[54:57], v[216:219], v[180:183], v[54:57]
	v_mfma_f32_16x16x32_bf16 v[50:53], v[224:227], v[180:183], v[50:53]
	v_mfma_f32_16x16x32_bf16 v[38:41], v[216:219], v[188:191], v[38:41]
	v_mfma_f32_16x16x32_bf16 v[34:37], v[224:227], v[188:191], v[34:37]
	v_mfma_f32_16x16x32_bf16 v[22:25], v[216:219], v[196:199], v[22:25]
	v_mfma_f32_16x16x32_bf16 v[18:21], v[224:227], v[196:199], v[18:21]
	v_mfma_f32_16x16x32_bf16 v[6:9], v[216:219], v[208:211], v[6:9]
	v_mfma_f32_16x16x32_bf16 v[2:5], v[224:227], v[208:211], v[2:5]
	s_add_i32 s55, 0, 0x18000
	v_add_u32_e32 v134, s55, v149
	s_barrier
	ds_read_b128 v[160:163], v134
	ds_read_b128 v[164:167], v134 offset:1024
	ds_read_b128 v[168:171], v134 offset:2048
	ds_read_b128 v[172:175], v134 offset:3072
	s_mov_b32 m0, s39
	ds_read_b128 v[176:179], v151 offset:32768
	ds_read_b128 v[180:183], v151 offset:33792
	ds_read_b128 v[184:187], v151 offset:34816
	ds_read_b128 v[188:191], v151 offset:35840
	ds_read_b128 v[192:195], v151 offset:36864
	ds_read_b128 v[196:199], v151 offset:37888
	ds_read_b128 v[200:203], v151 offset:38912
	ds_read_b128 v[208:211], v151 offset:39936
	v_cndmask_b32_e32 v134, v140, v153, vcc
	global_load_lds_dwordx4 v139, s[26:27]
	s_mov_b32 m0, s40
	s_nop 0
	global_load_lds_dwordx4 v134, s[26:27]
	s_add_u32 s90, s90, 1
	s_cmp_lt_u32 s90, 2
	s_cbranch_scc1 .Lpb8_p5n
	s_mov_b32 s90, 0
	s_cmp_ge_u32 s70, 0x28000
	s_cbranch_scc1 .Lpb8_p5n
	s_cmp_eq_u32 s80, 0
	s_cbranch_scc0 .Lpb8_adv4
	s_cmp_ge_u32 s70, 0x18000
	s_cselect_b32 s84, 0x18000, 0
	s_cselect_b32 s83, 0x10000000, 0
	s_mov_b32 s81, 0x4030000
	s_cselect_b32 s81, 0x14430000, s81
	s_sub_u32 s84, s70, s84
	s_lshr_b32 s85, s84, 2
	s_lshl_b32 s85, s85, 14
	s_and_b32 s86, s84, 1
	s_lshl_b32 s87, s86, 10
	s_add_u32 s87, s87, s85
	s_add_u32 s87, s87, s83
	s_bitcmp1_b32 s84, 1
	s_cselect_b64 s[72:73], s[76:77], s[74:75]
	s_add_u32 s72, s72, s87
	s_addc_u32 s73, s73, 0
	s_add_u32 s88, s72, 0x2000
	s_addc_u32 s89, s73, 0
	s_lshl_b32 s86, s86, 13
	s_add_u32 s85, s85, s86
	s_and_b32 s86, s84, 2
	s_lshl_b32 s86, s86, 10
	s_add_u32 s85, s85, s86
	s_add_u32 s85, s85, s81
	v_add_u32_e32 v253, s85, v252
	s_movk_i32 s81, 0x400
	s_branch .Lpb8_ld4

; #define PG8_STAGE(bufoff, gbase, v0, v1) do { \
;         __builtin_amdgcn_global_load_lds((const unsigned*)((const char*)(gbase) + (v0)), (LAS unsigned*)(lds + (bufoff) + ldsw), 16, 0, 0); \
;         __builtin_amdgcn_global_load_lds((const unsigned*)((const char*)(gbase) + (v1)), (LAS unsigned*)(lds + (bufoff) + ldsw + 8192), 16, 0, 0); } while (0)
; #define PG8_LDA(dst, b, h) do { _Pragma("unroll") for (int m = 0; m < 4; ++m) _Pragma("unroll") for (int k = 0; k < 2; ++k) dst[m][k] = *(const LAS bf16x8*)(lds + PG8_SA(b, h) + aoff + m * 2048 + k * 1024); } while (0)
; #define PG8_LDB(dst, b, h) do { _Pragma("unroll") for (int n = 0; n < 2; ++n) _Pragma("unroll") for (int k = 0; k < 2; ++k) dst[n][k] = *(const LAS bf16x8*)(lds + PG8_SB(b, h) + boff + n * 2048 + k * 1024); } while (0)
; #define PG8_MMA(ai, bj, At, Bt) do { __builtin_amdgcn_s_setprio(1); _Pragma("unroll") for (int m = 0; m < 4; ++m) _Pragma("unroll") for (int n = 0; n < 2; ++n) _Pragma("unroll") for (int k = 0; k < 2; ++k) \
;         acc[ai][bj][m][n] = __builtin_amdgcn_mfma_f32_16x16x32_bf16(Bt[n][k], At[m][k], acc[ai][bj][m][n], 0, 0, 0); __builtin_amdgcn_s_setprio(0); } while (0)
; #define PG8_WAIT_L(n) asm volatile("s_waitcnt lgkmcnt(" #n ")" ::: "memory")
; #define PG8_BAR __builtin_amdgcn_s_barrier()
; #define PG8_SCHED __builtin_amdgcn_sched_barrier(0)
; template <class Epi, class Sched>
; __device__ __forceinline__ void gemm_phase(LAS unsigned char* lds, const int K, const Sched& S, const Epi& E) {
;     ...
;             PG8_WAIT_L(8); PG8_BAR; PG8_WAIT_L(0); PG8_MMA(0, 0, At, B0); PG8_BAR; PG8_SCHED;
;             PG8_LDB(B1, 1, 1); PG8_STAGE(PG8_SB(1, 0), b3, voffB0, voffB1);
;             PG8_BAR; PG8_WAIT_L(0); PG8_MMA(0, 1, At, B1); PG8_BAR;
;             PG8_LDA(At, 1, 1); PG8_STAGE(PG8_SA(1, 0), a3, x00, x01);
;             PG8_BAR; PG8_WAIT_L(0); PG8_MMA(1, 0, At, B0); PG8_BAR; PG8_SCHED;
;             PG8_STAGE(PG8_SB(1, 1), b3 + hstep, voffB0, voffB1);
.Lpb8_p5n:
	s_waitcnt lgkmcnt(8)
	s_barrier
	s_waitcnt lgkmcnt(0)
	s_waitcnt lgkmcnt(0)
	v_mfma_f32_16x16x32_bf16 v[126:129], v[160:163], v[176:179], v[126:129]
	v_mfma_f32_16x16x32_bf16 v[122:125], v[168:171], v[176:179], v[122:125]
	v_mfma_f32_16x16x32_bf16 v[110:113], v[160:163], v[184:187], v[110:113]
	v_mfma_f32_16x16x32_bf16 v[106:109], v[168:171], v[184:187], v[106:109]
	v_mfma_f32_16x16x32_bf16 v[94:97], v[160:163], v[192:195], v[94:97]
	v_mfma_f32_16x16x32_bf16 v[90:93], v[168:171], v[192:195], v[90:93]
	v_mfma_f32_16x16x32_bf16 v[78:81], v[160:163], v[200:203], v[78:81]
	v_mfma_f32_16x16x32_bf16 v[74:77], v[168:171], v[200:203], v[74:77]
	v_mfma_f32_16x16x32_bf16 v[126:129], v[164:167], v[180:183], v[126:129]
	v_mfma_f32_16x16x32_bf16 v[122:125], v[172:175], v[180:183], v[122:125]
	v_mfma_f32_16x16x32_bf16 v[110:113], v[164:167], v[188:191], v[110:113]
	v_mfma_f32_16x16x32_bf16 v[106:109], v[172:175], v[188:191], v[106:109]
	v_mfma_f32_16x16x32_bf16 v[94:97], v[164:167], v[196:199], v[94:97]
	v_mfma_f32_16x16x32_bf16 v[90:93], v[172:175], v[196:199], v[90:93]
	v_mfma_f32_16x16x32_bf16 v[78:81], v[164:167], v[208:211], v[78:81]
	v_mfma_f32_16x16x32_bf16 v[74:77], v[172:175], v[208:211], v[74:77]
	s_barrier
	s_add_i32 s26, 0, 0x1c000
	s_add_i32 s27, s55, s36
	v_add_u32_e32 v134, s26, v149
	v_lshl_add_u64 v[206:207], s[24:25], 0, v[130:131]
	s_mov_b32 m0, s27
	ds_read_b128 v[212:215], v134
	ds_read_b128 v[216:219], v134 offset:1024
	ds_read_b128 v[220:223], v134 offset:2048
	ds_read_b128 v[224:227], v134 offset:3072
	global_load_lds_dwordx4 v[206:207], off
	v_lshl_add_u64 v[206:207], s[24:25], 0, v[132:133]
	s_add_i32 m0, s27, 0x2000
	s_nop 0
	global_load_lds_dwordx4 v[206:207], off
	s_barrier
	s_waitcnt lgkmcnt(0)
	s_waitcnt lgkmcnt(0)
	v_mfma_f32_16x16x32_bf16 v[118:121], v[212:215], v[176:179], v[118:121]
	v_mfma_f32_16x16x32_bf16 v[114:117], v[220:223], v[176:179], v[114:117]
	v_mfma_f32_16x16x32_bf16 v[102:105], v[212:215], v[184:187], v[102:105]
	v_mfma_f32_16x16x32_bf16 v[98:101], v[220:223], v[184:187], v[98:101]
	v_mfma_f32_16x16x32_bf16 v[86:89], v[212:215], v[192:195], v[86:89]
	v_mfma_f32_16x16x32_bf16 v[82:85], v[220:223], v[192:195], v[82:85]
	v_mfma_f32_16x16x32_bf16 v[70:73], v[212:215], v[200:203], v[70:73]
	v_mfma_f32_16x16x32_bf16 v[66:69], v[220:223], v[200:203], v[66:69]
	v_mfma_f32_16x16x32_bf16 v[118:121], v[216:219], v[180:183], v[118:121]
	v_mfma_f32_16x16x32_bf16 v[114:117], v[224:227], v[180:183], v[114:117]
	v_mfma_f32_16x16x32_bf16 v[102:105], v[216:219], v[188:191], v[102:105]
	v_mfma_f32_16x16x32_bf16 v[98:101], v[224:227], v[188:191], v[98:101]
	v_mfma_f32_16x16x32_bf16 v[86:89], v[216:219], v[196:199], v[86:89]
	v_mfma_f32_16x16x32_bf16 v[82:85], v[224:227], v[196:199], v[82:85]
	v_mfma_f32_16x16x32_bf16 v[70:73], v[216:219], v[208:211], v[70:73]
	v_mfma_f32_16x16x32_bf16 v[66:69], v[224:227], v[208:211], v[66:69]
	s_mov_b32 m0, s43
	v_lshl_add_u64 v[206:207], v[230:231], 0, s[10:11]
	s_barrier
	ds_read_b128 v[176:179], v151 offset:49152
	ds_read_b128 v[180:183], v151 offset:50176
	ds_read_b128 v[184:187], v151 offset:51200
	ds_read_b128 v[188:191], v151 offset:52224
	ds_read_b128 v[192:195], v151 offset:53248
	ds_read_b128 v[196:199], v151 offset:54272
	ds_read_b128 v[200:203], v151 offset:55296
	ds_read_b128 v[208:211], v151 offset:56320
	global_load_lds_dwordx4 v[206:207], off
	v_lshl_add_u64 v[204:205], v[204:205], 0, s[10:11]
	s_mov_b32 m0, s44
	s_nop 0
	global_load_lds_dwordx4 v[204:205], off
	s_barrier
	s_waitcnt lgkmcnt(0)
	s_waitcnt lgkmcnt(0)
	v_mfma_f32_16x16x32_bf16 v[62:65], v[160:163], v[176:179], v[62:65]
	v_mfma_f32_16x16x32_bf16 v[58:61], v[168:171], v[176:179], v[58:61]
	v_mfma_f32_16x16x32_bf16 v[46:49], v[160:163], v[184:187], v[46:49]
	v_mfma_f32_16x16x32_bf16 v[42:45], v[168:171], v[184:187], v[42:45]
	v_mfma_f32_16x16x32_bf16 v[30:33], v[160:163], v[192:195], v[30:33]
	v_mfma_f32_16x16x32_bf16 v[26:29], v[168:171], v[192:195], v[26:29]
	v_mfma_f32_16x16x32_bf16 v[14:17], v[160:163], v[200:203], v[14:17]
	v_mfma_f32_16x16x32_bf16 v[10:13], v[168:171], v[200:203], v[10:13]
	v_mfma_f32_16x16x32_bf16 v[62:65], v[164:167], v[180:183], v[62:65]
	v_mfma_f32_16x16x32_bf16 v[58:61], v[172:175], v[180:183], v[58:61]
	v_mfma_f32_16x16x32_bf16 v[46:49], v[164:167], v[188:191], v[46:49]
	v_mfma_f32_16x16x32_bf16 v[42:45], v[172:175], v[188:191], v[42:45]
	v_mfma_f32_16x16x32_bf16 v[30:33], v[164:167], v[196:199], v[30:33]
	v_mfma_f32_16x16x32_bf16 v[26:29], v[172:175], v[196:199], v[26:29]
	v_mfma_f32_16x16x32_bf16 v[14:17], v[164:167], v[208:211], v[14:17]
	v_mfma_f32_16x16x32_bf16 v[10:13], v[172:175], v[208:211], v[10:13]
	s_barrier
	s_add_u32 s22, s22, 0x20800
	s_addc_u32 s23, s23, 0
	s_add_i32 s24, s26, s36
	v_lshl_add_u64 v[160:161], s[22:23], 0, v[130:131]
	s_mov_b32 m0, s24
	s_nop 0
	global_load_lds_dwordx4 v[160:161], off
	v_lshl_add_u64 v[160:161], s[22:23], 0, v[132:133]
	s_add_i32 m0, s24, 0x2000
	s_nop 0
	global_load_lds_dwordx4 v[160:161], off
	s_cmp_eq_u32 s82, 0
	s_cbranch_scc1 .Lpb8_p8n
	s_waitcnt vmcnt(14)
	s_branch .Lpb8_p8j

; __device__ __forceinline__ unsigned cvt_pk_bf16(float lo, float hi) { unsigned r; asm volatile("v_cvt_pk_bf16_f32 %0, %1, %2" : "=v"(r) : "v"(lo), "v"(hi)); return r; }
; __device__ __forceinline__ float fdivf(float a, float b) { return a * __builtin_amdgcn_rcpf(b); }
; #define PG8_BAR __builtin_amdgcn_s_barrier()
; template <class Epi, class Sched>
; __device__ __forceinline__ void gemm_phase(LAS unsigned char* lds, const int K, const Sched& S, const Epi& E) {
;     ...
;             PG8_WAIT_V(6); PG8_BAR; PG8_MMA(1, 1, At, B1); PG8_BAR;
;         }
;         E(acc, cur, wr, wc, fr, fq);
;         if (!has_next) break;
;     __device__ __forceinline__ void a_off4(const Unit& u, int r0, int r1, unsigned& o00, unsigned& o01, unsigned& o10, unsigned& o11) const {
;         const int p0 = u.pm * BM + r0, p1 = u.pm * BM + r1, p2 = p0 + HALF, p3 = p1 + HALF;
;         if (u.e >= NE) { o00 = (unsigned)p0 * (unsigned)(D * 2); o01 = (unsigned)p1 * (unsigned)(D * 2); o10 = (unsigned)p2 * (unsigned)(D * 2); o11 = (unsigned)p3 * (unsigned)(D * 2); return; }
;         const int* lp = list + u.e * T;
;         int v0 = lp[p0], v1 = lp[p1], v2 = lp[p2], v3 = lp[p3];
;         asm volatile("" : "+v"(v0), "+v"(v1), "+v"(v2), "+v"(v3));
;         const int c = cnt[u.e];
;         o00 = p0 < c ? (unsigned)v0 * (unsigned)(D * 2) : 0u; o01 = p1 < c ? (unsigned)v1 * (unsigned)(D * 2) : 0u;
;         o10 = p2 < c ? (unsigned)v2 * (unsigned)(D * 2) : 0u; o11 = p3 < c ? (unsigned)v3 * (unsigned)(D * 2) : 0u;
;     __device__ __forceinline__ void operator()(const f32x4 (&acc)[2][2][4][2], const Unit& u, int wr, int wc, int fr, int fq) const {
;         const int row0 = u.rbase + wr * 64 + fr, col0 = u.pn * HALF + wc * 32 + 8 * fq;
; #pragma unroll
;         for (int ai = 0; ai < 2; ++ai)
; #pragma unroll
;             for (int m = 0; m < 4; ++m) { bf16_t* rowp = O + (size_t)(row0 + ai * HALF + m * 16) * FF + col0;
;                 float h[8];
; #pragma unroll
;                 for (int n = 0; n < 2; ++n)
; #pragma unroll
;                     for (int j = 0; j < 4; ++j) { const float g = acc[ai][0][m][n][j], up = acc[ai][1][m][n][j]; h[n * 4 + j] = fdivf(g, 1.f + __expf(-g)) * up; }
;                 u32x4 w; w.x = cvt_pk_bf16(h[0], h[1]); w.y = cvt_pk_bf16(h[2], h[3]); w.z = cvt_pk_bf16(h[4], h[5]); w.w = cvt_pk_bf16(h[6], h[7]);
;                 *(u32x4*)rowp = w; }
.Lpb8_p8j:
	s_barrier
	v_mfma_f32_16x16x32_bf16 v[54:57], v[212:215], v[176:179], v[54:57]
	v_mfma_f32_16x16x32_bf16 v[50:53], v[220:223], v[176:179], v[50:53]
	v_mfma_f32_16x16x32_bf16 v[38:41], v[212:215], v[184:187], v[38:41]
	v_mfma_f32_16x16x32_bf16 v[34:37], v[220:223], v[184:187], v[34:37]
	v_mfma_f32_16x16x32_bf16 v[22:25], v[212:215], v[192:195], v[22:25]
	v_mfma_f32_16x16x32_bf16 v[18:21], v[220:223], v[192:195], v[18:21]
	v_mfma_f32_16x16x32_bf16 v[6:9], v[212:215], v[200:203], v[6:9]
	v_mfma_f32_16x16x32_bf16 v[2:5], v[220:223], v[200:203], v[2:5]
	v_mfma_f32_16x16x32_bf16 v[54:57], v[216:219], v[180:183], v[54:57]
	v_mfma_f32_16x16x32_bf16 v[50:53], v[224:227], v[180:183], v[50:53]
	v_mfma_f32_16x16x32_bf16 v[38:41], v[216:219], v[188:191], v[38:41]
	v_mfma_f32_16x16x32_bf16 v[34:37], v[224:227], v[188:191], v[34:37]
	v_mfma_f32_16x16x32_bf16 v[22:25], v[216:219], v[196:199], v[22:25]
	v_mfma_f32_16x16x32_bf16 v[18:21], v[224:227], v[196:199], v[18:21]
	v_mfma_f32_16x16x32_bf16 v[6:9], v[216:219], v[208:211], v[6:9]
	v_mfma_f32_16x16x32_bf16 v[2:5], v[224:227], v[208:211], v[2:5]
	s_add_i32 s54, s54, 2
	s_add_u32 s13, s13, 0x40000
	s_addc_u32 s15, s15, 0
	s_add_u32 s20, s20, 0x100
	s_addc_u32 s21, s21, 0
	s_cmp_gt_u32 s54, 29
	s_barrier
	s_cbranch_scc0 .LBB0_1094
	v_mul_f32_e32 v134, 0xbfb8aa3b, v126
	v_exp_f32_e32 v134, v134
	v_mul_f32_e32 v136, 0xbfb8aa3b, v127
	v_exp_f32_e32 v136, v136
	v_add_u32_e32 v138, v157, v137
	v_add_f32_e32 v134, 1.0, v134
	v_rcp_f32_e32 v134, v134
	v_add_f32_e32 v136, 1.0, v136
	v_rcp_f32_e32 v136, v136
	v_ashrrev_i32_e32 v139, 31, v138
	v_mul_f32_e32 v126, v126, v134
	v_mul_f32_e32 v118, v126, v118
	v_mul_f32_e32 v126, v127, v136
	v_mul_f32_e32 v127, 0xbfb8aa3b, v128
	v_exp_f32_e32 v127, v127
	v_mul_f32_e32 v134, 0xbfb8aa3b, v129
	v_exp_f32_e32 v134, v134
	v_mul_f32_e32 v119, v126, v119
	v_add_f32_e32 v126, 1.0, v127
	v_rcp_f32_e32 v126, v126
	v_add_f32_e32 v127, 1.0, v134
	v_mul_f32_e32 v134, 0xbfb8aa3b, v122
	v_rcp_f32_e32 v127, v127
	v_exp_f32_e32 v134, v134
	v_mul_f32_e32 v126, v128, v126
	v_mul_f32_e32 v120, v126, v120
	v_mul_f32_e32 v126, v129, v127
	v_add_f32_e32 v127, 1.0, v134
	v_rcp_f32_e32 v127, v127
	v_mul_f32_e32 v128, 0xbfb8aa3b, v123
	v_exp_f32_e32 v128, v128
	v_mul_f32_e32 v121, v126, v121
	v_mul_f32_e32 v122, v122, v127
	v_mul_f32_e32 v122, v122, v114
	v_add_f32_e32 v114, 1.0, v128
	v_mul_f32_e32 v126, 0xbfb8aa3b, v124
	v_rcp_f32_e32 v114, v114
	v_exp_f32_e32 v126, v126
	v_mul_f32_e32 v127, 0xbfb8aa3b, v125
	v_exp_f32_e32 v127, v127
	v_mul_f32_e32 v114, v123, v114
	v_add_f32_e32 v123, 1.0, v126
	v_rcp_f32_e32 v123, v123
	v_add_f32_e32 v126, 1.0, v127
	v_rcp_f32_e32 v126, v126
	v_mul_f32_e32 v127, v114, v115
	v_mul_f32_e32 v114, v124, v123
	v_mul_f32_e32 v123, v114, v116
	v_mul_f32_e32 v114, v125, v126
	v_cvt_pk_bf16_f32 v116, v118, v119
	v_mul_f32_e32 v119, 0xbfb8aa3b, v110
	v_mul_f32_e32 v124, v114, v117
	v_cvt_pk_bf16_f32 v117, v120, v121
	v_exp_f32_e32 v120, v119
	v_mul_f32_e32 v119, 0xbfb8aa3b, v111
	v_exp_f32_e32 v121, v119
	v_lshl_or_b32 v140, s53, 7, v150
	v_add_f32_e32 v120, 1.0, v120
	v_rcp_f32_e32 v120, v120
	v_add_f32_e32 v121, 1.0, v121
	v_rcp_f32_e32 v121, v121
	v_lshlrev_b64 v[138:139], 10, v[138:139]
	v_ashrrev_i32_e32 v141, 31, v140
	v_lshl_add_u64 v[138:139], s[6:7], 0, v[138:139]
	v_mul_f32_e32 v110, v110, v120
	v_lshl_add_u64 v[114:115], v[140:141], 1, v[138:139]
	v_mul_f32_e32 v102, v110, v102
	v_mul_f32_e32 v110, v111, v121
	v_mul_f32_e32 v111, 0xbfb8aa3b, v112
	v_cvt_pk_bf16_f32 v118, v122, v127
	v_cvt_pk_bf16_f32 v119, v123, v124
	global_store_dwordx4 v[114:115], v[116:119], off
	v_exp_f32_e32 v111, v111
	v_mul_f32_e32 v103, v110, v103
	v_mul_f32_e32 v116, 0xbfb8aa3b, v113
	v_exp_f32_e32 v116, v116
	v_add_f32_e32 v110, 1.0, v111
	v_rcp_f32_e32 v110, v110
	v_mov_b32_e32 v157, v152
	v_add_f32_e32 v111, 1.0, v116
	v_mul_f32_e32 v116, 0xbfb8aa3b, v106
	v_rcp_f32_e32 v111, v111
	v_exp_f32_e32 v116, v116
	v_mul_f32_e32 v110, v112, v110
	v_mul_f32_e32 v104, v110, v104
	v_mul_f32_e32 v110, v113, v111
	v_add_f32_e32 v111, 1.0, v116
	v_rcp_f32_e32 v111, v111
	v_mul_f32_e32 v112, 0xbfb8aa3b, v107
	v_exp_f32_e32 v112, v112
	v_mul_f32_e32 v105, v110, v105
	v_mul_f32_e32 v106, v106, v111
	v_mul_f32_e32 v106, v106, v98
	v_add_f32_e32 v98, 1.0, v112
	v_mul_f32_e32 v110, 0xbfb8aa3b, v108
	v_rcp_f32_e32 v98, v98
	v_exp_f32_e32 v110, v110
	v_mul_f32_e32 v111, 0xbfb8aa3b, v109
	v_exp_f32_e32 v111, v111
	v_mul_f32_e32 v98, v107, v98
	v_add_f32_e32 v107, 1.0, v110
	v_rcp_f32_e32 v107, v107
	v_add_f32_e32 v110, 1.0, v111
	v_rcp_f32_e32 v110, v110
	v_mul_f32_e32 v111, v98, v99
	v_mul_f32_e32 v98, v108, v107
	v_mul_f32_e32 v107, v98, v100
	v_mul_f32_e32 v98, v109, v110
	v_mul_f32_e32 v101, v98, v101
	v_cvt_pk_bf16_f32 v98, v102, v103
	v_mul_f32_e32 v102, 0xbfb8aa3b, v94
	v_cvt_pk_bf16_f32 v99, v104, v105
	v_exp_f32_e32 v104, v102
	v_mul_f32_e32 v102, 0xbfb8aa3b, v95
	v_exp_f32_e32 v105, v102
	v_add_co_u32_e32 v102, vcc, s42, v114
	v_add_f32_e32 v104, 1.0, v104
	v_rcp_f32_e32 v104, v104
	v_add_f32_e32 v105, 1.0, v105
	v_rcp_f32_e32 v105, v105
	v_addc_co_u32_e32 v103, vcc, 0, v115, vcc
	v_mul_f32_e32 v94, v94, v104
	v_mul_f32_e32 v86, v94, v86
	v_mul_f32_e32 v94, v95, v105
	v_mul_f32_e32 v95, 0xbfb8aa3b, v96
	v_cvt_pk_bf16_f32 v100, v106, v111
	v_cvt_pk_bf16_f32 v101, v107, v101
	global_store_dwordx4 v[102:103], v[98:101], off
	v_exp_f32_e32 v95, v95
	v_mul_f32_e32 v87, v94, v87
	v_mul_f32_e32 v98, 0xbfb8aa3b, v97
	v_exp_f32_e32 v98, v98
	v_add_f32_e32 v94, 1.0, v95
	v_rcp_f32_e32 v94, v94
	s_mov_b32 s53, s12
	v_add_f32_e32 v95, 1.0, v98
	v_mul_f32_e32 v98, 0xbfb8aa3b, v90
; __device__ __forceinline__ unsigned cvt_pk_bf16(float lo, float hi) { unsigned r; asm volatile("v_cvt_pk_bf16_f32 %0, %1, %2" : "=v"(r) : "v"(lo), "v"(hi)); return r; }
; __device__ __forceinline__ float fdivf(float a, float b) { return a * __builtin_amdgcn_rcpf(b); }
;     __device__ __forceinline__ void operator()(const f32x4 (&acc)[2][2][4][2], const Unit& u, int wr, int wc, int fr, int fq) const {
;     ...
;         for (int ai = 0; ai < 2; ++ai)
; #pragma unroll
;             for (int m = 0; m < 4; ++m) { bf16_t* rowp = O + (size_t)(row0 + ai * HALF + m * 16) * FF + col0;
;                 float h[8];
; #pragma unroll
;                 for (int n = 0; n < 2; ++n)
; #pragma unroll
;                     for (int j = 0; j < 4; ++j) { const float g = acc[ai][0][m][n][j], up = acc[ai][1][m][n][j]; h[n * 4 + j] = fdivf(g, 1.f + __expf(-g)) * up; }
;                 u32x4 w; w.x = cvt_pk_bf16(h[0], h[1]); w.y = cvt_pk_bf16(h[2], h[3]); w.z = cvt_pk_bf16(h[4], h[5]); w.w = cvt_pk_bf16(h[6], h[7]);
;                 *(u32x4*)rowp = w; }
	v_rcp_f32_e32 v95, v95
	v_exp_f32_e32 v98, v98
	v_mul_f32_e32 v94, v96, v94
	v_mul_f32_e32 v88, v94, v88
	v_mul_f32_e32 v94, v97, v95
	v_add_f32_e32 v95, 1.0, v98
	v_rcp_f32_e32 v95, v95
	v_mul_f32_e32 v96, 0xbfb8aa3b, v91
	v_exp_f32_e32 v96, v96
	v_mul_f32_e32 v89, v94, v89
	v_mul_f32_e32 v90, v90, v95
	v_mul_f32_e32 v90, v90, v82
	v_add_f32_e32 v82, 1.0, v96
	v_mul_f32_e32 v94, 0xbfb8aa3b, v92
	v_rcp_f32_e32 v82, v82
	v_exp_f32_e32 v94, v94
	v_mul_f32_e32 v95, 0xbfb8aa3b, v93
	v_exp_f32_e32 v95, v95
	v_mul_f32_e32 v82, v91, v82
	v_add_f32_e32 v91, 1.0, v94
	v_rcp_f32_e32 v91, v91
	v_add_f32_e32 v94, 1.0, v95
	v_rcp_f32_e32 v94, v94
	v_mul_f32_e32 v95, v82, v83
	v_mul_f32_e32 v82, v92, v91
	v_mul_f32_e32 v91, v82, v84
	v_mul_f32_e32 v82, v93, v94
	v_mul_f32_e32 v85, v82, v85
	v_cvt_pk_bf16_f32 v82, v86, v87
	v_mul_f32_e32 v86, 0xbfb8aa3b, v78
	v_cvt_pk_bf16_f32 v83, v88, v89
	v_exp_f32_e32 v88, v86
	v_mul_f32_e32 v86, 0xbfb8aa3b, v79
	v_exp_f32_e32 v89, v86
	v_add_co_u32_e32 v86, vcc, s45, v114
	v_add_f32_e32 v88, 1.0, v88
	v_rcp_f32_e32 v88, v88
	v_add_f32_e32 v89, 1.0, v89
	v_rcp_f32_e32 v89, v89
	v_addc_co_u32_e32 v87, vcc, 0, v115, vcc
	v_mul_f32_e32 v78, v78, v88
	v_mul_f32_e32 v70, v78, v70
	v_mul_f32_e32 v78, v79, v89
	v_mul_f32_e32 v79, 0xbfb8aa3b, v80
	v_cvt_pk_bf16_f32 v84, v90, v95
	v_cvt_pk_bf16_f32 v85, v91, v85
	global_store_dwordx4 v[86:87], v[82:85], off
	v_exp_f32_e32 v79, v79
	v_mul_f32_e32 v71, v78, v71
	v_mul_f32_e32 v82, 0xbfb8aa3b, v81
	v_exp_f32_e32 v82, v82
	v_add_f32_e32 v78, 1.0, v79
	v_rcp_f32_e32 v78, v78
	v_mov_b32_e32 v158, v156
	v_add_f32_e32 v79, 1.0, v82
	v_mul_f32_e32 v82, 0xbfb8aa3b, v74
	v_rcp_f32_e32 v79, v79
	v_exp_f32_e32 v82, v82
	v_mul_f32_e32 v78, v80, v78
	v_mul_f32_e32 v72, v78, v72
	v_mul_f32_e32 v78, v81, v79
	v_add_f32_e32 v79, 1.0, v82
	v_rcp_f32_e32 v79, v79
	v_mul_f32_e32 v80, 0xbfb8aa3b, v75
	v_exp_f32_e32 v80, v80
	v_mul_f32_e32 v73, v78, v73
	v_mul_f32_e32 v74, v74, v79
	v_mul_f32_e32 v74, v74, v66
	v_add_f32_e32 v66, 1.0, v80
	v_mul_f32_e32 v78, 0xbfb8aa3b, v76
	v_rcp_f32_e32 v66, v66
	v_exp_f32_e32 v78, v78
	v_mul_f32_e32 v79, 0xbfb8aa3b, v77
	v_exp_f32_e32 v79, v79
	v_mul_f32_e32 v66, v75, v66
	v_add_f32_e32 v75, 1.0, v78
	v_rcp_f32_e32 v75, v75
	v_add_f32_e32 v78, 1.0, v79
	v_rcp_f32_e32 v78, v78
	v_mul_f32_e32 v79, v66, v67
	v_mul_f32_e32 v66, v76, v75
	v_mul_f32_e32 v75, v66, v68
	v_mul_f32_e32 v66, v77, v78
	v_mul_f32_e32 v69, v66, v69
	v_cvt_pk_bf16_f32 v66, v70, v71
	v_mul_f32_e32 v70, 0xbfb8aa3b, v62
	v_cvt_pk_bf16_f32 v67, v72, v73
	v_exp_f32_e32 v72, v70
	v_mul_f32_e32 v70, 0xbfb8aa3b, v63
	v_exp_f32_e32 v73, v70
	v_add_co_u32_e32 v70, vcc, s47, v114
	v_add_f32_e32 v72, 1.0, v72
	v_rcp_f32_e32 v72, v72
	v_add_f32_e32 v73, 1.0, v73
	v_rcp_f32_e32 v73, v73
	v_addc_co_u32_e32 v71, vcc, 0, v115, vcc
	v_mul_f32_e32 v62, v62, v72
	v_mul_f32_e32 v54, v62, v54
	v_mul_f32_e32 v62, v63, v73
	v_mul_f32_e32 v63, 0xbfb8aa3b, v64
	v_cvt_pk_bf16_f32 v68, v74, v79
	v_cvt_pk_bf16_f32 v69, v75, v69
	global_store_dwordx4 v[70:71], v[66:69], off
	v_exp_f32_e32 v63, v63
	v_mul_f32_e32 v55, v62, v55
	v_mul_f32_e32 v66, 0xbfb8aa3b, v65
	v_exp_f32_e32 v66, v66
	v_add_f32_e32 v62, 1.0, v63
	v_rcp_f32_e32 v62, v62
	v_mov_b32_e32 v136, v155
	v_add_f32_e32 v63, 1.0, v66
	v_mul_f32_e32 v66, 0xbfb8aa3b, v58
	v_rcp_f32_e32 v63, v63
	v_exp_f32_e32 v66, v66
	v_mul_f32_e32 v62, v64, v62
	v_mul_f32_e32 v56, v62, v56
	v_mul_f32_e32 v62, v65, v63
	v_add_f32_e32 v63, 1.0, v66
	v_rcp_f32_e32 v63, v63
	v_mul_f32_e32 v64, 0xbfb8aa3b, v59
	v_exp_f32_e32 v64, v64
	v_mul_f32_e32 v57, v62, v57
	v_mul_f32_e32 v58, v58, v63
	v_mul_f32_e32 v58, v58, v50
	v_add_f32_e32 v50, 1.0, v64
	v_mul_f32_e32 v62, 0xbfb8aa3b, v60
	v_rcp_f32_e32 v50, v50
	v_exp_f32_e32 v62, v62
	v_mul_f32_e32 v63, 0xbfb8aa3b, v61
	v_exp_f32_e32 v63, v63
	v_mul_f32_e32 v50, v59, v50
	v_add_f32_e32 v59, 1.0, v62
	v_rcp_f32_e32 v59, v59
	v_add_f32_e32 v62, 1.0, v63
	v_rcp_f32_e32 v62, v62
	v_mul_f32_e32 v63, v50, v51
	v_mul_f32_e32 v50, v60, v59
	v_mul_f32_e32 v59, v50, v52
	v_mul_f32_e32 v50, v61, v62
	v_mul_f32_e32 v53, v50, v53
	v_cvt_pk_bf16_f32 v50, v54, v55
	v_mul_f32_e32 v54, 0xbfb8aa3b, v46
	v_cvt_pk_bf16_f32 v51, v56, v57
	v_exp_f32_e32 v56, v54
	v_mul_f32_e32 v54, 0xbfb8aa3b, v47
	v_exp_f32_e32 v57, v54
	v_add_co_u32_e32 v54, vcc, s49, v114
	v_add_f32_e32 v56, 1.0, v56
	v_rcp_f32_e32 v56, v56
	v_add_f32_e32 v57, 1.0, v57
	v_rcp_f32_e32 v57, v57
	v_addc_co_u32_e32 v55, vcc, 0, v115, vcc
	v_mul_f32_e32 v46, v46, v56
	v_mul_f32_e32 v38, v46, v38
	v_mul_f32_e32 v46, v47, v57
	v_mul_f32_e32 v47, 0xbfb8aa3b, v48
	v_cvt_pk_bf16_f32 v52, v58, v63
	v_cvt_pk_bf16_f32 v53, v59, v53
	global_store_dwordx4 v[54:55], v[50:53], off
	v_exp_f32_e32 v47, v47
; __device__ __forceinline__ unsigned cvt_pk_bf16(float lo, float hi) { unsigned r; asm volatile("v_cvt_pk_bf16_f32 %0, %1, %2" : "=v"(r) : "v"(lo), "v"(hi)); return r; }
; __device__ __forceinline__ float fdivf(float a, float b) { return a * __builtin_amdgcn_rcpf(b); }
; #define PG8_WAIT_V(n) asm volatile("s_waitcnt vmcnt(" #n ")" ::: "memory")
; #define PG8_BAR __builtin_amdgcn_s_barrier()
; template <class Epi, class Sched>
; __device__ __forceinline__ void gemm_phase(LAS unsigned char* lds, const int K, const Sched& S, const Epi& E) {
;     ...
;         if (!has_next) break;
; #pragma unroll
;         for (int a = 0; a < 2; ++a)
; #pragma unroll
;             for (int b = 0; b < 2; ++b)
; #pragma unroll
;                 for (int m = 0; m < 4; ++m)
; #pragma unroll
;                     for (int n = 0; n < 2; ++n) acc[a][b][m][n] = (f32x4){0.f, 0.f, 0.f, 0.f};
;         cur = nxt; cB = nB; c00 = n00; c01 = n01; c10 = n10; c11 = n11; ++ui;
;     }
;     PG8_WAIT_V(0);
;     if (wr == 0) PG8_BAR;
;     PG8_BAR;
;     __device__ __forceinline__ void operator()(const f32x4 (&acc)[2][2][4][2], const Unit& u, int wr, int wc, int fr, int fq) const {
;     ...
;         for (int ai = 0; ai < 2; ++ai)
; #pragma unroll
;             for (int m = 0; m < 4; ++m) { bf16_t* rowp = O + (size_t)(row0 + ai * HALF + m * 16) * FF + col0;
;                 float h[8];
; #pragma unroll
;                 for (int n = 0; n < 2; ++n)
; #pragma unroll
;                     for (int j = 0; j < 4; ++j) { const float g = acc[ai][0][m][n][j], up = acc[ai][1][m][n][j]; h[n * 4 + j] = fdivf(g, 1.f + __expf(-g)) * up; }
;                 u32x4 w; w.x = cvt_pk_bf16(h[0], h[1]); w.y = cvt_pk_bf16(h[2], h[3]); w.z = cvt_pk_bf16(h[4], h[5]); w.w = cvt_pk_bf16(h[6], h[7]);
;                 *(u32x4*)rowp = w; }
	v_mul_f32_e32 v39, v46, v39
	v_mul_f32_e32 v50, 0xbfb8aa3b, v49
	v_exp_f32_e32 v50, v50
	v_add_f32_e32 v46, 1.0, v47
	v_rcp_f32_e32 v46, v46
	v_mov_b32_e32 v138, v154
	v_add_f32_e32 v47, 1.0, v50
	v_mul_f32_e32 v50, 0xbfb8aa3b, v42
	v_rcp_f32_e32 v47, v47
	v_exp_f32_e32 v50, v50
	v_mul_f32_e32 v46, v48, v46
	v_mul_f32_e32 v40, v46, v40
	v_mul_f32_e32 v46, v49, v47
	v_add_f32_e32 v47, 1.0, v50
	v_rcp_f32_e32 v47, v47
	v_mul_f32_e32 v48, 0xbfb8aa3b, v43
	v_exp_f32_e32 v48, v48
	v_mul_f32_e32 v41, v46, v41
	v_mul_f32_e32 v42, v42, v47
	v_mul_f32_e32 v42, v42, v34
	v_add_f32_e32 v34, 1.0, v48
	v_mul_f32_e32 v46, 0xbfb8aa3b, v44
	v_rcp_f32_e32 v34, v34
	v_exp_f32_e32 v46, v46
	v_mul_f32_e32 v47, 0xbfb8aa3b, v45
	v_exp_f32_e32 v47, v47
	v_mul_f32_e32 v34, v43, v34
	v_add_f32_e32 v43, 1.0, v46
	v_rcp_f32_e32 v43, v43
	v_add_f32_e32 v46, 1.0, v47
	v_rcp_f32_e32 v46, v46
	v_mul_f32_e32 v47, v34, v35
	v_mul_f32_e32 v34, v44, v43
	v_mul_f32_e32 v43, v34, v36
	v_mul_f32_e32 v34, v45, v46
	v_mul_f32_e32 v37, v34, v37
	v_cvt_pk_bf16_f32 v34, v38, v39
	v_mul_f32_e32 v38, 0xbfb8aa3b, v30
	v_cvt_pk_bf16_f32 v35, v40, v41
	v_exp_f32_e32 v40, v38
	v_mul_f32_e32 v38, 0xbfb8aa3b, v31
	v_exp_f32_e32 v41, v38
	v_add_co_u32_e32 v38, vcc, s50, v114
	v_add_f32_e32 v40, 1.0, v40
	v_rcp_f32_e32 v40, v40
	v_add_f32_e32 v41, 1.0, v41
	v_rcp_f32_e32 v41, v41
	v_addc_co_u32_e32 v39, vcc, 0, v115, vcc
	v_mul_f32_e32 v30, v30, v40
	v_mul_f32_e32 v22, v30, v22
	v_mul_f32_e32 v30, v31, v41
	v_mul_f32_e32 v31, 0xbfb8aa3b, v32
	v_cvt_pk_bf16_f32 v36, v42, v47
	v_cvt_pk_bf16_f32 v37, v43, v37
	global_store_dwordx4 v[38:39], v[34:37], off
	v_exp_f32_e32 v31, v31
	v_mul_f32_e32 v23, v30, v23
	v_mul_f32_e32 v34, 0xbfb8aa3b, v33
	v_exp_f32_e32 v34, v34
	v_add_f32_e32 v30, 1.0, v31
	v_rcp_f32_e32 v30, v30
	v_mov_b32_e32 v140, v153
	v_add_f32_e32 v31, 1.0, v34
	v_mul_f32_e32 v34, 0xbfb8aa3b, v26
	v_rcp_f32_e32 v31, v31
	v_exp_f32_e32 v34, v34
	v_mul_f32_e32 v30, v32, v30
	v_mul_f32_e32 v24, v30, v24
	v_mul_f32_e32 v30, v33, v31
	v_add_f32_e32 v31, 1.0, v34
	v_rcp_f32_e32 v31, v31
	v_mul_f32_e32 v32, 0xbfb8aa3b, v27
	v_exp_f32_e32 v32, v32
	v_mul_f32_e32 v25, v30, v25
	v_mul_f32_e32 v26, v26, v31
	v_mul_f32_e32 v26, v26, v18
	v_add_f32_e32 v18, 1.0, v32
	v_mul_f32_e32 v30, 0xbfb8aa3b, v28
	v_rcp_f32_e32 v18, v18
	v_exp_f32_e32 v30, v30
	v_mul_f32_e32 v31, 0xbfb8aa3b, v29
	v_exp_f32_e32 v31, v31
	v_mul_f32_e32 v18, v27, v18
	v_add_f32_e32 v27, 1.0, v30
	v_rcp_f32_e32 v27, v27
	v_add_f32_e32 v30, 1.0, v31
	v_rcp_f32_e32 v30, v30
	v_mul_f32_e32 v31, v18, v19
	v_mul_f32_e32 v18, v28, v27
	v_mul_f32_e32 v27, v18, v20
	v_mul_f32_e32 v18, v29, v30
	v_mul_f32_e32 v21, v18, v21
	v_cvt_pk_bf16_f32 v18, v22, v23
	v_mul_f32_e32 v22, 0xbfb8aa3b, v14
	v_cvt_pk_bf16_f32 v19, v24, v25
	v_exp_f32_e32 v24, v22
	v_mul_f32_e32 v22, 0xbfb8aa3b, v15
	v_exp_f32_e32 v25, v22
	v_add_co_u32_e32 v22, vcc, s51, v114
	v_add_f32_e32 v24, 1.0, v24
	v_rcp_f32_e32 v24, v24
	v_add_f32_e32 v25, 1.0, v25
	v_rcp_f32_e32 v25, v25
	v_addc_co_u32_e32 v23, vcc, 0, v115, vcc
	v_mul_f32_e32 v14, v14, v24
	v_mul_f32_e32 v6, v14, v6
	v_mul_f32_e32 v14, v15, v25
	v_mul_f32_e32 v15, 0xbfb8aa3b, v16
	v_cvt_pk_bf16_f32 v20, v26, v31
	v_cvt_pk_bf16_f32 v21, v27, v21
	global_store_dwordx4 v[22:23], v[18:21], off
	v_exp_f32_e32 v15, v15
	v_mul_f32_e32 v7, v14, v7
	v_mul_f32_e32 v18, 0xbfb8aa3b, v17
	v_exp_f32_e32 v18, v18
	v_add_f32_e32 v14, 1.0, v15
	v_rcp_f32_e32 v14, v14
	s_mov_b64 s[20:21], s[18:19]
	v_add_f32_e32 v15, 1.0, v18
	v_mul_f32_e32 v18, 0xbfb8aa3b, v10
	v_rcp_f32_e32 v15, v15
	v_exp_f32_e32 v18, v18
	v_mul_f32_e32 v14, v16, v14
	v_mul_f32_e32 v8, v14, v8
	v_mul_f32_e32 v14, v17, v15
	v_add_f32_e32 v15, 1.0, v18
	v_rcp_f32_e32 v15, v15
	v_mul_f32_e32 v16, 0xbfb8aa3b, v11
	v_exp_f32_e32 v16, v16
	v_mul_f32_e32 v9, v14, v9
	v_mul_f32_e32 v10, v10, v15
	v_mul_f32_e32 v10, v10, v2
	v_add_f32_e32 v2, 1.0, v16
	v_mul_f32_e32 v14, 0xbfb8aa3b, v12
	v_rcp_f32_e32 v2, v2
	v_exp_f32_e32 v14, v14
	v_mul_f32_e32 v15, 0xbfb8aa3b, v13
	v_exp_f32_e32 v15, v15
	v_mul_f32_e32 v2, v11, v2
	v_add_f32_e32 v11, 1.0, v14
	v_rcp_f32_e32 v11, v11
	v_add_f32_e32 v14, 1.0, v15
	v_rcp_f32_e32 v14, v14
	v_mul_f32_e32 v15, v2, v3
	v_mul_f32_e32 v2, v12, v11
	v_mul_f32_e32 v11, v2, v4
	v_mul_f32_e32 v2, v13, v14
	v_mul_f32_e32 v5, v2, v5
	v_cvt_pk_bf16_f32 v2, v6, v7
	v_add_co_u32_e32 v6, vcc, 0x2c000, v114
	v_cvt_pk_bf16_f32 v3, v8, v9
	v_cvt_pk_bf16_f32 v4, v10, v15
	v_cvt_pk_bf16_f32 v5, v11, v5
	s_nop 1
	v_addc_co_u32_e32 v7, vcc, 0, v115, vcc
	s_and_b64 vcc, exec, s[16:17]
	global_store_dwordx4 v[6:7], v[2:5], off
	s_cbranch_vccz .LBB0_1085
	s_waitcnt vmcnt(0)
	s_cmpk_gt_u32 s30, 0xff
	s_cbranch_scc1 .LBB0_1098
	s_barrier

; #define PG8_STAGE(bufoff, gbase, v0, v1) do { \
;         __builtin_amdgcn_global_load_lds((const unsigned*)((const char*)(gbase) + (v0)), (LAS unsigned*)(lds + (bufoff) + ldsw), 16, 0, 0); \
;         __builtin_amdgcn_global_load_lds((const unsigned*)((const char*)(gbase) + (v1)), (LAS unsigned*)(lds + (bufoff) + ldsw + 8192), 16, 0, 0); } while (0)
; #define PG8_LDA(dst, b, h) do { _Pragma("unroll") for (int m = 0; m < 4; ++m) _Pragma("unroll") for (int k = 0; k < 2; ++k) dst[m][k] = *(const LAS bf16x8*)(lds + PG8_SA(b, h) + aoff + m * 2048 + k * 1024); } while (0)
; #define PG8_LDB(dst, b, h) do { _Pragma("unroll") for (int n = 0; n < 2; ++n) _Pragma("unroll") for (int k = 0; k < 2; ++k) dst[n][k] = *(const LAS bf16x8*)(lds + PG8_SB(b, h) + boff + n * 2048 + k * 1024); } while (0)
; #define PG8_WAIT_V(n) asm volatile("s_waitcnt vmcnt(" #n ")" ::: "memory")
; #define PG8_WAIT_L(n) asm volatile("s_waitcnt lgkmcnt(" #n ")" ::: "memory")
; #define PG8_BAR __builtin_amdgcn_s_barrier()
; #define PG8_SCHED __builtin_amdgcn_sched_barrier(0)
; template <class Epi, class Sched>
; __device__ __forceinline__ void gemm_phase(LAS unsigned char* lds, const int K, const Sched& S, const Epi& E) {
;     ...
;         for (int t = 0; t < nt; t += 2) {
;             const bool last = (t == nt - 2);
;             const char* a1 = gA + (size_t)(t + 1) * kstep;
;             const char* a2 = last ? gA : gA + (size_t)(t + 2) * kstep; const char* b2 = last ? nB : cB + (size_t)(t + 2) * kstepB;
;             const char* a3 = a2 + kstep; const char* b3 = b2 + kstepB;
;             const unsigned x00 = last ? n00 : c00, x01 = last ? n01 : c01, x10 = last ? n10 : c10, x11 = last ? n11 : c11;
;             PG8_LDB(B0, 0, 0); PG8_SCHED; PG8_LDA(At, 0, 0); PG8_STAGE(PG8_SA(1, 1), a1, c10, c11);
;             PG8_WAIT_L(8); PG8_BAR; PG8_WAIT_L(0); PG8_MMA(0, 0, At, B0); PG8_BAR; PG8_SCHED;
;             PG8_LDB(B1, 0, 1); PG8_STAGE(PG8_SB(0, 0), b2, voffB0, voffB1);
;             PG8_BAR; PG8_WAIT_L(0); PG8_MMA(0, 1, At, B1); PG8_BAR;
;             PG8_LDA(At, 0, 1); PG8_STAGE(PG8_SA(0, 0), a2, x00, x01);
;             PG8_BAR; PG8_WAIT_L(0); PG8_MMA(1, 0, At, B0); PG8_BAR; PG8_SCHED;
;             PG8_STAGE(PG8_SB(0, 1), b2 + hstep, voffB0, voffB1);
;             PG8_WAIT_V(6); PG8_BAR; PG8_MMA(1, 1, At, B1); PG8_BAR;
.LBB0_1161:
	s_add_u32 s40, s0, s38
	ds_read_b128 v[164:167], v153
	ds_read_b128 v[168:171], v153 offset:1024
	ds_read_b128 v[172:175], v153 offset:2048
	ds_read_b128 v[176:179], v153 offset:3072
	s_addc_u32 s41, s1, s39
	s_add_u32 s42, s40, 0x3ee90100
	s_addc_u32 s43, s41, 0
	s_cmpk_eq_i32 s38, 0x300
	s_cselect_b64 vcc, -1, 0
	s_and_b64 s[40:41], vcc, exec
	v_cndmask_b32_e32 v134, v162, v157, vcc
	s_cselect_b32 s45, s3, s43
	s_cselect_b32 s44, s2, s42
	v_cndmask_b32_e32 v139, v138, v159, vcc
	s_cselect_b32 s41, s37, s31
	s_cselect_b32 s40, s36, s29
	v_cndmask_b32_e32 v204, v136, v158, vcc
	s_add_u32 s42, s40, 0x40000
	s_addc_u32 s43, s41, 0
	v_lshl_add_u64 v[206:207], v[144:145], 0, s[38:39]
	s_add_i32 m0, s49, 0xc000
	ds_read_b128 v[180:183], v154
	ds_read_b128 v[184:187], v154 offset:1024
	ds_read_b128 v[188:191], v154 offset:2048
	ds_read_b128 v[192:195], v154 offset:3072
	ds_read_b128 v[196:199], v154 offset:4096
	ds_read_b128 v[200:203], v154 offset:5120
	ds_read_b128 v[208:211], v154 offset:6144
	ds_read_b128 v[212:215], v154 offset:7168
	global_load_lds_dwordx4 v[206:207], off
	v_lshl_add_u64 v[206:207], v[142:143], 0, s[38:39]
	s_add_i32 m0, s49, 0xe000
	s_nop 0
	global_load_lds_dwordx4 v[206:207], off
	s_waitcnt lgkmcnt(8)
	s_barrier
	s_waitcnt lgkmcnt(0)
	s_waitcnt lgkmcnt(0)
	v_mfma_f32_16x16x32_bf16 v[126:129], v[164:167], v[180:183], v[126:129]
	v_mfma_f32_16x16x32_bf16 v[122:125], v[172:175], v[180:183], v[122:125]
	v_mfma_f32_16x16x32_bf16 v[114:117], v[164:167], v[188:191], v[114:117]
	v_mfma_f32_16x16x32_bf16 v[106:109], v[172:175], v[188:191], v[106:109]
	v_mfma_f32_16x16x32_bf16 v[98:101], v[164:167], v[196:199], v[98:101]
	v_mfma_f32_16x16x32_bf16 v[90:93], v[172:175], v[196:199], v[90:93]
	v_mfma_f32_16x16x32_bf16 v[82:85], v[164:167], v[208:211], v[82:85]
	v_mfma_f32_16x16x32_bf16 v[74:77], v[172:175], v[208:211], v[74:77]
	v_mfma_f32_16x16x32_bf16 v[126:129], v[168:171], v[184:187], v[126:129]
	v_mfma_f32_16x16x32_bf16 v[122:125], v[176:179], v[184:187], v[122:125]
	v_mfma_f32_16x16x32_bf16 v[114:117], v[168:171], v[192:195], v[114:117]
	v_mfma_f32_16x16x32_bf16 v[106:109], v[176:179], v[192:195], v[106:109]
	v_mfma_f32_16x16x32_bf16 v[98:101], v[168:171], v[200:203], v[98:101]
	v_mfma_f32_16x16x32_bf16 v[90:93], v[176:179], v[200:203], v[90:93]
	v_mfma_f32_16x16x32_bf16 v[82:85], v[168:171], v[212:215], v[82:85]
	v_mfma_f32_16x16x32_bf16 v[74:77], v[176:179], v[212:215], v[74:77]
	s_barrier
	s_add_i32 s67, s59, s48
	v_lshl_add_u64 v[206:207], s[40:41], 0, v[132:133]
	s_mov_b32 m0, s67
	ds_read_b128 v[216:219], v155
	ds_read_b128 v[220:223], v155 offset:1024
	ds_read_b128 v[224:227], v155 offset:2048
	ds_read_b128 v[228:231], v155 offset:3072
	global_load_lds_dwordx4 v[206:207], off
	v_lshl_add_u64 v[232:233], s[40:41], 0, v[130:131]
	s_add_i32 m0, s67, 0x2000
	s_nop 0
	global_load_lds_dwordx4 v[232:233], off
	s_barrier
	s_waitcnt lgkmcnt(0)
	s_waitcnt lgkmcnt(0)
	v_mfma_f32_16x16x32_bf16 v[118:121], v[216:219], v[180:183], v[118:121]
	v_mfma_f32_16x16x32_bf16 v[110:113], v[224:227], v[180:183], v[110:113]
	v_mfma_f32_16x16x32_bf16 v[102:105], v[216:219], v[188:191], v[102:105]
	v_mfma_f32_16x16x32_bf16 v[94:97], v[224:227], v[188:191], v[94:97]
	v_mfma_f32_16x16x32_bf16 v[86:89], v[216:219], v[196:199], v[86:89]
	v_mfma_f32_16x16x32_bf16 v[78:81], v[224:227], v[196:199], v[78:81]
	v_mfma_f32_16x16x32_bf16 v[70:73], v[216:219], v[208:211], v[70:73]
	v_mfma_f32_16x16x32_bf16 v[66:69], v[224:227], v[208:211], v[66:69]
	v_mfma_f32_16x16x32_bf16 v[118:121], v[220:223], v[184:187], v[118:121]
	v_mfma_f32_16x16x32_bf16 v[110:113], v[228:231], v[184:187], v[110:113]
	v_mfma_f32_16x16x32_bf16 v[102:105], v[220:223], v[192:195], v[102:105]
	v_mfma_f32_16x16x32_bf16 v[94:97], v[228:231], v[192:195], v[94:97]
	v_mfma_f32_16x16x32_bf16 v[86:89], v[220:223], v[200:203], v[86:89]
	v_mfma_f32_16x16x32_bf16 v[78:81], v[228:231], v[200:203], v[78:81]
	v_mfma_f32_16x16x32_bf16 v[70:73], v[220:223], v[212:215], v[70:73]
	v_mfma_f32_16x16x32_bf16 v[66:69], v[228:231], v[212:215], v[66:69]
	s_mov_b32 m0, s49
	s_barrier
	ds_read_b128 v[180:183], v154 offset:16384
	ds_read_b128 v[184:187], v154 offset:17408
	ds_read_b128 v[188:191], v154 offset:18432
	ds_read_b128 v[192:195], v154 offset:19456
	ds_read_b128 v[196:199], v154 offset:20480
	ds_read_b128 v[200:203], v154 offset:21504
	ds_read_b128 v[208:211], v154 offset:22528
	ds_read_b128 v[212:215], v154 offset:23552
	global_load_lds_dwordx4 v134, s[44:45]
	s_mov_b32 m0, s50
	v_mov_b32_e32 v205, v135
	global_load_lds_dwordx4 v204, s[44:45]
	s_barrier
	s_waitcnt lgkmcnt(0)
	v_lshl_add_u64 v[234:235], s[44:45], 0, v[134:135]
	v_lshl_add_u64 v[204:205], s[44:45], 0, v[204:205]
	s_waitcnt lgkmcnt(0)
	v_mfma_f32_16x16x32_bf16 v[62:65], v[164:167], v[180:183], v[62:65]
	v_mfma_f32_16x16x32_bf16 v[58:61], v[172:175], v[180:183], v[58:61]
	v_mfma_f32_16x16x32_bf16 v[46:49], v[164:167], v[188:191], v[46:49]
	v_mfma_f32_16x16x32_bf16 v[42:45], v[172:175], v[188:191], v[42:45]
	v_mfma_f32_16x16x32_bf16 v[30:33], v[164:167], v[196:199], v[30:33]
	v_mfma_f32_16x16x32_bf16 v[26:29], v[172:175], v[196:199], v[26:29]
	v_mfma_f32_16x16x32_bf16 v[14:17], v[164:167], v[208:211], v[14:17]
	v_mfma_f32_16x16x32_bf16 v[10:13], v[172:175], v[208:211], v[10:13]
	v_mfma_f32_16x16x32_bf16 v[62:65], v[168:171], v[184:187], v[62:65]
	v_mfma_f32_16x16x32_bf16 v[58:61], v[176:179], v[184:187], v[58:61]
	v_mfma_f32_16x16x32_bf16 v[46:49], v[168:171], v[192:195], v[46:49]
	v_mfma_f32_16x16x32_bf16 v[42:45], v[176:179], v[192:195], v[42:45]
	v_mfma_f32_16x16x32_bf16 v[30:33], v[168:171], v[200:203], v[30:33]
	v_mfma_f32_16x16x32_bf16 v[26:29], v[176:179], v[200:203], v[26:29]
	v_mfma_f32_16x16x32_bf16 v[14:17], v[168:171], v[212:215], v[14:17]
	v_mfma_f32_16x16x32_bf16 v[10:13], v[176:179], v[212:215], v[10:13]
	s_barrier
	s_add_i32 s67, s60, s48
	v_lshl_add_u64 v[164:165], v[206:207], 0, s[4:5]
	s_mov_b32 m0, s67
	s_nop 0
	global_load_lds_dwordx4 v[164:165], off
	v_lshl_add_u64 v[164:165], v[232:233], 0, s[4:5]
	s_add_i32 m0, s67, 0x2000
	s_nop 0
	global_load_lds_dwordx4 v[164:165], off
	s_cmp_eq_u32 s82, 0
	s_cbranch_scc1 .Lpb9_p4n
	s_waitcnt vmcnt(14)
	v_cvt_pk_bf16_f32 v244, v244, v245
	v_cvt_pk_bf16_f32 v245, v246, v247
	v_cvt_pk_bf16_f32 v246, v248, v249
	v_cvt_pk_bf16_f32 v247, v250, v251
	global_store_dwordx4 v253, v[244:247], s[78:79] nt
	s_mov_b32 s82, 0
	s_waitcnt vmcnt(7)
	s_branch .Lpb9_p4j

; #define PG8_STAGE(bufoff, gbase, v0, v1) do { \
;         __builtin_amdgcn_global_load_lds((const unsigned*)((const char*)(gbase) + (v0)), (LAS unsigned*)(lds + (bufoff) + ldsw), 16, 0, 0); \
;         __builtin_amdgcn_global_load_lds((const unsigned*)((const char*)(gbase) + (v1)), (LAS unsigned*)(lds + (bufoff) + ldsw + 8192), 16, 0, 0); } while (0)
; #define PG8_LDA(dst, b, h) do { _Pragma("unroll") for (int m = 0; m < 4; ++m) _Pragma("unroll") for (int k = 0; k < 2; ++k) dst[m][k] = *(const LAS bf16x8*)(lds + PG8_SA(b, h) + aoff + m * 2048 + k * 1024); } while (0)
; #define PG8_WAIT_V(n) asm volatile("s_waitcnt vmcnt(" #n ")" ::: "memory")
; #define PG8_WAIT_L(n) asm volatile("s_waitcnt lgkmcnt(" #n ")" ::: "memory")
; #define PG8_BAR __builtin_amdgcn_s_barrier()
; template <class Epi, class Sched>
; __device__ __forceinline__ void gemm_phase(LAS unsigned char* lds, const int K, const Sched& S, const Epi& E) {
;     ...
;             PG8_WAIT_V(6); PG8_BAR; PG8_MMA(1, 1, At, B1); PG8_BAR;
;             PG8_LDB(B0, 1, 0); PG8_SCHED; PG8_LDA(At, 1, 0); PG8_STAGE(PG8_SA(0, 1), a2, x10, x11);
;             PG8_WAIT_L(8); PG8_BAR; PG8_WAIT_L(0); PG8_MMA(0, 0, At, B0); PG8_BAR; PG8_SCHED;
;             PG8_LDB(B1, 1, 1); PG8_STAGE(PG8_SB(1, 0), b3, voffB0, voffB1);
;             PG8_BAR; PG8_WAIT_L(0); PG8_MMA(0, 1, At, B1); PG8_BAR;
;             PG8_LDA(At, 1, 1); PG8_STAGE(PG8_SA(1, 0), a3, x00, x01);
; __device__ __forceinline__ bool bg_decode(int st, int wg, int NW, int lane, KP kp, const float*& src, int& ldS, bf16_t*& dst, int& o2) {
;     ...
;     const int l = g / 98304, r = g - l * 98304;
;     unsigned char* ws = kp->ws;
;     if (r < 65536) {
;         const int e = r >> 10, kc = (r >> 2) & 255, kind = (r >> 1) & 1, cc = r & 1, n = cc * 256 + lane;
;         ldS = FF; o2 = 256 * 8;
;         src = kp->in[27 + kind] + ((size_t)(l * NE + e) * D + kc * 8) * FF + n;
;         const int drow = (n >> 7) * 256 + kind * 128 + (n & 127);
;         dst = (bf16_t*)(ws + WS_WGU) + l * WGU_L + (size_t)e * 1024 * D + ((size_t)kc * 1024 + drow) * 8;
;     } else {
;         const int r2 = r - 65536, e = r2 >> 9, kc = (r2 >> 3) & 63, cc = r2 & 7, n = cc * 256 + lane;
;         ldS = D; o2 = 128 * 8;
;         src = kp->in[29] + ((size_t)(l * NE + e) * FF + kc * 8) * D + n;
;         dst = (bf16_t*)(ws + WS_WD) + l * WD_L + (size_t)e * D * FF + ((size_t)kc * D + n) * 8;
.Lpb9_p4j:
	s_barrier
	v_mfma_f32_16x16x32_bf16 v[54:57], v[216:219], v[180:183], v[54:57]
	v_mfma_f32_16x16x32_bf16 v[50:53], v[224:227], v[180:183], v[50:53]
	v_mfma_f32_16x16x32_bf16 v[38:41], v[216:219], v[188:191], v[38:41]
	v_mfma_f32_16x16x32_bf16 v[34:37], v[224:227], v[188:191], v[34:37]
	v_mfma_f32_16x16x32_bf16 v[22:25], v[216:219], v[196:199], v[22:25]
	v_mfma_f32_16x16x32_bf16 v[18:21], v[224:227], v[196:199], v[18:21]
	v_mfma_f32_16x16x32_bf16 v[6:9], v[216:219], v[208:211], v[6:9]
	v_mfma_f32_16x16x32_bf16 v[2:5], v[224:227], v[208:211], v[2:5]
	v_mfma_f32_16x16x32_bf16 v[54:57], v[220:223], v[184:187], v[54:57]
	v_mfma_f32_16x16x32_bf16 v[50:53], v[228:231], v[184:187], v[50:53]
	v_mfma_f32_16x16x32_bf16 v[38:41], v[220:223], v[192:195], v[38:41]
	v_mfma_f32_16x16x32_bf16 v[34:37], v[228:231], v[192:195], v[34:37]
	v_mfma_f32_16x16x32_bf16 v[22:25], v[220:223], v[200:203], v[22:25]
	v_mfma_f32_16x16x32_bf16 v[18:21], v[228:231], v[200:203], v[18:21]
	v_mfma_f32_16x16x32_bf16 v[6:9], v[220:223], v[212:215], v[6:9]
	v_mfma_f32_16x16x32_bf16 v[2:5], v[228:231], v[212:215], v[2:5]
	s_add_i32 s67, 0, 0x18000
	v_add_u32_e32 v134, s67, v151
	s_barrier
	ds_read_b128 v[164:167], v134
	ds_read_b128 v[168:171], v134 offset:1024
	ds_read_b128 v[172:175], v134 offset:2048
	ds_read_b128 v[176:179], v134 offset:3072
	s_mov_b32 m0, s51
	ds_read_b128 v[180:183], v154 offset:32768
	ds_read_b128 v[184:187], v154 offset:33792
	ds_read_b128 v[188:191], v154 offset:34816
	ds_read_b128 v[192:195], v154 offset:35840
	ds_read_b128 v[196:199], v154 offset:36864
	ds_read_b128 v[200:203], v154 offset:37888
	ds_read_b128 v[208:211], v154 offset:38912
	ds_read_b128 v[212:215], v154 offset:39936
	v_cndmask_b32_e32 v134, v140, v160, vcc
	global_load_lds_dwordx4 v139, s[44:45]
	s_mov_b32 m0, s52
	s_nop 0
	global_load_lds_dwordx4 v134, s[44:45]
	s_cmp_ge_u32 s70, 0x24000
	s_cbranch_scc1 .Lpb9_p5n
	s_cmp_eq_u32 s80, 0
	s_cbranch_scc0 .Lpb9_adv2
	s_cmp_ge_u32 s70, 0x18000
	s_cselect_b32 s84, 0x18000, 0
	s_cselect_b32 s83, 0x10000000, 0
	s_mov_b32 s81, 0x4030000
	s_cselect_b32 s81, 0x14430000, s81
	s_sub_u32 s84, s70, s84
	s_lshr_b32 s85, s84, 2
	s_lshl_b32 s85, s85, 14
	s_and_b32 s86, s84, 1
	s_lshl_b32 s87, s86, 10
	s_add_u32 s87, s87, s85
	s_add_u32 s87, s87, s83
	s_bitcmp1_b32 s84, 1
	s_cselect_b64 s[72:73], s[76:77], s[74:75]
	s_add_u32 s72, s72, s87
	s_addc_u32 s73, s73, 0
	s_add_u32 s88, s72, 0x2000
	s_addc_u32 s89, s73, 0
	s_lshl_b32 s86, s86, 13
	s_add_u32 s85, s85, s86
	s_and_b32 s86, s84, 2
	s_lshl_b32 s86, s86, 10
	s_add_u32 s85, s85, s86
	s_add_u32 s85, s85, s81
	v_add_u32_e32 v253, s85, v252
	s_movk_i32 s81, 0x400
	s_branch .Lpb9_ld2

; #define PG8_STAGE(bufoff, gbase, v0, v1) do { \
;         __builtin_amdgcn_global_load_lds((const unsigned*)((const char*)(gbase) + (v0)), (LAS unsigned*)(lds + (bufoff) + ldsw), 16, 0, 0); \
;         __builtin_amdgcn_global_load_lds((const unsigned*)((const char*)(gbase) + (v1)), (LAS unsigned*)(lds + (bufoff) + ldsw + 8192), 16, 0, 0); } while (0)
; #define PG8_LDA(dst, b, h) do { _Pragma("unroll") for (int m = 0; m < 4; ++m) _Pragma("unroll") for (int k = 0; k < 2; ++k) dst[m][k] = *(const LAS bf16x8*)(lds + PG8_SA(b, h) + aoff + m * 2048 + k * 1024); } while (0)
; #define PG8_LDB(dst, b, h) do { _Pragma("unroll") for (int n = 0; n < 2; ++n) _Pragma("unroll") for (int k = 0; k < 2; ++k) dst[n][k] = *(const LAS bf16x8*)(lds + PG8_SB(b, h) + boff + n * 2048 + k * 1024); } while (0)
; #define PG8_MMA(ai, bj, At, Bt) do { __builtin_amdgcn_s_setprio(1); _Pragma("unroll") for (int m = 0; m < 4; ++m) _Pragma("unroll") for (int n = 0; n < 2; ++n) _Pragma("unroll") for (int k = 0; k < 2; ++k) \
;         acc[ai][bj][m][n] = __builtin_amdgcn_mfma_f32_16x16x32_bf16(Bt[n][k], At[m][k], acc[ai][bj][m][n], 0, 0, 0); __builtin_amdgcn_s_setprio(0); } while (0)
; #define PG8_WAIT_L(n) asm volatile("s_waitcnt lgkmcnt(" #n ")" ::: "memory")
; #define PG8_BAR __builtin_amdgcn_s_barrier()
; #define PG8_SCHED __builtin_amdgcn_sched_barrier(0)
; template <class Epi, class Sched>
; __device__ __forceinline__ void gemm_phase(LAS unsigned char* lds, const int K, const Sched& S, const Epi& E) {
;     ...
;             PG8_WAIT_L(8); PG8_BAR; PG8_WAIT_L(0); PG8_MMA(0, 0, At, B0); PG8_BAR; PG8_SCHED;
;             PG8_LDB(B1, 1, 1); PG8_STAGE(PG8_SB(1, 0), b3, voffB0, voffB1);
;             PG8_BAR; PG8_WAIT_L(0); PG8_MMA(0, 1, At, B1); PG8_BAR;
;             PG8_LDA(At, 1, 1); PG8_STAGE(PG8_SA(1, 0), a3, x00, x01);
;             PG8_BAR; PG8_WAIT_L(0); PG8_MMA(1, 0, At, B0); PG8_BAR; PG8_SCHED;
;             PG8_STAGE(PG8_SB(1, 1), b3 + hstep, voffB0, voffB1);
.Lpb9_p5n:
	s_waitcnt lgkmcnt(8)
	s_barrier
	s_waitcnt lgkmcnt(0)
	s_waitcnt lgkmcnt(0)
	v_mfma_f32_16x16x32_bf16 v[126:129], v[164:167], v[180:183], v[126:129]
	v_mfma_f32_16x16x32_bf16 v[122:125], v[172:175], v[180:183], v[122:125]
	v_mfma_f32_16x16x32_bf16 v[114:117], v[164:167], v[188:191], v[114:117]
	v_mfma_f32_16x16x32_bf16 v[106:109], v[172:175], v[188:191], v[106:109]
	v_mfma_f32_16x16x32_bf16 v[98:101], v[164:167], v[196:199], v[98:101]
	v_mfma_f32_16x16x32_bf16 v[90:93], v[172:175], v[196:199], v[90:93]
	v_mfma_f32_16x16x32_bf16 v[82:85], v[164:167], v[208:211], v[82:85]
	v_mfma_f32_16x16x32_bf16 v[74:77], v[172:175], v[208:211], v[74:77]
	v_mfma_f32_16x16x32_bf16 v[126:129], v[168:171], v[184:187], v[126:129]
	v_mfma_f32_16x16x32_bf16 v[122:125], v[176:179], v[184:187], v[122:125]
	v_mfma_f32_16x16x32_bf16 v[114:117], v[168:171], v[192:195], v[114:117]
	v_mfma_f32_16x16x32_bf16 v[106:109], v[176:179], v[192:195], v[106:109]
	v_mfma_f32_16x16x32_bf16 v[98:101], v[168:171], v[200:203], v[98:101]
	v_mfma_f32_16x16x32_bf16 v[90:93], v[176:179], v[200:203], v[90:93]
	v_mfma_f32_16x16x32_bf16 v[82:85], v[168:171], v[212:215], v[82:85]
	v_mfma_f32_16x16x32_bf16 v[74:77], v[176:179], v[212:215], v[74:77]
	s_barrier
	s_add_i32 s44, 0, 0x1c000
	s_add_i32 s45, s67, s48
	v_add_u32_e32 v134, s44, v151
	v_lshl_add_u64 v[206:207], s[42:43], 0, v[132:133]
	s_mov_b32 m0, s45
	ds_read_b128 v[216:219], v134
	ds_read_b128 v[220:223], v134 offset:1024
	ds_read_b128 v[224:227], v134 offset:2048
	ds_read_b128 v[228:231], v134 offset:3072
	global_load_lds_dwordx4 v[206:207], off
	v_lshl_add_u64 v[206:207], s[42:43], 0, v[130:131]
	s_add_i32 m0, s45, 0x2000
	s_nop 0
	global_load_lds_dwordx4 v[206:207], off
	s_barrier
	s_waitcnt lgkmcnt(0)
	s_waitcnt lgkmcnt(0)
	v_mfma_f32_16x16x32_bf16 v[118:121], v[216:219], v[180:183], v[118:121]
	v_mfma_f32_16x16x32_bf16 v[110:113], v[224:227], v[180:183], v[110:113]
	v_mfma_f32_16x16x32_bf16 v[102:105], v[216:219], v[188:191], v[102:105]
	v_mfma_f32_16x16x32_bf16 v[94:97], v[224:227], v[188:191], v[94:97]
	v_mfma_f32_16x16x32_bf16 v[86:89], v[216:219], v[196:199], v[86:89]
	v_mfma_f32_16x16x32_bf16 v[78:81], v[224:227], v[196:199], v[78:81]
	v_mfma_f32_16x16x32_bf16 v[70:73], v[216:219], v[208:211], v[70:73]
	v_mfma_f32_16x16x32_bf16 v[66:69], v[224:227], v[208:211], v[66:69]
	v_mfma_f32_16x16x32_bf16 v[118:121], v[220:223], v[184:187], v[118:121]
	v_mfma_f32_16x16x32_bf16 v[110:113], v[228:231], v[184:187], v[110:113]
	v_mfma_f32_16x16x32_bf16 v[102:105], v[220:223], v[192:195], v[102:105]
	v_mfma_f32_16x16x32_bf16 v[94:97], v[228:231], v[192:195], v[94:97]
	v_mfma_f32_16x16x32_bf16 v[86:89], v[220:223], v[200:203], v[86:89]
	v_mfma_f32_16x16x32_bf16 v[78:81], v[228:231], v[200:203], v[78:81]
	v_mfma_f32_16x16x32_bf16 v[70:73], v[220:223], v[212:215], v[70:73]
	v_mfma_f32_16x16x32_bf16 v[66:69], v[228:231], v[212:215], v[66:69]
	s_mov_b32 m0, s55
	v_lshl_add_u64 v[206:207], v[234:235], 0, s[12:13]
	s_barrier
	ds_read_b128 v[180:183], v154 offset:49152
	ds_read_b128 v[184:187], v154 offset:50176
	ds_read_b128 v[188:191], v154 offset:51200
	ds_read_b128 v[192:195], v154 offset:52224
	ds_read_b128 v[196:199], v154 offset:53248
	ds_read_b128 v[200:203], v154 offset:54272
	ds_read_b128 v[208:211], v154 offset:55296
	ds_read_b128 v[212:215], v154 offset:56320
	global_load_lds_dwordx4 v[206:207], off
	v_lshl_add_u64 v[204:205], v[204:205], 0, s[12:13]
	s_mov_b32 m0, s56
	s_nop 0
	global_load_lds_dwordx4 v[204:205], off
	s_barrier
	s_waitcnt lgkmcnt(0)
	s_waitcnt lgkmcnt(0)
	v_mfma_f32_16x16x32_bf16 v[62:65], v[164:167], v[180:183], v[62:65]
	v_mfma_f32_16x16x32_bf16 v[58:61], v[172:175], v[180:183], v[58:61]
	v_mfma_f32_16x16x32_bf16 v[46:49], v[164:167], v[188:191], v[46:49]
	v_mfma_f32_16x16x32_bf16 v[42:45], v[172:175], v[188:191], v[42:45]
	v_mfma_f32_16x16x32_bf16 v[30:33], v[164:167], v[196:199], v[30:33]
	v_mfma_f32_16x16x32_bf16 v[26:29], v[172:175], v[196:199], v[26:29]
	v_mfma_f32_16x16x32_bf16 v[14:17], v[164:167], v[208:211], v[14:17]
	v_mfma_f32_16x16x32_bf16 v[10:13], v[172:175], v[208:211], v[10:13]
	v_mfma_f32_16x16x32_bf16 v[62:65], v[168:171], v[184:187], v[62:65]
	v_mfma_f32_16x16x32_bf16 v[58:61], v[176:179], v[184:187], v[58:61]
	v_mfma_f32_16x16x32_bf16 v[46:49], v[168:171], v[192:195], v[46:49]
	v_mfma_f32_16x16x32_bf16 v[42:45], v[176:179], v[192:195], v[42:45]
	v_mfma_f32_16x16x32_bf16 v[30:33], v[168:171], v[200:203], v[30:33]
	v_mfma_f32_16x16x32_bf16 v[26:29], v[176:179], v[200:203], v[26:29]
	v_mfma_f32_16x16x32_bf16 v[14:17], v[168:171], v[212:215], v[14:17]
	v_mfma_f32_16x16x32_bf16 v[10:13], v[176:179], v[212:215], v[10:13]
	s_barrier
	s_add_u32 s40, s40, 0x40800
	s_addc_u32 s41, s41, 0
	s_add_i32 s42, s44, s48
	v_lshl_add_u64 v[164:165], s[40:41], 0, v[132:133]
	s_mov_b32 m0, s42
	s_nop 0
	global_load_lds_dwordx4 v[164:165], off
	v_lshl_add_u64 v[164:165], s[40:41], 0, v[130:131]
	s_add_i32 m0, s42, 0x2000
	s_nop 0
	global_load_lds_dwordx4 v[164:165], off
	s_cmp_eq_u32 s82, 0
	s_cbranch_scc1 .Lpb9_p8n
	s_waitcnt vmcnt(14)
	s_branch .Lpb9_p8j

; #define PG8_MMA(ai, bj, At, Bt) do { __builtin_amdgcn_s_setprio(1); _Pragma("unroll") for (int m = 0; m < 4; ++m) _Pragma("unroll") for (int n = 0; n < 2; ++n) _Pragma("unroll") for (int k = 0; k < 2; ++k) \
;         acc[ai][bj][m][n] = __builtin_amdgcn_mfma_f32_16x16x32_bf16(Bt[n][k], At[m][k], acc[ai][bj][m][n], 0, 0, 0); __builtin_amdgcn_s_setprio(0); } while (0)
; #define PG8_WAIT_V(n) asm volatile("s_waitcnt vmcnt(" #n ")" ::: "memory")
; #define PG8_BAR __builtin_amdgcn_s_barrier()
; __device__ __forceinline__ unsigned pk4_fp8(float a, float b, float c, float d) { int w = 0; w = __builtin_amdgcn_cvt_pk_fp8_f32(a, b, w, false); w = __builtin_amdgcn_cvt_pk_fp8_f32(c, d, w, true); return (unsigned)w; }
; template <class Epi, class Sched>
; __device__ __forceinline__ void gemm_phase(LAS unsigned char* lds, const int K, const Sched& S, const Epi& E) {
;     ...
;             PG8_WAIT_V(6); PG8_BAR; PG8_MMA(1, 1, At, B1); PG8_BAR;
;     __device__ __forceinline__ void operator()(const f32x4 (&acc)[2][2][4][2], const Unit& u, int wr, int wc, int fr, int fq) const {
;         const int row0 = u.rbase + wr * 64 + fr, col0 = u.pn * BM + wc * 32 + 8 * fq;
; #pragma unroll
;         for (int ai = 0; ai < 2; ++ai)
; #pragma unroll
;             for (int m = 0; m < 4; ++m) { unsigned char* rowp = O + (size_t)(row0 + ai * HALF + m * 16) * ldc + col0;
; #pragma unroll
;                 for (int bj = 0; bj < 2; ++bj) { const f32x4 v0 = acc[ai][bj][m][0] * scale, v1 = acc[ai][bj][m][1] * scale;
;                     u32x2 w; w.x = pk4_fp8(v0[0], v0[1], v0[2], v0[3]); w.y = pk4_fp8(v1[0], v1[1], v1[2], v1[3]);
;                     *(u32x2*)(rowp + bj * HALF) = w; } }
.Lpb9_p8j:
	s_barrier
	v_mfma_f32_16x16x32_bf16 v[54:57], v[216:219], v[180:183], v[54:57]
	v_mfma_f32_16x16x32_bf16 v[50:53], v[224:227], v[180:183], v[50:53]
	v_mfma_f32_16x16x32_bf16 v[38:41], v[216:219], v[188:191], v[38:41]
	v_mfma_f32_16x16x32_bf16 v[34:37], v[224:227], v[188:191], v[34:37]
	v_mfma_f32_16x16x32_bf16 v[22:25], v[216:219], v[196:199], v[22:25]
	v_mfma_f32_16x16x32_bf16 v[18:21], v[224:227], v[196:199], v[18:21]
	v_mfma_f32_16x16x32_bf16 v[6:9], v[216:219], v[208:211], v[6:9]
	v_mfma_f32_16x16x32_bf16 v[2:5], v[224:227], v[208:211], v[2:5]
	v_mfma_f32_16x16x32_bf16 v[54:57], v[220:223], v[184:187], v[54:57]
	v_mfma_f32_16x16x32_bf16 v[50:53], v[228:231], v[184:187], v[50:53]
	v_mfma_f32_16x16x32_bf16 v[38:41], v[220:223], v[192:195], v[38:41]
	v_mfma_f32_16x16x32_bf16 v[34:37], v[228:231], v[192:195], v[34:37]
	v_mfma_f32_16x16x32_bf16 v[22:25], v[220:223], v[200:203], v[22:25]
	v_mfma_f32_16x16x32_bf16 v[18:21], v[228:231], v[200:203], v[18:21]
	v_mfma_f32_16x16x32_bf16 v[6:9], v[220:223], v[212:215], v[6:9]
	v_mfma_f32_16x16x32_bf16 v[2:5], v[228:231], v[212:215], v[2:5]
	s_add_i32 s66, s66, 2
	s_add_u32 s29, s29, 0x80000
	s_addc_u32 s31, s31, 0
	s_add_u32 s38, s38, 0x100
	s_addc_u32 s39, s39, 0
	s_cmp_gt_u32 s66, 5
	s_barrier
	s_cbranch_scc0 .LBB0_1161
	v_pk_mul_f32 v[126:127], v[126:127], s[14:15] op_sel_hi:[1,0]
	v_mov_b32_e32 v142, v135
	v_cvt_pk_fp8_f32 v142, v126, v127
	v_pk_mul_f32 v[122:123], v[122:123], s[14:15] op_sel_hi:[1,0]
	v_mov_b32_e32 v143, v135
	v_cvt_pk_fp8_f32 v143, v122, v123
	v_pk_mul_f32 v[122:123], v[128:129], s[14:15] op_sel_hi:[1,0]
	v_pk_mul_f32 v[118:119], v[118:119], s[14:15] op_sel_hi:[1,0]
	v_cvt_pk_fp8_f32 v142, v122, v123 op_sel:[0,0,1]
	v_mov_b32_e32 v122, v135
	v_cvt_pk_fp8_f32 v122, v118, v119
	v_pk_mul_f32 v[114:115], v[114:115], s[14:15] op_sel_hi:[1,0]
	v_mov_b32_e32 v118, v135
	v_cvt_pk_fp8_f32 v118, v114, v115
	v_pk_mul_f32 v[106:107], v[106:107], s[14:15] op_sel_hi:[1,0]
	v_mov_b32_e32 v119, v135
	v_cvt_pk_fp8_f32 v119, v106, v107
	v_pk_mul_f32 v[106:107], v[116:117], s[14:15] op_sel_hi:[1,0]
	v_pk_mul_f32 v[94:95], v[94:95], s[14:15] op_sel_hi:[1,0]
	v_cvt_pk_fp8_f32 v118, v106, v107 op_sel:[0,0,1]
	v_mov_b32_e32 v107, v135
	v_cvt_pk_fp8_f32 v107, v94, v95
	v_pk_mul_f32 v[96:97], v[96:97], s[14:15] op_sel_hi:[1,0]
	v_pk_mul_f32 v[90:91], v[90:91], s[14:15] op_sel_hi:[1,0]
	v_pk_mul_f32 v[78:79], v[78:79], s[14:15] op_sel_hi:[1,0]
	v_cvt_pk_fp8_f32 v107, v96, v97 op_sel:[0,0,1]
	v_pk_mul_f32 v[96:97], v[98:99], s[14:15] op_sel_hi:[1,0]
	v_mov_b32_e32 v98, v135
	v_cvt_pk_fp8_f32 v98, v96, v97
	v_mov_b32_e32 v99, v135
	v_cvt_pk_fp8_f32 v99, v90, v91
	v_pk_mul_f32 v[90:91], v[100:101], s[14:15] op_sel_hi:[1,0]
	v_pk_mul_f32 v[80:81], v[80:81], s[14:15] op_sel_hi:[1,0]
	v_cvt_pk_fp8_f32 v98, v90, v91 op_sel:[0,0,1]
	v_mov_b32_e32 v91, v135
	v_cvt_pk_fp8_f32 v91, v78, v79
	v_pk_mul_f32 v[74:75], v[74:75], s[14:15] op_sel_hi:[1,0]
	v_pk_mul_f32 v[66:67], v[66:67], s[14:15] op_sel_hi:[1,0]
	v_pk_mul_f32 v[68:69], v[68:69], s[14:15] op_sel_hi:[1,0]
	v_cvt_pk_fp8_f32 v91, v80, v81 op_sel:[0,0,1]
	v_pk_mul_f32 v[80:81], v[82:83], s[14:15] op_sel_hi:[1,0]
	v_mov_b32_e32 v82, v135
	v_cvt_pk_fp8_f32 v82, v80, v81
	v_mov_b32_e32 v83, v135
	v_cvt_pk_fp8_f32 v83, v74, v75
	v_pk_mul_f32 v[74:75], v[84:85], s[14:15] op_sel_hi:[1,0]
	v_pk_mul_f32 v[62:63], v[62:63], s[14:15] op_sel_hi:[1,0]
	v_cvt_pk_fp8_f32 v82, v74, v75 op_sel:[0,0,1]
	v_mov_b32_e32 v75, v135
	v_cvt_pk_fp8_f32 v75, v66, v67
	v_pk_mul_f32 v[58:59], v[58:59], s[14:15] op_sel_hi:[1,0]
	v_pk_mul_f32 v[50:51], v[50:51], s[14:15] op_sel_hi:[1,0]
	v_pk_mul_f32 v[52:53], v[52:53], s[14:15] op_sel_hi:[1,0]
	v_cvt_pk_fp8_f32 v75, v68, v69 op_sel:[0,0,1]
	v_mov_b32_e32 v68, v135
	v_cvt_pk_fp8_f32 v68, v62, v63
	v_mov_b32_e32 v69, v135
	v_cvt_pk_fp8_f32 v69, v58, v59
	v_pk_mul_f32 v[58:59], v[64:65], s[14:15] op_sel_hi:[1,0]
	v_pk_mul_f32 v[46:47], v[46:47], s[14:15] op_sel_hi:[1,0]
	v_cvt_pk_fp8_f32 v68, v58, v59 op_sel:[0,0,1]
	v_mov_b32_e32 v59, v135
	v_cvt_pk_fp8_f32 v59, v50, v51
	v_pk_mul_f32 v[42:43], v[42:43], s[14:15] op_sel_hi:[1,0]
	v_pk_mul_f32 v[34:35], v[34:35], s[14:15] op_sel_hi:[1,0]
	v_pk_mul_f32 v[36:37], v[36:37], s[14:15] op_sel_hi:[1,0]
	v_cvt_pk_fp8_f32 v59, v52, v53 op_sel:[0,0,1]
	v_mov_b32_e32 v52, v135
	v_cvt_pk_fp8_f32 v52, v46, v47
	v_mov_b32_e32 v53, v135
	v_cvt_pk_fp8_f32 v53, v42, v43
	v_pk_mul_f32 v[42:43], v[48:49], s[14:15] op_sel_hi:[1,0]
	v_pk_mul_f32 v[30:31], v[30:31], s[14:15] op_sel_hi:[1,0]
	v_cvt_pk_fp8_f32 v52, v42, v43 op_sel:[0,0,1]
	v_mov_b32_e32 v43, v135
	v_cvt_pk_fp8_f32 v43, v34, v35
	v_add_u32_e32 v138, v161, v137
	v_pk_mul_f32 v[102:103], v[102:103], s[14:15] op_sel_hi:[1,0]
	v_mov_b32_e32 v106, v135
	v_cvt_pk_fp8_f32 v43, v36, v37 op_sel:[0,0,1]
	v_mov_b32_e32 v36, v135
	v_cvt_pk_fp8_f32 v36, v30, v31
	v_pk_mul_f32 v[26:27], v[26:27], s[14:15] op_sel_hi:[1,0]
	v_mov_b32_e32 v37, v135
	v_ashrrev_i32_e32 v139, 31, v138
	v_pk_mul_f32 v[110:111], v[110:111], s[14:15] op_sel_hi:[1,0]
	v_mov_b32_e32 v123, v135
	v_cvt_pk_fp8_f32 v106, v102, v103
	v_cvt_pk_fp8_f32 v37, v26, v27
	v_pk_mul_f32 v[26:27], v[32:33], s[14:15] op_sel_hi:[1,0]
	v_lshl_or_b32 v140, s65, 8, v152
	v_lshlrev_b64 v[138:139], 11, v[138:139]
	v_cvt_pk_fp8_f32 v123, v110, v111
	v_pk_mul_f32 v[110:111], v[120:121], s[14:15] op_sel_hi:[1,0]
	v_pk_mul_f32 v[86:87], v[86:87], s[14:15] op_sel_hi:[1,0]
	v_mov_b32_e32 v90, v135
; #define PG8_WAIT_V(n) asm volatile("s_waitcnt vmcnt(" #n ")" ::: "memory")
; #define PG8_BAR __builtin_amdgcn_s_barrier()
; __device__ __forceinline__ unsigned pk4_fp8(float a, float b, float c, float d) { int w = 0; w = __builtin_amdgcn_cvt_pk_fp8_f32(a, b, w, false); w = __builtin_amdgcn_cvt_pk_fp8_f32(c, d, w, true); return (unsigned)w; }
; template <class Epi, class Sched>
; __device__ __forceinline__ void gemm_phase(LAS unsigned char* lds, const int K, const Sched& S, const Epi& E) {
;     ...
;         if (!has_next) break;
; #pragma unroll
;         for (int a = 0; a < 2; ++a)
; #pragma unroll
;             for (int b = 0; b < 2; ++b)
; #pragma unroll
;                 for (int m = 0; m < 4; ++m)
; #pragma unroll
;                     for (int n = 0; n < 2; ++n) acc[a][b][m][n] = (f32x4){0.f, 0.f, 0.f, 0.f};
;         cur = nxt; cB = nB; c00 = n00; c01 = n01; c10 = n10; c11 = n11; ++ui;
;     }
;     PG8_WAIT_V(0);
;     if (wr == 0) PG8_BAR;
;     PG8_BAR;
;     __device__ __forceinline__ void operator()(const f32x4 (&acc)[2][2][4][2], const Unit& u, int wr, int wc, int fr, int fq) const {
;     ...
; #pragma unroll
;         for (int ai = 0; ai < 2; ++ai)
; #pragma unroll
;             for (int m = 0; m < 4; ++m) { unsigned char* rowp = O + (size_t)(row0 + ai * HALF + m * 16) * ldc + col0;
; #pragma unroll
;                 for (int bj = 0; bj < 2; ++bj) { const f32x4 v0 = acc[ai][bj][m][0] * scale, v1 = acc[ai][bj][m][1] * scale;
;                     u32x2 w; w.x = pk4_fp8(v0[0], v0[1], v0[2], v0[3]); w.y = pk4_fp8(v1[0], v1[1], v1[2], v1[3]);
;                     *(u32x2*)(rowp + bj * HALF) = w; } }
	v_cvt_pk_fp8_f32 v36, v26, v27 op_sel:[0,0,1]
	v_pk_mul_f32 v[18:19], v[18:19], s[14:15] op_sel_hi:[1,0]
	v_mov_b32_e32 v27, v135
	v_ashrrev_i32_e32 v141, 31, v140
	v_cvt_pk_fp8_f32 v122, v110, v111 op_sel:[0,0,1]
	v_lshl_add_u64 v[110:111], s[6:7], 0, v[138:139]
	v_cvt_pk_fp8_f32 v90, v86, v87
	v_cvt_pk_fp8_f32 v27, v18, v19
	v_lshl_add_u64 v[110:111], v[110:111], 0, v[140:141]
	v_pk_mul_f32 v[94:95], v[104:105], s[14:15] op_sel_hi:[1,0]
	v_pk_mul_f32 v[70:71], v[70:71], s[14:15] op_sel_hi:[1,0]
	v_mov_b32_e32 v74, v135
	v_cvt_pk_fp8_f32 v106, v94, v95 op_sel:[0,0,1]
	v_add_co_u32_e32 v94, vcc, s58, v110
	v_cvt_pk_fp8_f32 v74, v70, v71
	s_nop 0
	v_addc_co_u32_e32 v95, vcc, 0, v111, vcc
	v_pk_mul_f32 v[78:79], v[88:89], s[14:15] op_sel_hi:[1,0]
	v_pk_mul_f32 v[54:55], v[54:55], s[14:15] op_sel_hi:[1,0]
	v_mov_b32_e32 v58, v135
	v_pk_mul_f32 v[20:21], v[20:21], s[14:15] op_sel_hi:[1,0]
	v_cvt_pk_fp8_f32 v90, v78, v79 op_sel:[0,0,1]
	v_add_co_u32_e32 v78, vcc, s54, v110
	v_cvt_pk_fp8_f32 v58, v54, v55
	v_cvt_pk_fp8_f32 v27, v20, v21 op_sel:[0,0,1]
	v_pk_mul_f32 v[14:15], v[14:15], s[14:15] op_sel_hi:[1,0]
	v_mov_b32_e32 v20, v135
	v_addc_co_u32_e32 v79, vcc, 0, v111, vcc
	v_pk_mul_f32 v[66:67], v[72:73], s[14:15] op_sel_hi:[1,0]
	v_pk_mul_f32 v[38:39], v[38:39], s[14:15] op_sel_hi:[1,0]
	v_mov_b32_e32 v42, v135
	v_cvt_pk_fp8_f32 v20, v14, v15
	v_cvt_pk_fp8_f32 v74, v66, v67 op_sel:[0,0,1]
	v_add_co_u32_e32 v66, vcc, s57, v110
	v_cvt_pk_fp8_f32 v42, v38, v39
	s_nop 0
	v_addc_co_u32_e32 v67, vcc, 0, v111, vcc
	v_pk_mul_f32 v[50:51], v[56:57], s[14:15] op_sel_hi:[1,0]
	v_pk_mul_f32 v[22:23], v[22:23], s[14:15] op_sel_hi:[1,0]
	v_mov_b32_e32 v26, v135
	v_pk_mul_f32 v[10:11], v[10:11], s[14:15] op_sel_hi:[1,0]
	v_mov_b32_e32 v21, v135
	v_cvt_pk_fp8_f32 v58, v50, v51 op_sel:[0,0,1]
	v_add_co_u32_e32 v50, vcc, s61, v110
	v_cvt_pk_fp8_f32 v26, v22, v23
	v_cvt_pk_fp8_f32 v21, v10, v11
	v_pk_mul_f32 v[10:11], v[16:17], s[14:15] op_sel_hi:[1,0]
	v_addc_co_u32_e32 v51, vcc, 0, v111, vcc
	v_pk_mul_f32 v[34:35], v[40:41], s[14:15] op_sel_hi:[1,0]
	v_cvt_pk_fp8_f32 v20, v10, v11 op_sel:[0,0,1]
	v_pk_mul_f32 v[6:7], v[6:7], s[14:15] op_sel_hi:[1,0]
	v_pk_mul_f32 v[2:3], v[2:3], s[14:15] op_sel_hi:[1,0]
	v_mov_b32_e32 v10, v135
	v_mov_b32_e32 v11, v135
	v_cvt_pk_fp8_f32 v42, v34, v35 op_sel:[0,0,1]
	v_add_co_u32_e32 v34, vcc, s62, v110
	v_cvt_pk_fp8_f32 v10, v6, v7
	v_cvt_pk_fp8_f32 v11, v2, v3
	v_addc_co_u32_e32 v35, vcc, 0, v111, vcc
	v_pk_mul_f32 v[18:19], v[24:25], s[14:15] op_sel_hi:[1,0]
	v_pk_mul_f32 v[124:125], v[124:125], s[14:15] op_sel_hi:[1,0]
	v_pk_mul_f32 v[108:109], v[108:109], s[14:15] op_sel_hi:[1,0]
	v_pk_mul_f32 v[92:93], v[92:93], s[14:15] op_sel_hi:[1,0]
	v_pk_mul_f32 v[76:77], v[76:77], s[14:15] op_sel_hi:[1,0]
	v_pk_mul_f32 v[60:61], v[60:61], s[14:15] op_sel_hi:[1,0]
	v_pk_mul_f32 v[44:45], v[44:45], s[14:15] op_sel_hi:[1,0]
	v_pk_mul_f32 v[28:29], v[28:29], s[14:15] op_sel_hi:[1,0]
	v_cvt_pk_fp8_f32 v26, v18, v19 op_sel:[0,0,1]
	v_add_co_u32_e32 v18, vcc, s63, v110
	v_pk_mul_f32 v[12:13], v[12:13], s[14:15] op_sel_hi:[1,0]
	v_cvt_pk_fp8_f32 v143, v124, v125 op_sel:[0,0,1]
	v_pk_mul_f32 v[112:113], v[112:113], s[14:15] op_sel_hi:[1,0]
	v_cvt_pk_fp8_f32 v119, v108, v109 op_sel:[0,0,1]
	v_cvt_pk_fp8_f32 v99, v92, v93 op_sel:[0,0,1]
	v_cvt_pk_fp8_f32 v83, v76, v77 op_sel:[0,0,1]
	v_cvt_pk_fp8_f32 v69, v60, v61 op_sel:[0,0,1]
	v_cvt_pk_fp8_f32 v53, v44, v45 op_sel:[0,0,1]
	v_cvt_pk_fp8_f32 v37, v28, v29 op_sel:[0,0,1]
	v_addc_co_u32_e32 v19, vcc, 0, v111, vcc
	v_cvt_pk_fp8_f32 v21, v12, v13 op_sel:[0,0,1]
	v_pk_mul_f32 v[2:3], v[8:9], s[14:15] op_sel_hi:[1,0]
	v_pk_mul_f32 v[4:5], v[4:5], s[14:15] op_sel_hi:[1,0]
	v_cvt_pk_fp8_f32 v123, v112, v113 op_sel:[0,0,1]
	v_cvt_pk_fp8_f32 v10, v2, v3 op_sel:[0,0,1]
	v_cvt_pk_fp8_f32 v11, v4, v5 op_sel:[0,0,1]
	v_add_co_u32_e32 v2, vcc, s64, v110
	v_mov_b32_e32 v161, v156
	s_nop 0
	v_addc_co_u32_e32 v3, vcc, 0, v111, vcc
	s_and_b64 vcc, exec, s[34:35]
	s_mov_b32 s65, s28
	v_mov_b32_e32 v162, v157
	v_mov_b32_e32 v136, v158
	v_mov_b32_e32 v138, v159
	v_mov_b32_e32 v140, v160
	s_mov_b64 s[38:39], s[36:37]
	global_store_dwordx2 v[110:111], v[142:143], off
	global_store_dwordx2 v[110:111], v[122:123], off offset:128
	v_lshl_add_u64 v[112:113], v[110:111], 0, s[16:17]
	global_store_dwordx2 v[94:95], v[118:119], off
	global_store_dwordx2 v[112:113], v[106:107], off offset:128
	v_lshl_add_u64 v[94:95], v[110:111], 0, s[18:19]
	global_store_dwordx2 v[78:79], v[98:99], off
	global_store_dwordx2 v[94:95], v[90:91], off offset:128
	v_lshl_add_u64 v[78:79], v[110:111], 0, s[20:21]
	global_store_dwordx2 v[66:67], v[82:83], off
	global_store_dwordx2 v[78:79], v[74:75], off offset:128
	v_lshl_add_u64 v[66:67], v[110:111], 0, s[10:11]
	global_store_dwordx2 v[50:51], v[68:69], off
	global_store_dwordx2 v[66:67], v[58:59], off offset:128
	v_lshl_add_u64 v[50:51], v[110:111], 0, s[22:23]
	global_store_dwordx2 v[34:35], v[52:53], off
	global_store_dwordx2 v[50:51], v[42:43], off offset:128
	v_lshl_add_u64 v[34:35], v[110:111], 0, s[24:25]
	global_store_dwordx2 v[18:19], v[36:37], off
	global_store_dwordx2 v[34:35], v[26:27], off offset:128
	v_lshl_add_u64 v[18:19], v[110:111], 0, s[26:27]
	global_store_dwordx2 v[2:3], v[20:21], off
	global_store_dwordx2 v[18:19], v[10:11], off offset:128
	s_cbranch_vccz .LBB0_1156
	s_waitcnt vmcnt(0)
	s_cmpk_gt_u32 s33, 0xff
	s_cbranch_scc1 .LBB0_1165
	s_barrier

; #define PG8_STAGE(bufoff, gbase, v0, v1) do { \
;         __builtin_amdgcn_global_load_lds((const unsigned*)((const char*)(gbase) + (v0)), (LAS unsigned*)(lds + (bufoff) + ldsw), 16, 0, 0); \
;         __builtin_amdgcn_global_load_lds((const unsigned*)((const char*)(gbase) + (v1)), (LAS unsigned*)(lds + (bufoff) + ldsw + 8192), 16, 0, 0); } while (0)
; #define PG8_LDA(dst, b, h) do { _Pragma("unroll") for (int m = 0; m < 4; ++m) _Pragma("unroll") for (int k = 0; k < 2; ++k) dst[m][k] = *(const LAS bf16x8*)(lds + PG8_SA(b, h) + aoff + m * 2048 + k * 1024); } while (0)
; #define PG8_LDB(dst, b, h) do { _Pragma("unroll") for (int n = 0; n < 2; ++n) _Pragma("unroll") for (int k = 0; k < 2; ++k) dst[n][k] = *(const LAS bf16x8*)(lds + PG8_SB(b, h) + boff + n * 2048 + k * 1024); } while (0)
; #define PG8_WAIT_V(n) asm volatile("s_waitcnt vmcnt(" #n ")" ::: "memory")
; #define PG8_WAIT_L(n) asm volatile("s_waitcnt lgkmcnt(" #n ")" ::: "memory")
; #define PG8_BAR __builtin_amdgcn_s_barrier()
; #define PG8_SCHED __builtin_amdgcn_sched_barrier(0)
; template <class Epi, class Sched>
; __device__ __forceinline__ void gemm_phase(LAS unsigned char* lds, const int K, const Sched& S, const Epi& E) {
;     ...
;         for (int t = 0; t < nt; t += 2) {
;             const bool last = (t == nt - 2);
;             const char* a1 = gA + (size_t)(t + 1) * kstep;
;             const char* a2 = last ? gA : gA + (size_t)(t + 2) * kstep; const char* b2 = last ? nB : cB + (size_t)(t + 2) * kstepB;
;             const char* a3 = a2 + kstep; const char* b3 = b2 + kstepB;
;             const unsigned x00 = last ? n00 : c00, x01 = last ? n01 : c01, x10 = last ? n10 : c10, x11 = last ? n11 : c11;
;             PG8_LDB(B0, 0, 0); PG8_SCHED; PG8_LDA(At, 0, 0); PG8_STAGE(PG8_SA(1, 1), a1, c10, c11);
;             PG8_WAIT_L(8); PG8_BAR; PG8_WAIT_L(0); PG8_MMA(0, 0, At, B0); PG8_BAR; PG8_SCHED;
;             PG8_LDB(B1, 0, 1); PG8_STAGE(PG8_SB(0, 0), b2, voffB0, voffB1);
;             PG8_BAR; PG8_WAIT_L(0); PG8_MMA(0, 1, At, B1); PG8_BAR;
;             PG8_LDA(At, 0, 1); PG8_STAGE(PG8_SA(0, 0), a2, x00, x01);
;             PG8_BAR; PG8_WAIT_L(0); PG8_MMA(1, 0, At, B0); PG8_BAR; PG8_SCHED;
;             PG8_STAGE(PG8_SB(0, 1), b2 + hstep, voffB0, voffB1);
;             PG8_WAIT_V(6); PG8_BAR; PG8_MMA(1, 1, At, B1); PG8_BAR;
.LBB0_1290:
	s_add_u32 s20, s4, s18
	s_addc_u32 s21, s5, s19
	s_add_u32 s22, s20, 0x34c30100
	ds_read_b128 v[166:169], v158
	ds_read_b128 v[170:173], v158 offset:1024
	ds_read_b128 v[174:177], v158 offset:2048
	ds_read_b128 v[178:181], v158 offset:3072
	s_addc_u32 s23, s21, 0
	s_add_u32 s47, s17, s18
	s_addc_u32 s48, s45, s19
	s_cmpk_eq_i32 s18, 0xf00
	s_cselect_b64 vcc, -1, 0
	s_and_b64 s[20:21], vcc, exec
	v_cndmask_b32_e32 v134, v141, v161, vcc
	s_cselect_b32 s23, s7, s23
	s_cselect_b32 s22, s6, s22
	v_cndmask_b32_e32 v143, v142, v163, vcc
	s_cselect_b32 s21, s3, s48
	s_cselect_b32 s20, s2, s47
	v_cndmask_b32_e32 v206, v140, v162, vcc
	s_mov_b32 m0, s40
	v_lshl_add_u64 v[216:217], v[148:149], 0, s[18:19]
	ds_read_b128 v[182:185], v159
	ds_read_b128 v[186:189], v159 offset:1024
	ds_read_b128 v[190:193], v159 offset:2048
	ds_read_b128 v[194:197], v159 offset:3072
	ds_read_b128 v[198:201], v159 offset:4096
	ds_read_b128 v[202:205], v159 offset:5120
	ds_read_b128 v[208:211], v159 offset:6144
	ds_read_b128 v[212:215], v159 offset:7168
	global_load_lds_dwordx4 v[216:217], off
	v_lshl_add_u64 v[216:217], v[146:147], 0, s[18:19]
	s_add_i32 m0, s29, 0xe000
	s_nop 0
	global_load_lds_dwordx4 v[216:217], off
	s_waitcnt lgkmcnt(8)
	s_barrier
	s_waitcnt lgkmcnt(0)
	s_waitcnt lgkmcnt(0)
	v_mfma_f32_16x16x32_bf16 v[126:129], v[166:169], v[182:185], v[126:129]
	v_mfma_f32_16x16x32_bf16 v[122:125], v[174:177], v[182:185], v[122:125]
	v_mfma_f32_16x16x32_bf16 v[118:121], v[166:169], v[190:193], v[118:121]
	v_mfma_f32_16x16x32_bf16 v[110:113], v[174:177], v[190:193], v[110:113]
	v_mfma_f32_16x16x32_bf16 v[102:105], v[166:169], v[198:201], v[102:105]
	v_mfma_f32_16x16x32_bf16 v[94:97], v[174:177], v[198:201], v[94:97]
	v_mfma_f32_16x16x32_bf16 v[86:89], v[166:169], v[208:211], v[86:89]
	v_mfma_f32_16x16x32_bf16 v[78:81], v[174:177], v[208:211], v[78:81]
	v_mfma_f32_16x16x32_bf16 v[126:129], v[170:173], v[186:189], v[126:129]
	v_mfma_f32_16x16x32_bf16 v[122:125], v[178:181], v[186:189], v[122:125]
	v_mfma_f32_16x16x32_bf16 v[118:121], v[170:173], v[194:197], v[118:121]
	v_mfma_f32_16x16x32_bf16 v[110:113], v[178:181], v[194:197], v[110:113]
	v_mfma_f32_16x16x32_bf16 v[102:105], v[170:173], v[202:205], v[102:105]
	v_mfma_f32_16x16x32_bf16 v[94:97], v[178:181], v[202:205], v[94:97]
	v_mfma_f32_16x16x32_bf16 v[86:89], v[170:173], v[212:215], v[86:89]
	v_mfma_f32_16x16x32_bf16 v[78:81], v[178:181], v[212:215], v[78:81]
	s_barrier
	s_add_i32 s47, s37, s27
	v_lshl_add_u64 v[232:233], s[20:21], 0, v[132:133]
	s_mov_b32 m0, s47
	ds_read_b128 v[216:219], v160
	ds_read_b128 v[220:223], v160 offset:1024
	ds_read_b128 v[224:227], v160 offset:2048
	ds_read_b128 v[228:231], v160 offset:3072
	global_load_lds_dwordx4 v[232:233], off
	v_lshl_add_u64 v[234:235], s[20:21], 0, v[130:131]
	s_add_i32 m0, s47, 0x2000
	s_nop 0
	global_load_lds_dwordx4 v[234:235], off
	s_barrier
	s_waitcnt lgkmcnt(0)
	s_waitcnt lgkmcnt(0)
	v_mfma_f32_16x16x32_bf16 v[114:117], v[216:219], v[182:185], v[114:117]
	v_mfma_f32_16x16x32_bf16 v[106:109], v[224:227], v[182:185], v[106:109]
	v_mfma_f32_16x16x32_bf16 v[98:101], v[216:219], v[190:193], v[98:101]
	v_mfma_f32_16x16x32_bf16 v[90:93], v[224:227], v[190:193], v[90:93]
	v_mfma_f32_16x16x32_bf16 v[82:85], v[216:219], v[198:201], v[82:85]
	v_mfma_f32_16x16x32_bf16 v[74:77], v[224:227], v[198:201], v[74:77]
	v_mfma_f32_16x16x32_bf16 v[70:73], v[216:219], v[208:211], v[70:73]
	v_mfma_f32_16x16x32_bf16 v[66:69], v[224:227], v[208:211], v[66:69]
	v_mfma_f32_16x16x32_bf16 v[114:117], v[220:223], v[186:189], v[114:117]
	v_mfma_f32_16x16x32_bf16 v[106:109], v[228:231], v[186:189], v[106:109]
	v_mfma_f32_16x16x32_bf16 v[98:101], v[220:223], v[194:197], v[98:101]
	v_mfma_f32_16x16x32_bf16 v[90:93], v[228:231], v[194:197], v[90:93]
	v_mfma_f32_16x16x32_bf16 v[82:85], v[220:223], v[202:205], v[82:85]
	v_mfma_f32_16x16x32_bf16 v[74:77], v[228:231], v[202:205], v[74:77]
	v_mfma_f32_16x16x32_bf16 v[70:73], v[220:223], v[212:215], v[70:73]
	v_mfma_f32_16x16x32_bf16 v[66:69], v[228:231], v[212:215], v[66:69]
	s_mov_b32 m0, s29
	s_barrier
	ds_read_b128 v[182:185], v159 offset:16384
	ds_read_b128 v[186:189], v159 offset:17408
	ds_read_b128 v[190:193], v159 offset:18432
	ds_read_b128 v[194:197], v159 offset:19456
	ds_read_b128 v[198:201], v159 offset:20480
	ds_read_b128 v[202:205], v159 offset:21504
	ds_read_b128 v[208:211], v159 offset:22528
	ds_read_b128 v[212:215], v159 offset:23552
	global_load_lds_dwordx4 v134, s[22:23]
	s_mov_b32 m0, s30
	v_mov_b32_e32 v207, v135
	global_load_lds_dwordx4 v206, s[22:23]
	s_barrier
	s_waitcnt lgkmcnt(0)
	v_lshl_add_u64 v[236:237], s[22:23], 0, v[134:135]
	v_lshl_add_u64 v[206:207], s[22:23], 0, v[206:207]
	s_waitcnt lgkmcnt(0)
	v_mfma_f32_16x16x32_bf16 v[62:65], v[166:169], v[182:185], v[62:65]
	v_mfma_f32_16x16x32_bf16 v[58:61], v[174:177], v[182:185], v[58:61]
	v_mfma_f32_16x16x32_bf16 v[54:57], v[166:169], v[190:193], v[54:57]
	v_mfma_f32_16x16x32_bf16 v[46:49], v[174:177], v[190:193], v[46:49]
	v_mfma_f32_16x16x32_bf16 v[38:41], v[166:169], v[198:201], v[38:41]
	v_mfma_f32_16x16x32_bf16 v[30:33], v[174:177], v[198:201], v[30:33]
	v_mfma_f32_16x16x32_bf16 v[22:25], v[166:169], v[208:211], v[22:25]
	v_mfma_f32_16x16x32_bf16 v[14:17], v[174:177], v[208:211], v[14:17]
	v_mfma_f32_16x16x32_bf16 v[62:65], v[170:173], v[186:189], v[62:65]
	v_mfma_f32_16x16x32_bf16 v[58:61], v[178:181], v[186:189], v[58:61]
	v_mfma_f32_16x16x32_bf16 v[54:57], v[170:173], v[194:197], v[54:57]
	v_mfma_f32_16x16x32_bf16 v[46:49], v[178:181], v[194:197], v[46:49]
	v_mfma_f32_16x16x32_bf16 v[38:41], v[170:173], v[202:205], v[38:41]
	v_mfma_f32_16x16x32_bf16 v[30:33], v[178:181], v[202:205], v[30:33]
	v_mfma_f32_16x16x32_bf16 v[22:25], v[170:173], v[212:215], v[22:25]
	v_mfma_f32_16x16x32_bf16 v[14:17], v[178:181], v[212:215], v[14:17]
	s_barrier
; #define PG8_STAGE(bufoff, gbase, v0, v1) do { \
;         __builtin_amdgcn_global_load_lds((const unsigned*)((const char*)(gbase) + (v0)), (LAS unsigned*)(lds + (bufoff) + ldsw), 16, 0, 0); \
;         __builtin_amdgcn_global_load_lds((const unsigned*)((const char*)(gbase) + (v1)), (LAS unsigned*)(lds + (bufoff) + ldsw + 8192), 16, 0, 0); } while (0)
; #define PG8_LDA(dst, b, h) do { _Pragma("unroll") for (int m = 0; m < 4; ++m) _Pragma("unroll") for (int k = 0; k < 2; ++k) dst[m][k] = *(const LAS bf16x8*)(lds + PG8_SA(b, h) + aoff + m * 2048 + k * 1024); } while (0)
; #define PG8_LDB(dst, b, h) do { _Pragma("unroll") for (int n = 0; n < 2; ++n) _Pragma("unroll") for (int k = 0; k < 2; ++k) dst[n][k] = *(const LAS bf16x8*)(lds + PG8_SB(b, h) + boff + n * 2048 + k * 1024); } while (0)
; #define PG8_MMA(ai, bj, At, Bt) do { __builtin_amdgcn_s_setprio(1); _Pragma("unroll") for (int m = 0; m < 4; ++m) _Pragma("unroll") for (int n = 0; n < 2; ++n) _Pragma("unroll") for (int k = 0; k < 2; ++k) \
;         acc[ai][bj][m][n] = __builtin_amdgcn_mfma_f32_16x16x32_bf16(Bt[n][k], At[m][k], acc[ai][bj][m][n], 0, 0, 0); __builtin_amdgcn_s_setprio(0); } while (0)
; #define PG8_WAIT_V(n) asm volatile("s_waitcnt vmcnt(" #n ")" ::: "memory")
; #define PG8_WAIT_L(n) asm volatile("s_waitcnt lgkmcnt(" #n ")" ::: "memory")
; #define PG8_BAR __builtin_amdgcn_s_barrier()
; #define PG8_SCHED __builtin_amdgcn_sched_barrier(0)
; template <class Epi, class Sched>
; __device__ __forceinline__ void gemm_phase(LAS unsigned char* lds, const int K, const Sched& S, const Epi& E) {
;     ...
;             PG8_STAGE(PG8_SB(0, 1), b2 + hstep, voffB0, voffB1);
;             PG8_WAIT_V(6); PG8_BAR; PG8_MMA(1, 1, At, B1); PG8_BAR;
;             PG8_LDB(B0, 1, 0); PG8_SCHED; PG8_LDA(At, 1, 0); PG8_STAGE(PG8_SA(0, 1), a2, x10, x11);
;             PG8_WAIT_L(8); PG8_BAR; PG8_WAIT_L(0); PG8_MMA(0, 0, At, B0); PG8_BAR; PG8_SCHED;
;             PG8_LDB(B1, 1, 1); PG8_STAGE(PG8_SB(1, 0), b3, voffB0, voffB1);
;             PG8_BAR; PG8_WAIT_L(0); PG8_MMA(0, 1, At, B1); PG8_BAR;
;             PG8_LDA(At, 1, 1); PG8_STAGE(PG8_SA(1, 0), a3, x00, x01);
;             PG8_BAR; PG8_WAIT_L(0); PG8_MMA(1, 0, At, B0); PG8_BAR; PG8_SCHED;
;             PG8_STAGE(PG8_SB(1, 1), b3 + hstep, voffB0, voffB1);
	s_add_u32 s48, s20, 0x80000
	s_addc_u32 s49, s21, 0
	s_add_i32 s47, s38, s27
	v_lshl_add_u64 v[166:167], s[48:49], 0, v[132:133]
	s_mov_b32 m0, s47
	s_nop 0
	global_load_lds_dwordx4 v[166:167], off
	v_lshl_add_u64 v[166:167], s[48:49], 0, v[130:131]
	s_add_i32 m0, s47, 0x2000
	s_nop 0
	global_load_lds_dwordx4 v[166:167], off
	s_waitcnt vmcnt(6)
	s_barrier
	v_mfma_f32_16x16x32_bf16 v[50:53], v[216:219], v[182:185], v[50:53]
	v_mfma_f32_16x16x32_bf16 v[42:45], v[224:227], v[182:185], v[42:45]
	v_mfma_f32_16x16x32_bf16 v[34:37], v[216:219], v[190:193], v[34:37]
	v_mfma_f32_16x16x32_bf16 v[26:29], v[224:227], v[190:193], v[26:29]
	v_mfma_f32_16x16x32_bf16 v[18:21], v[216:219], v[198:201], v[18:21]
	v_mfma_f32_16x16x32_bf16 v[10:13], v[224:227], v[198:201], v[10:13]
	v_mfma_f32_16x16x32_bf16 v[6:9], v[216:219], v[208:211], v[6:9]
	v_mfma_f32_16x16x32_bf16 v[2:5], v[224:227], v[208:211], v[2:5]
	v_mfma_f32_16x16x32_bf16 v[50:53], v[220:223], v[186:189], v[50:53]
	v_mfma_f32_16x16x32_bf16 v[42:45], v[228:231], v[186:189], v[42:45]
	v_mfma_f32_16x16x32_bf16 v[34:37], v[220:223], v[194:197], v[34:37]
	v_mfma_f32_16x16x32_bf16 v[26:29], v[228:231], v[194:197], v[26:29]
	v_mfma_f32_16x16x32_bf16 v[18:21], v[220:223], v[202:205], v[18:21]
	v_mfma_f32_16x16x32_bf16 v[10:13], v[228:231], v[202:205], v[10:13]
	v_mfma_f32_16x16x32_bf16 v[6:9], v[220:223], v[212:215], v[6:9]
	v_mfma_f32_16x16x32_bf16 v[2:5], v[228:231], v[212:215], v[2:5]
	s_add_i32 s47, 0, 0x18000
	v_add_u32_e32 v134, s47, v156
	s_barrier
	ds_read_b128 v[166:169], v134
	ds_read_b128 v[170:173], v134 offset:1024
	ds_read_b128 v[174:177], v134 offset:2048
	ds_read_b128 v[178:181], v134 offset:3072
	s_mov_b32 m0, s31
	ds_read_b128 v[182:185], v159 offset:32768
	ds_read_b128 v[186:189], v159 offset:33792
	ds_read_b128 v[190:193], v159 offset:34816
	ds_read_b128 v[194:197], v159 offset:35840
	ds_read_b128 v[198:201], v159 offset:36864
	ds_read_b128 v[202:205], v159 offset:37888
	ds_read_b128 v[208:211], v159 offset:38912
	ds_read_b128 v[212:215], v159 offset:39936
	v_cndmask_b32_e32 v134, v144, v164, vcc
	global_load_lds_dwordx4 v143, s[22:23]
	s_mov_b32 m0, s33
	s_nop 0
	global_load_lds_dwordx4 v134, s[22:23]
	s_waitcnt lgkmcnt(8)
	s_barrier
	s_waitcnt lgkmcnt(0)
	s_waitcnt lgkmcnt(0)
	v_mfma_f32_16x16x32_bf16 v[126:129], v[166:169], v[182:185], v[126:129]
	v_mfma_f32_16x16x32_bf16 v[122:125], v[174:177], v[182:185], v[122:125]
	v_mfma_f32_16x16x32_bf16 v[118:121], v[166:169], v[190:193], v[118:121]
	v_mfma_f32_16x16x32_bf16 v[110:113], v[174:177], v[190:193], v[110:113]
	v_mfma_f32_16x16x32_bf16 v[102:105], v[166:169], v[198:201], v[102:105]
	v_mfma_f32_16x16x32_bf16 v[94:97], v[174:177], v[198:201], v[94:97]
	v_mfma_f32_16x16x32_bf16 v[86:89], v[166:169], v[208:211], v[86:89]
	v_mfma_f32_16x16x32_bf16 v[78:81], v[174:177], v[208:211], v[78:81]
	v_mfma_f32_16x16x32_bf16 v[126:129], v[170:173], v[186:189], v[126:129]
	v_mfma_f32_16x16x32_bf16 v[122:125], v[178:181], v[186:189], v[122:125]
	v_mfma_f32_16x16x32_bf16 v[118:121], v[170:173], v[194:197], v[118:121]
	v_mfma_f32_16x16x32_bf16 v[110:113], v[178:181], v[194:197], v[110:113]
	v_mfma_f32_16x16x32_bf16 v[102:105], v[170:173], v[202:205], v[102:105]
	v_mfma_f32_16x16x32_bf16 v[94:97], v[178:181], v[202:205], v[94:97]
	v_mfma_f32_16x16x32_bf16 v[86:89], v[170:173], v[212:215], v[86:89]
	v_mfma_f32_16x16x32_bf16 v[78:81], v[178:181], v[212:215], v[78:81]
	s_barrier
	s_add_i32 s22, 0, 0x1c000
	s_add_i32 s23, s47, s27
	v_add_u32_e32 v134, s22, v156
	v_lshl_add_u64 v[232:233], v[232:233], 0, s[14:15]
	s_mov_b32 m0, s23
	ds_read_b128 v[216:219], v134
	ds_read_b128 v[220:223], v134 offset:1024
	ds_read_b128 v[224:227], v134 offset:2048
	ds_read_b128 v[228:231], v134 offset:3072
	global_load_lds_dwordx4 v[232:233], off
	v_lshl_add_u64 v[232:233], v[234:235], 0, s[14:15]
	s_add_i32 m0, s23, 0x2000
	s_nop 0
	global_load_lds_dwordx4 v[232:233], off
	s_barrier
	s_waitcnt lgkmcnt(0)
	s_waitcnt lgkmcnt(0)
	v_mfma_f32_16x16x32_bf16 v[114:117], v[216:219], v[182:185], v[114:117]
	v_mfma_f32_16x16x32_bf16 v[106:109], v[224:227], v[182:185], v[106:109]
	v_mfma_f32_16x16x32_bf16 v[98:101], v[216:219], v[190:193], v[98:101]
	v_mfma_f32_16x16x32_bf16 v[90:93], v[224:227], v[190:193], v[90:93]
	v_mfma_f32_16x16x32_bf16 v[82:85], v[216:219], v[198:201], v[82:85]
	v_mfma_f32_16x16x32_bf16 v[74:77], v[224:227], v[198:201], v[74:77]
	v_mfma_f32_16x16x32_bf16 v[70:73], v[216:219], v[208:211], v[70:73]
	v_mfma_f32_16x16x32_bf16 v[66:69], v[224:227], v[208:211], v[66:69]
	v_mfma_f32_16x16x32_bf16 v[114:117], v[220:223], v[186:189], v[114:117]
	v_mfma_f32_16x16x32_bf16 v[106:109], v[228:231], v[186:189], v[106:109]
	v_mfma_f32_16x16x32_bf16 v[98:101], v[220:223], v[194:197], v[98:101]
	v_mfma_f32_16x16x32_bf16 v[90:93], v[228:231], v[194:197], v[90:93]
	v_mfma_f32_16x16x32_bf16 v[82:85], v[220:223], v[202:205], v[82:85]
	v_mfma_f32_16x16x32_bf16 v[74:77], v[228:231], v[202:205], v[74:77]
	v_mfma_f32_16x16x32_bf16 v[70:73], v[220:223], v[212:215], v[70:73]
	v_mfma_f32_16x16x32_bf16 v[66:69], v[228:231], v[212:215], v[66:69]
	s_mov_b32 m0, s35
	v_lshl_add_u64 v[232:233], v[236:237], 0, s[14:15]
	s_barrier
	ds_read_b128 v[182:185], v159 offset:49152
	ds_read_b128 v[186:189], v159 offset:50176
	ds_read_b128 v[190:193], v159 offset:51200
	ds_read_b128 v[194:197], v159 offset:52224
	ds_read_b128 v[198:201], v159 offset:53248
	ds_read_b128 v[202:205], v159 offset:54272
	ds_read_b128 v[208:211], v159 offset:55296
	ds_read_b128 v[212:215], v159 offset:56320
	global_load_lds_dwordx4 v[232:233], off
	v_lshl_add_u64 v[206:207], v[206:207], 0, s[14:15]
	s_mov_b32 m0, s36
	s_nop 0
	global_load_lds_dwordx4 v[206:207], off
	s_barrier
; #define PG8_STAGE(bufoff, gbase, v0, v1) do { \
;         __builtin_amdgcn_global_load_lds((const unsigned*)((const char*)(gbase) + (v0)), (LAS unsigned*)(lds + (bufoff) + ldsw), 16, 0, 0); \
;         __builtin_amdgcn_global_load_lds((const unsigned*)((const char*)(gbase) + (v1)), (LAS unsigned*)(lds + (bufoff) + ldsw + 8192), 16, 0, 0); } while (0)
; #define PG8_LDA(dst, b, h) do { _Pragma("unroll") for (int m = 0; m < 4; ++m) _Pragma("unroll") for (int k = 0; k < 2; ++k) dst[m][k] = *(const LAS bf16x8*)(lds + PG8_SA(b, h) + aoff + m * 2048 + k * 1024); } while (0)
; #define PG8_MMA(ai, bj, At, Bt) do { __builtin_amdgcn_s_setprio(1); _Pragma("unroll") for (int m = 0; m < 4; ++m) _Pragma("unroll") for (int n = 0; n < 2; ++n) _Pragma("unroll") for (int k = 0; k < 2; ++k) \
;         acc[ai][bj][m][n] = __builtin_amdgcn_mfma_f32_16x16x32_bf16(Bt[n][k], At[m][k], acc[ai][bj][m][n], 0, 0, 0); __builtin_amdgcn_s_setprio(0); } while (0)
; #define PG8_WAIT_V(n) asm volatile("s_waitcnt vmcnt(" #n ")" ::: "memory")
; #define PG8_WAIT_L(n) asm volatile("s_waitcnt lgkmcnt(" #n ")" ::: "memory")
; #define PG8_BAR __builtin_amdgcn_s_barrier()
; #define PG8_SCHED __builtin_amdgcn_sched_barrier(0)
; template <class Epi, class Sched>
; __device__ __forceinline__ void gemm_phase(LAS unsigned char* lds, const int K, const Sched& S, const Epi& E) {
;     ...
;             PG8_LDA(At, 1, 1); PG8_STAGE(PG8_SA(1, 0), a3, x00, x01);
;             PG8_BAR; PG8_WAIT_L(0); PG8_MMA(1, 0, At, B0); PG8_BAR; PG8_SCHED;
;             PG8_STAGE(PG8_SB(1, 1), b3 + hstep, voffB0, voffB1);
;             PG8_WAIT_V(6); PG8_BAR; PG8_MMA(1, 1, At, B1); PG8_BAR;
	s_waitcnt lgkmcnt(0)
	s_waitcnt lgkmcnt(0)
	v_mfma_f32_16x16x32_bf16 v[62:65], v[166:169], v[182:185], v[62:65]
	v_mfma_f32_16x16x32_bf16 v[58:61], v[174:177], v[182:185], v[58:61]
	v_mfma_f32_16x16x32_bf16 v[54:57], v[166:169], v[190:193], v[54:57]
	v_mfma_f32_16x16x32_bf16 v[46:49], v[174:177], v[190:193], v[46:49]
	v_mfma_f32_16x16x32_bf16 v[38:41], v[166:169], v[198:201], v[38:41]
	v_mfma_f32_16x16x32_bf16 v[30:33], v[174:177], v[198:201], v[30:33]
	v_mfma_f32_16x16x32_bf16 v[22:25], v[166:169], v[208:211], v[22:25]
	v_mfma_f32_16x16x32_bf16 v[14:17], v[174:177], v[208:211], v[14:17]
	v_mfma_f32_16x16x32_bf16 v[62:65], v[170:173], v[186:189], v[62:65]
	v_mfma_f32_16x16x32_bf16 v[58:61], v[178:181], v[186:189], v[58:61]
	v_mfma_f32_16x16x32_bf16 v[54:57], v[170:173], v[194:197], v[54:57]
	v_mfma_f32_16x16x32_bf16 v[46:49], v[178:181], v[194:197], v[46:49]
	v_mfma_f32_16x16x32_bf16 v[38:41], v[170:173], v[202:205], v[38:41]
	v_mfma_f32_16x16x32_bf16 v[30:33], v[178:181], v[202:205], v[30:33]
	v_mfma_f32_16x16x32_bf16 v[22:25], v[170:173], v[212:215], v[22:25]
	v_mfma_f32_16x16x32_bf16 v[14:17], v[178:181], v[212:215], v[14:17]
	s_barrier
	s_add_u32 s20, s20, 0x80080
	s_addc_u32 s21, s21, 0
	s_add_i32 s22, s22, s27
	v_lshl_add_u64 v[166:167], s[20:21], 0, v[132:133]
	s_mov_b32 m0, s22
	s_nop 0
	global_load_lds_dwordx4 v[166:167], off
	v_lshl_add_u64 v[166:167], s[20:21], 0, v[130:131]
	s_add_i32 m0, s22, 0x2000
	s_nop 0
	global_load_lds_dwordx4 v[166:167], off
	s_waitcnt vmcnt(6)
	s_barrier
	v_mfma_f32_16x16x32_bf16 v[50:53], v[216:219], v[182:185], v[50:53]
	v_mfma_f32_16x16x32_bf16 v[42:45], v[224:227], v[182:185], v[42:45]
	v_mfma_f32_16x16x32_bf16 v[34:37], v[216:219], v[190:193], v[34:37]
	v_mfma_f32_16x16x32_bf16 v[26:29], v[224:227], v[190:193], v[26:29]
	v_mfma_f32_16x16x32_bf16 v[18:21], v[216:219], v[198:201], v[18:21]
	v_mfma_f32_16x16x32_bf16 v[10:13], v[224:227], v[198:201], v[10:13]
	v_mfma_f32_16x16x32_bf16 v[6:9], v[216:219], v[208:211], v[6:9]
	v_mfma_f32_16x16x32_bf16 v[2:5], v[224:227], v[208:211], v[2:5]
	v_mfma_f32_16x16x32_bf16 v[50:53], v[220:223], v[186:189], v[50:53]
	v_mfma_f32_16x16x32_bf16 v[42:45], v[228:231], v[186:189], v[42:45]
	v_mfma_f32_16x16x32_bf16 v[34:37], v[220:223], v[194:197], v[34:37]
	v_mfma_f32_16x16x32_bf16 v[26:29], v[228:231], v[194:197], v[26:29]
	v_mfma_f32_16x16x32_bf16 v[18:21], v[220:223], v[202:205], v[18:21]
	v_mfma_f32_16x16x32_bf16 v[10:13], v[228:231], v[202:205], v[10:13]
	v_mfma_f32_16x16x32_bf16 v[6:9], v[220:223], v[212:215], v[6:9]
	v_mfma_f32_16x16x32_bf16 v[2:5], v[228:231], v[212:215], v[2:5]
	s_add_i32 s46, s46, 2
	s_add_u32 s18, s18, 0x100
	s_addc_u32 s19, s19, 0
	s_cmp_gt_u32 s46, 29
	s_barrier
	s_cbranch_scc0 .LBB0_1290
; __device__ __forceinline__ unsigned cvt_pk_bf16(float lo, float hi) { unsigned r; asm volatile("v_cvt_pk_bf16_f32 %0, %1, %2" : "=v"(r) : "v"(lo), "v"(hi)); return r; }
; #define PG8_WAIT_V(n) asm volatile("s_waitcnt vmcnt(" #n ")" ::: "memory")
; #define PG8_BAR __builtin_amdgcn_s_barrier()
; template <class Epi, class Sched>
; __device__ __forceinline__ void gemm_phase(LAS unsigned char* lds, const int K, const Sched& S, const Epi& E) {
;     ...
;         if (!has_next) break;
; #pragma unroll
;         for (int a = 0; a < 2; ++a)
; #pragma unroll
;             for (int b = 0; b < 2; ++b)
; #pragma unroll
;                 for (int m = 0; m < 4; ++m)
; #pragma unroll
;                     for (int n = 0; n < 2; ++n) acc[a][b][m][n] = (f32x4){0.f, 0.f, 0.f, 0.f};
;         cur = nxt; cB = nB; c00 = n00; c01 = n01; c10 = n10; c11 = n11; ++ui;
;     }
;     PG8_WAIT_V(0);
;     if (wr == 0) PG8_BAR;
;     PG8_BAR;
;     __device__ __forceinline__ void operator()(const f32x4 (&acc)[2][2][4][2], const Unit& u, int wr, int wc, int fr, int fq) const {
;         const int row0 = u.rbase + wr * 64 + fr, col0 = u.pn * BM + wc * 32 + 8 * fq;
; #pragma unroll
;         for (int ai = 0; ai < 2; ++ai)
; #pragma unroll
;             for (int m = 0; m < 4; ++m) { bf16_t* rowp = O + (size_t)(row0 + ai * HALF + m * 16) * ldc + col0;
; #pragma unroll
;                 for (int bj = 0; bj < 2; ++bj) { const f32x4 v0 = acc[ai][bj][m][0], v1 = acc[ai][bj][m][1];
;                     u32x4 w; w.x = cvt_pk_bf16(v0[0], v0[1]); w.y = cvt_pk_bf16(v0[2], v0[3]); w.z = cvt_pk_bf16(v1[0], v1[1]); w.w = cvt_pk_bf16(v1[2], v1[3]);
;                     *(u32x4*)(rowp + bj * HALF) = w; } }
	v_lshl_or_b32 v142, s44, 8, v157
	v_add_u32_e32 v134, s43, v155
	v_ashrrev_i32_e32 v143, 31, v142
	v_mov_b64_e32 v[140:141], s[10:11]
	v_mad_i64_i32 v[144:145], s[18:19], v134, s39, v[140:141]
	v_lshlrev_b64 v[142:143], 1, v[142:143]
	v_lshl_add_u64 v[144:145], v[144:145], 0, v[142:143]
	v_cvt_pk_bf16_f32 v126, v126, v127
	v_cvt_pk_bf16_f32 v127, v128, v129
	v_cvt_pk_bf16_f32 v128, v122, v123
	v_cvt_pk_bf16_f32 v129, v124, v125
	global_store_dwordx4 v[144:145], v[126:129], off
	v_cvt_pk_bf16_f32 v114, v114, v115
	v_cvt_pk_bf16_f32 v115, v116, v117
	v_cvt_pk_bf16_f32 v116, v106, v107
	v_add_u32_e32 v106, 16, v134
	v_mad_i64_i32 v[106:107], s[18:19], v106, s39, v[140:141]
	v_cvt_pk_bf16_f32 v117, v108, v109
	global_store_dwordx4 v[144:145], v[114:117], off offset:256
	s_and_b64 vcc, exec, s[0:1]
	s_mov_b32 s44, s16
	v_lshl_add_u64 v[114:115], v[106:107], 0, v[142:143]
	v_cvt_pk_bf16_f32 v106, v118, v119
	v_cvt_pk_bf16_f32 v107, v120, v121
	v_cvt_pk_bf16_f32 v108, v110, v111
	v_cvt_pk_bf16_f32 v109, v112, v113
	global_store_dwordx4 v[114:115], v[106:109], off
	v_cvt_pk_bf16_f32 v98, v98, v99
	v_cvt_pk_bf16_f32 v99, v100, v101
	v_cvt_pk_bf16_f32 v100, v90, v91
	v_add_u32_e32 v90, 32, v134
	v_mad_i64_i32 v[90:91], s[18:19], v90, s39, v[140:141]
	v_cvt_pk_bf16_f32 v101, v92, v93
	global_store_dwordx4 v[114:115], v[98:101], off offset:256
	s_mov_b32 s43, s41
	v_mov_b32_e32 v144, v164
	v_lshl_add_u64 v[98:99], v[90:91], 0, v[142:143]
	v_cvt_pk_bf16_f32 v90, v102, v103
	v_cvt_pk_bf16_f32 v91, v104, v105
	v_cvt_pk_bf16_f32 v92, v94, v95
	v_cvt_pk_bf16_f32 v93, v96, v97
	global_store_dwordx4 v[98:99], v[90:93], off
	v_cvt_pk_bf16_f32 v82, v82, v83
	v_cvt_pk_bf16_f32 v83, v84, v85
	v_cvt_pk_bf16_f32 v84, v74, v75
	v_add_u32_e32 v74, 48, v134
	v_mad_i64_i32 v[74:75], s[18:19], v74, s39, v[140:141]
	v_cvt_pk_bf16_f32 v85, v76, v77
	global_store_dwordx4 v[98:99], v[82:85], off offset:256
	s_nop 1
	v_lshl_add_u64 v[82:83], v[74:75], 0, v[142:143]
	v_cvt_pk_bf16_f32 v74, v86, v87
	v_cvt_pk_bf16_f32 v75, v88, v89
	v_cvt_pk_bf16_f32 v76, v78, v79
	v_cvt_pk_bf16_f32 v77, v80, v81
	global_store_dwordx4 v[82:83], v[74:77], off
	v_cvt_pk_bf16_f32 v70, v70, v71
	v_cvt_pk_bf16_f32 v71, v72, v73
	v_cvt_pk_bf16_f32 v72, v66, v67
	v_add_u32_e32 v66, 0x80, v134
	v_mad_i64_i32 v[66:67], s[18:19], v66, s39, v[140:141]
	v_lshl_add_u64 v[66:67], v[66:67], 0, v[142:143]
	v_cvt_pk_bf16_f32 v73, v68, v69
	global_store_dwordx4 v[82:83], v[70:73], off offset:256
	v_cvt_pk_bf16_f32 v62, v62, v63
	v_cvt_pk_bf16_f32 v63, v64, v65
	v_cvt_pk_bf16_f32 v64, v58, v59
	v_cvt_pk_bf16_f32 v65, v60, v61
	global_store_dwordx4 v[66:67], v[62:65], off
	v_cvt_pk_bf16_f32 v50, v50, v51
	v_cvt_pk_bf16_f32 v51, v52, v53
	v_cvt_pk_bf16_f32 v52, v42, v43
	v_add_u32_e32 v42, 0x90, v134
	v_mad_i64_i32 v[42:43], s[18:19], v42, s39, v[140:141]
	v_cvt_pk_bf16_f32 v53, v44, v45
	global_store_dwordx4 v[66:67], v[50:53], off offset:256
	s_nop 1
	v_lshl_add_u64 v[50:51], v[42:43], 0, v[142:143]
	v_cvt_pk_bf16_f32 v42, v54, v55
	v_cvt_pk_bf16_f32 v43, v56, v57
	v_cvt_pk_bf16_f32 v44, v46, v47
	v_cvt_pk_bf16_f32 v45, v48, v49
	global_store_dwordx4 v[50:51], v[42:45], off
	v_cvt_pk_bf16_f32 v34, v34, v35
	v_cvt_pk_bf16_f32 v35, v36, v37
	v_cvt_pk_bf16_f32 v36, v26, v27
	v_add_u32_e32 v26, 0xa0, v134
	v_mad_i64_i32 v[26:27], s[18:19], v26, s39, v[140:141]
	v_cvt_pk_bf16_f32 v37, v28, v29
	global_store_dwordx4 v[50:51], v[34:37], off offset:256
	s_nop 1
	v_lshl_add_u64 v[34:35], v[26:27], 0, v[142:143]
	v_cvt_pk_bf16_f32 v26, v38, v39
	v_cvt_pk_bf16_f32 v27, v40, v41
	v_cvt_pk_bf16_f32 v28, v30, v31
	v_cvt_pk_bf16_f32 v29, v32, v33
	global_store_dwordx4 v[34:35], v[26:29], off
	v_cvt_pk_bf16_f32 v18, v18, v19
	v_cvt_pk_bf16_f32 v19, v20, v21
	v_cvt_pk_bf16_f32 v20, v10, v11
	v_add_u32_e32 v10, 0xb0, v134
	v_mad_i64_i32 v[10:11], s[18:19], v10, s39, v[140:141]
	v_cvt_pk_bf16_f32 v21, v12, v13
	global_store_dwordx4 v[34:35], v[18:21], off offset:256
	v_mov_b32_e32 v141, v161
	v_mov_b32_e32 v140, v162
	v_lshl_add_u64 v[18:19], v[10:11], 0, v[142:143]
	v_mov_b32_e32 v142, v163
	s_mov_b64 s[18:19], s[2:3]
	v_cvt_pk_bf16_f32 v10, v22, v23
	v_cvt_pk_bf16_f32 v11, v24, v25
	v_cvt_pk_bf16_f32 v12, v14, v15
	v_cvt_pk_bf16_f32 v13, v16, v17
	global_store_dwordx4 v[18:19], v[10:13], off
	v_cvt_pk_bf16_f32 v6, v6, v7
	v_cvt_pk_bf16_f32 v7, v8, v9
	v_cvt_pk_bf16_f32 v8, v2, v3
	v_cvt_pk_bf16_f32 v9, v4, v5
	global_store_dwordx4 v[18:19], v[6:9], off offset:256
	s_cbranch_vccz .LBB0_1285
	s_waitcnt vmcnt(0)
	s_cmpk_gt_u32 s24, 0xff
	s_cbranch_scc1 .LBB0_1294
	s_barrier

; #define PG8_STAGE(bufoff, gbase, v0, v1) do { \
;         __builtin_amdgcn_global_load_lds((const unsigned*)((const char*)(gbase) + (v0)), (LAS unsigned*)(lds + (bufoff) + ldsw), 16, 0, 0); \
;         __builtin_amdgcn_global_load_lds((const unsigned*)((const char*)(gbase) + (v1)), (LAS unsigned*)(lds + (bufoff) + ldsw + 8192), 16, 0, 0); } while (0)
; #define PG8_LDA(dst, b, h) do { _Pragma("unroll") for (int m = 0; m < 4; ++m) _Pragma("unroll") for (int k = 0; k < 2; ++k) dst[m][k] = *(const LAS bf16x8*)(lds + PG8_SA(b, h) + aoff + m * 2048 + k * 1024); } while (0)
; #define PG8_LDB(dst, b, h) do { _Pragma("unroll") for (int n = 0; n < 2; ++n) _Pragma("unroll") for (int k = 0; k < 2; ++k) dst[n][k] = *(const LAS bf16x8*)(lds + PG8_SB(b, h) + boff + n * 2048 + k * 1024); } while (0)
; #define PG8_WAIT_V(n) asm volatile("s_waitcnt vmcnt(" #n ")" ::: "memory")
; #define PG8_WAIT_L(n) asm volatile("s_waitcnt lgkmcnt(" #n ")" ::: "memory")
; #define PG8_BAR __builtin_amdgcn_s_barrier()
; #define PG8_SCHED __builtin_amdgcn_sched_barrier(0)
; template <class Epi, class Sched>
; __device__ __forceinline__ void gemm_phase(LAS unsigned char* lds, const int K, const Sched& S, const Epi& E) {
;     ...
;         for (int t = 0; t < nt; t += 2) {
;             const bool last = (t == nt - 2);
;             const char* a1 = gA + (size_t)(t + 1) * kstep;
;             const char* a2 = last ? gA : gA + (size_t)(t + 2) * kstep; const char* b2 = last ? nB : cB + (size_t)(t + 2) * kstepB;
;             const char* a3 = a2 + kstep; const char* b3 = b2 + kstepB;
;             const unsigned x00 = last ? n00 : c00, x01 = last ? n01 : c01, x10 = last ? n10 : c10, x11 = last ? n11 : c11;
;             PG8_LDB(B0, 0, 0); PG8_SCHED; PG8_LDA(At, 0, 0); PG8_STAGE(PG8_SA(1, 1), a1, c10, c11);
;             PG8_WAIT_L(8); PG8_BAR; PG8_WAIT_L(0); PG8_MMA(0, 0, At, B0); PG8_BAR; PG8_SCHED;
;             PG8_LDB(B1, 0, 1); PG8_STAGE(PG8_SB(0, 0), b2, voffB0, voffB1);
;             PG8_BAR; PG8_WAIT_L(0); PG8_MMA(0, 1, At, B1); PG8_BAR;
;             PG8_LDA(At, 0, 1); PG8_STAGE(PG8_SA(0, 0), a2, x00, x01);
;             PG8_BAR; PG8_WAIT_L(0); PG8_MMA(1, 0, At, B0); PG8_BAR; PG8_SCHED;
;             PG8_STAGE(PG8_SB(0, 1), b2 + hstep, voffB0, voffB1);
;             PG8_WAIT_V(6); PG8_BAR; PG8_MMA(1, 1, At, B1); PG8_BAR;
.LBB0_1679:
	s_add_u32 s40, s4, s38
	s_addc_u32 s41, s5, s39
	s_add_u32 s42, s40, 0x34c30100
	ds_read_b128 v[110:113], v174
	ds_read_b128 v[156:159], v174 offset:1024
	ds_read_b128 v[160:163], v174 offset:2048
	ds_read_b128 v[182:185], v174 offset:3072
	s_addc_u32 s43, s41, 0
	s_add_u32 s62, s37, s38
	s_addc_u32 s63, s60, s39
	s_cmpk_eq_i32 s38, 0xf00
	s_cselect_b64 vcc, -1, 0
	s_and_b64 s[40:41], vcc, exec
	v_cndmask_b32_e32 v150, v79, v177, vcc
	s_cselect_b32 s43, s7, s43
	s_cselect_b32 s42, s6, s42
	v_cndmask_b32_e32 v81, v80, v179, vcc
	s_cselect_b32 s41, s1, s63
	s_cselect_b32 s40, s0, s62
	v_cndmask_b32_e32 v164, v78, v178, vcc
	v_lshl_add_u64 v[96:97], v[94:95], 0, s[38:39]
	s_add_i32 m0, s47, 0xc000
	ds_read_b128 v[186:189], v175
	ds_read_b128 v[190:193], v175 offset:1024
	ds_read_b128 v[194:197], v175 offset:2048
	ds_read_b128 v[198:201], v175 offset:3072
	ds_read_b128 v[202:205], v175 offset:4096
	ds_read_b128 v[206:209], v175 offset:5120
	ds_read_b128 v[210:213], v175 offset:6144
	ds_read_b128 v[214:217], v175 offset:7168
	global_load_lds_dwordx4 v[96:97], off
	v_lshl_add_u64 v[96:97], v[88:89], 0, s[38:39]
	s_add_i32 m0, s47, 0xe000
	s_nop 0
	global_load_lds_dwordx4 v[96:97], off
	s_waitcnt lgkmcnt(8)
	s_barrier
	s_waitcnt lgkmcnt(0)
	s_waitcnt lgkmcnt(0)
	v_mfma_f32_16x16x32_bf16 v[142:145], v[110:113], v[186:189], v[142:145]
	v_mfma_f32_16x16x32_bf16 v[138:141], v[160:163], v[186:189], v[138:141]
	v_mfma_f32_16x16x32_bf16 v[134:137], v[110:113], v[194:197], v[134:137]
	v_mfma_f32_16x16x32_bf16 v[130:133], v[160:163], v[194:197], v[130:133]
	v_mfma_f32_16x16x32_bf16 v[122:125], v[110:113], v[202:205], v[122:125]
	v_mfma_f32_16x16x32_bf16 v[114:117], v[160:163], v[202:205], v[114:117]
	v_mfma_f32_16x16x32_bf16 v[102:105], v[110:113], v[210:213], v[102:105]
	v_mfma_f32_16x16x32_bf16 v[90:93], v[160:163], v[210:213], v[90:93]
	v_mfma_f32_16x16x32_bf16 v[142:145], v[156:159], v[190:193], v[142:145]
	v_mfma_f32_16x16x32_bf16 v[138:141], v[182:185], v[190:193], v[138:141]
	v_mfma_f32_16x16x32_bf16 v[134:137], v[156:159], v[198:201], v[134:137]
	v_mfma_f32_16x16x32_bf16 v[130:133], v[182:185], v[198:201], v[130:133]
	v_mfma_f32_16x16x32_bf16 v[122:125], v[156:159], v[206:209], v[122:125]
	v_mfma_f32_16x16x32_bf16 v[114:117], v[182:185], v[206:209], v[114:117]
	v_mfma_f32_16x16x32_bf16 v[102:105], v[156:159], v[214:217], v[102:105]
	v_mfma_f32_16x16x32_bf16 v[90:93], v[182:185], v[214:217], v[90:93]
	s_barrier
	s_add_i32 s62, s54, s46
	v_lshl_add_u64 v[234:235], s[40:41], 0, v[148:149]
	s_mov_b32 m0, s62
	ds_read_b128 v[218:221], v176
	ds_read_b128 v[222:225], v176 offset:1024
	ds_read_b128 v[226:229], v176 offset:2048
	ds_read_b128 v[230:233], v176 offset:3072
	global_load_lds_dwordx4 v[234:235], off
	v_lshl_add_u64 v[236:237], s[40:41], 0, v[146:147]
	s_add_i32 m0, s62, 0x2000
	s_nop 0
	global_load_lds_dwordx4 v[236:237], off
	s_barrier
	s_waitcnt lgkmcnt(0)
	s_waitcnt lgkmcnt(0)
	v_mfma_f32_16x16x32_bf16 v[126:129], v[218:221], v[186:189], v[126:129]
	v_mfma_f32_16x16x32_bf16 v[118:121], v[226:229], v[186:189], v[118:121]
	v_mfma_f32_16x16x32_bf16 v[106:109], v[218:221], v[194:197], v[106:109]
	v_mfma_f32_16x16x32_bf16 v[96:99], v[226:229], v[194:197], v[98:101]
	v_mfma_f32_16x16x32_bf16 v[82:85], v[218:221], v[202:205], v[82:85]
	v_mfma_f32_16x16x32_bf16 v[74:77], v[226:229], v[202:205], v[74:77]
	v_mfma_f32_16x16x32_bf16 v[70:73], v[218:221], v[210:213], v[70:73]
	v_mfma_f32_16x16x32_bf16 v[66:69], v[226:229], v[210:213], v[66:69]
	v_mfma_f32_16x16x32_bf16 v[126:129], v[222:225], v[190:193], v[126:129]
	v_mfma_f32_16x16x32_bf16 v[118:121], v[230:233], v[190:193], v[118:121]
	v_mfma_f32_16x16x32_bf16 v[106:109], v[222:225], v[198:201], v[106:109]
	v_mfma_f32_16x16x32_bf16 v[96:99], v[230:233], v[198:201], v[96:99]
	v_mfma_f32_16x16x32_bf16 v[82:85], v[222:225], v[206:209], v[82:85]
	v_mfma_f32_16x16x32_bf16 v[74:77], v[230:233], v[206:209], v[74:77]
	v_mfma_f32_16x16x32_bf16 v[70:73], v[222:225], v[214:217], v[70:73]
	v_mfma_f32_16x16x32_bf16 v[66:69], v[230:233], v[214:217], v[66:69]
	s_mov_b32 m0, s47
	s_barrier
	ds_read_b128 v[186:189], v175 offset:16384
	ds_read_b128 v[190:193], v175 offset:17408
	ds_read_b128 v[194:197], v175 offset:18432
	ds_read_b128 v[198:201], v175 offset:19456
	ds_read_b128 v[202:205], v175 offset:20480
	ds_read_b128 v[206:209], v175 offset:21504
	ds_read_b128 v[210:213], v175 offset:22528
	ds_read_b128 v[214:217], v175 offset:23552
	global_load_lds_dwordx4 v150, s[42:43]
	s_mov_b32 m0, s48
	v_mov_b32_e32 v165, v151
	global_load_lds_dwordx4 v164, s[42:43]
	s_barrier
	s_waitcnt lgkmcnt(0)
	v_lshl_add_u64 v[238:239], s[42:43], 0, v[150:151]
	v_lshl_add_u64 v[164:165], s[42:43], 0, v[164:165]
	s_waitcnt lgkmcnt(0)
	v_mfma_f32_16x16x32_bf16 v[62:65], v[110:113], v[186:189], v[62:65]
	v_mfma_f32_16x16x32_bf16 v[58:61], v[160:163], v[186:189], v[58:61]
	v_mfma_f32_16x16x32_bf16 v[54:57], v[110:113], v[194:197], v[54:57]
	v_mfma_f32_16x16x32_bf16 v[46:49], v[160:163], v[194:197], v[46:49]
	v_mfma_f32_16x16x32_bf16 v[38:41], v[110:113], v[202:205], v[38:41]
	v_mfma_f32_16x16x32_bf16 v[30:33], v[160:163], v[202:205], v[30:33]
	v_mfma_f32_16x16x32_bf16 v[22:25], v[110:113], v[210:213], v[22:25]
	v_mfma_f32_16x16x32_bf16 v[14:17], v[160:163], v[210:213], v[14:17]
	v_mfma_f32_16x16x32_bf16 v[62:65], v[156:159], v[190:193], v[62:65]
	v_mfma_f32_16x16x32_bf16 v[58:61], v[182:185], v[190:193], v[58:61]
	v_mfma_f32_16x16x32_bf16 v[54:57], v[156:159], v[198:201], v[54:57]
	v_mfma_f32_16x16x32_bf16 v[46:49], v[182:185], v[198:201], v[46:49]
	v_mfma_f32_16x16x32_bf16 v[38:41], v[156:159], v[206:209], v[38:41]
	v_mfma_f32_16x16x32_bf16 v[30:33], v[182:185], v[206:209], v[30:33]
	v_mfma_f32_16x16x32_bf16 v[22:25], v[156:159], v[214:217], v[22:25]
	v_mfma_f32_16x16x32_bf16 v[14:17], v[182:185], v[214:217], v[14:17]
	s_barrier
; #define PG8_STAGE(bufoff, gbase, v0, v1) do { \
;         __builtin_amdgcn_global_load_lds((const unsigned*)((const char*)(gbase) + (v0)), (LAS unsigned*)(lds + (bufoff) + ldsw), 16, 0, 0); \
;         __builtin_amdgcn_global_load_lds((const unsigned*)((const char*)(gbase) + (v1)), (LAS unsigned*)(lds + (bufoff) + ldsw + 8192), 16, 0, 0); } while (0)
; #define PG8_LDA(dst, b, h) do { _Pragma("unroll") for (int m = 0; m < 4; ++m) _Pragma("unroll") for (int k = 0; k < 2; ++k) dst[m][k] = *(const LAS bf16x8*)(lds + PG8_SA(b, h) + aoff + m * 2048 + k * 1024); } while (0)
; #define PG8_LDB(dst, b, h) do { _Pragma("unroll") for (int n = 0; n < 2; ++n) _Pragma("unroll") for (int k = 0; k < 2; ++k) dst[n][k] = *(const LAS bf16x8*)(lds + PG8_SB(b, h) + boff + n * 2048 + k * 1024); } while (0)
; #define PG8_MMA(ai, bj, At, Bt) do { __builtin_amdgcn_s_setprio(1); _Pragma("unroll") for (int m = 0; m < 4; ++m) _Pragma("unroll") for (int n = 0; n < 2; ++n) _Pragma("unroll") for (int k = 0; k < 2; ++k) \
;         acc[ai][bj][m][n] = __builtin_amdgcn_mfma_f32_16x16x32_bf16(Bt[n][k], At[m][k], acc[ai][bj][m][n], 0, 0, 0); __builtin_amdgcn_s_setprio(0); } while (0)
; #define PG8_WAIT_V(n) asm volatile("s_waitcnt vmcnt(" #n ")" ::: "memory")
; #define PG8_WAIT_L(n) asm volatile("s_waitcnt lgkmcnt(" #n ")" ::: "memory")
; #define PG8_BAR __builtin_amdgcn_s_barrier()
; #define PG8_SCHED __builtin_amdgcn_sched_barrier(0)
; template <class Epi, class Sched>
; __device__ __forceinline__ void gemm_phase(LAS unsigned char* lds, const int K, const Sched& S, const Epi& E) {
;     ...
;             PG8_STAGE(PG8_SB(0, 1), b2 + hstep, voffB0, voffB1);
;             PG8_WAIT_V(6); PG8_BAR; PG8_MMA(1, 1, At, B1); PG8_BAR;
;             PG8_LDB(B0, 1, 0); PG8_SCHED; PG8_LDA(At, 1, 0); PG8_STAGE(PG8_SA(0, 1), a2, x10, x11);
;             PG8_WAIT_L(8); PG8_BAR; PG8_WAIT_L(0); PG8_MMA(0, 0, At, B0); PG8_BAR; PG8_SCHED;
;             PG8_LDB(B1, 1, 1); PG8_STAGE(PG8_SB(1, 0), b3, voffB0, voffB1);
;             PG8_BAR; PG8_WAIT_L(0); PG8_MMA(0, 1, At, B1); PG8_BAR;
;             PG8_LDA(At, 1, 1); PG8_STAGE(PG8_SA(1, 0), a3, x00, x01);
;             PG8_BAR; PG8_WAIT_L(0); PG8_MMA(1, 0, At, B0); PG8_BAR; PG8_SCHED;
;             PG8_STAGE(PG8_SB(1, 1), b3 + hstep, voffB0, voffB1);
	s_add_u32 s62, s40, 0x80000
	s_addc_u32 s63, s41, 0
	s_add_i32 s64, s55, s46
	v_lshl_add_u64 v[100:101], s[62:63], 0, v[148:149]
	s_mov_b32 m0, s64
	s_nop 0
	global_load_lds_dwordx4 v[100:101], off
	v_lshl_add_u64 v[100:101], s[62:63], 0, v[146:147]
	s_add_i32 m0, s64, 0x2000
	s_nop 0
	global_load_lds_dwordx4 v[100:101], off
	s_waitcnt vmcnt(6)
	s_barrier
	v_mfma_f32_16x16x32_bf16 v[50:53], v[218:221], v[186:189], v[50:53]
	v_mfma_f32_16x16x32_bf16 v[42:45], v[226:229], v[186:189], v[42:45]
	v_mfma_f32_16x16x32_bf16 v[34:37], v[218:221], v[194:197], v[34:37]
	v_mfma_f32_16x16x32_bf16 v[26:29], v[226:229], v[194:197], v[26:29]
	v_mfma_f32_16x16x32_bf16 v[18:21], v[218:221], v[202:205], v[18:21]
	v_mfma_f32_16x16x32_bf16 v[10:13], v[226:229], v[202:205], v[10:13]
	v_mfma_f32_16x16x32_bf16 v[6:9], v[218:221], v[210:213], v[6:9]
	v_mfma_f32_16x16x32_bf16 v[2:5], v[226:229], v[210:213], v[2:5]
	v_mfma_f32_16x16x32_bf16 v[50:53], v[222:225], v[190:193], v[50:53]
	v_mfma_f32_16x16x32_bf16 v[42:45], v[230:233], v[190:193], v[42:45]
	v_mfma_f32_16x16x32_bf16 v[34:37], v[222:225], v[198:201], v[34:37]
	v_mfma_f32_16x16x32_bf16 v[26:29], v[230:233], v[198:201], v[26:29]
	v_mfma_f32_16x16x32_bf16 v[18:21], v[222:225], v[206:209], v[18:21]
	v_mfma_f32_16x16x32_bf16 v[10:13], v[230:233], v[206:209], v[10:13]
	v_mfma_f32_16x16x32_bf16 v[6:9], v[222:225], v[214:217], v[6:9]
	v_mfma_f32_16x16x32_bf16 v[2:5], v[230:233], v[214:217], v[2:5]
	s_add_i32 s62, 0, 0x18000
	v_add_u32_e32 v87, s62, v172
	s_barrier
	ds_read_b128 v[110:113], v87
	ds_read_b128 v[156:159], v87 offset:1024
	ds_read_b128 v[160:163], v87 offset:2048
	ds_read_b128 v[182:185], v87 offset:3072
	s_mov_b32 m0, s49
	ds_read_b128 v[186:189], v175 offset:32768
	ds_read_b128 v[190:193], v175 offset:33792
	ds_read_b128 v[194:197], v175 offset:34816
	ds_read_b128 v[198:201], v175 offset:35840
	ds_read_b128 v[202:205], v175 offset:36864
	ds_read_b128 v[206:209], v175 offset:37888
	ds_read_b128 v[210:213], v175 offset:38912
	ds_read_b128 v[214:217], v175 offset:39936
	v_cndmask_b32_e32 v87, v86, v180, vcc
	global_load_lds_dwordx4 v81, s[42:43]
	s_mov_b32 m0, s50
	s_nop 0
	global_load_lds_dwordx4 v87, s[42:43]
	s_waitcnt lgkmcnt(8)
	s_barrier
	s_waitcnt lgkmcnt(0)
	s_waitcnt lgkmcnt(0)
	v_mfma_f32_16x16x32_bf16 v[142:145], v[110:113], v[186:189], v[142:145]
	v_mfma_f32_16x16x32_bf16 v[138:141], v[160:163], v[186:189], v[138:141]
	v_mfma_f32_16x16x32_bf16 v[134:137], v[110:113], v[194:197], v[134:137]
	v_mfma_f32_16x16x32_bf16 v[130:133], v[160:163], v[194:197], v[130:133]
	v_mfma_f32_16x16x32_bf16 v[122:125], v[110:113], v[202:205], v[122:125]
	v_mfma_f32_16x16x32_bf16 v[114:117], v[160:163], v[202:205], v[114:117]
	v_mfma_f32_16x16x32_bf16 v[100:103], v[110:113], v[210:213], v[102:105]
	v_mfma_f32_16x16x32_bf16 v[90:93], v[160:163], v[210:213], v[90:93]
	v_mfma_f32_16x16x32_bf16 v[142:145], v[156:159], v[190:193], v[142:145]
	v_mfma_f32_16x16x32_bf16 v[138:141], v[182:185], v[190:193], v[138:141]
	v_mfma_f32_16x16x32_bf16 v[134:137], v[156:159], v[198:201], v[134:137]
	v_mfma_f32_16x16x32_bf16 v[130:133], v[182:185], v[198:201], v[130:133]
	v_mfma_f32_16x16x32_bf16 v[122:125], v[156:159], v[206:209], v[122:125]
	v_mfma_f32_16x16x32_bf16 v[114:117], v[182:185], v[206:209], v[114:117]
	v_mfma_f32_16x16x32_bf16 v[102:105], v[156:159], v[214:217], v[100:103]
	v_mfma_f32_16x16x32_bf16 v[90:93], v[182:185], v[214:217], v[90:93]
	s_barrier
	s_add_i32 s42, 0, 0x1c000
	s_add_i32 s43, s62, s46
	v_add_u32_e32 v81, s42, v172
	v_lshl_add_u64 v[100:101], v[234:235], 0, s[18:19]
	s_mov_b32 m0, s43
	ds_read_b128 v[218:221], v81
	ds_read_b128 v[222:225], v81 offset:1024
	ds_read_b128 v[226:229], v81 offset:2048
	ds_read_b128 v[230:233], v81 offset:3072
	global_load_lds_dwordx4 v[100:101], off
	v_lshl_add_u64 v[100:101], v[236:237], 0, s[18:19]
	s_add_i32 m0, s43, 0x2000
	s_nop 0
	global_load_lds_dwordx4 v[100:101], off
	s_barrier
	s_waitcnt lgkmcnt(0)
	s_waitcnt lgkmcnt(0)
	v_mfma_f32_16x16x32_bf16 v[126:129], v[218:221], v[186:189], v[126:129]
	v_mfma_f32_16x16x32_bf16 v[118:121], v[226:229], v[186:189], v[118:121]
	v_mfma_f32_16x16x32_bf16 v[106:109], v[218:221], v[194:197], v[106:109]
	v_mfma_f32_16x16x32_bf16 v[96:99], v[226:229], v[194:197], v[96:99]
	v_mfma_f32_16x16x32_bf16 v[82:85], v[218:221], v[202:205], v[82:85]
	v_mfma_f32_16x16x32_bf16 v[74:77], v[226:229], v[202:205], v[74:77]
	v_mfma_f32_16x16x32_bf16 v[70:73], v[218:221], v[210:213], v[70:73]
	v_mfma_f32_16x16x32_bf16 v[66:69], v[226:229], v[210:213], v[66:69]
	v_mfma_f32_16x16x32_bf16 v[126:129], v[222:225], v[190:193], v[126:129]
	v_mfma_f32_16x16x32_bf16 v[118:121], v[230:233], v[190:193], v[118:121]
	v_mfma_f32_16x16x32_bf16 v[106:109], v[222:225], v[198:201], v[106:109]
	v_mfma_f32_16x16x32_bf16 v[98:101], v[230:233], v[198:201], v[96:99]
	v_mfma_f32_16x16x32_bf16 v[82:85], v[222:225], v[206:209], v[82:85]
	v_mfma_f32_16x16x32_bf16 v[74:77], v[230:233], v[206:209], v[74:77]
	v_mfma_f32_16x16x32_bf16 v[70:73], v[222:225], v[214:217], v[70:73]
	v_mfma_f32_16x16x32_bf16 v[66:69], v[230:233], v[214:217], v[66:69]
	s_mov_b32 m0, s52
	v_lshl_add_u64 v[96:97], v[238:239], 0, s[18:19]
	s_barrier
	ds_read_b128 v[186:189], v175 offset:49152
	ds_read_b128 v[190:193], v175 offset:50176
	ds_read_b128 v[194:197], v175 offset:51200
	ds_read_b128 v[198:201], v175 offset:52224
	ds_read_b128 v[202:205], v175 offset:53248
	ds_read_b128 v[206:209], v175 offset:54272
	ds_read_b128 v[210:213], v175 offset:55296
	ds_read_b128 v[214:217], v175 offset:56320
	global_load_lds_dwordx4 v[96:97], off
	v_lshl_add_u64 v[96:97], v[164:165], 0, s[18:19]
	s_mov_b32 m0, s53
	s_nop 0
	global_load_lds_dwordx4 v[96:97], off
	s_barrier
; #define PG8_STAGE(bufoff, gbase, v0, v1) do { \
;         __builtin_amdgcn_global_load_lds((const unsigned*)((const char*)(gbase) + (v0)), (LAS unsigned*)(lds + (bufoff) + ldsw), 16, 0, 0); \
;         __builtin_amdgcn_global_load_lds((const unsigned*)((const char*)(gbase) + (v1)), (LAS unsigned*)(lds + (bufoff) + ldsw + 8192), 16, 0, 0); } while (0)
; #define PG8_LDA(dst, b, h) do { _Pragma("unroll") for (int m = 0; m < 4; ++m) _Pragma("unroll") for (int k = 0; k < 2; ++k) dst[m][k] = *(const LAS bf16x8*)(lds + PG8_SA(b, h) + aoff + m * 2048 + k * 1024); } while (0)
; #define PG8_MMA(ai, bj, At, Bt) do { __builtin_amdgcn_s_setprio(1); _Pragma("unroll") for (int m = 0; m < 4; ++m) _Pragma("unroll") for (int n = 0; n < 2; ++n) _Pragma("unroll") for (int k = 0; k < 2; ++k) \
;         acc[ai][bj][m][n] = __builtin_amdgcn_mfma_f32_16x16x32_bf16(Bt[n][k], At[m][k], acc[ai][bj][m][n], 0, 0, 0); __builtin_amdgcn_s_setprio(0); } while (0)
; #define PG8_WAIT_V(n) asm volatile("s_waitcnt vmcnt(" #n ")" ::: "memory")
; #define PG8_WAIT_L(n) asm volatile("s_waitcnt lgkmcnt(" #n ")" ::: "memory")
; template <class Epi, class Sched>
; __device__ __forceinline__ void gemm_phase(LAS unsigned char* lds, const int K, const Sched& S, const Epi& E) {
;     ...
;             PG8_LDA(At, 1, 1); PG8_STAGE(PG8_SA(1, 0), a3, x00, x01);
;             PG8_BAR; PG8_WAIT_L(0); PG8_MMA(1, 0, At, B0); PG8_BAR; PG8_SCHED;
;             PG8_STAGE(PG8_SB(1, 1), b3 + hstep, voffB0, voffB1);
;             PG8_WAIT_V(6); PG8_BAR; PG8_MMA(1, 1, At, B1); PG8_BAR;
;     __device__ __forceinline__ void operator()(const f32x4 (&acc)[2][2][4][2], const Unit& u, int wr, int wc, int fr, int fq) const {
;         const int row0 = u.rbase + wr * 64 + fr, col0 = u.pn * BM + wc * 32 + 4 * fq;
;         f32x4 gv[2][2];
; #pragma unroll
;         for (int bj = 0; bj < 2; ++bj)
; #pragma unroll
;             for (int n = 0; n < 2; ++n) gv[bj][n] = *(const f32x4*)(gate + col0 + bj * HALF + n * 16);
; #pragma unroll
;         for (int ai = 0; ai < 2; ++ai) {
;             f32x4 xv[4][2][2];
; #pragma unroll
;             for (int m = 0; m < 4; ++m) { const size_t ro = (size_t)(row0 + ai * HALF + m * 16) * D + col0;
; #pragma unroll
;                 for (int bj = 0; bj < 2; ++bj)
; #pragma unroll
;                     for (int n = 0; n < 2; ++n) xv[m][bj][n] = *(const f32x4*)(xin + ro + bj * HALF + n * 16); }
	s_waitcnt lgkmcnt(0)
	s_waitcnt lgkmcnt(0)
	v_mfma_f32_16x16x32_bf16 v[62:65], v[110:113], v[186:189], v[62:65]
	v_mfma_f32_16x16x32_bf16 v[58:61], v[160:163], v[186:189], v[58:61]
	v_mfma_f32_16x16x32_bf16 v[54:57], v[110:113], v[194:197], v[54:57]
	v_mfma_f32_16x16x32_bf16 v[46:49], v[160:163], v[194:197], v[46:49]
	v_mfma_f32_16x16x32_bf16 v[38:41], v[110:113], v[202:205], v[38:41]
	v_mfma_f32_16x16x32_bf16 v[30:33], v[160:163], v[202:205], v[30:33]
	v_mfma_f32_16x16x32_bf16 v[22:25], v[110:113], v[210:213], v[22:25]
	v_mfma_f32_16x16x32_bf16 v[14:17], v[160:163], v[210:213], v[14:17]
	v_mfma_f32_16x16x32_bf16 v[62:65], v[156:159], v[190:193], v[62:65]
	v_mfma_f32_16x16x32_bf16 v[58:61], v[182:185], v[190:193], v[58:61]
	v_mfma_f32_16x16x32_bf16 v[54:57], v[156:159], v[198:201], v[54:57]
	v_mfma_f32_16x16x32_bf16 v[46:49], v[182:185], v[198:201], v[46:49]
	v_mfma_f32_16x16x32_bf16 v[38:41], v[156:159], v[206:209], v[38:41]
	v_mfma_f32_16x16x32_bf16 v[30:33], v[182:185], v[206:209], v[30:33]
	v_mfma_f32_16x16x32_bf16 v[22:25], v[156:159], v[214:217], v[22:25]
	v_mfma_f32_16x16x32_bf16 v[14:17], v[182:185], v[214:217], v[14:17]
	s_barrier
	s_add_u32 s40, s40, 0x80080
	s_addc_u32 s41, s41, 0
	s_add_i32 s42, s42, s46
	v_lshl_add_u64 v[96:97], s[40:41], 0, v[148:149]
	s_mov_b32 m0, s42
	s_nop 0
	global_load_lds_dwordx4 v[96:97], off
	v_lshl_add_u64 v[96:97], s[40:41], 0, v[146:147]
	s_add_i32 m0, s42, 0x2000
	s_nop 0
	global_load_lds_dwordx4 v[96:97], off
	s_waitcnt vmcnt(6)
	s_barrier
	v_mfma_f32_16x16x32_bf16 v[50:53], v[218:221], v[186:189], v[50:53]
	v_mfma_f32_16x16x32_bf16 v[42:45], v[226:229], v[186:189], v[42:45]
	v_mfma_f32_16x16x32_bf16 v[34:37], v[218:221], v[194:197], v[34:37]
	v_mfma_f32_16x16x32_bf16 v[26:29], v[226:229], v[194:197], v[26:29]
	v_mfma_f32_16x16x32_bf16 v[18:21], v[218:221], v[202:205], v[18:21]
	v_mfma_f32_16x16x32_bf16 v[10:13], v[226:229], v[202:205], v[10:13]
	v_mfma_f32_16x16x32_bf16 v[6:9], v[218:221], v[210:213], v[6:9]
	v_mfma_f32_16x16x32_bf16 v[2:5], v[226:229], v[210:213], v[2:5]
	v_mfma_f32_16x16x32_bf16 v[50:53], v[222:225], v[190:193], v[50:53]
	v_mfma_f32_16x16x32_bf16 v[42:45], v[230:233], v[190:193], v[42:45]
	v_mfma_f32_16x16x32_bf16 v[34:37], v[222:225], v[198:201], v[34:37]
	v_mfma_f32_16x16x32_bf16 v[26:29], v[230:233], v[198:201], v[26:29]
	v_mfma_f32_16x16x32_bf16 v[18:21], v[222:225], v[206:209], v[18:21]
	v_mfma_f32_16x16x32_bf16 v[10:13], v[230:233], v[206:209], v[10:13]
	v_mfma_f32_16x16x32_bf16 v[6:9], v[222:225], v[214:217], v[6:9]
	v_mfma_f32_16x16x32_bf16 v[2:5], v[230:233], v[214:217], v[2:5]
	s_add_i32 s61, s61, 2
	s_add_u32 s38, s38, 0x100
	s_addc_u32 s39, s39, 0
	s_cmp_gt_u32 s61, 29
	s_barrier
	s_cbranch_scc0 .LBB0_1679
	v_lshl_or_b32 v78, s59, 8, v173
	v_ashrrev_i32_e32 v79, 31, v78
	v_add_u32_e32 v160, s58, v171
	v_lshlrev_b64 v[156:157], 2, v[78:79]
	v_ashrrev_i32_e32 v161, 31, v160
	v_lshl_add_u64 v[158:159], s[10:11], 0, v[156:157]
	v_lshlrev_b64 v[160:161], 13, v[160:161]
	v_lshl_add_u64 v[78:79], s[14:15], 0, v[156:157]
	v_lshl_add_u64 v[190:191], v[158:159], 0, v[160:161]
	global_load_dwordx4 v[110:113], v[78:79], off
	global_load_dwordx4 v[94:97], v[78:79], off offset:64
	global_load_dwordx4 v[86:89], v[78:79], off offset:512
	s_nop 0
	global_load_dwordx4 v[78:81], v[78:79], off offset:576
	s_nop 0
	global_load_dwordx4 v[162:165], v[190:191], off
	global_load_dwordx4 v[182:185], v[190:191], off offset:64
	global_load_dwordx4 v[186:189], v[190:191], off offset:512
	s_nop 0
	global_load_dwordx4 v[190:193], v[190:191], off offset:576
	v_lshl_add_u64 v[242:243], v[160:161], 0, s[20:21]
	v_lshl_add_u64 v[206:207], v[158:159], 0, v[242:243]
	global_load_dwordx4 v[194:197], v[206:207], off
	global_load_dwordx4 v[198:201], v[206:207], off offset:64
	global_load_dwordx4 v[202:205], v[206:207], off offset:512
	s_nop 0
	global_load_dwordx4 v[206:209], v[206:207], off offset:576
	v_lshl_add_u64 v[244:245], v[160:161], 0, s[22:23]
	v_lshl_add_u64 v[222:223], v[158:159], 0, v[244:245]
	global_load_dwordx4 v[210:213], v[222:223], off
	global_load_dwordx4 v[214:217], v[222:223], off offset:64
	global_load_dwordx4 v[218:221], v[222:223], off offset:512
	s_nop 0
	global_load_dwordx4 v[222:225], v[222:223], off offset:576
	v_lshl_add_u64 v[246:247], v[160:161], 0, s[24:25]
	v_lshl_add_u64 v[238:239], v[158:159], 0, v[246:247]
	global_load_dwordx4 v[226:229], v[238:239], off
	global_load_dwordx4 v[230:233], v[238:239], off offset:64
	global_load_dwordx4 v[234:237], v[238:239], off offset:512
	s_nop 0
	global_load_dwordx4 v[238:241], v[238:239], off offset:576
	s_and_b64 vcc, exec, s[2:3]
	s_mov_b32 s59, s36
	s_mov_b32 s58, s56
	s_mov_b64 s[38:39], s[0:1]
	s_waitcnt vmcnt(0)
;     __device__ __forceinline__ void operator()(const f32x4 (&acc)[2][2][4][2], const Unit& u, int wr, int wc, int fr, int fq) const {
;     ...
;         for (int ai = 0; ai < 2; ++ai) {
;             f32x4 xv[4][2][2];
; #pragma unroll
;             for (int m = 0; m < 4; ++m) { const size_t ro = (size_t)(row0 + ai * HALF + m * 16) * D + col0;
; #pragma unroll
;                 for (int bj = 0; bj < 2; ++bj)
; #pragma unroll
;                     for (int n = 0; n < 2; ++n) xv[m][bj][n] = *(const f32x4*)(xin + ro + bj * HALF + n * 16); }
; #pragma unroll
;             for (int m = 0; m < 4; ++m) { const size_t ro = (size_t)(row0 + ai * HALF + m * 16) * D + col0;
; #pragma unroll
;                 for (int bj = 0; bj < 2; ++bj)
; #pragma unroll
;                     for (int n = 0; n < 2; ++n) *(f32x4*)(out + ro + bj * HALF + n * 16) = xv[m][bj][n] + gv[bj][n] * acc[ai][bj][m][n]; }
	v_pk_fma_f32 v[142:143], v[142:143], v[110:111], v[162:163]
	v_lshl_add_u64 v[162:163], s[12:13], 0, v[160:161]
	v_lshl_add_u64 v[162:163], v[162:163], 0, v[156:157]
	v_pk_fma_f32 v[128:129], v[128:129], v[88:89], v[188:189]
	v_pk_fma_f32 v[126:127], v[126:127], v[86:87], v[186:187]
	global_store_dwordx4 v[162:163], v[126:129], off offset:512
	v_pk_fma_f32 v[108:109], v[108:109], v[88:89], v[204:205]
	v_pk_fma_f32 v[106:107], v[106:107], v[86:87], v[202:203]
	v_lshl_add_u64 v[126:127], s[12:13], 0, v[242:243]
	v_lshl_add_u64 v[126:127], v[126:127], 0, v[156:157]
	global_store_dwordx4 v[126:127], v[106:109], off offset:512
	v_pk_fma_f32 v[84:85], v[84:85], v[88:89], v[220:221]
	v_pk_fma_f32 v[82:83], v[82:83], v[86:87], v[218:219]
	v_lshl_add_u64 v[106:107], s[12:13], 0, v[244:245]
	v_lshl_add_u64 v[106:107], v[106:107], 0, v[156:157]
	v_pk_fma_f32 v[120:121], v[120:121], v[80:81], v[192:193]
	v_pk_fma_f32 v[118:119], v[118:119], v[78:79], v[190:191]
	v_pk_fma_f32 v[100:101], v[100:101], v[80:81], v[208:209]
	v_pk_fma_f32 v[98:99], v[98:99], v[78:79], v[206:207]
	global_store_dwordx4 v[106:107], v[82:85], off offset:512
	v_pk_fma_f32 v[76:77], v[76:77], v[80:81], v[224:225]
	v_pk_fma_f32 v[74:75], v[74:75], v[78:79], v[222:223]
	v_lshl_add_u64 v[82:83], s[12:13], 0, v[246:247]
	global_store_dwordx4 v[162:163], v[118:121], off offset:576
	global_store_dwordx4 v[126:127], v[98:101], off offset:576
	global_store_dwordx4 v[106:107], v[74:77], off offset:576
	v_pk_fma_f32 v[120:121], v[136:137], v[112:113], v[196:197]
	v_pk_fma_f32 v[118:119], v[134:135], v[110:111], v[194:195]
	v_pk_fma_f32 v[100:101], v[124:125], v[112:113], v[212:213]
	v_pk_fma_f32 v[98:99], v[122:123], v[110:111], v[210:211]
	v_pk_fma_f32 v[76:77], v[104:105], v[112:113], v[228:229]
	v_pk_fma_f32 v[74:75], v[102:103], v[110:111], v[226:227]
	v_lshl_add_u64 v[82:83], v[82:83], 0, v[156:157]
	v_pk_fma_f32 v[144:145], v[144:145], v[112:113], v[164:165]
	v_pk_fma_f32 v[140:141], v[140:141], v[96:97], v[184:185]
	v_pk_fma_f32 v[138:139], v[138:139], v[94:95], v[182:183]
	global_store_dwordx4 v[126:127], v[118:121], off
	global_store_dwordx4 v[106:107], v[98:101], off
	global_store_dwordx4 v[82:83], v[74:77], off
	v_pk_fma_f32 v[120:121], v[132:133], v[96:97], v[200:201]
	v_pk_fma_f32 v[118:119], v[130:131], v[94:95], v[198:199]
	v_pk_fma_f32 v[100:101], v[116:117], v[96:97], v[216:217]
	v_pk_fma_f32 v[98:99], v[114:115], v[94:95], v[214:215]
	v_pk_fma_f32 v[76:77], v[92:93], v[96:97], v[232:233]
	v_pk_fma_f32 v[74:75], v[90:91], v[94:95], v[230:231]
	v_pk_fma_f32 v[72:73], v[72:73], v[88:89], v[236:237]
	v_pk_fma_f32 v[70:71], v[70:71], v[86:87], v[234:235]
	v_pk_fma_f32 v[68:69], v[68:69], v[80:81], v[240:241]
	v_pk_fma_f32 v[66:67], v[66:67], v[78:79], v[238:239]
	v_lshl_add_u64 v[164:165], v[160:161], 0, s[26:27]
	global_store_dwordx4 v[162:163], v[142:145], off
	global_store_dwordx4 v[162:163], v[138:141], off offset:64
	global_store_dwordx4 v[126:127], v[118:121], off offset:64
	global_store_dwordx4 v[106:107], v[98:101], off offset:64
	global_store_dwordx4 v[82:83], v[74:77], off offset:64
	global_store_dwordx4 v[82:83], v[70:73], off offset:512
	global_store_dwordx4 v[82:83], v[66:69], off offset:576
	v_lshl_add_u64 v[162:163], v[160:161], 0, s[28:29]
	v_lshl_add_u64 v[142:143], v[160:161], 0, s[30:31]
	v_lshl_add_u64 v[66:67], v[158:159], 0, v[164:165]
	global_load_dwordx4 v[130:133], v[66:67], off
	global_load_dwordx4 v[122:125], v[66:67], off offset:64
	global_load_dwordx4 v[118:121], v[66:67], off offset:512
	global_load_dwordx4 v[106:109], v[66:67], off offset:576
	v_lshl_add_u64 v[66:67], v[158:159], 0, v[162:163]
	global_load_dwordx4 v[114:117], v[66:67], off
	global_load_dwordx4 v[102:105], v[66:67], off offset:64
	global_load_dwordx4 v[90:93], v[66:67], off offset:512
	global_load_dwordx4 v[74:77], v[66:67], off offset:576
	v_lshl_add_u64 v[66:67], v[158:159], 0, v[142:143]
	global_load_dwordx4 v[98:101], v[66:67], off
	global_load_dwordx4 v[82:85], v[66:67], off offset:64
	global_load_dwordx4 v[70:73], v[66:67], off offset:512
	s_nop 0
	global_load_dwordx4 v[66:69], v[66:67], off offset:576
	v_lshl_add_u64 v[144:145], v[160:161], 0, s[34:35]
	v_lshl_add_u64 v[138:139], v[158:159], 0, v[144:145]
	global_load_dwordx4 v[158:161], v[138:139], off
	global_load_dwordx4 v[134:137], v[138:139], off offset:64
	global_load_dwordx4 v[126:129], v[138:139], off offset:512
	s_nop 0
	global_load_dwordx4 v[138:141], v[138:139], off offset:576
	s_waitcnt vmcnt(0)
; #define PG8_WAIT_V(n) asm volatile("s_waitcnt vmcnt(" #n ")" ::: "memory")
; #define PG8_BAR __builtin_amdgcn_s_barrier()
; template <class Epi, class Sched>
; __device__ __forceinline__ void gemm_phase(LAS unsigned char* lds, const int K, const Sched& S, const Epi& E) {
;     ...
;         if (!has_next) break;
; #pragma unroll
;         for (int a = 0; a < 2; ++a)
; #pragma unroll
;             for (int b = 0; b < 2; ++b)
; #pragma unroll
;                 for (int m = 0; m < 4; ++m)
; #pragma unroll
;                     for (int n = 0; n < 2; ++n) acc[a][b][m][n] = (f32x4){0.f, 0.f, 0.f, 0.f};
;         cur = nxt; cB = nB; c00 = n00; c01 = n01; c10 = n10; c11 = n11; ++ui;
;     }
;     PG8_WAIT_V(0);
;     if (wr == 0) PG8_BAR;
;     PG8_BAR;
;     __device__ __forceinline__ void operator()(const f32x4 (&acc)[2][2][4][2], const Unit& u, int wr, int wc, int fr, int fq) const {
;     ...
;             for (int m = 0; m < 4; ++m) { const size_t ro = (size_t)(row0 + ai * HALF + m * 16) * D + col0;
; #pragma unroll
;                 for (int bj = 0; bj < 2; ++bj)
; #pragma unroll
;                     for (int n = 0; n < 2; ++n) *(f32x4*)(out + ro + bj * HALF + n * 16) = xv[m][bj][n] + gv[bj][n] * acc[ai][bj][m][n]; }
	v_pk_fma_f32 v[62:63], v[62:63], v[110:111], v[130:131]
	v_lshl_add_u64 v[130:131], s[12:13], 0, v[164:165]
	v_lshl_add_u64 v[130:131], v[130:131], 0, v[156:157]
	v_pk_fma_f32 v[52:53], v[52:53], v[88:89], v[120:121]
	v_pk_fma_f32 v[50:51], v[50:51], v[86:87], v[118:119]
	global_store_dwordx4 v[130:131], v[50:53], off offset:512
	v_pk_fma_f32 v[36:37], v[36:37], v[88:89], v[92:93]
	v_pk_fma_f32 v[34:35], v[34:35], v[86:87], v[90:91]
	v_lshl_add_u64 v[50:51], s[12:13], 0, v[162:163]
	v_lshl_add_u64 v[50:51], v[50:51], 0, v[156:157]
	global_store_dwordx4 v[50:51], v[34:37], off offset:512
	v_pk_fma_f32 v[20:21], v[20:21], v[88:89], v[72:73]
	v_pk_fma_f32 v[18:19], v[18:19], v[86:87], v[70:71]
	v_lshl_add_u64 v[34:35], s[12:13], 0, v[142:143]
	v_lshl_add_u64 v[34:35], v[34:35], 0, v[156:157]
	v_pk_fma_f32 v[44:45], v[44:45], v[80:81], v[108:109]
	v_pk_fma_f32 v[42:43], v[42:43], v[78:79], v[106:107]
	v_pk_fma_f32 v[28:29], v[28:29], v[80:81], v[76:77]
	v_pk_fma_f32 v[26:27], v[26:27], v[78:79], v[74:75]
	global_store_dwordx4 v[34:35], v[18:21], off offset:512
	v_pk_fma_f32 v[12:13], v[12:13], v[80:81], v[68:69]
	v_pk_fma_f32 v[10:11], v[10:11], v[78:79], v[66:67]
	v_lshl_add_u64 v[18:19], s[12:13], 0, v[144:145]
	global_store_dwordx4 v[130:131], v[42:45], off offset:576
	global_store_dwordx4 v[50:51], v[26:29], off offset:576
	global_store_dwordx4 v[34:35], v[10:13], off offset:576
	v_pk_fma_f32 v[44:45], v[56:57], v[112:113], v[116:117]
	v_pk_fma_f32 v[42:43], v[54:55], v[110:111], v[114:115]
	v_pk_fma_f32 v[28:29], v[40:41], v[112:113], v[100:101]
	v_pk_fma_f32 v[26:27], v[38:39], v[110:111], v[98:99]
	v_pk_fma_f32 v[12:13], v[24:25], v[112:113], v[160:161]
	v_pk_fma_f32 v[10:11], v[22:23], v[110:111], v[158:159]
	v_lshl_add_u64 v[18:19], v[18:19], 0, v[156:157]
	v_pk_fma_f32 v[64:65], v[64:65], v[112:113], v[132:133]
	v_pk_fma_f32 v[60:61], v[60:61], v[96:97], v[124:125]
	v_pk_fma_f32 v[58:59], v[58:59], v[94:95], v[122:123]
	global_store_dwordx4 v[50:51], v[42:45], off
	global_store_dwordx4 v[34:35], v[26:29], off
	global_store_dwordx4 v[18:19], v[10:13], off
	v_pk_fma_f32 v[44:45], v[48:49], v[96:97], v[104:105]
	v_pk_fma_f32 v[42:43], v[46:47], v[94:95], v[102:103]
	v_pk_fma_f32 v[28:29], v[32:33], v[96:97], v[84:85]
	v_pk_fma_f32 v[26:27], v[30:31], v[94:95], v[82:83]
	v_pk_fma_f32 v[12:13], v[16:17], v[96:97], v[136:137]
	v_pk_fma_f32 v[10:11], v[14:15], v[94:95], v[134:135]
	v_pk_fma_f32 v[8:9], v[8:9], v[88:89], v[128:129]
	v_pk_fma_f32 v[6:7], v[6:7], v[86:87], v[126:127]
	v_pk_fma_f32 v[4:5], v[4:5], v[80:81], v[140:141]
	v_pk_fma_f32 v[2:3], v[2:3], v[78:79], v[138:139]
	v_mov_b32_e32 v79, v177
	v_mov_b32_e32 v78, v178
	v_mov_b32_e32 v80, v179
	v_mov_b32_e32 v86, v180
	global_store_dwordx4 v[130:131], v[62:65], off
	global_store_dwordx4 v[130:131], v[58:61], off offset:64
	global_store_dwordx4 v[50:51], v[42:45], off offset:64
	global_store_dwordx4 v[34:35], v[26:29], off offset:64
	global_store_dwordx4 v[18:19], v[10:13], off offset:64
	global_store_dwordx4 v[18:19], v[6:9], off offset:512
	global_store_dwordx4 v[18:19], v[2:5], off offset:576
	s_cbranch_vccz .LBB0_1670
	s_waitcnt vmcnt(0)
	s_cmpk_gt_u32 s33, 0xff
	s_cbranch_scc1 .LBB0_1683
	s_barrier

; #define PG8_STAGE(bufoff, gbase, v0, v1) do { \
;         __builtin_amdgcn_global_load_lds((const unsigned*)((const char*)(gbase) + (v0)), (LAS unsigned*)(lds + (bufoff) + ldsw), 16, 0, 0); \
;         __builtin_amdgcn_global_load_lds((const unsigned*)((const char*)(gbase) + (v1)), (LAS unsigned*)(lds + (bufoff) + ldsw + 8192), 16, 0, 0); } while (0)
; #define PG8_LDA(dst, b, h) do { _Pragma("unroll") for (int m = 0; m < 4; ++m) _Pragma("unroll") for (int k = 0; k < 2; ++k) dst[m][k] = *(const LAS bf16x8*)(lds + PG8_SA(b, h) + aoff + m * 2048 + k * 1024); } while (0)
; #define PG8_LDB(dst, b, h) do { _Pragma("unroll") for (int n = 0; n < 2; ++n) _Pragma("unroll") for (int k = 0; k < 2; ++k) dst[n][k] = *(const LAS bf16x8*)(lds + PG8_SB(b, h) + boff + n * 2048 + k * 1024); } while (0)
; #define PG8_WAIT_V(n) asm volatile("s_waitcnt vmcnt(" #n ")" ::: "memory")
; #define PG8_WAIT_L(n) asm volatile("s_waitcnt lgkmcnt(" #n ")" ::: "memory")
; #define PG8_BAR __builtin_amdgcn_s_barrier()
; #define PG8_SCHED __builtin_amdgcn_sched_barrier(0)
; template <class Epi, class Sched>
; __device__ __forceinline__ void gemm_phase(LAS unsigned char* lds, const int K, const Sched& S, const Epi& E) {
;     ...
;         for (int t = 0; t < nt; t += 2) {
;             const bool last = (t == nt - 2);
;             const char* a1 = gA + (size_t)(t + 1) * kstep;
;             const char* a2 = last ? gA : gA + (size_t)(t + 2) * kstep; const char* b2 = last ? nB : cB + (size_t)(t + 2) * kstepB;
;             const char* a3 = a2 + kstep; const char* b3 = b2 + kstepB;
;             const unsigned x00 = last ? n00 : c00, x01 = last ? n01 : c01, x10 = last ? n10 : c10, x11 = last ? n11 : c11;
;             PG8_LDB(B0, 0, 0); PG8_SCHED; PG8_LDA(At, 0, 0); PG8_STAGE(PG8_SA(1, 1), a1, c10, c11);
;             PG8_WAIT_L(8); PG8_BAR; PG8_WAIT_L(0); PG8_MMA(0, 0, At, B0); PG8_BAR; PG8_SCHED;
;             PG8_LDB(B1, 0, 1); PG8_STAGE(PG8_SB(0, 0), b2, voffB0, voffB1);
;             PG8_BAR; PG8_WAIT_L(0); PG8_MMA(0, 1, At, B1); PG8_BAR;
;             PG8_LDA(At, 0, 1); PG8_STAGE(PG8_SA(0, 0), a2, x00, x01);
;             PG8_BAR; PG8_WAIT_L(0); PG8_MMA(1, 0, At, B0); PG8_BAR; PG8_SCHED;
;             PG8_STAGE(PG8_SB(0, 1), b2 + hstep, voffB0, voffB1);
;             PG8_WAIT_V(6); PG8_BAR; PG8_MMA(1, 1, At, B1); PG8_BAR;
.LBB0_1831:
	v_add_u32_e32 v139, s46, v149
	s_add_u32 s22, s0, s20
	ds_read_b128 v[160:163], v139
	ds_read_b128 v[164:167], v139 offset:1024
	ds_read_b128 v[168:171], v139 offset:2048
	ds_read_b128 v[172:175], v139 offset:3072
	s_addc_u32 s23, s1, s21
	s_add_u32 s24, s22, 0x34c30100
	s_addc_u32 s25, s23, 0
	s_cmpk_eq_i32 s20, 0xf00
	s_cselect_b64 vcc, -1, 0
	s_and_b64 s[22:23], vcc, exec
	v_cndmask_b32_e32 v134, v158, v156, vcc
	s_cselect_b32 s27, s3, s25
	s_cselect_b32 s26, s2, s24
	v_cndmask_b32_e32 v139, v138, v154, vcc
	s_cselect_b32 s23, s19, s15
	s_cselect_b32 s22, s18, s13
	v_cndmask_b32_e32 v224, v136, v155, vcc
	s_add_u32 s24, s22, 0x20000
	s_addc_u32 s25, s23, 0
	v_lshl_add_u64 v[208:209], v[144:145], 0, s[20:21]
	s_add_i32 m0, s37, 0xc000
	ds_read_b128 v[176:179], v151
	ds_read_b128 v[180:183], v151 offset:1024
	ds_read_b128 v[184:187], v151 offset:2048
	ds_read_b128 v[188:191], v151 offset:3072
	ds_read_b128 v[192:195], v151 offset:4096
	ds_read_b128 v[196:199], v151 offset:5120
	ds_read_b128 v[200:203], v151 offset:6144
	ds_read_b128 v[204:207], v151 offset:7168
	global_load_lds_dwordx4 v[208:209], off
	v_lshl_add_u64 v[208:209], v[142:143], 0, s[20:21]
	s_add_i32 m0, s37, 0xe000
	s_nop 0
	global_load_lds_dwordx4 v[208:209], off
	s_waitcnt lgkmcnt(8)
	s_barrier
	s_waitcnt lgkmcnt(0)
	s_waitcnt lgkmcnt(0)
	v_mfma_f32_16x16x32_bf16 v[126:129], v[160:163], v[176:179], v[126:129]
	v_mfma_f32_16x16x32_bf16 v[122:125], v[168:171], v[176:179], v[122:125]
	v_mfma_f32_16x16x32_bf16 v[110:113], v[160:163], v[184:187], v[110:113]
	v_mfma_f32_16x16x32_bf16 v[106:109], v[168:171], v[184:187], v[106:109]
	v_mfma_f32_16x16x32_bf16 v[94:97], v[160:163], v[192:195], v[94:97]
	v_mfma_f32_16x16x32_bf16 v[90:93], v[168:171], v[192:195], v[90:93]
	v_mfma_f32_16x16x32_bf16 v[78:81], v[160:163], v[200:203], v[78:81]
	v_mfma_f32_16x16x32_bf16 v[74:77], v[168:171], v[200:203], v[74:77]
	v_mfma_f32_16x16x32_bf16 v[126:129], v[164:167], v[180:183], v[126:129]
	v_mfma_f32_16x16x32_bf16 v[122:125], v[172:175], v[180:183], v[122:125]
	v_mfma_f32_16x16x32_bf16 v[110:113], v[164:167], v[188:191], v[110:113]
	v_mfma_f32_16x16x32_bf16 v[106:109], v[172:175], v[188:191], v[106:109]
	v_mfma_f32_16x16x32_bf16 v[94:97], v[164:167], v[196:199], v[94:97]
	v_mfma_f32_16x16x32_bf16 v[90:93], v[172:175], v[196:199], v[90:93]
	v_mfma_f32_16x16x32_bf16 v[78:81], v[164:167], v[204:207], v[78:81]
	v_mfma_f32_16x16x32_bf16 v[74:77], v[172:175], v[204:207], v[74:77]
	s_barrier
	s_add_i32 s54, s46, s36
	v_add_u32_e32 v141, s48, v149
	v_lshl_add_u64 v[226:227], s[22:23], 0, v[130:131]
	s_mov_b32 m0, s54
	ds_read_b128 v[208:211], v141
	ds_read_b128 v[212:215], v141 offset:1024
	ds_read_b128 v[216:219], v141 offset:2048
	ds_read_b128 v[220:223], v141 offset:3072
	global_load_lds_dwordx4 v[226:227], off
	v_lshl_add_u64 v[228:229], s[22:23], 0, v[132:133]
	s_add_i32 m0, s54, 0x2000
	s_nop 0
	global_load_lds_dwordx4 v[228:229], off
	s_barrier
	s_waitcnt lgkmcnt(0)
	s_waitcnt lgkmcnt(0)
	v_mfma_f32_16x16x32_bf16 v[118:121], v[208:211], v[176:179], v[118:121]
	v_mfma_f32_16x16x32_bf16 v[114:117], v[216:219], v[176:179], v[114:117]
	v_mfma_f32_16x16x32_bf16 v[102:105], v[208:211], v[184:187], v[102:105]
	v_mfma_f32_16x16x32_bf16 v[98:101], v[216:219], v[184:187], v[98:101]
	v_mfma_f32_16x16x32_bf16 v[86:89], v[208:211], v[192:195], v[86:89]
	v_mfma_f32_16x16x32_bf16 v[82:85], v[216:219], v[192:195], v[82:85]
	v_mfma_f32_16x16x32_bf16 v[70:73], v[208:211], v[200:203], v[70:73]
	v_mfma_f32_16x16x32_bf16 v[66:69], v[216:219], v[200:203], v[66:69]
	v_mfma_f32_16x16x32_bf16 v[118:121], v[212:215], v[180:183], v[118:121]
	v_mfma_f32_16x16x32_bf16 v[114:117], v[220:223], v[180:183], v[114:117]
	v_mfma_f32_16x16x32_bf16 v[102:105], v[212:215], v[188:191], v[102:105]
	v_mfma_f32_16x16x32_bf16 v[98:101], v[220:223], v[188:191], v[98:101]
	v_mfma_f32_16x16x32_bf16 v[86:89], v[212:215], v[196:199], v[86:89]
	v_mfma_f32_16x16x32_bf16 v[82:85], v[220:223], v[196:199], v[82:85]
	v_mfma_f32_16x16x32_bf16 v[70:73], v[212:215], v[204:207], v[70:73]
	v_mfma_f32_16x16x32_bf16 v[66:69], v[220:223], v[204:207], v[66:69]
	s_mov_b32 m0, s37
	s_barrier
	ds_read_b128 v[176:179], v151 offset:16384
	ds_read_b128 v[180:183], v151 offset:17408
	ds_read_b128 v[184:187], v151 offset:18432
	ds_read_b128 v[188:191], v151 offset:19456
	ds_read_b128 v[192:195], v151 offset:20480
	ds_read_b128 v[196:199], v151 offset:21504
	ds_read_b128 v[200:203], v151 offset:22528
	ds_read_b128 v[204:207], v151 offset:23552
	global_load_lds_dwordx4 v134, s[26:27]
	s_mov_b32 m0, s38
	v_mov_b32_e32 v225, v135
	global_load_lds_dwordx4 v224, s[26:27]
	s_barrier
	s_waitcnt lgkmcnt(0)
	v_lshl_add_u64 v[230:231], s[26:27], 0, v[134:135]
	v_lshl_add_u64 v[224:225], s[26:27], 0, v[224:225]
	s_waitcnt lgkmcnt(0)
	v_mfma_f32_16x16x32_bf16 v[62:65], v[160:163], v[176:179], v[62:65]
	v_mfma_f32_16x16x32_bf16 v[58:61], v[168:171], v[176:179], v[58:61]
	v_mfma_f32_16x16x32_bf16 v[46:49], v[160:163], v[184:187], v[46:49]
	v_mfma_f32_16x16x32_bf16 v[42:45], v[168:171], v[184:187], v[42:45]
	v_mfma_f32_16x16x32_bf16 v[30:33], v[160:163], v[192:195], v[30:33]
	v_mfma_f32_16x16x32_bf16 v[26:29], v[168:171], v[192:195], v[26:29]
	v_mfma_f32_16x16x32_bf16 v[14:17], v[160:163], v[200:203], v[14:17]
	v_mfma_f32_16x16x32_bf16 v[10:13], v[168:171], v[200:203], v[10:13]
	v_mfma_f32_16x16x32_bf16 v[62:65], v[164:167], v[180:183], v[62:65]
	v_mfma_f32_16x16x32_bf16 v[58:61], v[172:175], v[180:183], v[58:61]
	v_mfma_f32_16x16x32_bf16 v[46:49], v[164:167], v[188:191], v[46:49]
	v_mfma_f32_16x16x32_bf16 v[42:45], v[172:175], v[188:191], v[42:45]
	v_mfma_f32_16x16x32_bf16 v[30:33], v[164:167], v[196:199], v[30:33]
	v_mfma_f32_16x16x32_bf16 v[26:29], v[172:175], v[196:199], v[26:29]
	v_mfma_f32_16x16x32_bf16 v[14:17], v[164:167], v[204:207], v[14:17]
	v_mfma_f32_16x16x32_bf16 v[10:13], v[172:175], v[204:207], v[10:13]
	s_barrier
	s_add_i32 s54, s48, s36
	v_lshl_add_u64 v[160:161], v[226:227], 0, s[4:5]
	s_mov_b32 m0, s54
	s_nop 0
	global_load_lds_dwordx4 v[160:161], off
	v_lshl_add_u64 v[160:161], v[228:229], 0, s[4:5]
	s_add_i32 m0, s54, 0x2000
	s_nop 0
	global_load_lds_dwordx4 v[160:161], off
	s_cmp_eq_u32 s82, 0
	s_cbranch_scc1 .Lpb17_p4n
	s_waitcnt vmcnt(14)
	v_cvt_pk_bf16_f32 v244, v244, v245
	v_cvt_pk_bf16_f32 v245, v246, v247
	v_cvt_pk_bf16_f32 v246, v248, v249
	v_cvt_pk_bf16_f32 v247, v250, v251
	global_store_dwordx4 v253, v[244:247], s[78:79] nt
	s_mov_b32 s82, 0
	s_waitcnt vmcnt(7)
	s_branch .Lpb17_p4j

; #define PG8_STAGE(bufoff, gbase, v0, v1) do { \
;         __builtin_amdgcn_global_load_lds((const unsigned*)((const char*)(gbase) + (v0)), (LAS unsigned*)(lds + (bufoff) + ldsw), 16, 0, 0); \
;         __builtin_amdgcn_global_load_lds((const unsigned*)((const char*)(gbase) + (v1)), (LAS unsigned*)(lds + (bufoff) + ldsw + 8192), 16, 0, 0); } while (0)
; #define PG8_LDA(dst, b, h) do { _Pragma("unroll") for (int m = 0; m < 4; ++m) _Pragma("unroll") for (int k = 0; k < 2; ++k) dst[m][k] = *(const LAS bf16x8*)(lds + PG8_SA(b, h) + aoff + m * 2048 + k * 1024); } while (0)
; #define PG8_LDB(dst, b, h) do { _Pragma("unroll") for (int n = 0; n < 2; ++n) _Pragma("unroll") for (int k = 0; k < 2; ++k) dst[n][k] = *(const LAS bf16x8*)(lds + PG8_SB(b, h) + boff + n * 2048 + k * 1024); } while (0)
; #define PG8_MMA(ai, bj, At, Bt) do { __builtin_amdgcn_s_setprio(1); _Pragma("unroll") for (int m = 0; m < 4; ++m) _Pragma("unroll") for (int n = 0; n < 2; ++n) _Pragma("unroll") for (int k = 0; k < 2; ++k) \
;         acc[ai][bj][m][n] = __builtin_amdgcn_mfma_f32_16x16x32_bf16(Bt[n][k], At[m][k], acc[ai][bj][m][n], 0, 0, 0); __builtin_amdgcn_s_setprio(0); } while (0)
; #define PG8_WAIT_V(n) asm volatile("s_waitcnt vmcnt(" #n ")" ::: "memory")
; #define PG8_BAR __builtin_amdgcn_s_barrier()
; template <class Epi, class Sched>
; __device__ __forceinline__ void gemm_phase(LAS unsigned char* lds, const int K, const Sched& S, const Epi& E) {
;     ...
;             PG8_WAIT_V(6); PG8_BAR; PG8_MMA(1, 1, At, B1); PG8_BAR;
;             PG8_LDB(B0, 1, 0); PG8_SCHED; PG8_LDA(At, 1, 0); PG8_STAGE(PG8_SA(0, 1), a2, x10, x11);
;             PG8_WAIT_L(8); PG8_BAR; PG8_WAIT_L(0); PG8_MMA(0, 0, At, B0); PG8_BAR; PG8_SCHED;
;             PG8_LDB(B1, 1, 1); PG8_STAGE(PG8_SB(1, 0), b3, voffB0, voffB1);
;             PG8_BAR; PG8_WAIT_L(0); PG8_MMA(0, 1, At, B1); PG8_BAR;
;             PG8_LDA(At, 1, 1); PG8_STAGE(PG8_SA(1, 0), a3, x00, x01);
; __device__ __forceinline__ bool bg_decode(int st, int wg, int NW, int lane, KP kp, const float*& src, int& ldS, bf16_t*& dst, int& o2) {
;     ...
;         const int r2 = r - 65536, e = r2 >> 9, kc = (r2 >> 3) & 63, cc = r2 & 7, n = cc * 256 + lane;
;         ldS = D; o2 = 128 * 8;
;         src = kp->in[29] + ((size_t)(l * NE + e) * FF + kc * 8) * D + n;
;         dst = (bf16_t*)(ws + WS_WD) + l * WD_L + (size_t)e * D * FF + ((size_t)kc * D + n) * 8;
.Lpb17_p4j:
	s_barrier
	v_mfma_f32_16x16x32_bf16 v[54:57], v[208:211], v[176:179], v[54:57]
	v_mfma_f32_16x16x32_bf16 v[50:53], v[216:219], v[176:179], v[50:53]
	v_mfma_f32_16x16x32_bf16 v[38:41], v[208:211], v[184:187], v[38:41]
	v_mfma_f32_16x16x32_bf16 v[34:37], v[216:219], v[184:187], v[34:37]
	v_mfma_f32_16x16x32_bf16 v[22:25], v[208:211], v[192:195], v[22:25]
	v_mfma_f32_16x16x32_bf16 v[18:21], v[216:219], v[192:195], v[18:21]
	v_mfma_f32_16x16x32_bf16 v[6:9], v[208:211], v[200:203], v[6:9]
	v_mfma_f32_16x16x32_bf16 v[2:5], v[216:219], v[200:203], v[2:5]
	v_mfma_f32_16x16x32_bf16 v[54:57], v[212:215], v[180:183], v[54:57]
	v_mfma_f32_16x16x32_bf16 v[50:53], v[220:223], v[180:183], v[50:53]
	v_mfma_f32_16x16x32_bf16 v[38:41], v[212:215], v[188:191], v[38:41]
	v_mfma_f32_16x16x32_bf16 v[34:37], v[220:223], v[188:191], v[34:37]
	v_mfma_f32_16x16x32_bf16 v[22:25], v[212:215], v[196:199], v[22:25]
	v_mfma_f32_16x16x32_bf16 v[18:21], v[220:223], v[196:199], v[18:21]
	v_mfma_f32_16x16x32_bf16 v[6:9], v[212:215], v[204:207], v[6:9]
	v_mfma_f32_16x16x32_bf16 v[2:5], v[220:223], v[204:207], v[2:5]
	s_add_i32 s54, 0, 0x18000
	v_add_u32_e32 v134, s54, v149
	s_barrier
	ds_read_b128 v[160:163], v134
	ds_read_b128 v[164:167], v134 offset:1024
	ds_read_b128 v[168:171], v134 offset:2048
	ds_read_b128 v[172:175], v134 offset:3072
	s_mov_b32 m0, s39
	ds_read_b128 v[176:179], v151 offset:32768
	ds_read_b128 v[180:183], v151 offset:33792
	ds_read_b128 v[184:187], v151 offset:34816
	ds_read_b128 v[188:191], v151 offset:35840
	ds_read_b128 v[192:195], v151 offset:36864
	ds_read_b128 v[196:199], v151 offset:37888
	ds_read_b128 v[200:203], v151 offset:38912
	ds_read_b128 v[204:207], v151 offset:39936
	v_cndmask_b32_e32 v134, v140, v153, vcc
	global_load_lds_dwordx4 v139, s[26:27]
	s_mov_b32 m0, s40
	s_nop 0
	global_load_lds_dwordx4 v134, s[26:27]
	s_cmp_ge_u32 s70, 0x30000
	s_cbranch_scc1 .Lpb17_p5n
	s_cmp_eq_u32 s80, 0
	s_cbranch_scc0 .Lpb17_adv6
	s_cmp_ge_u32 s70, 0x28000
	s_mov_b32 s84, 0x10000
	s_cselect_b32 s84, 0x28000, s84
	s_cselect_b32 s83, 0x10000000, 0
	s_mov_b32 s81, 0x24830000
	s_cselect_b32 s81, 0x2ca30000, s81
	s_sub_u32 s84, s70, s84
	s_lshr_b32 s85, s84, 3
	s_and_b32 s86, s84, 7
	s_lshl_b32 s87, s85, 16
	s_lshl_b32 s84, s86, 10
	s_add_u32 s87, s87, s84
	s_add_u32 s87, s87, s83
	s_add_u32 s72, s74, s87
	s_addc_u32 s73, s75, 0
	s_add_u32 s88, s72, 0x8000
	s_addc_u32 s89, s73, 0
	s_lshl_b32 s85, s85, 15
	s_lshl_b32 s86, s86, 12
	s_add_u32 s85, s85, s86
	s_add_u32 s85, s85, s81
	v_add_u32_e32 v253, s85, v252
	s_branch .Lpb17_ld6

; #define PG8_STAGE(bufoff, gbase, v0, v1) do { \
;         __builtin_amdgcn_global_load_lds((const unsigned*)((const char*)(gbase) + (v0)), (LAS unsigned*)(lds + (bufoff) + ldsw), 16, 0, 0); \
;         __builtin_amdgcn_global_load_lds((const unsigned*)((const char*)(gbase) + (v1)), (LAS unsigned*)(lds + (bufoff) + ldsw + 8192), 16, 0, 0); } while (0)
; #define PG8_LDA(dst, b, h) do { _Pragma("unroll") for (int m = 0; m < 4; ++m) _Pragma("unroll") for (int k = 0; k < 2; ++k) dst[m][k] = *(const LAS bf16x8*)(lds + PG8_SA(b, h) + aoff + m * 2048 + k * 1024); } while (0)
; #define PG8_LDB(dst, b, h) do { _Pragma("unroll") for (int n = 0; n < 2; ++n) _Pragma("unroll") for (int k = 0; k < 2; ++k) dst[n][k] = *(const LAS bf16x8*)(lds + PG8_SB(b, h) + boff + n * 2048 + k * 1024); } while (0)
; #define PG8_MMA(ai, bj, At, Bt) do { __builtin_amdgcn_s_setprio(1); _Pragma("unroll") for (int m = 0; m < 4; ++m) _Pragma("unroll") for (int n = 0; n < 2; ++n) _Pragma("unroll") for (int k = 0; k < 2; ++k) \
;         acc[ai][bj][m][n] = __builtin_amdgcn_mfma_f32_16x16x32_bf16(Bt[n][k], At[m][k], acc[ai][bj][m][n], 0, 0, 0); __builtin_amdgcn_s_setprio(0); } while (0)
; #define PG8_WAIT_L(n) asm volatile("s_waitcnt lgkmcnt(" #n ")" ::: "memory")
; #define PG8_BAR __builtin_amdgcn_s_barrier()
; #define PG8_SCHED __builtin_amdgcn_sched_barrier(0)
; template <class Epi, class Sched>
; __device__ __forceinline__ void gemm_phase(LAS unsigned char* lds, const int K, const Sched& S, const Epi& E) {
;     ...
;             PG8_WAIT_L(8); PG8_BAR; PG8_WAIT_L(0); PG8_MMA(0, 0, At, B0); PG8_BAR; PG8_SCHED;
;             PG8_LDB(B1, 1, 1); PG8_STAGE(PG8_SB(1, 0), b3, voffB0, voffB1);
;             PG8_BAR; PG8_WAIT_L(0); PG8_MMA(0, 1, At, B1); PG8_BAR;
;             PG8_LDA(At, 1, 1); PG8_STAGE(PG8_SA(1, 0), a3, x00, x01);
;             PG8_BAR; PG8_WAIT_L(0); PG8_MMA(1, 0, At, B0); PG8_BAR; PG8_SCHED;
;             PG8_STAGE(PG8_SB(1, 1), b3 + hstep, voffB0, voffB1);
.Lpb17_p5n:
	s_waitcnt lgkmcnt(8)
	s_barrier
	s_waitcnt lgkmcnt(0)
	s_waitcnt lgkmcnt(0)
	v_mfma_f32_16x16x32_bf16 v[126:129], v[160:163], v[176:179], v[126:129]
	v_mfma_f32_16x16x32_bf16 v[122:125], v[168:171], v[176:179], v[122:125]
	v_mfma_f32_16x16x32_bf16 v[110:113], v[160:163], v[184:187], v[110:113]
	v_mfma_f32_16x16x32_bf16 v[106:109], v[168:171], v[184:187], v[106:109]
	v_mfma_f32_16x16x32_bf16 v[94:97], v[160:163], v[192:195], v[94:97]
	v_mfma_f32_16x16x32_bf16 v[90:93], v[168:171], v[192:195], v[90:93]
	v_mfma_f32_16x16x32_bf16 v[78:81], v[160:163], v[200:203], v[78:81]
	v_mfma_f32_16x16x32_bf16 v[74:77], v[168:171], v[200:203], v[74:77]
	v_mfma_f32_16x16x32_bf16 v[126:129], v[164:167], v[180:183], v[126:129]
	v_mfma_f32_16x16x32_bf16 v[122:125], v[172:175], v[180:183], v[122:125]
	v_mfma_f32_16x16x32_bf16 v[110:113], v[164:167], v[188:191], v[110:113]
	v_mfma_f32_16x16x32_bf16 v[106:109], v[172:175], v[188:191], v[106:109]
	v_mfma_f32_16x16x32_bf16 v[94:97], v[164:167], v[196:199], v[94:97]
	v_mfma_f32_16x16x32_bf16 v[90:93], v[172:175], v[196:199], v[90:93]
	v_mfma_f32_16x16x32_bf16 v[78:81], v[164:167], v[204:207], v[78:81]
	v_mfma_f32_16x16x32_bf16 v[74:77], v[172:175], v[204:207], v[74:77]
	s_barrier
	s_add_i32 s26, 0, 0x1c000
	s_add_i32 s27, s54, s36
	v_add_u32_e32 v134, s26, v149
	v_lshl_add_u64 v[226:227], s[24:25], 0, v[130:131]
	s_mov_b32 m0, s27
	ds_read_b128 v[208:211], v134
	ds_read_b128 v[212:215], v134 offset:1024
	ds_read_b128 v[216:219], v134 offset:2048
	ds_read_b128 v[220:223], v134 offset:3072
	global_load_lds_dwordx4 v[226:227], off
	v_lshl_add_u64 v[226:227], s[24:25], 0, v[132:133]
	s_add_i32 m0, s27, 0x2000
	s_nop 0
	global_load_lds_dwordx4 v[226:227], off
	s_barrier
	s_waitcnt lgkmcnt(0)
	s_waitcnt lgkmcnt(0)
	v_mfma_f32_16x16x32_bf16 v[118:121], v[208:211], v[176:179], v[118:121]
	v_mfma_f32_16x16x32_bf16 v[114:117], v[216:219], v[176:179], v[114:117]
	v_mfma_f32_16x16x32_bf16 v[102:105], v[208:211], v[184:187], v[102:105]
	v_mfma_f32_16x16x32_bf16 v[98:101], v[216:219], v[184:187], v[98:101]
	v_mfma_f32_16x16x32_bf16 v[86:89], v[208:211], v[192:195], v[86:89]
	v_mfma_f32_16x16x32_bf16 v[82:85], v[216:219], v[192:195], v[82:85]
	v_mfma_f32_16x16x32_bf16 v[70:73], v[208:211], v[200:203], v[70:73]
	v_mfma_f32_16x16x32_bf16 v[66:69], v[216:219], v[200:203], v[66:69]
	v_mfma_f32_16x16x32_bf16 v[118:121], v[212:215], v[180:183], v[118:121]
	v_mfma_f32_16x16x32_bf16 v[114:117], v[220:223], v[180:183], v[114:117]
	v_mfma_f32_16x16x32_bf16 v[102:105], v[212:215], v[188:191], v[102:105]
	v_mfma_f32_16x16x32_bf16 v[98:101], v[220:223], v[188:191], v[98:101]
	v_mfma_f32_16x16x32_bf16 v[86:89], v[212:215], v[196:199], v[86:89]
	v_mfma_f32_16x16x32_bf16 v[82:85], v[220:223], v[196:199], v[82:85]
	v_mfma_f32_16x16x32_bf16 v[70:73], v[212:215], v[204:207], v[70:73]
	v_mfma_f32_16x16x32_bf16 v[66:69], v[220:223], v[204:207], v[66:69]
	s_mov_b32 m0, s43
	v_lshl_add_u64 v[226:227], v[230:231], 0, s[10:11]
	s_barrier
	ds_read_b128 v[176:179], v151 offset:49152
	ds_read_b128 v[180:183], v151 offset:50176
	ds_read_b128 v[184:187], v151 offset:51200
	ds_read_b128 v[188:191], v151 offset:52224
	ds_read_b128 v[192:195], v151 offset:53248
	ds_read_b128 v[196:199], v151 offset:54272
	ds_read_b128 v[200:203], v151 offset:55296
	ds_read_b128 v[204:207], v151 offset:56320
	global_load_lds_dwordx4 v[226:227], off
	v_lshl_add_u64 v[224:225], v[224:225], 0, s[10:11]
	s_mov_b32 m0, s44
	s_nop 0
	global_load_lds_dwordx4 v[224:225], off
	s_barrier
	s_waitcnt lgkmcnt(0)
	s_waitcnt lgkmcnt(0)
	v_mfma_f32_16x16x32_bf16 v[62:65], v[160:163], v[176:179], v[62:65]
	v_mfma_f32_16x16x32_bf16 v[58:61], v[168:171], v[176:179], v[58:61]
	v_mfma_f32_16x16x32_bf16 v[46:49], v[160:163], v[184:187], v[46:49]
	v_mfma_f32_16x16x32_bf16 v[42:45], v[168:171], v[184:187], v[42:45]
	v_mfma_f32_16x16x32_bf16 v[30:33], v[160:163], v[192:195], v[30:33]
	v_mfma_f32_16x16x32_bf16 v[26:29], v[168:171], v[192:195], v[26:29]
	v_mfma_f32_16x16x32_bf16 v[14:17], v[160:163], v[200:203], v[14:17]
	v_mfma_f32_16x16x32_bf16 v[10:13], v[168:171], v[200:203], v[10:13]
	v_mfma_f32_16x16x32_bf16 v[62:65], v[164:167], v[180:183], v[62:65]
	v_mfma_f32_16x16x32_bf16 v[58:61], v[172:175], v[180:183], v[58:61]
	v_mfma_f32_16x16x32_bf16 v[46:49], v[164:167], v[188:191], v[46:49]
	v_mfma_f32_16x16x32_bf16 v[42:45], v[172:175], v[188:191], v[42:45]
	v_mfma_f32_16x16x32_bf16 v[30:33], v[164:167], v[196:199], v[30:33]
	v_mfma_f32_16x16x32_bf16 v[26:29], v[172:175], v[196:199], v[26:29]
	v_mfma_f32_16x16x32_bf16 v[14:17], v[164:167], v[204:207], v[14:17]
	v_mfma_f32_16x16x32_bf16 v[10:13], v[172:175], v[204:207], v[10:13]
	s_barrier
	s_add_u32 s22, s22, 0x20800
	s_addc_u32 s23, s23, 0
	s_add_i32 s24, s26, s36
	v_lshl_add_u64 v[160:161], s[22:23], 0, v[130:131]
	s_mov_b32 m0, s24
	s_nop 0
	global_load_lds_dwordx4 v[160:161], off
	v_lshl_add_u64 v[160:161], s[22:23], 0, v[132:133]
	s_add_i32 m0, s24, 0x2000
	s_nop 0
	global_load_lds_dwordx4 v[160:161], off
	s_cmp_eq_u32 s82, 0
	s_cbranch_scc1 .Lpb17_p8n
	s_waitcnt vmcnt(14)
	s_branch .Lpb17_p8j

; __device__ __forceinline__ unsigned cvt_pk_bf16(float lo, float hi) { unsigned r; asm volatile("v_cvt_pk_bf16_f32 %0, %1, %2" : "=v"(r) : "v"(lo), "v"(hi)); return r; }
; __device__ __forceinline__ float fdivf(float a, float b) { return a * __builtin_amdgcn_rcpf(b); }
; #define PG8_BAR __builtin_amdgcn_s_barrier()
; template <class Epi, class Sched>
; __device__ __forceinline__ void gemm_phase(LAS unsigned char* lds, const int K, const Sched& S, const Epi& E) {
;     ...
;             PG8_WAIT_V(6); PG8_BAR; PG8_MMA(1, 1, At, B1); PG8_BAR;
;         }
;         E(acc, cur, wr, wc, fr, fq);
;         if (!has_next) break;
;     __device__ __forceinline__ void a_off4(const Unit& u, int r0, int r1, unsigned& o00, unsigned& o01, unsigned& o10, unsigned& o11) const {
;         const int p0 = u.pm * BM + r0, p1 = u.pm * BM + r1, p2 = p0 + HALF, p3 = p1 + HALF;
;         if (u.e >= NE) { o00 = (unsigned)p0 * (unsigned)(D * 2); o01 = (unsigned)p1 * (unsigned)(D * 2); o10 = (unsigned)p2 * (unsigned)(D * 2); o11 = (unsigned)p3 * (unsigned)(D * 2); return; }
;         const int* lp = list + u.e * T;
;         int v0 = lp[p0], v1 = lp[p1], v2 = lp[p2], v3 = lp[p3];
;         asm volatile("" : "+v"(v0), "+v"(v1), "+v"(v2), "+v"(v3));
;         const int c = cnt[u.e];
;         o00 = p0 < c ? (unsigned)v0 * (unsigned)(D * 2) : 0u; o01 = p1 < c ? (unsigned)v1 * (unsigned)(D * 2) : 0u;
;         o10 = p2 < c ? (unsigned)v2 * (unsigned)(D * 2) : 0u; o11 = p3 < c ? (unsigned)v3 * (unsigned)(D * 2) : 0u;
;     __device__ __forceinline__ void operator()(const f32x4 (&acc)[2][2][4][2], const Unit& u, int wr, int wc, int fr, int fq) const {
;         const int row0 = u.rbase + wr * 64 + fr, col0 = u.pn * HALF + wc * 32 + 8 * fq;
; #pragma unroll
;         for (int ai = 0; ai < 2; ++ai)
; #pragma unroll
;             for (int m = 0; m < 4; ++m) { bf16_t* rowp = O + (size_t)(row0 + ai * HALF + m * 16) * FF + col0;
;                 float h[8];
; #pragma unroll
;                 for (int n = 0; n < 2; ++n)
; #pragma unroll
;                     for (int j = 0; j < 4; ++j) { const float g = acc[ai][0][m][n][j], up = acc[ai][1][m][n][j]; h[n * 4 + j] = fdivf(g, 1.f + __expf(-g)) * up; }
;                 u32x4 w; w.x = cvt_pk_bf16(h[0], h[1]); w.y = cvt_pk_bf16(h[2], h[3]); w.z = cvt_pk_bf16(h[4], h[5]); w.w = cvt_pk_bf16(h[6], h[7]);
;                 *(u32x4*)rowp = w; }
.Lpb17_p8j:
	s_barrier
	v_mfma_f32_16x16x32_bf16 v[54:57], v[208:211], v[176:179], v[54:57]
	v_mfma_f32_16x16x32_bf16 v[50:53], v[216:219], v[176:179], v[50:53]
	v_mfma_f32_16x16x32_bf16 v[38:41], v[208:211], v[184:187], v[38:41]
	v_mfma_f32_16x16x32_bf16 v[34:37], v[216:219], v[184:187], v[34:37]
	v_mfma_f32_16x16x32_bf16 v[22:25], v[208:211], v[192:195], v[22:25]
	v_mfma_f32_16x16x32_bf16 v[18:21], v[216:219], v[192:195], v[18:21]
	v_mfma_f32_16x16x32_bf16 v[6:9], v[208:211], v[200:203], v[6:9]
	v_mfma_f32_16x16x32_bf16 v[2:5], v[216:219], v[200:203], v[2:5]
	v_mfma_f32_16x16x32_bf16 v[54:57], v[212:215], v[180:183], v[54:57]
	v_mfma_f32_16x16x32_bf16 v[50:53], v[220:223], v[180:183], v[50:53]
	v_mfma_f32_16x16x32_bf16 v[38:41], v[212:215], v[188:191], v[38:41]
	v_mfma_f32_16x16x32_bf16 v[34:37], v[220:223], v[188:191], v[34:37]
	v_mfma_f32_16x16x32_bf16 v[22:25], v[212:215], v[196:199], v[22:25]
	v_mfma_f32_16x16x32_bf16 v[18:21], v[220:223], v[196:199], v[18:21]
	v_mfma_f32_16x16x32_bf16 v[6:9], v[212:215], v[204:207], v[6:9]
	v_mfma_f32_16x16x32_bf16 v[2:5], v[220:223], v[204:207], v[2:5]
	s_add_i32 s53, s53, 2
	s_add_u32 s13, s13, 0x40000
	s_addc_u32 s15, s15, 0
	s_add_u32 s20, s20, 0x100
	s_addc_u32 s21, s21, 0
	s_cmp_gt_u32 s53, 29
	s_barrier
	s_cbranch_scc0 .LBB0_1831
	v_mul_f32_e32 v134, 0xbfb8aa3b, v126
	v_exp_f32_e32 v134, v134
	v_mul_f32_e32 v136, 0xbfb8aa3b, v127
	v_exp_f32_e32 v136, v136
	v_add_u32_e32 v138, v157, v137
	v_add_f32_e32 v134, 1.0, v134
	v_rcp_f32_e32 v134, v134
	v_add_f32_e32 v136, 1.0, v136
	v_rcp_f32_e32 v136, v136
	v_readlane_b32 s13, v254, 27
	v_mul_f32_e32 v126, v126, v134
	v_mul_f32_e32 v118, v126, v118
	v_mul_f32_e32 v126, v127, v136
	v_mul_f32_e32 v127, 0xbfb8aa3b, v128
	v_exp_f32_e32 v127, v127
	v_mul_f32_e32 v134, 0xbfb8aa3b, v129
	v_exp_f32_e32 v134, v134
	v_mul_f32_e32 v119, v126, v119
	v_add_f32_e32 v126, 1.0, v127
	v_rcp_f32_e32 v126, v126
	v_add_f32_e32 v127, 1.0, v134
	v_mul_f32_e32 v134, 0xbfb8aa3b, v122
	v_rcp_f32_e32 v127, v127
	v_exp_f32_e32 v134, v134
	v_mul_f32_e32 v126, v128, v126
	v_mul_f32_e32 v120, v126, v120
	v_mul_f32_e32 v126, v129, v127
	v_add_f32_e32 v127, 1.0, v134
	v_rcp_f32_e32 v127, v127
	v_mul_f32_e32 v128, 0xbfb8aa3b, v123
	v_exp_f32_e32 v128, v128
	v_mul_f32_e32 v121, v126, v121
	v_mul_f32_e32 v122, v122, v127
	v_mul_f32_e32 v122, v122, v114
	v_add_f32_e32 v114, 1.0, v128
	v_mul_f32_e32 v126, 0xbfb8aa3b, v124
	v_rcp_f32_e32 v114, v114
	v_exp_f32_e32 v126, v126
	v_mul_f32_e32 v127, 0xbfb8aa3b, v125
	v_exp_f32_e32 v127, v127
	v_mul_f32_e32 v114, v123, v114
	v_add_f32_e32 v123, 1.0, v126
	v_rcp_f32_e32 v123, v123
	v_add_f32_e32 v126, 1.0, v127
	v_rcp_f32_e32 v126, v126
	v_mul_f32_e32 v127, v114, v115
	v_mul_f32_e32 v114, v124, v123
	v_mul_f32_e32 v123, v114, v116
	v_mul_f32_e32 v114, v125, v126
	v_cvt_pk_bf16_f32 v116, v118, v119
	v_mul_f32_e32 v119, 0xbfb8aa3b, v110
	v_mul_f32_e32 v124, v114, v117
	v_cvt_pk_bf16_f32 v117, v120, v121
	v_exp_f32_e32 v120, v119
	v_mul_f32_e32 v119, 0xbfb8aa3b, v111
	v_exp_f32_e32 v121, v119
	v_ashrrev_i32_e32 v139, 31, v138
	v_add_f32_e32 v120, 1.0, v120
	v_rcp_f32_e32 v120, v120
	v_add_f32_e32 v121, 1.0, v121
	v_rcp_f32_e32 v121, v121
	v_lshl_or_b32 v140, s13, 7, v150
	v_lshlrev_b64 v[138:139], 10, v[138:139]
	v_ashrrev_i32_e32 v141, 31, v140
	v_lshl_add_u64 v[138:139], s[6:7], 0, v[138:139]
	v_mul_f32_e32 v110, v110, v120
	v_lshl_add_u64 v[114:115], v[140:141], 1, v[138:139]
	v_mul_f32_e32 v102, v110, v102
	v_mul_f32_e32 v110, v111, v121
	v_mul_f32_e32 v111, 0xbfb8aa3b, v112
	v_cvt_pk_bf16_f32 v118, v122, v127
	v_cvt_pk_bf16_f32 v119, v123, v124
	global_store_dwordx4 v[114:115], v[116:119], off
	v_exp_f32_e32 v111, v111
	v_mul_f32_e32 v103, v110, v103
	v_mul_f32_e32 v116, 0xbfb8aa3b, v113
	v_exp_f32_e32 v116, v116
	v_add_f32_e32 v110, 1.0, v111
	v_rcp_f32_e32 v110, v110
	s_mov_b32 s13, s12
	v_add_f32_e32 v111, 1.0, v116
	v_mul_f32_e32 v116, 0xbfb8aa3b, v106
	v_rcp_f32_e32 v111, v111
	v_exp_f32_e32 v116, v116
	v_mul_f32_e32 v110, v112, v110
	v_mul_f32_e32 v104, v110, v104
	v_mul_f32_e32 v110, v113, v111
	v_add_f32_e32 v111, 1.0, v116
	v_rcp_f32_e32 v111, v111
	v_mul_f32_e32 v112, 0xbfb8aa3b, v107
	v_exp_f32_e32 v112, v112
	v_mul_f32_e32 v105, v110, v105
	v_mul_f32_e32 v106, v106, v111
	v_mul_f32_e32 v106, v106, v98
	v_add_f32_e32 v98, 1.0, v112
	v_mul_f32_e32 v110, 0xbfb8aa3b, v108
	v_rcp_f32_e32 v98, v98
	v_exp_f32_e32 v110, v110
	v_mul_f32_e32 v111, 0xbfb8aa3b, v109
	v_exp_f32_e32 v111, v111
	v_mul_f32_e32 v98, v107, v98
	v_add_f32_e32 v107, 1.0, v110
	v_rcp_f32_e32 v107, v107
	v_add_f32_e32 v110, 1.0, v111
	v_rcp_f32_e32 v110, v110
	v_mul_f32_e32 v111, v98, v99
	v_mul_f32_e32 v98, v108, v107
	v_mul_f32_e32 v107, v98, v100
	v_mul_f32_e32 v98, v109, v110
	v_mul_f32_e32 v101, v98, v101
	v_cvt_pk_bf16_f32 v98, v102, v103
	v_mul_f32_e32 v102, 0xbfb8aa3b, v94
	v_cvt_pk_bf16_f32 v99, v104, v105
	v_exp_f32_e32 v104, v102
	v_mul_f32_e32 v102, 0xbfb8aa3b, v95
	v_exp_f32_e32 v105, v102
	v_add_co_u32_e32 v102, vcc, s42, v114
	v_add_f32_e32 v104, 1.0, v104
	v_rcp_f32_e32 v104, v104
	v_add_f32_e32 v105, 1.0, v105
	v_rcp_f32_e32 v105, v105
	v_addc_co_u32_e32 v103, vcc, 0, v115, vcc
	v_mul_f32_e32 v94, v94, v104
	v_mul_f32_e32 v86, v94, v86
	v_mul_f32_e32 v94, v95, v105
	v_mul_f32_e32 v95, 0xbfb8aa3b, v96
	v_cvt_pk_bf16_f32 v100, v106, v111
	v_cvt_pk_bf16_f32 v101, v107, v101
	global_store_dwordx4 v[102:103], v[98:101], off
	v_exp_f32_e32 v95, v95
	v_mul_f32_e32 v87, v94, v87
	v_mul_f32_e32 v98, 0xbfb8aa3b, v97
	v_exp_f32_e32 v98, v98
	v_add_f32_e32 v94, 1.0, v95
	v_rcp_f32_e32 v94, v94
	v_mov_b32_e32 v157, v152
	v_add_f32_e32 v95, 1.0, v98
; __device__ __forceinline__ unsigned cvt_pk_bf16(float lo, float hi) { unsigned r; asm volatile("v_cvt_pk_bf16_f32 %0, %1, %2" : "=v"(r) : "v"(lo), "v"(hi)); return r; }
; __device__ __forceinline__ float fdivf(float a, float b) { return a * __builtin_amdgcn_rcpf(b); }
;     __device__ __forceinline__ void operator()(const f32x4 (&acc)[2][2][4][2], const Unit& u, int wr, int wc, int fr, int fq) const {
;         const int row0 = u.rbase + wr * 64 + fr, col0 = u.pn * HALF + wc * 32 + 8 * fq;
; #pragma unroll
;         for (int ai = 0; ai < 2; ++ai)
; #pragma unroll
;             for (int m = 0; m < 4; ++m) { bf16_t* rowp = O + (size_t)(row0 + ai * HALF + m * 16) * FF + col0;
;                 float h[8];
; #pragma unroll
;                 for (int n = 0; n < 2; ++n)
; #pragma unroll
;                     for (int j = 0; j < 4; ++j) { const float g = acc[ai][0][m][n][j], up = acc[ai][1][m][n][j]; h[n * 4 + j] = fdivf(g, 1.f + __expf(-g)) * up; }
;                 u32x4 w; w.x = cvt_pk_bf16(h[0], h[1]); w.y = cvt_pk_bf16(h[2], h[3]); w.z = cvt_pk_bf16(h[4], h[5]); w.w = cvt_pk_bf16(h[6], h[7]);
;                 *(u32x4*)rowp = w; }
;     }
	v_mul_f32_e32 v98, 0xbfb8aa3b, v90
	v_rcp_f32_e32 v95, v95
	v_exp_f32_e32 v98, v98
	v_mul_f32_e32 v94, v96, v94
	v_mul_f32_e32 v88, v94, v88
	v_mul_f32_e32 v94, v97, v95
	v_add_f32_e32 v95, 1.0, v98
	v_rcp_f32_e32 v95, v95
	v_mul_f32_e32 v96, 0xbfb8aa3b, v91
	v_exp_f32_e32 v96, v96
	v_mul_f32_e32 v89, v94, v89
	v_mul_f32_e32 v90, v90, v95
	v_mul_f32_e32 v90, v90, v82
	v_add_f32_e32 v82, 1.0, v96
	v_mul_f32_e32 v94, 0xbfb8aa3b, v92
	v_rcp_f32_e32 v82, v82
	v_exp_f32_e32 v94, v94
	v_mul_f32_e32 v95, 0xbfb8aa3b, v93
	v_exp_f32_e32 v95, v95
	v_mul_f32_e32 v82, v91, v82
	v_add_f32_e32 v91, 1.0, v94
	v_rcp_f32_e32 v91, v91
	v_add_f32_e32 v94, 1.0, v95
	v_rcp_f32_e32 v94, v94
	v_mul_f32_e32 v95, v82, v83
	v_mul_f32_e32 v82, v92, v91
	v_mul_f32_e32 v91, v82, v84
	v_mul_f32_e32 v82, v93, v94
	v_mul_f32_e32 v85, v82, v85
	v_cvt_pk_bf16_f32 v82, v86, v87
	v_mul_f32_e32 v86, 0xbfb8aa3b, v78
	v_cvt_pk_bf16_f32 v83, v88, v89
	v_exp_f32_e32 v88, v86
	v_mul_f32_e32 v86, 0xbfb8aa3b, v79
	v_exp_f32_e32 v89, v86
	v_add_co_u32_e32 v86, vcc, s45, v114
	v_add_f32_e32 v88, 1.0, v88
	v_rcp_f32_e32 v88, v88
	v_add_f32_e32 v89, 1.0, v89
	v_rcp_f32_e32 v89, v89
	v_addc_co_u32_e32 v87, vcc, 0, v115, vcc
	v_mul_f32_e32 v78, v78, v88
	v_mul_f32_e32 v70, v78, v70
	v_mul_f32_e32 v78, v79, v89
	v_mul_f32_e32 v79, 0xbfb8aa3b, v80
	v_cvt_pk_bf16_f32 v84, v90, v95
	v_cvt_pk_bf16_f32 v85, v91, v85
	global_store_dwordx4 v[86:87], v[82:85], off
	v_exp_f32_e32 v79, v79
	v_mul_f32_e32 v71, v78, v71
	v_mul_f32_e32 v82, 0xbfb8aa3b, v81
	v_exp_f32_e32 v82, v82
	v_add_f32_e32 v78, 1.0, v79
	v_rcp_f32_e32 v78, v78
	v_writelane_b32 v254, s13, 27
	v_add_f32_e32 v79, 1.0, v82
	v_mul_f32_e32 v82, 0xbfb8aa3b, v74
	v_rcp_f32_e32 v79, v79
	v_exp_f32_e32 v82, v82
	v_mul_f32_e32 v78, v80, v78
	v_mul_f32_e32 v72, v78, v72
	v_mul_f32_e32 v78, v81, v79
	v_add_f32_e32 v79, 1.0, v82
	v_rcp_f32_e32 v79, v79
	v_mul_f32_e32 v80, 0xbfb8aa3b, v75
	v_exp_f32_e32 v80, v80
	v_mul_f32_e32 v73, v78, v73
	v_mul_f32_e32 v74, v74, v79
	v_mul_f32_e32 v74, v74, v66
	v_add_f32_e32 v66, 1.0, v80
	v_mul_f32_e32 v78, 0xbfb8aa3b, v76
	v_rcp_f32_e32 v66, v66
	v_exp_f32_e32 v78, v78
	v_mul_f32_e32 v79, 0xbfb8aa3b, v77
	v_exp_f32_e32 v79, v79
	v_mul_f32_e32 v66, v75, v66
	v_add_f32_e32 v75, 1.0, v78
	v_rcp_f32_e32 v75, v75
	v_add_f32_e32 v78, 1.0, v79
	v_rcp_f32_e32 v78, v78
	v_mul_f32_e32 v79, v66, v67
	v_mul_f32_e32 v66, v76, v75
	v_mul_f32_e32 v75, v66, v68
	v_mul_f32_e32 v66, v77, v78
	v_mul_f32_e32 v69, v66, v69
	v_cvt_pk_bf16_f32 v66, v70, v71
	v_mul_f32_e32 v70, 0xbfb8aa3b, v62
	v_cvt_pk_bf16_f32 v67, v72, v73
	v_exp_f32_e32 v72, v70
	v_mul_f32_e32 v70, 0xbfb8aa3b, v63
	v_exp_f32_e32 v73, v70
	v_add_co_u32_e32 v70, vcc, s47, v114
	v_add_f32_e32 v72, 1.0, v72
	v_rcp_f32_e32 v72, v72
	v_add_f32_e32 v73, 1.0, v73
	v_rcp_f32_e32 v73, v73
	v_addc_co_u32_e32 v71, vcc, 0, v115, vcc
	v_mul_f32_e32 v62, v62, v72
	v_mul_f32_e32 v54, v62, v54
	v_mul_f32_e32 v62, v63, v73
	v_mul_f32_e32 v63, 0xbfb8aa3b, v64
	v_cvt_pk_bf16_f32 v68, v74, v79
	v_cvt_pk_bf16_f32 v69, v75, v69
	global_store_dwordx4 v[70:71], v[66:69], off
	v_exp_f32_e32 v63, v63
	v_mul_f32_e32 v55, v62, v55
	v_mul_f32_e32 v66, 0xbfb8aa3b, v65
	v_exp_f32_e32 v66, v66
	v_add_f32_e32 v62, 1.0, v63
	v_rcp_f32_e32 v62, v62
	v_mov_b32_e32 v158, v156
	v_add_f32_e32 v63, 1.0, v66
	v_mul_f32_e32 v66, 0xbfb8aa3b, v58
	v_rcp_f32_e32 v63, v63
	v_exp_f32_e32 v66, v66
	v_mul_f32_e32 v62, v64, v62
	v_mul_f32_e32 v56, v62, v56
	v_mul_f32_e32 v62, v65, v63
	v_add_f32_e32 v63, 1.0, v66
	v_rcp_f32_e32 v63, v63
	v_mul_f32_e32 v64, 0xbfb8aa3b, v59
	v_exp_f32_e32 v64, v64
	v_mul_f32_e32 v57, v62, v57
	v_mul_f32_e32 v58, v58, v63
	v_mul_f32_e32 v58, v58, v50
	v_add_f32_e32 v50, 1.0, v64
	v_mul_f32_e32 v62, 0xbfb8aa3b, v60
	v_rcp_f32_e32 v50, v50
	v_exp_f32_e32 v62, v62
	v_mul_f32_e32 v63, 0xbfb8aa3b, v61
	v_exp_f32_e32 v63, v63
	v_mul_f32_e32 v50, v59, v50
	v_add_f32_e32 v59, 1.0, v62
	v_rcp_f32_e32 v59, v59
	v_add_f32_e32 v62, 1.0, v63
	v_rcp_f32_e32 v62, v62
	v_mul_f32_e32 v63, v50, v51
	v_mul_f32_e32 v50, v60, v59
	v_mul_f32_e32 v59, v50, v52
	v_mul_f32_e32 v50, v61, v62
	v_mul_f32_e32 v53, v50, v53
	v_cvt_pk_bf16_f32 v50, v54, v55
	v_mul_f32_e32 v54, 0xbfb8aa3b, v46
	v_cvt_pk_bf16_f32 v51, v56, v57
	v_exp_f32_e32 v56, v54
	v_mul_f32_e32 v54, 0xbfb8aa3b, v47
	v_exp_f32_e32 v57, v54
	v_add_co_u32_e32 v54, vcc, s49, v114
	v_add_f32_e32 v56, 1.0, v56
	v_rcp_f32_e32 v56, v56
	v_add_f32_e32 v57, 1.0, v57
	v_rcp_f32_e32 v57, v57
	v_addc_co_u32_e32 v55, vcc, 0, v115, vcc
	v_mul_f32_e32 v46, v46, v56
	v_mul_f32_e32 v38, v46, v38
	v_mul_f32_e32 v46, v47, v57
	v_mul_f32_e32 v47, 0xbfb8aa3b, v48
	v_cvt_pk_bf16_f32 v52, v58, v63
	v_cvt_pk_bf16_f32 v53, v59, v53
	global_store_dwordx4 v[54:55], v[50:53], off
; __device__ __forceinline__ unsigned cvt_pk_bf16(float lo, float hi) { unsigned r; asm volatile("v_cvt_pk_bf16_f32 %0, %1, %2" : "=v"(r) : "v"(lo), "v"(hi)); return r; }
; __device__ __forceinline__ float fdivf(float a, float b) { return a * __builtin_amdgcn_rcpf(b); }
; #define PG8_WAIT_V(n) asm volatile("s_waitcnt vmcnt(" #n ")" ::: "memory")
; #define PG8_BAR __builtin_amdgcn_s_barrier()
; template <class Epi, class Sched>
; __device__ __forceinline__ void gemm_phase(LAS unsigned char* lds, const int K, const Sched& S, const Epi& E) {
;     ...
;         E(acc, cur, wr, wc, fr, fq);
;         if (!has_next) break;
; #pragma unroll
;         for (int a = 0; a < 2; ++a)
; #pragma unroll
;             for (int b = 0; b < 2; ++b)
; #pragma unroll
;                 for (int m = 0; m < 4; ++m)
; #pragma unroll
;                     for (int n = 0; n < 2; ++n) acc[a][b][m][n] = (f32x4){0.f, 0.f, 0.f, 0.f};
;         cur = nxt; cB = nB; c00 = n00; c01 = n01; c10 = n10; c11 = n11; ++ui;
;     }
;     PG8_WAIT_V(0);
;     if (wr == 0) PG8_BAR;
;     PG8_BAR;
;     __device__ __forceinline__ void operator()(const f32x4 (&acc)[2][2][4][2], const Unit& u, int wr, int wc, int fr, int fq) const {
;         const int row0 = u.rbase + wr * 64 + fr, col0 = u.pn * HALF + wc * 32 + 8 * fq;
; #pragma unroll
;         for (int ai = 0; ai < 2; ++ai)
; #pragma unroll
;             for (int m = 0; m < 4; ++m) { bf16_t* rowp = O + (size_t)(row0 + ai * HALF + m * 16) * FF + col0;
;                 float h[8];
; #pragma unroll
;                 for (int n = 0; n < 2; ++n)
; #pragma unroll
;                     for (int j = 0; j < 4; ++j) { const float g = acc[ai][0][m][n][j], up = acc[ai][1][m][n][j]; h[n * 4 + j] = fdivf(g, 1.f + __expf(-g)) * up; }
;                 u32x4 w; w.x = cvt_pk_bf16(h[0], h[1]); w.y = cvt_pk_bf16(h[2], h[3]); w.z = cvt_pk_bf16(h[4], h[5]); w.w = cvt_pk_bf16(h[6], h[7]);
;                 *(u32x4*)rowp = w; }
;     }
	v_exp_f32_e32 v47, v47
	v_mul_f32_e32 v39, v46, v39
	v_mul_f32_e32 v50, 0xbfb8aa3b, v49
	v_exp_f32_e32 v50, v50
	v_add_f32_e32 v46, 1.0, v47
	v_rcp_f32_e32 v46, v46
	v_mov_b32_e32 v136, v155
	v_add_f32_e32 v47, 1.0, v50
	v_mul_f32_e32 v50, 0xbfb8aa3b, v42
	v_rcp_f32_e32 v47, v47
	v_exp_f32_e32 v50, v50
	v_mul_f32_e32 v46, v48, v46
	v_mul_f32_e32 v40, v46, v40
	v_mul_f32_e32 v46, v49, v47
	v_add_f32_e32 v47, 1.0, v50
	v_rcp_f32_e32 v47, v47
	v_mul_f32_e32 v48, 0xbfb8aa3b, v43
	v_exp_f32_e32 v48, v48
	v_mul_f32_e32 v41, v46, v41
	v_mul_f32_e32 v42, v42, v47
	v_mul_f32_e32 v42, v42, v34
	v_add_f32_e32 v34, 1.0, v48
	v_mul_f32_e32 v46, 0xbfb8aa3b, v44
	v_rcp_f32_e32 v34, v34
	v_exp_f32_e32 v46, v46
	v_mul_f32_e32 v47, 0xbfb8aa3b, v45
	v_exp_f32_e32 v47, v47
	v_mul_f32_e32 v34, v43, v34
	v_add_f32_e32 v43, 1.0, v46
	v_rcp_f32_e32 v43, v43
	v_add_f32_e32 v46, 1.0, v47
	v_rcp_f32_e32 v46, v46
	v_mul_f32_e32 v47, v34, v35
	v_mul_f32_e32 v34, v44, v43
	v_mul_f32_e32 v43, v34, v36
	v_mul_f32_e32 v34, v45, v46
	v_mul_f32_e32 v37, v34, v37
	v_cvt_pk_bf16_f32 v34, v38, v39
	v_mul_f32_e32 v38, 0xbfb8aa3b, v30
	v_cvt_pk_bf16_f32 v35, v40, v41
	v_exp_f32_e32 v40, v38
	v_mul_f32_e32 v38, 0xbfb8aa3b, v31
	v_exp_f32_e32 v41, v38
	v_add_co_u32_e32 v38, vcc, s50, v114
	v_add_f32_e32 v40, 1.0, v40
	v_rcp_f32_e32 v40, v40
	v_add_f32_e32 v41, 1.0, v41
	v_rcp_f32_e32 v41, v41
	v_addc_co_u32_e32 v39, vcc, 0, v115, vcc
	v_mul_f32_e32 v30, v30, v40
	v_mul_f32_e32 v22, v30, v22
	v_mul_f32_e32 v30, v31, v41
	v_mul_f32_e32 v31, 0xbfb8aa3b, v32
	v_cvt_pk_bf16_f32 v36, v42, v47
	v_cvt_pk_bf16_f32 v37, v43, v37
	global_store_dwordx4 v[38:39], v[34:37], off
	v_exp_f32_e32 v31, v31
	v_mul_f32_e32 v23, v30, v23
	v_mul_f32_e32 v34, 0xbfb8aa3b, v33
	v_exp_f32_e32 v34, v34
	v_add_f32_e32 v30, 1.0, v31
	v_rcp_f32_e32 v30, v30
	v_mov_b32_e32 v138, v154
	v_add_f32_e32 v31, 1.0, v34
	v_mul_f32_e32 v34, 0xbfb8aa3b, v26
	v_rcp_f32_e32 v31, v31
	v_exp_f32_e32 v34, v34
	v_mul_f32_e32 v30, v32, v30
	v_mul_f32_e32 v24, v30, v24
	v_mul_f32_e32 v30, v33, v31
	v_add_f32_e32 v31, 1.0, v34
	v_rcp_f32_e32 v31, v31
	v_mul_f32_e32 v32, 0xbfb8aa3b, v27
	v_exp_f32_e32 v32, v32
	v_mul_f32_e32 v25, v30, v25
	v_mul_f32_e32 v26, v26, v31
	v_mul_f32_e32 v26, v26, v18
	v_add_f32_e32 v18, 1.0, v32
	v_mul_f32_e32 v30, 0xbfb8aa3b, v28
	v_rcp_f32_e32 v18, v18
	v_exp_f32_e32 v30, v30
	v_mul_f32_e32 v31, 0xbfb8aa3b, v29
	v_exp_f32_e32 v31, v31
	v_mul_f32_e32 v18, v27, v18
	v_add_f32_e32 v27, 1.0, v30
	v_rcp_f32_e32 v27, v27
	v_add_f32_e32 v30, 1.0, v31
	v_rcp_f32_e32 v30, v30
	v_mul_f32_e32 v31, v18, v19
	v_mul_f32_e32 v18, v28, v27
	v_mul_f32_e32 v27, v18, v20
	v_mul_f32_e32 v18, v29, v30
	v_mul_f32_e32 v21, v18, v21
	v_cvt_pk_bf16_f32 v18, v22, v23
	v_mul_f32_e32 v22, 0xbfb8aa3b, v14
	v_cvt_pk_bf16_f32 v19, v24, v25
	v_exp_f32_e32 v24, v22
	v_mul_f32_e32 v22, 0xbfb8aa3b, v15
	v_exp_f32_e32 v25, v22
	v_add_co_u32_e32 v22, vcc, s51, v114
	v_add_f32_e32 v24, 1.0, v24
	v_rcp_f32_e32 v24, v24
	v_add_f32_e32 v25, 1.0, v25
	v_rcp_f32_e32 v25, v25
	v_addc_co_u32_e32 v23, vcc, 0, v115, vcc
	v_mul_f32_e32 v14, v14, v24
	v_mul_f32_e32 v6, v14, v6
	v_mul_f32_e32 v14, v15, v25
	v_mul_f32_e32 v15, 0xbfb8aa3b, v16
	v_cvt_pk_bf16_f32 v20, v26, v31
	v_cvt_pk_bf16_f32 v21, v27, v21
	global_store_dwordx4 v[22:23], v[18:21], off
	v_exp_f32_e32 v15, v15
	v_mul_f32_e32 v7, v14, v7
	v_mul_f32_e32 v18, 0xbfb8aa3b, v17
	v_exp_f32_e32 v18, v18
	v_add_f32_e32 v14, 1.0, v15
	v_rcp_f32_e32 v14, v14
	v_mov_b32_e32 v140, v153
	v_add_f32_e32 v15, 1.0, v18
	v_mul_f32_e32 v18, 0xbfb8aa3b, v10
	v_rcp_f32_e32 v15, v15
	v_exp_f32_e32 v18, v18
	v_mul_f32_e32 v14, v16, v14
	v_mul_f32_e32 v8, v14, v8
	v_mul_f32_e32 v14, v17, v15
	v_add_f32_e32 v15, 1.0, v18
	v_rcp_f32_e32 v15, v15
	v_mul_f32_e32 v16, 0xbfb8aa3b, v11
	v_exp_f32_e32 v16, v16
	v_mul_f32_e32 v9, v14, v9
	v_mul_f32_e32 v10, v10, v15
	v_mul_f32_e32 v10, v10, v2
	v_add_f32_e32 v2, 1.0, v16
	v_mul_f32_e32 v14, 0xbfb8aa3b, v12
	v_rcp_f32_e32 v2, v2
	v_exp_f32_e32 v14, v14
	v_mul_f32_e32 v15, 0xbfb8aa3b, v13
	v_exp_f32_e32 v15, v15
	v_mul_f32_e32 v2, v11, v2
	v_add_f32_e32 v11, 1.0, v14
	v_rcp_f32_e32 v11, v11
	v_add_f32_e32 v14, 1.0, v15
	v_rcp_f32_e32 v14, v14
	v_mul_f32_e32 v15, v2, v3
	v_mul_f32_e32 v2, v12, v11
	v_mul_f32_e32 v11, v2, v4
	v_mul_f32_e32 v2, v13, v14
	v_mul_f32_e32 v5, v2, v5
	v_cvt_pk_bf16_f32 v2, v6, v7
	v_add_co_u32_e32 v6, vcc, 0x2c000, v114
	s_mov_b64 s[20:21], s[18:19]
	s_nop 0
	v_addc_co_u32_e32 v7, vcc, 0, v115, vcc
	s_and_b64 vcc, exec, s[16:17]
	v_cvt_pk_bf16_f32 v3, v8, v9
	v_cvt_pk_bf16_f32 v4, v10, v15
	v_cvt_pk_bf16_f32 v5, v11, v5
	global_store_dwordx4 v[6:7], v[2:5], off
	s_cbranch_vccz .LBB0_1822
	s_waitcnt vmcnt(0)
	s_cmpk_gt_u32 s30, 0xff
	s_cbranch_scc1 .LBB0_1835
	s_barrier

; #define PG8_STAGE(bufoff, gbase, v0, v1) do { \
;         __builtin_amdgcn_global_load_lds((const unsigned*)((const char*)(gbase) + (v0)), (LAS unsigned*)(lds + (bufoff) + ldsw), 16, 0, 0); \
;         __builtin_amdgcn_global_load_lds((const unsigned*)((const char*)(gbase) + (v1)), (LAS unsigned*)(lds + (bufoff) + ldsw + 8192), 16, 0, 0); } while (0)
; #define PG8_LDA(dst, b, h) do { _Pragma("unroll") for (int m = 0; m < 4; ++m) _Pragma("unroll") for (int k = 0; k < 2; ++k) dst[m][k] = *(const LAS bf16x8*)(lds + PG8_SA(b, h) + aoff + m * 2048 + k * 1024); } while (0)
; #define PG8_LDB(dst, b, h) do { _Pragma("unroll") for (int n = 0; n < 2; ++n) _Pragma("unroll") for (int k = 0; k < 2; ++k) dst[n][k] = *(const LAS bf16x8*)(lds + PG8_SB(b, h) + boff + n * 2048 + k * 1024); } while (0)
; #define PG8_MMA(ai, bj, At, Bt) do { __builtin_amdgcn_s_setprio(1); _Pragma("unroll") for (int m = 0; m < 4; ++m) _Pragma("unroll") for (int n = 0; n < 2; ++n) _Pragma("unroll") for (int k = 0; k < 2; ++k) \
;         acc[ai][bj][m][n] = __builtin_amdgcn_mfma_f32_16x16x32_bf16(Bt[n][k], At[m][k], acc[ai][bj][m][n], 0, 0, 0); __builtin_amdgcn_s_setprio(0); } while (0)
; #define PG8_WAIT_V(n) asm volatile("s_waitcnt vmcnt(" #n ")" ::: "memory")
; #define PG8_WAIT_L(n) asm volatile("s_waitcnt lgkmcnt(" #n ")" ::: "memory")
; #define PG8_BAR __builtin_amdgcn_s_barrier()
; #define PG8_SCHED __builtin_amdgcn_sched_barrier(0)
; template <class Epi, class Sched>
; __device__ __forceinline__ void gemm_phase(LAS unsigned char* lds, const int K, const Sched& S, const Epi& E) {
;     ...
;             PG8_LDB(B0, 0, 0); PG8_SCHED; PG8_LDA(At, 0, 0); PG8_STAGE(PG8_SA(1, 1), a1, c10, c11);
;             PG8_WAIT_L(8); PG8_BAR; PG8_WAIT_L(0); PG8_MMA(0, 0, At, B0); PG8_BAR; PG8_SCHED;
;             PG8_LDB(B1, 0, 1); PG8_STAGE(PG8_SB(0, 0), b2, voffB0, voffB1);
;             PG8_BAR; PG8_WAIT_L(0); PG8_MMA(0, 1, At, B1); PG8_BAR;
;             PG8_LDA(At, 0, 1); PG8_STAGE(PG8_SA(0, 0), a2, x00, x01);
;             PG8_BAR; PG8_WAIT_L(0); PG8_MMA(1, 0, At, B0); PG8_BAR; PG8_SCHED;
;             PG8_STAGE(PG8_SB(0, 1), b2 + hstep, voffB0, voffB1);
;             PG8_WAIT_V(6); PG8_BAR; PG8_MMA(1, 1, At, B1); PG8_BAR;
.LBB0_1898:
	s_add_u32 s40, s0, s38
	ds_read_b128 v[164:167], v153
	ds_read_b128 v[168:171], v153 offset:1024
	ds_read_b128 v[172:175], v153 offset:2048
	ds_read_b128 v[176:179], v153 offset:3072
	s_addc_u32 s41, s1, s39
	s_add_u32 s42, s40, 0x3ee90100
	s_addc_u32 s43, s41, 0
	s_cmpk_eq_i32 s38, 0x300
	s_cselect_b64 vcc, -1, 0
	s_and_b64 s[40:41], vcc, exec
	v_cndmask_b32_e32 v134, v162, v157, vcc
	s_cselect_b32 s45, s3, s43
	s_cselect_b32 s44, s2, s42
	v_cndmask_b32_e32 v139, v138, v159, vcc
	s_cselect_b32 s41, s37, s31
	s_cselect_b32 s40, s36, s29
	v_cndmask_b32_e32 v228, v136, v158, vcc
	s_add_u32 s42, s40, 0x40000
	s_addc_u32 s43, s41, 0
	v_lshl_add_u64 v[212:213], v[144:145], 0, s[38:39]
	s_add_i32 m0, s49, 0xc000
	ds_read_b128 v[180:183], v154
	ds_read_b128 v[184:187], v154 offset:1024
	ds_read_b128 v[188:191], v154 offset:2048
	ds_read_b128 v[192:195], v154 offset:3072
	ds_read_b128 v[196:199], v154 offset:4096
	ds_read_b128 v[200:203], v154 offset:5120
	ds_read_b128 v[204:207], v154 offset:6144
	ds_read_b128 v[208:211], v154 offset:7168
	global_load_lds_dwordx4 v[212:213], off
	v_lshl_add_u64 v[212:213], v[142:143], 0, s[38:39]
	s_add_i32 m0, s49, 0xe000
	s_nop 0
	global_load_lds_dwordx4 v[212:213], off
	s_waitcnt lgkmcnt(8)
	s_barrier
	s_waitcnt lgkmcnt(0)
	s_waitcnt lgkmcnt(0)
	v_mfma_f32_16x16x32_bf16 v[126:129], v[164:167], v[180:183], v[126:129]
	v_mfma_f32_16x16x32_bf16 v[122:125], v[172:175], v[180:183], v[122:125]
	v_mfma_f32_16x16x32_bf16 v[114:117], v[164:167], v[188:191], v[114:117]
	v_mfma_f32_16x16x32_bf16 v[106:109], v[172:175], v[188:191], v[106:109]
	v_mfma_f32_16x16x32_bf16 v[98:101], v[164:167], v[196:199], v[98:101]
	v_mfma_f32_16x16x32_bf16 v[90:93], v[172:175], v[196:199], v[90:93]
	v_mfma_f32_16x16x32_bf16 v[82:85], v[164:167], v[204:207], v[82:85]
	v_mfma_f32_16x16x32_bf16 v[74:77], v[172:175], v[204:207], v[74:77]
	v_mfma_f32_16x16x32_bf16 v[126:129], v[168:171], v[184:187], v[126:129]
	v_mfma_f32_16x16x32_bf16 v[122:125], v[176:179], v[184:187], v[122:125]
	v_mfma_f32_16x16x32_bf16 v[114:117], v[168:171], v[192:195], v[114:117]
	v_mfma_f32_16x16x32_bf16 v[106:109], v[176:179], v[192:195], v[106:109]
	v_mfma_f32_16x16x32_bf16 v[98:101], v[168:171], v[200:203], v[98:101]
	v_mfma_f32_16x16x32_bf16 v[90:93], v[176:179], v[200:203], v[90:93]
	v_mfma_f32_16x16x32_bf16 v[82:85], v[168:171], v[208:211], v[82:85]
	v_mfma_f32_16x16x32_bf16 v[74:77], v[176:179], v[208:211], v[74:77]
	s_barrier
	s_add_i32 s66, s59, s48
	v_lshl_add_u64 v[230:231], s[40:41], 0, v[132:133]
	s_mov_b32 m0, s66
	ds_read_b128 v[212:215], v155
	ds_read_b128 v[216:219], v155 offset:1024
	ds_read_b128 v[220:223], v155 offset:2048
	ds_read_b128 v[224:227], v155 offset:3072
	global_load_lds_dwordx4 v[230:231], off
	v_lshl_add_u64 v[232:233], s[40:41], 0, v[130:131]
	s_add_i32 m0, s66, 0x2000
	s_nop 0
	global_load_lds_dwordx4 v[232:233], off
	s_barrier
	s_waitcnt lgkmcnt(0)
	s_waitcnt lgkmcnt(0)
	v_mfma_f32_16x16x32_bf16 v[118:121], v[212:215], v[180:183], v[118:121]
	v_mfma_f32_16x16x32_bf16 v[110:113], v[220:223], v[180:183], v[110:113]
	v_mfma_f32_16x16x32_bf16 v[102:105], v[212:215], v[188:191], v[102:105]
	v_mfma_f32_16x16x32_bf16 v[94:97], v[220:223], v[188:191], v[94:97]
	v_mfma_f32_16x16x32_bf16 v[86:89], v[212:215], v[196:199], v[86:89]
	v_mfma_f32_16x16x32_bf16 v[78:81], v[220:223], v[196:199], v[78:81]
	v_mfma_f32_16x16x32_bf16 v[70:73], v[212:215], v[204:207], v[70:73]
	v_mfma_f32_16x16x32_bf16 v[66:69], v[220:223], v[204:207], v[66:69]
	v_mfma_f32_16x16x32_bf16 v[118:121], v[216:219], v[184:187], v[118:121]
	v_mfma_f32_16x16x32_bf16 v[110:113], v[224:227], v[184:187], v[110:113]
	v_mfma_f32_16x16x32_bf16 v[102:105], v[216:219], v[192:195], v[102:105]
	v_mfma_f32_16x16x32_bf16 v[94:97], v[224:227], v[192:195], v[94:97]
	v_mfma_f32_16x16x32_bf16 v[86:89], v[216:219], v[200:203], v[86:89]
	v_mfma_f32_16x16x32_bf16 v[78:81], v[224:227], v[200:203], v[78:81]
	v_mfma_f32_16x16x32_bf16 v[70:73], v[216:219], v[208:211], v[70:73]
	v_mfma_f32_16x16x32_bf16 v[66:69], v[224:227], v[208:211], v[66:69]
	s_mov_b32 m0, s49
	s_barrier
	ds_read_b128 v[180:183], v154 offset:16384
	ds_read_b128 v[184:187], v154 offset:17408
	ds_read_b128 v[188:191], v154 offset:18432
	ds_read_b128 v[192:195], v154 offset:19456
	ds_read_b128 v[196:199], v154 offset:20480
	ds_read_b128 v[200:203], v154 offset:21504
	ds_read_b128 v[204:207], v154 offset:22528
	ds_read_b128 v[208:211], v154 offset:23552
	global_load_lds_dwordx4 v134, s[44:45]
	s_mov_b32 m0, s50
	v_mov_b32_e32 v229, v135
	global_load_lds_dwordx4 v228, s[44:45]
	s_barrier
	s_waitcnt lgkmcnt(0)
	v_lshl_add_u64 v[234:235], s[44:45], 0, v[134:135]
	v_lshl_add_u64 v[228:229], s[44:45], 0, v[228:229]
	s_waitcnt lgkmcnt(0)
	v_mfma_f32_16x16x32_bf16 v[62:65], v[164:167], v[180:183], v[62:65]
	v_mfma_f32_16x16x32_bf16 v[58:61], v[172:175], v[180:183], v[58:61]
	v_mfma_f32_16x16x32_bf16 v[46:49], v[164:167], v[188:191], v[46:49]
	v_mfma_f32_16x16x32_bf16 v[42:45], v[172:175], v[188:191], v[42:45]
	v_mfma_f32_16x16x32_bf16 v[30:33], v[164:167], v[196:199], v[30:33]
	v_mfma_f32_16x16x32_bf16 v[26:29], v[172:175], v[196:199], v[26:29]
	v_mfma_f32_16x16x32_bf16 v[14:17], v[164:167], v[204:207], v[14:17]
	v_mfma_f32_16x16x32_bf16 v[10:13], v[172:175], v[204:207], v[10:13]
	v_mfma_f32_16x16x32_bf16 v[62:65], v[168:171], v[184:187], v[62:65]
	v_mfma_f32_16x16x32_bf16 v[58:61], v[176:179], v[184:187], v[58:61]
	v_mfma_f32_16x16x32_bf16 v[46:49], v[168:171], v[192:195], v[46:49]
	v_mfma_f32_16x16x32_bf16 v[42:45], v[176:179], v[192:195], v[42:45]
	v_mfma_f32_16x16x32_bf16 v[30:33], v[168:171], v[200:203], v[30:33]
	v_mfma_f32_16x16x32_bf16 v[26:29], v[176:179], v[200:203], v[26:29]
	v_mfma_f32_16x16x32_bf16 v[14:17], v[168:171], v[208:211], v[14:17]
	v_mfma_f32_16x16x32_bf16 v[10:13], v[176:179], v[208:211], v[10:13]
	s_barrier
; #define PG8_STAGE(bufoff, gbase, v0, v1) do { \
;         __builtin_amdgcn_global_load_lds((const unsigned*)((const char*)(gbase) + (v0)), (LAS unsigned*)(lds + (bufoff) + ldsw), 16, 0, 0); \
;         __builtin_amdgcn_global_load_lds((const unsigned*)((const char*)(gbase) + (v1)), (LAS unsigned*)(lds + (bufoff) + ldsw + 8192), 16, 0, 0); } while (0)
; #define PG8_LDA(dst, b, h) do { _Pragma("unroll") for (int m = 0; m < 4; ++m) _Pragma("unroll") for (int k = 0; k < 2; ++k) dst[m][k] = *(const LAS bf16x8*)(lds + PG8_SA(b, h) + aoff + m * 2048 + k * 1024); } while (0)
; #define PG8_LDB(dst, b, h) do { _Pragma("unroll") for (int n = 0; n < 2; ++n) _Pragma("unroll") for (int k = 0; k < 2; ++k) dst[n][k] = *(const LAS bf16x8*)(lds + PG8_SB(b, h) + boff + n * 2048 + k * 1024); } while (0)
; #define PG8_MMA(ai, bj, At, Bt) do { __builtin_amdgcn_s_setprio(1); _Pragma("unroll") for (int m = 0; m < 4; ++m) _Pragma("unroll") for (int n = 0; n < 2; ++n) _Pragma("unroll") for (int k = 0; k < 2; ++k) \
;         acc[ai][bj][m][n] = __builtin_amdgcn_mfma_f32_16x16x32_bf16(Bt[n][k], At[m][k], acc[ai][bj][m][n], 0, 0, 0); __builtin_amdgcn_s_setprio(0); } while (0)
; #define PG8_WAIT_V(n) asm volatile("s_waitcnt vmcnt(" #n ")" ::: "memory")
; #define PG8_WAIT_L(n) asm volatile("s_waitcnt lgkmcnt(" #n ")" ::: "memory")
; #define PG8_BAR __builtin_amdgcn_s_barrier()
; #define PG8_SCHED __builtin_amdgcn_sched_barrier(0)
; template <class Epi, class Sched>
; __device__ __forceinline__ void gemm_phase(LAS unsigned char* lds, const int K, const Sched& S, const Epi& E) {
;     ...
;             PG8_WAIT_V(6); PG8_BAR; PG8_MMA(1, 1, At, B1); PG8_BAR;
;             PG8_LDB(B0, 1, 0); PG8_SCHED; PG8_LDA(At, 1, 0); PG8_STAGE(PG8_SA(0, 1), a2, x10, x11);
;             PG8_WAIT_L(8); PG8_BAR; PG8_WAIT_L(0); PG8_MMA(0, 0, At, B0); PG8_BAR; PG8_SCHED;
;             PG8_LDB(B1, 1, 1); PG8_STAGE(PG8_SB(1, 0), b3, voffB0, voffB1);
;             PG8_BAR; PG8_WAIT_L(0); PG8_MMA(0, 1, At, B1); PG8_BAR;
;             PG8_LDA(At, 1, 1); PG8_STAGE(PG8_SA(1, 0), a3, x00, x01);
;             PG8_BAR; PG8_WAIT_L(0); PG8_MMA(1, 0, At, B0); PG8_BAR; PG8_SCHED;
	s_add_i32 s66, s60, s48
	v_lshl_add_u64 v[164:165], v[230:231], 0, s[4:5]
	s_mov_b32 m0, s66
	s_nop 0
	global_load_lds_dwordx4 v[164:165], off
	v_lshl_add_u64 v[164:165], v[232:233], 0, s[4:5]
	s_add_i32 m0, s66, 0x2000
	s_nop 0
	global_load_lds_dwordx4 v[164:165], off
	s_waitcnt vmcnt(6)
	s_barrier
	v_mfma_f32_16x16x32_bf16 v[54:57], v[212:215], v[180:183], v[54:57]
	v_mfma_f32_16x16x32_bf16 v[50:53], v[220:223], v[180:183], v[50:53]
	v_mfma_f32_16x16x32_bf16 v[38:41], v[212:215], v[188:191], v[38:41]
	v_mfma_f32_16x16x32_bf16 v[34:37], v[220:223], v[188:191], v[34:37]
	v_mfma_f32_16x16x32_bf16 v[22:25], v[212:215], v[196:199], v[22:25]
	v_mfma_f32_16x16x32_bf16 v[18:21], v[220:223], v[196:199], v[18:21]
	v_mfma_f32_16x16x32_bf16 v[6:9], v[212:215], v[204:207], v[6:9]
	v_mfma_f32_16x16x32_bf16 v[2:5], v[220:223], v[204:207], v[2:5]
	v_mfma_f32_16x16x32_bf16 v[54:57], v[216:219], v[184:187], v[54:57]
	v_mfma_f32_16x16x32_bf16 v[50:53], v[224:227], v[184:187], v[50:53]
	v_mfma_f32_16x16x32_bf16 v[38:41], v[216:219], v[192:195], v[38:41]
	v_mfma_f32_16x16x32_bf16 v[34:37], v[224:227], v[192:195], v[34:37]
	v_mfma_f32_16x16x32_bf16 v[22:25], v[216:219], v[200:203], v[22:25]
	v_mfma_f32_16x16x32_bf16 v[18:21], v[224:227], v[200:203], v[18:21]
	v_mfma_f32_16x16x32_bf16 v[6:9], v[216:219], v[208:211], v[6:9]
	v_mfma_f32_16x16x32_bf16 v[2:5], v[224:227], v[208:211], v[2:5]
	s_add_i32 s66, 0, 0x18000
	v_add_u32_e32 v134, s66, v151
	s_barrier
	ds_read_b128 v[164:167], v134
	ds_read_b128 v[168:171], v134 offset:1024
	ds_read_b128 v[172:175], v134 offset:2048
	ds_read_b128 v[176:179], v134 offset:3072
	s_mov_b32 m0, s51
	ds_read_b128 v[180:183], v154 offset:32768
	ds_read_b128 v[184:187], v154 offset:33792
	ds_read_b128 v[188:191], v154 offset:34816
	ds_read_b128 v[192:195], v154 offset:35840
	ds_read_b128 v[196:199], v154 offset:36864
	ds_read_b128 v[200:203], v154 offset:37888
	ds_read_b128 v[204:207], v154 offset:38912
	ds_read_b128 v[208:211], v154 offset:39936
	v_cndmask_b32_e32 v134, v140, v160, vcc
	global_load_lds_dwordx4 v139, s[44:45]
	s_mov_b32 m0, s52
	s_nop 0
	global_load_lds_dwordx4 v134, s[44:45]
	s_waitcnt lgkmcnt(8)
	s_barrier
	s_waitcnt lgkmcnt(0)
	s_waitcnt lgkmcnt(0)
	v_mfma_f32_16x16x32_bf16 v[126:129], v[164:167], v[180:183], v[126:129]
	v_mfma_f32_16x16x32_bf16 v[122:125], v[172:175], v[180:183], v[122:125]
	v_mfma_f32_16x16x32_bf16 v[114:117], v[164:167], v[188:191], v[114:117]
	v_mfma_f32_16x16x32_bf16 v[106:109], v[172:175], v[188:191], v[106:109]
	v_mfma_f32_16x16x32_bf16 v[98:101], v[164:167], v[196:199], v[98:101]
	v_mfma_f32_16x16x32_bf16 v[90:93], v[172:175], v[196:199], v[90:93]
	v_mfma_f32_16x16x32_bf16 v[82:85], v[164:167], v[204:207], v[82:85]
	v_mfma_f32_16x16x32_bf16 v[74:77], v[172:175], v[204:207], v[74:77]
	v_mfma_f32_16x16x32_bf16 v[126:129], v[168:171], v[184:187], v[126:129]
	v_mfma_f32_16x16x32_bf16 v[122:125], v[176:179], v[184:187], v[122:125]
	v_mfma_f32_16x16x32_bf16 v[114:117], v[168:171], v[192:195], v[114:117]
	v_mfma_f32_16x16x32_bf16 v[106:109], v[176:179], v[192:195], v[106:109]
	v_mfma_f32_16x16x32_bf16 v[98:101], v[168:171], v[200:203], v[98:101]
	v_mfma_f32_16x16x32_bf16 v[90:93], v[176:179], v[200:203], v[90:93]
	v_mfma_f32_16x16x32_bf16 v[82:85], v[168:171], v[208:211], v[82:85]
	v_mfma_f32_16x16x32_bf16 v[74:77], v[176:179], v[208:211], v[74:77]
	s_barrier
	s_add_i32 s44, 0, 0x1c000
	s_add_i32 s45, s66, s48
	v_add_u32_e32 v134, s44, v151
	v_lshl_add_u64 v[230:231], s[42:43], 0, v[132:133]
	s_mov_b32 m0, s45
	ds_read_b128 v[212:215], v134
	ds_read_b128 v[216:219], v134 offset:1024
	ds_read_b128 v[220:223], v134 offset:2048
	ds_read_b128 v[224:227], v134 offset:3072
	global_load_lds_dwordx4 v[230:231], off
	v_lshl_add_u64 v[230:231], s[42:43], 0, v[130:131]
	s_add_i32 m0, s45, 0x2000
	s_nop 0
	global_load_lds_dwordx4 v[230:231], off
	s_barrier
	s_waitcnt lgkmcnt(0)
	s_waitcnt lgkmcnt(0)
	v_mfma_f32_16x16x32_bf16 v[118:121], v[212:215], v[180:183], v[118:121]
	v_mfma_f32_16x16x32_bf16 v[110:113], v[220:223], v[180:183], v[110:113]
	v_mfma_f32_16x16x32_bf16 v[102:105], v[212:215], v[188:191], v[102:105]
	v_mfma_f32_16x16x32_bf16 v[94:97], v[220:223], v[188:191], v[94:97]
	v_mfma_f32_16x16x32_bf16 v[86:89], v[212:215], v[196:199], v[86:89]
	v_mfma_f32_16x16x32_bf16 v[78:81], v[220:223], v[196:199], v[78:81]
	v_mfma_f32_16x16x32_bf16 v[70:73], v[212:215], v[204:207], v[70:73]
	v_mfma_f32_16x16x32_bf16 v[66:69], v[220:223], v[204:207], v[66:69]
	v_mfma_f32_16x16x32_bf16 v[118:121], v[216:219], v[184:187], v[118:121]
	v_mfma_f32_16x16x32_bf16 v[110:113], v[224:227], v[184:187], v[110:113]
	v_mfma_f32_16x16x32_bf16 v[102:105], v[216:219], v[192:195], v[102:105]
	v_mfma_f32_16x16x32_bf16 v[94:97], v[224:227], v[192:195], v[94:97]
	v_mfma_f32_16x16x32_bf16 v[86:89], v[216:219], v[200:203], v[86:89]
	v_mfma_f32_16x16x32_bf16 v[78:81], v[224:227], v[200:203], v[78:81]
	v_mfma_f32_16x16x32_bf16 v[70:73], v[216:219], v[208:211], v[70:73]
	v_mfma_f32_16x16x32_bf16 v[66:69], v[224:227], v[208:211], v[66:69]
	s_mov_b32 m0, s55
	v_lshl_add_u64 v[230:231], v[234:235], 0, s[12:13]
	s_barrier
	ds_read_b128 v[180:183], v154 offset:49152
	ds_read_b128 v[184:187], v154 offset:50176
	ds_read_b128 v[188:191], v154 offset:51200
	ds_read_b128 v[192:195], v154 offset:52224
	ds_read_b128 v[196:199], v154 offset:53248
	ds_read_b128 v[200:203], v154 offset:54272
	ds_read_b128 v[204:207], v154 offset:55296
	ds_read_b128 v[208:211], v154 offset:56320
	global_load_lds_dwordx4 v[230:231], off
	v_lshl_add_u64 v[228:229], v[228:229], 0, s[12:13]
	s_mov_b32 m0, s56
	s_nop 0
	global_load_lds_dwordx4 v[228:229], off
	s_barrier
; #define PG8_STAGE(bufoff, gbase, v0, v1) do { \
;         __builtin_amdgcn_global_load_lds((const unsigned*)((const char*)(gbase) + (v0)), (LAS unsigned*)(lds + (bufoff) + ldsw), 16, 0, 0); \
;         __builtin_amdgcn_global_load_lds((const unsigned*)((const char*)(gbase) + (v1)), (LAS unsigned*)(lds + (bufoff) + ldsw + 8192), 16, 0, 0); } while (0)
; #define PG8_MMA(ai, bj, At, Bt) do { __builtin_amdgcn_s_setprio(1); _Pragma("unroll") for (int m = 0; m < 4; ++m) _Pragma("unroll") for (int n = 0; n < 2; ++n) _Pragma("unroll") for (int k = 0; k < 2; ++k) \
;         acc[ai][bj][m][n] = __builtin_amdgcn_mfma_f32_16x16x32_bf16(Bt[n][k], At[m][k], acc[ai][bj][m][n], 0, 0, 0); __builtin_amdgcn_s_setprio(0); } while (0)
; #define PG8_WAIT_V(n) asm volatile("s_waitcnt vmcnt(" #n ")" ::: "memory")
; #define PG8_WAIT_L(n) asm volatile("s_waitcnt lgkmcnt(" #n ")" ::: "memory")
; #define PG8_BAR __builtin_amdgcn_s_barrier()
; #define PG8_SCHED __builtin_amdgcn_sched_barrier(0)
; __device__ __forceinline__ unsigned pk4_fp8(float a, float b, float c, float d) { int w = 0; w = __builtin_amdgcn_cvt_pk_fp8_f32(a, b, w, false); w = __builtin_amdgcn_cvt_pk_fp8_f32(c, d, w, true); return (unsigned)w; }
; template <class Epi, class Sched>
; __device__ __forceinline__ void gemm_phase(LAS unsigned char* lds, const int K, const Sched& S, const Epi& E) {
;     ...
;             PG8_BAR; PG8_WAIT_L(0); PG8_MMA(1, 0, At, B0); PG8_BAR; PG8_SCHED;
;             PG8_STAGE(PG8_SB(1, 1), b3 + hstep, voffB0, voffB1);
;             PG8_WAIT_V(6); PG8_BAR; PG8_MMA(1, 1, At, B1); PG8_BAR;
;     __device__ __forceinline__ void operator()(const f32x4 (&acc)[2][2][4][2], const Unit& u, int wr, int wc, int fr, int fq) const {
;         const int row0 = u.rbase + wr * 64 + fr, col0 = u.pn * BM + wc * 32 + 8 * fq;
; #pragma unroll
;         for (int ai = 0; ai < 2; ++ai)
; #pragma unroll
;             for (int m = 0; m < 4; ++m) { unsigned char* rowp = O + (size_t)(row0 + ai * HALF + m * 16) * ldc + col0;
; #pragma unroll
;                 for (int bj = 0; bj < 2; ++bj) { const f32x4 v0 = acc[ai][bj][m][0] * scale, v1 = acc[ai][bj][m][1] * scale;
;                     u32x2 w; w.x = pk4_fp8(v0[0], v0[1], v0[2], v0[3]); w.y = pk4_fp8(v1[0], v1[1], v1[2], v1[3]);
;                     *(u32x2*)(rowp + bj * HALF) = w; } }
;     }
	s_waitcnt lgkmcnt(0)
	s_waitcnt lgkmcnt(0)
	v_mfma_f32_16x16x32_bf16 v[62:65], v[164:167], v[180:183], v[62:65]
	v_mfma_f32_16x16x32_bf16 v[58:61], v[172:175], v[180:183], v[58:61]
	v_mfma_f32_16x16x32_bf16 v[46:49], v[164:167], v[188:191], v[46:49]
	v_mfma_f32_16x16x32_bf16 v[42:45], v[172:175], v[188:191], v[42:45]
	v_mfma_f32_16x16x32_bf16 v[30:33], v[164:167], v[196:199], v[30:33]
	v_mfma_f32_16x16x32_bf16 v[26:29], v[172:175], v[196:199], v[26:29]
	v_mfma_f32_16x16x32_bf16 v[14:17], v[164:167], v[204:207], v[14:17]
	v_mfma_f32_16x16x32_bf16 v[10:13], v[172:175], v[204:207], v[10:13]
	v_mfma_f32_16x16x32_bf16 v[62:65], v[168:171], v[184:187], v[62:65]
	v_mfma_f32_16x16x32_bf16 v[58:61], v[176:179], v[184:187], v[58:61]
	v_mfma_f32_16x16x32_bf16 v[46:49], v[168:171], v[192:195], v[46:49]
	v_mfma_f32_16x16x32_bf16 v[42:45], v[176:179], v[192:195], v[42:45]
	v_mfma_f32_16x16x32_bf16 v[30:33], v[168:171], v[200:203], v[30:33]
	v_mfma_f32_16x16x32_bf16 v[26:29], v[176:179], v[200:203], v[26:29]
	v_mfma_f32_16x16x32_bf16 v[14:17], v[168:171], v[208:211], v[14:17]
	v_mfma_f32_16x16x32_bf16 v[10:13], v[176:179], v[208:211], v[10:13]
	s_barrier
	s_add_u32 s40, s40, 0x40800
	s_addc_u32 s41, s41, 0
	s_add_i32 s42, s44, s48
	v_lshl_add_u64 v[164:165], s[40:41], 0, v[132:133]
	s_mov_b32 m0, s42
	s_nop 0
	global_load_lds_dwordx4 v[164:165], off
	v_lshl_add_u64 v[164:165], s[40:41], 0, v[130:131]
	s_add_i32 m0, s42, 0x2000
	s_nop 0
	global_load_lds_dwordx4 v[164:165], off
	s_waitcnt vmcnt(6)
	s_barrier
	v_mfma_f32_16x16x32_bf16 v[54:57], v[212:215], v[180:183], v[54:57]
	v_mfma_f32_16x16x32_bf16 v[50:53], v[220:223], v[180:183], v[50:53]
	v_mfma_f32_16x16x32_bf16 v[38:41], v[212:215], v[188:191], v[38:41]
	v_mfma_f32_16x16x32_bf16 v[34:37], v[220:223], v[188:191], v[34:37]
	v_mfma_f32_16x16x32_bf16 v[22:25], v[212:215], v[196:199], v[22:25]
	v_mfma_f32_16x16x32_bf16 v[18:21], v[220:223], v[196:199], v[18:21]
	v_mfma_f32_16x16x32_bf16 v[6:9], v[212:215], v[204:207], v[6:9]
	v_mfma_f32_16x16x32_bf16 v[2:5], v[220:223], v[204:207], v[2:5]
	v_mfma_f32_16x16x32_bf16 v[54:57], v[216:219], v[184:187], v[54:57]
	v_mfma_f32_16x16x32_bf16 v[50:53], v[224:227], v[184:187], v[50:53]
	v_mfma_f32_16x16x32_bf16 v[38:41], v[216:219], v[192:195], v[38:41]
	v_mfma_f32_16x16x32_bf16 v[34:37], v[224:227], v[192:195], v[34:37]
	v_mfma_f32_16x16x32_bf16 v[22:25], v[216:219], v[200:203], v[22:25]
	v_mfma_f32_16x16x32_bf16 v[18:21], v[224:227], v[200:203], v[18:21]
	v_mfma_f32_16x16x32_bf16 v[6:9], v[216:219], v[208:211], v[6:9]
	v_mfma_f32_16x16x32_bf16 v[2:5], v[224:227], v[208:211], v[2:5]
	s_add_i32 s65, s65, 2
	s_add_u32 s29, s29, 0x80000
	s_addc_u32 s31, s31, 0
	s_add_u32 s38, s38, 0x100
	s_addc_u32 s39, s39, 0
	s_cmp_gt_u32 s65, 5
	s_barrier
	s_cbranch_scc0 .LBB0_1898
	v_pk_mul_f32 v[126:127], v[126:127], s[14:15] op_sel_hi:[1,0]
	v_mov_b32_e32 v142, v135
	v_cvt_pk_fp8_f32 v142, v126, v127
	v_pk_mul_f32 v[122:123], v[122:123], s[14:15] op_sel_hi:[1,0]
	v_mov_b32_e32 v143, v135
	v_cvt_pk_fp8_f32 v143, v122, v123
	v_pk_mul_f32 v[122:123], v[128:129], s[14:15] op_sel_hi:[1,0]
	v_pk_mul_f32 v[118:119], v[118:119], s[14:15] op_sel_hi:[1,0]
	v_cvt_pk_fp8_f32 v142, v122, v123 op_sel:[0,0,1]
	v_mov_b32_e32 v122, v135
	v_cvt_pk_fp8_f32 v122, v118, v119
	v_pk_mul_f32 v[114:115], v[114:115], s[14:15] op_sel_hi:[1,0]
	v_mov_b32_e32 v118, v135
	v_cvt_pk_fp8_f32 v118, v114, v115
	v_pk_mul_f32 v[106:107], v[106:107], s[14:15] op_sel_hi:[1,0]
	v_mov_b32_e32 v119, v135
	v_cvt_pk_fp8_f32 v119, v106, v107
	v_pk_mul_f32 v[106:107], v[116:117], s[14:15] op_sel_hi:[1,0]
	v_pk_mul_f32 v[94:95], v[94:95], s[14:15] op_sel_hi:[1,0]
	v_cvt_pk_fp8_f32 v118, v106, v107 op_sel:[0,0,1]
	v_mov_b32_e32 v107, v135
	v_cvt_pk_fp8_f32 v107, v94, v95
	v_pk_mul_f32 v[96:97], v[96:97], s[14:15] op_sel_hi:[1,0]
	v_pk_mul_f32 v[90:91], v[90:91], s[14:15] op_sel_hi:[1,0]
	v_pk_mul_f32 v[78:79], v[78:79], s[14:15] op_sel_hi:[1,0]
	v_cvt_pk_fp8_f32 v107, v96, v97 op_sel:[0,0,1]
	v_pk_mul_f32 v[96:97], v[98:99], s[14:15] op_sel_hi:[1,0]
	v_mov_b32_e32 v98, v135
	v_cvt_pk_fp8_f32 v98, v96, v97
	v_mov_b32_e32 v99, v135
	v_cvt_pk_fp8_f32 v99, v90, v91
	v_pk_mul_f32 v[90:91], v[100:101], s[14:15] op_sel_hi:[1,0]
	v_pk_mul_f32 v[80:81], v[80:81], s[14:15] op_sel_hi:[1,0]
	v_cvt_pk_fp8_f32 v98, v90, v91 op_sel:[0,0,1]
	v_mov_b32_e32 v91, v135
	v_cvt_pk_fp8_f32 v91, v78, v79
	v_pk_mul_f32 v[74:75], v[74:75], s[14:15] op_sel_hi:[1,0]
	v_pk_mul_f32 v[66:67], v[66:67], s[14:15] op_sel_hi:[1,0]
	v_pk_mul_f32 v[68:69], v[68:69], s[14:15] op_sel_hi:[1,0]
	v_cvt_pk_fp8_f32 v91, v80, v81 op_sel:[0,0,1]
	v_pk_mul_f32 v[80:81], v[82:83], s[14:15] op_sel_hi:[1,0]
	v_mov_b32_e32 v82, v135
	v_cvt_pk_fp8_f32 v82, v80, v81
	v_mov_b32_e32 v83, v135
	v_cvt_pk_fp8_f32 v83, v74, v75
	v_pk_mul_f32 v[74:75], v[84:85], s[14:15] op_sel_hi:[1,0]
	v_pk_mul_f32 v[62:63], v[62:63], s[14:15] op_sel_hi:[1,0]
	v_cvt_pk_fp8_f32 v82, v74, v75 op_sel:[0,0,1]
	v_mov_b32_e32 v75, v135
	v_cvt_pk_fp8_f32 v75, v66, v67
	v_pk_mul_f32 v[58:59], v[58:59], s[14:15] op_sel_hi:[1,0]
	v_pk_mul_f32 v[50:51], v[50:51], s[14:15] op_sel_hi:[1,0]
	v_pk_mul_f32 v[52:53], v[52:53], s[14:15] op_sel_hi:[1,0]
	v_cvt_pk_fp8_f32 v75, v68, v69 op_sel:[0,0,1]
	v_mov_b32_e32 v68, v135
	v_cvt_pk_fp8_f32 v68, v62, v63
	v_mov_b32_e32 v69, v135
	v_cvt_pk_fp8_f32 v69, v58, v59
	v_pk_mul_f32 v[58:59], v[64:65], s[14:15] op_sel_hi:[1,0]
	v_pk_mul_f32 v[46:47], v[46:47], s[14:15] op_sel_hi:[1,0]
	v_cvt_pk_fp8_f32 v68, v58, v59 op_sel:[0,0,1]
	v_mov_b32_e32 v59, v135
	v_cvt_pk_fp8_f32 v59, v50, v51
	v_pk_mul_f32 v[42:43], v[42:43], s[14:15] op_sel_hi:[1,0]
; #define PG8_WAIT_V(n) asm volatile("s_waitcnt vmcnt(" #n ")" ::: "memory")
; #define PG8_BAR __builtin_amdgcn_s_barrier()
; __device__ __forceinline__ unsigned pk4_fp8(float a, float b, float c, float d) { int w = 0; w = __builtin_amdgcn_cvt_pk_fp8_f32(a, b, w, false); w = __builtin_amdgcn_cvt_pk_fp8_f32(c, d, w, true); return (unsigned)w; }
; template <class Epi, class Sched>
; __device__ __forceinline__ void gemm_phase(LAS unsigned char* lds, const int K, const Sched& S, const Epi& E) {
;     ...
;         E(acc, cur, wr, wc, fr, fq);
;         if (!has_next) break;
; #pragma unroll
;         for (int a = 0; a < 2; ++a)
; #pragma unroll
;             for (int b = 0; b < 2; ++b)
; #pragma unroll
;                 for (int m = 0; m < 4; ++m)
; #pragma unroll
;                     for (int n = 0; n < 2; ++n) acc[a][b][m][n] = (f32x4){0.f, 0.f, 0.f, 0.f};
;         cur = nxt; cB = nB; c00 = n00; c01 = n01; c10 = n10; c11 = n11; ++ui;
;     }
;     PG8_WAIT_V(0);
;     if (wr == 0) PG8_BAR;
;     PG8_BAR;
;     __device__ __forceinline__ void operator()(const f32x4 (&acc)[2][2][4][2], const Unit& u, int wr, int wc, int fr, int fq) const {
;         const int row0 = u.rbase + wr * 64 + fr, col0 = u.pn * BM + wc * 32 + 8 * fq;
; #pragma unroll
;         for (int ai = 0; ai < 2; ++ai)
; #pragma unroll
;             for (int m = 0; m < 4; ++m) { unsigned char* rowp = O + (size_t)(row0 + ai * HALF + m * 16) * ldc + col0;
; #pragma unroll
;                 for (int bj = 0; bj < 2; ++bj) { const f32x4 v0 = acc[ai][bj][m][0] * scale, v1 = acc[ai][bj][m][1] * scale;
;                     u32x2 w; w.x = pk4_fp8(v0[0], v0[1], v0[2], v0[3]); w.y = pk4_fp8(v1[0], v1[1], v1[2], v1[3]);
;                     *(u32x2*)(rowp + bj * HALF) = w; } }
;     }
	v_pk_mul_f32 v[34:35], v[34:35], s[14:15] op_sel_hi:[1,0]
	v_pk_mul_f32 v[36:37], v[36:37], s[14:15] op_sel_hi:[1,0]
	v_cvt_pk_fp8_f32 v59, v52, v53 op_sel:[0,0,1]
	v_mov_b32_e32 v52, v135
	v_cvt_pk_fp8_f32 v52, v46, v47
	v_mov_b32_e32 v53, v135
	v_cvt_pk_fp8_f32 v53, v42, v43
	v_pk_mul_f32 v[42:43], v[48:49], s[14:15] op_sel_hi:[1,0]
	v_pk_mul_f32 v[30:31], v[30:31], s[14:15] op_sel_hi:[1,0]
	v_cvt_pk_fp8_f32 v52, v42, v43 op_sel:[0,0,1]
	v_mov_b32_e32 v43, v135
	v_cvt_pk_fp8_f32 v43, v34, v35
	v_add_u32_e32 v138, v161, v137
	v_pk_mul_f32 v[102:103], v[102:103], s[14:15] op_sel_hi:[1,0]
	v_mov_b32_e32 v106, v135
	v_cvt_pk_fp8_f32 v43, v36, v37 op_sel:[0,0,1]
	v_mov_b32_e32 v36, v135
	v_cvt_pk_fp8_f32 v36, v30, v31
	v_pk_mul_f32 v[26:27], v[26:27], s[14:15] op_sel_hi:[1,0]
	v_mov_b32_e32 v37, v135
	v_readlane_b32 s29, v254, 39
	v_ashrrev_i32_e32 v139, 31, v138
	v_pk_mul_f32 v[110:111], v[110:111], s[14:15] op_sel_hi:[1,0]
	v_mov_b32_e32 v123, v135
	v_cvt_pk_fp8_f32 v106, v102, v103
	v_cvt_pk_fp8_f32 v37, v26, v27
	v_pk_mul_f32 v[26:27], v[32:33], s[14:15] op_sel_hi:[1,0]
	v_lshl_or_b32 v140, s29, 8, v152
	v_lshlrev_b64 v[138:139], 11, v[138:139]
	v_cvt_pk_fp8_f32 v123, v110, v111
	v_pk_mul_f32 v[110:111], v[120:121], s[14:15] op_sel_hi:[1,0]
	v_pk_mul_f32 v[86:87], v[86:87], s[14:15] op_sel_hi:[1,0]
	v_mov_b32_e32 v90, v135
	v_cvt_pk_fp8_f32 v36, v26, v27 op_sel:[0,0,1]
	v_pk_mul_f32 v[18:19], v[18:19], s[14:15] op_sel_hi:[1,0]
	v_mov_b32_e32 v27, v135
	v_ashrrev_i32_e32 v141, 31, v140
	v_cvt_pk_fp8_f32 v122, v110, v111 op_sel:[0,0,1]
	v_lshl_add_u64 v[110:111], s[6:7], 0, v[138:139]
	v_cvt_pk_fp8_f32 v90, v86, v87
	v_cvt_pk_fp8_f32 v27, v18, v19
	v_lshl_add_u64 v[110:111], v[110:111], 0, v[140:141]
	v_pk_mul_f32 v[94:95], v[104:105], s[14:15] op_sel_hi:[1,0]
	v_pk_mul_f32 v[70:71], v[70:71], s[14:15] op_sel_hi:[1,0]
	v_mov_b32_e32 v74, v135
	v_cvt_pk_fp8_f32 v106, v94, v95 op_sel:[0,0,1]
	v_add_co_u32_e32 v94, vcc, s58, v110
	v_cvt_pk_fp8_f32 v74, v70, v71
	s_nop 0
	v_addc_co_u32_e32 v95, vcc, 0, v111, vcc
	v_pk_mul_f32 v[78:79], v[88:89], s[14:15] op_sel_hi:[1,0]
	v_pk_mul_f32 v[54:55], v[54:55], s[14:15] op_sel_hi:[1,0]
	v_mov_b32_e32 v58, v135
	v_pk_mul_f32 v[20:21], v[20:21], s[14:15] op_sel_hi:[1,0]
	v_cvt_pk_fp8_f32 v90, v78, v79 op_sel:[0,0,1]
	v_add_co_u32_e32 v78, vcc, s54, v110
	v_cvt_pk_fp8_f32 v58, v54, v55
	v_cvt_pk_fp8_f32 v27, v20, v21 op_sel:[0,0,1]
	v_pk_mul_f32 v[14:15], v[14:15], s[14:15] op_sel_hi:[1,0]
	v_mov_b32_e32 v20, v135
	v_addc_co_u32_e32 v79, vcc, 0, v111, vcc
	v_pk_mul_f32 v[66:67], v[72:73], s[14:15] op_sel_hi:[1,0]
	v_pk_mul_f32 v[38:39], v[38:39], s[14:15] op_sel_hi:[1,0]
	v_mov_b32_e32 v42, v135
	v_cvt_pk_fp8_f32 v20, v14, v15
	v_cvt_pk_fp8_f32 v74, v66, v67 op_sel:[0,0,1]
	v_add_co_u32_e32 v66, vcc, s57, v110
	v_cvt_pk_fp8_f32 v42, v38, v39
	s_nop 0
	v_addc_co_u32_e32 v67, vcc, 0, v111, vcc
	v_pk_mul_f32 v[50:51], v[56:57], s[14:15] op_sel_hi:[1,0]
	v_pk_mul_f32 v[22:23], v[22:23], s[14:15] op_sel_hi:[1,0]
	v_mov_b32_e32 v26, v135
	v_pk_mul_f32 v[10:11], v[10:11], s[14:15] op_sel_hi:[1,0]
	v_mov_b32_e32 v21, v135
	v_cvt_pk_fp8_f32 v58, v50, v51 op_sel:[0,0,1]
	v_add_co_u32_e32 v50, vcc, s61, v110
	v_cvt_pk_fp8_f32 v26, v22, v23
	v_cvt_pk_fp8_f32 v21, v10, v11
	v_pk_mul_f32 v[10:11], v[16:17], s[14:15] op_sel_hi:[1,0]
	v_addc_co_u32_e32 v51, vcc, 0, v111, vcc
	v_pk_mul_f32 v[34:35], v[40:41], s[14:15] op_sel_hi:[1,0]
	v_cvt_pk_fp8_f32 v20, v10, v11 op_sel:[0,0,1]
	v_pk_mul_f32 v[6:7], v[6:7], s[14:15] op_sel_hi:[1,0]
	v_pk_mul_f32 v[2:3], v[2:3], s[14:15] op_sel_hi:[1,0]
	v_mov_b32_e32 v10, v135
	v_mov_b32_e32 v11, v135
	v_cvt_pk_fp8_f32 v42, v34, v35 op_sel:[0,0,1]
	v_add_co_u32_e32 v34, vcc, s62, v110
	v_cvt_pk_fp8_f32 v10, v6, v7
	v_cvt_pk_fp8_f32 v11, v2, v3
	v_addc_co_u32_e32 v35, vcc, 0, v111, vcc
	v_pk_mul_f32 v[18:19], v[24:25], s[14:15] op_sel_hi:[1,0]
	v_pk_mul_f32 v[124:125], v[124:125], s[14:15] op_sel_hi:[1,0]
	v_pk_mul_f32 v[108:109], v[108:109], s[14:15] op_sel_hi:[1,0]
	v_pk_mul_f32 v[92:93], v[92:93], s[14:15] op_sel_hi:[1,0]
	v_pk_mul_f32 v[76:77], v[76:77], s[14:15] op_sel_hi:[1,0]
	v_pk_mul_f32 v[60:61], v[60:61], s[14:15] op_sel_hi:[1,0]
	v_pk_mul_f32 v[44:45], v[44:45], s[14:15] op_sel_hi:[1,0]
	v_pk_mul_f32 v[28:29], v[28:29], s[14:15] op_sel_hi:[1,0]
	v_cvt_pk_fp8_f32 v26, v18, v19 op_sel:[0,0,1]
	v_add_co_u32_e32 v18, vcc, s63, v110
	v_pk_mul_f32 v[12:13], v[12:13], s[14:15] op_sel_hi:[1,0]
	v_cvt_pk_fp8_f32 v143, v124, v125 op_sel:[0,0,1]
	v_pk_mul_f32 v[112:113], v[112:113], s[14:15] op_sel_hi:[1,0]
	v_cvt_pk_fp8_f32 v119, v108, v109 op_sel:[0,0,1]
	v_cvt_pk_fp8_f32 v99, v92, v93 op_sel:[0,0,1]
	v_cvt_pk_fp8_f32 v83, v76, v77 op_sel:[0,0,1]
	v_cvt_pk_fp8_f32 v69, v60, v61 op_sel:[0,0,1]
	v_cvt_pk_fp8_f32 v53, v44, v45 op_sel:[0,0,1]
	v_cvt_pk_fp8_f32 v37, v28, v29 op_sel:[0,0,1]
	v_addc_co_u32_e32 v19, vcc, 0, v111, vcc
	v_cvt_pk_fp8_f32 v21, v12, v13 op_sel:[0,0,1]
	v_pk_mul_f32 v[2:3], v[8:9], s[14:15] op_sel_hi:[1,0]
	v_pk_mul_f32 v[4:5], v[4:5], s[14:15] op_sel_hi:[1,0]
	v_cvt_pk_fp8_f32 v123, v112, v113 op_sel:[0,0,1]
	v_cvt_pk_fp8_f32 v10, v2, v3 op_sel:[0,0,1]
	v_cvt_pk_fp8_f32 v11, v4, v5 op_sel:[0,0,1]
	v_add_co_u32_e32 v2, vcc, s64, v110
	s_mov_b32 s29, s28
	s_nop 0
	v_addc_co_u32_e32 v3, vcc, 0, v111, vcc
	s_and_b64 vcc, exec, s[34:35]
	v_mov_b32_e32 v161, v156
	v_writelane_b32 v254, s29, 39
	v_mov_b32_e32 v162, v157
	v_mov_b32_e32 v136, v158
	v_mov_b32_e32 v138, v159
	v_mov_b32_e32 v140, v160
	s_mov_b64 s[38:39], s[36:37]
	global_store_dwordx2 v[110:111], v[142:143], off
	global_store_dwordx2 v[110:111], v[122:123], off offset:128
	v_lshl_add_u64 v[112:113], v[110:111], 0, s[16:17]
	global_store_dwordx2 v[94:95], v[118:119], off
	global_store_dwordx2 v[112:113], v[106:107], off offset:128
	v_lshl_add_u64 v[94:95], v[110:111], 0, s[18:19]
	global_store_dwordx2 v[78:79], v[98:99], off
	global_store_dwordx2 v[94:95], v[90:91], off offset:128
	v_lshl_add_u64 v[78:79], v[110:111], 0, s[20:21]
	global_store_dwordx2 v[66:67], v[82:83], off
	global_store_dwordx2 v[78:79], v[74:75], off offset:128
	v_lshl_add_u64 v[66:67], v[110:111], 0, s[10:11]
	global_store_dwordx2 v[50:51], v[68:69], off
	global_store_dwordx2 v[66:67], v[58:59], off offset:128
	v_lshl_add_u64 v[50:51], v[110:111], 0, s[22:23]
	global_store_dwordx2 v[34:35], v[52:53], off
	global_store_dwordx2 v[50:51], v[42:43], off offset:128
	v_lshl_add_u64 v[34:35], v[110:111], 0, s[24:25]
	global_store_dwordx2 v[18:19], v[36:37], off
	global_store_dwordx2 v[34:35], v[26:27], off offset:128
	v_lshl_add_u64 v[18:19], v[110:111], 0, s[26:27]
	global_store_dwordx2 v[2:3], v[20:21], off
	global_store_dwordx2 v[18:19], v[10:11], off offset:128
	s_cbranch_vccz .LBB0_1893
	s_waitcnt vmcnt(0)
	s_cmpk_gt_u32 s33, 0xff
	s_cbranch_scc1 .LBB0_1902
	s_barrier
